# wait cleanup: five provably satisfied lgkmcnt waits removed from the attention loop's second half; the vmcnt(8)/lgkmcnt(0) pair before each K-loop barrier merged into one s_waitcnt
# baseline (speedup 1.0000x reference)
.Lpeelph1b_0:
	s_add_i32 s73, s60, 2
	s_add_u32 s61, s58, 0xfffc0080
	s_addc_u32 s62, s59, -1
	s_add_i32 s74, 0, 0x10000
	s_cmp_eq_u32 s68, s60
	s_cselect_b32 s63, s39, s62
	s_cselect_b32 s62, s43, s61
	s_cselect_b32 s61, s47, s72
	s_cselect_b32 s60, s55, s71
	s_add_i32 s76, 0, 0x14000
	v_add_u32_e32 v156, s74, v165
	v_add_u32_e32 v166, s76, v165
	ds_read_b128 v[144:147], v156
	ds_read_b128 v[148:151], v156 offset:1024
	ds_read_b128 v[152:155], v156 offset:2048
	ds_read_b128 v[156:159], v156 offset:3072
	ds_read_b128 v[160:163], v166
	ds_read_b128 v[170:173], v166 offset:1024
	ds_read_b128 v[174:177], v166 offset:2048
	ds_read_b128 v[180:183], v166 offset:3072
	v_lshl_add_u64 v[216:217], s[58:59], 0, v[142:143]
	s_add_i32 m0, s8, 0xc000
	ds_read_b128 v[184:187], v178
	ds_read_b128 v[188:191], v178 offset:1024
	ds_read_b128 v[192:195], v178 offset:2048
	ds_read_b128 v[196:199], v178 offset:3072
	ds_read_b128 v[200:203], v178 offset:4096
	ds_read_b128 v[204:207], v178 offset:5120
	ds_read_b128 v[208:211], v178 offset:6144
	ds_read_b128 v[212:215], v178 offset:7168
	global_load_lds_dwordx4 v[216:217], off
	v_lshl_add_u64 v[216:217], s[58:59], 0, v[140:141]
	s_add_i32 m0, s8, 0xe000
	s_nop 0
	global_load_lds_dwordx4 v[216:217], off
	s_waitcnt vmcnt(8) lgkmcnt(0)
	s_barrier
	s_setprio 1
	v_mfma_f32_16x16x32_bf16 v[126:129], v[144:147], v[184:187], 0
	v_mfma_f32_16x16x32_bf16 v[122:125], v[152:155], v[184:187], 0
	v_mfma_f32_16x16x32_bf16 v[110:113], v[144:147], v[192:195], 0
	v_mfma_f32_16x16x32_bf16 v[106:109], v[152:155], v[192:195], 0
	v_mfma_f32_16x16x32_bf16 v[94:97], v[144:147], v[200:203], 0
	v_mfma_f32_16x16x32_bf16 v[90:93], v[152:155], v[200:203], 0
	v_mfma_f32_16x16x32_bf16 v[78:81], v[144:147], v[208:211], 0
	v_mfma_f32_16x16x32_bf16 v[74:77], v[152:155], v[208:211], 0
	v_mfma_f32_16x16x32_bf16 v[126:129], v[148:151], v[188:191], v[126:129]
	v_mfma_f32_16x16x32_bf16 v[122:125], v[156:159], v[188:191], v[122:125]
	v_mfma_f32_16x16x32_bf16 v[110:113], v[148:151], v[196:199], v[110:113]
	v_mfma_f32_16x16x32_bf16 v[106:109], v[156:159], v[196:199], v[106:109]
	v_mfma_f32_16x16x32_bf16 v[94:97], v[148:151], v[204:207], v[94:97]
	v_mfma_f32_16x16x32_bf16 v[90:93], v[156:159], v[204:207], v[90:93]
	v_mfma_f32_16x16x32_bf16 v[78:81], v[148:151], v[212:215], v[78:81]
	v_mfma_f32_16x16x32_bf16 v[74:77], v[156:159], v[212:215], v[74:77]
	s_setprio 0
	s_setprio 1
	v_mfma_f32_16x16x32_bf16 v[118:121], v[160:163], v[184:187], 0
	v_mfma_f32_16x16x32_bf16 v[114:117], v[174:177], v[184:187], 0
	v_mfma_f32_16x16x32_bf16 v[102:105], v[160:163], v[192:195], 0
	v_mfma_f32_16x16x32_bf16 v[98:101], v[174:177], v[192:195], 0
	v_mfma_f32_16x16x32_bf16 v[86:89], v[160:163], v[200:203], 0
	v_mfma_f32_16x16x32_bf16 v[82:85], v[174:177], v[200:203], 0
	v_mfma_f32_16x16x32_bf16 v[70:73], v[160:163], v[208:211], 0
	v_mfma_f32_16x16x32_bf16 v[66:69], v[174:177], v[208:211], 0
	v_mfma_f32_16x16x32_bf16 v[118:121], v[170:173], v[188:191], v[118:121]
	v_mfma_f32_16x16x32_bf16 v[114:117], v[180:183], v[188:191], v[114:117]
	v_mfma_f32_16x16x32_bf16 v[102:105], v[170:173], v[196:199], v[102:105]
	v_mfma_f32_16x16x32_bf16 v[98:101], v[180:183], v[196:199], v[98:101]
	v_mfma_f32_16x16x32_bf16 v[86:89], v[170:173], v[204:207], v[86:89]
	v_mfma_f32_16x16x32_bf16 v[82:85], v[180:183], v[204:207], v[82:85]
	v_mfma_f32_16x16x32_bf16 v[70:73], v[170:173], v[212:215], v[70:73]
	v_mfma_f32_16x16x32_bf16 v[66:69], v[180:183], v[212:215], v[66:69]
	s_setprio 0
	s_barrier
	s_add_i32 s74, s74, s1
	v_lshl_add_u64 v[216:217], s[60:61], 0, v[130:131]
	s_mov_b32 m0, s74
	ds_read_b128 v[184:187], v178 offset:16384
	ds_read_b128 v[188:191], v178 offset:17408
	ds_read_b128 v[192:195], v178 offset:18432
	ds_read_b128 v[196:199], v178 offset:19456
	ds_read_b128 v[200:203], v178 offset:20480
	ds_read_b128 v[204:207], v178 offset:21504
	ds_read_b128 v[208:211], v178 offset:22528
	ds_read_b128 v[212:215], v178 offset:23552
	global_load_lds_dwordx4 v[216:217], off
	s_add_i32 m0, s74, 0x2000
	s_add_u32 s74, s60, 0x40000
	v_lshl_add_u64 v[218:219], s[60:61], 0, v[132:133]
	s_addc_u32 s75, s61, 0
	s_add_i32 s76, s76, s1
	global_load_lds_dwordx4 v[218:219], off
	v_lshl_add_u64 v[220:221], s[74:75], 0, v[130:131]
	s_mov_b32 m0, s76
	v_lshl_add_u64 v[222:223], s[62:63], 0, v[136:137]
	global_load_lds_dwordx4 v[220:221], off
	v_lshl_add_u64 v[220:221], s[74:75], 0, v[132:133]
	s_add_i32 m0, s76, 0x2000
	s_nop 0
	global_load_lds_dwordx4 v[220:221], off
	v_lshl_add_u64 v[220:221], s[62:63], 0, v[134:135]
	s_mov_b32 m0, s8
	s_nop 0
	global_load_lds_dwordx4 v[220:221], off
	s_mov_b32 m0, s11
	s_nop 0
	global_load_lds_dwordx4 v[222:223], off
	s_waitcnt vmcnt(8) lgkmcnt(0)
	s_barrier
	s_setprio 1
	v_mfma_f32_16x16x32_bf16 v[62:65], v[144:147], v[184:187], 0
	v_mfma_f32_16x16x32_bf16 v[58:61], v[152:155], v[184:187], 0
	v_mfma_f32_16x16x32_bf16 v[46:49], v[144:147], v[192:195], 0
	v_mfma_f32_16x16x32_bf16 v[42:45], v[152:155], v[192:195], 0
	v_mfma_f32_16x16x32_bf16 v[30:33], v[144:147], v[200:203], 0
	v_mfma_f32_16x16x32_bf16 v[26:29], v[152:155], v[200:203], 0
	v_mfma_f32_16x16x32_bf16 v[14:17], v[144:147], v[208:211], 0
	v_mfma_f32_16x16x32_bf16 v[10:13], v[152:155], v[208:211], 0
	v_mfma_f32_16x16x32_bf16 v[62:65], v[148:151], v[188:191], v[62:65]
	v_mfma_f32_16x16x32_bf16 v[58:61], v[156:159], v[188:191], v[58:61]
	v_mfma_f32_16x16x32_bf16 v[46:49], v[148:151], v[196:199], v[46:49]
	v_mfma_f32_16x16x32_bf16 v[42:45], v[156:159], v[196:199], v[42:45]
	v_mfma_f32_16x16x32_bf16 v[30:33], v[148:151], v[204:207], v[30:33]
	v_mfma_f32_16x16x32_bf16 v[26:29], v[156:159], v[204:207], v[26:29]
	v_mfma_f32_16x16x32_bf16 v[14:17], v[148:151], v[212:215], v[14:17]
	v_mfma_f32_16x16x32_bf16 v[10:13], v[156:159], v[212:215], v[10:13]
	s_setprio 0
	s_setprio 1
	v_mfma_f32_16x16x32_bf16 v[54:57], v[160:163], v[184:187], 0
	v_mfma_f32_16x16x32_bf16 v[50:53], v[174:177], v[184:187], 0
	v_mfma_f32_16x16x32_bf16 v[38:41], v[160:163], v[192:195], 0
	v_mfma_f32_16x16x32_bf16 v[34:37], v[174:177], v[192:195], 0
	v_mfma_f32_16x16x32_bf16 v[22:25], v[160:163], v[200:203], 0
	v_mfma_f32_16x16x32_bf16 v[18:21], v[174:177], v[200:203], 0
	v_mfma_f32_16x16x32_bf16 v[6:9], v[160:163], v[208:211], 0
	v_mfma_f32_16x16x32_bf16 v[2:5], v[174:177], v[208:211], 0
	v_mfma_f32_16x16x32_bf16 v[54:57], v[170:173], v[188:191], v[54:57]
	v_mfma_f32_16x16x32_bf16 v[50:53], v[180:183], v[188:191], v[50:53]
	v_mfma_f32_16x16x32_bf16 v[38:41], v[170:173], v[196:199], v[38:41]
	v_mfma_f32_16x16x32_bf16 v[34:37], v[180:183], v[196:199], v[34:37]
	v_mfma_f32_16x16x32_bf16 v[22:25], v[170:173], v[204:207], v[22:25]
	v_mfma_f32_16x16x32_bf16 v[18:21], v[180:183], v[204:207], v[18:21]
	v_mfma_f32_16x16x32_bf16 v[6:9], v[170:173], v[212:215], v[6:9]
	v_mfma_f32_16x16x32_bf16 v[2:5], v[180:183], v[212:215], v[2:5]
	s_setprio 0
	s_barrier
	s_add_i32 s74, 0, 0x18000
	s_add_i32 s75, 0, 0x1c000
	v_add_u32_e32 v156, s74, v165
	v_add_u32_e32 v166, s75, v165
	ds_read_b128 v[144:147], v156
	ds_read_b128 v[148:151], v156 offset:1024
	ds_read_b128 v[152:155], v156 offset:2048
	ds_read_b128 v[156:159], v156 offset:3072
	ds_read_b128 v[160:163], v166
	ds_read_b128 v[170:173], v166 offset:1024
	ds_read_b128 v[174:177], v166 offset:2048
	ds_read_b128 v[180:183], v166 offset:3072
	s_add_u32 s62, s62, 0x40000
	s_addc_u32 s63, s63, 0
	s_mov_b32 m0, s16
	v_lshl_add_u64 v[232:233], s[62:63], 0, v[134:135]
	ds_read_b128 v[184:187], v178 offset:32768
	ds_read_b128 v[188:191], v178 offset:33792
	ds_read_b128 v[192:195], v178 offset:34816
	ds_read_b128 v[196:199], v178 offset:35840
	ds_read_b128 v[200:203], v178 offset:36864
	ds_read_b128 v[204:207], v178 offset:37888
	ds_read_b128 v[208:211], v178 offset:38912
	ds_read_b128 v[212:215], v178 offset:39936
	global_load_lds_dwordx4 v[232:233], off
	v_lshl_add_u64 v[232:233], s[62:63], 0, v[136:137]
	s_mov_b32 m0, s25
	s_nop 0
	global_load_lds_dwordx4 v[232:233], off
	s_waitcnt vmcnt(8) lgkmcnt(0)
	s_barrier
	s_setprio 1
	v_mfma_f32_16x16x32_bf16 v[126:129], v[144:147], v[184:187], v[126:129]
	v_mfma_f32_16x16x32_bf16 v[122:125], v[152:155], v[184:187], v[122:125]
	v_mfma_f32_16x16x32_bf16 v[110:113], v[144:147], v[192:195], v[110:113]
	v_mfma_f32_16x16x32_bf16 v[106:109], v[152:155], v[192:195], v[106:109]
	v_mfma_f32_16x16x32_bf16 v[94:97], v[144:147], v[200:203], v[94:97]
	v_mfma_f32_16x16x32_bf16 v[90:93], v[152:155], v[200:203], v[90:93]
	v_mfma_f32_16x16x32_bf16 v[78:81], v[144:147], v[208:211], v[78:81]
	v_mfma_f32_16x16x32_bf16 v[74:77], v[152:155], v[208:211], v[74:77]
	v_mfma_f32_16x16x32_bf16 v[126:129], v[148:151], v[188:191], v[126:129]
	v_mfma_f32_16x16x32_bf16 v[122:125], v[156:159], v[188:191], v[122:125]
	v_mfma_f32_16x16x32_bf16 v[110:113], v[148:151], v[196:199], v[110:113]
	v_mfma_f32_16x16x32_bf16 v[106:109], v[156:159], v[196:199], v[106:109]
	v_mfma_f32_16x16x32_bf16 v[94:97], v[148:151], v[204:207], v[94:97]
	v_mfma_f32_16x16x32_bf16 v[90:93], v[156:159], v[204:207], v[90:93]
	v_mfma_f32_16x16x32_bf16 v[78:81], v[148:151], v[212:215], v[78:81]
	v_mfma_f32_16x16x32_bf16 v[74:77], v[156:159], v[212:215], v[74:77]
	s_setprio 0
	s_setprio 1
	v_mfma_f32_16x16x32_bf16 v[118:121], v[160:163], v[184:187], v[118:121]
	v_mfma_f32_16x16x32_bf16 v[114:117], v[174:177], v[184:187], v[114:117]
	v_mfma_f32_16x16x32_bf16 v[102:105], v[160:163], v[192:195], v[102:105]
	v_mfma_f32_16x16x32_bf16 v[98:101], v[174:177], v[192:195], v[98:101]
	v_mfma_f32_16x16x32_bf16 v[86:89], v[160:163], v[200:203], v[86:89]
	v_mfma_f32_16x16x32_bf16 v[82:85], v[174:177], v[200:203], v[82:85]
	v_mfma_f32_16x16x32_bf16 v[70:73], v[160:163], v[208:211], v[70:73]
	v_mfma_f32_16x16x32_bf16 v[66:69], v[174:177], v[208:211], v[66:69]
	v_mfma_f32_16x16x32_bf16 v[118:121], v[170:173], v[188:191], v[118:121]
	v_mfma_f32_16x16x32_bf16 v[114:117], v[180:183], v[188:191], v[114:117]
	v_mfma_f32_16x16x32_bf16 v[102:105], v[170:173], v[196:199], v[102:105]
	v_mfma_f32_16x16x32_bf16 v[98:101], v[180:183], v[196:199], v[98:101]
	v_mfma_f32_16x16x32_bf16 v[86:89], v[170:173], v[204:207], v[86:89]
	v_mfma_f32_16x16x32_bf16 v[82:85], v[180:183], v[204:207], v[82:85]
	v_mfma_f32_16x16x32_bf16 v[70:73], v[170:173], v[212:215], v[70:73]
	v_mfma_f32_16x16x32_bf16 v[66:69], v[180:183], v[212:215], v[66:69]
	s_setprio 0
	s_barrier
	s_add_i32 s62, s74, s1
	v_lshl_add_u64 v[216:217], v[216:217], 0, s[56:57]
	s_mov_b32 m0, s62
	ds_read_b128 v[184:187], v178 offset:49152
	ds_read_b128 v[188:191], v178 offset:50176
	ds_read_b128 v[192:195], v178 offset:51200
	ds_read_b128 v[196:199], v178 offset:52224
	ds_read_b128 v[200:203], v178 offset:53248
	ds_read_b128 v[204:207], v178 offset:54272
	ds_read_b128 v[208:211], v178 offset:55296
	ds_read_b128 v[212:215], v178 offset:56320
	global_load_lds_dwordx4 v[216:217], off
	s_add_i32 m0, s62, 0x2000
	s_add_u32 s60, s60, 0x40080
	v_lshl_add_u64 v[216:217], v[218:219], 0, s[56:57]
	s_addc_u32 s61, s61, 0
	s_add_i32 s62, s75, s1
	global_load_lds_dwordx4 v[216:217], off
	v_lshl_add_u64 v[216:217], s[60:61], 0, v[130:131]
	s_mov_b32 m0, s62
	s_nop 0
	global_load_lds_dwordx4 v[216:217], off
	v_lshl_add_u64 v[216:217], s[60:61], 0, v[132:133]
	s_add_i32 m0, s62, 0x2000
	s_nop 0
	global_load_lds_dwordx4 v[216:217], off
	v_lshl_add_u64 v[216:217], v[220:221], 0, s[56:57]
	s_mov_b32 m0, s64
	s_nop 0
	global_load_lds_dwordx4 v[216:217], off
	v_lshl_add_u64 v[216:217], v[222:223], 0, s[56:57]
	s_mov_b32 m0, s65
	s_nop 0
	global_load_lds_dwordx4 v[216:217], off
	s_waitcnt vmcnt(8) lgkmcnt(0)
	s_barrier
	s_setprio 1
	v_mfma_f32_16x16x32_bf16 v[62:65], v[144:147], v[184:187], v[62:65]
	v_mfma_f32_16x16x32_bf16 v[58:61], v[152:155], v[184:187], v[58:61]
	v_mfma_f32_16x16x32_bf16 v[46:49], v[144:147], v[192:195], v[46:49]
	v_mfma_f32_16x16x32_bf16 v[42:45], v[152:155], v[192:195], v[42:45]
	v_mfma_f32_16x16x32_bf16 v[30:33], v[144:147], v[200:203], v[30:33]
	v_mfma_f32_16x16x32_bf16 v[26:29], v[152:155], v[200:203], v[26:29]
	v_mfma_f32_16x16x32_bf16 v[14:17], v[144:147], v[208:211], v[14:17]
	v_mfma_f32_16x16x32_bf16 v[10:13], v[152:155], v[208:211], v[10:13]
	v_mfma_f32_16x16x32_bf16 v[62:65], v[148:151], v[188:191], v[62:65]
	v_mfma_f32_16x16x32_bf16 v[58:61], v[156:159], v[188:191], v[58:61]
	v_mfma_f32_16x16x32_bf16 v[46:49], v[148:151], v[196:199], v[46:49]
	v_mfma_f32_16x16x32_bf16 v[42:45], v[156:159], v[196:199], v[42:45]
	v_mfma_f32_16x16x32_bf16 v[30:33], v[148:151], v[204:207], v[30:33]
	v_mfma_f32_16x16x32_bf16 v[26:29], v[156:159], v[204:207], v[26:29]
	v_mfma_f32_16x16x32_bf16 v[14:17], v[148:151], v[212:215], v[14:17]
	v_mfma_f32_16x16x32_bf16 v[10:13], v[156:159], v[212:215], v[10:13]
	s_setprio 0
	s_setprio 1
	v_mfma_f32_16x16x32_bf16 v[54:57], v[160:163], v[184:187], v[54:57]
	v_mfma_f32_16x16x32_bf16 v[50:53], v[174:177], v[184:187], v[50:53]
	v_mfma_f32_16x16x32_bf16 v[38:41], v[160:163], v[192:195], v[38:41]
	v_mfma_f32_16x16x32_bf16 v[34:37], v[174:177], v[192:195], v[34:37]
	v_mfma_f32_16x16x32_bf16 v[22:25], v[160:163], v[200:203], v[22:25]
	v_mfma_f32_16x16x32_bf16 v[18:21], v[174:177], v[200:203], v[18:21]
	v_mfma_f32_16x16x32_bf16 v[6:9], v[160:163], v[208:211], v[6:9]
	v_mfma_f32_16x16x32_bf16 v[2:5], v[174:177], v[208:211], v[2:5]
	v_mfma_f32_16x16x32_bf16 v[54:57], v[170:173], v[188:191], v[54:57]
	v_mfma_f32_16x16x32_bf16 v[50:53], v[180:183], v[188:191], v[50:53]
	v_mfma_f32_16x16x32_bf16 v[38:41], v[170:173], v[196:199], v[38:41]
	v_mfma_f32_16x16x32_bf16 v[34:37], v[180:183], v[196:199], v[34:37]
	v_mfma_f32_16x16x32_bf16 v[22:25], v[170:173], v[204:207], v[22:25]
	v_mfma_f32_16x16x32_bf16 v[18:21], v[180:183], v[204:207], v[18:21]
	v_mfma_f32_16x16x32_bf16 v[6:9], v[170:173], v[212:215], v[6:9]
	v_mfma_f32_16x16x32_bf16 v[2:5], v[180:183], v[212:215], v[2:5]
	s_setprio 0
	s_barrier
	s_add_u32 s71, s71, 0x100
	s_addc_u32 s72, s72, 0
	s_add_u32 s58, s58, 0x100
	s_addc_u32 s59, s59, 0
	s_cmp_ge_i32 s73, s0
	s_mov_b32 s60, s73
	s_cbranch_scc0 .LBB0_229
	s_branch .Lpeelexitph1b
.LBB0_229:
	s_add_i32 s73, s60, 2
	s_add_u32 s61, s58, 0xfffc0080
	s_addc_u32 s62, s59, -1
	s_add_i32 s74, 0, 0x10000
	s_cmp_eq_u32 s68, s60
	s_cselect_b32 s63, s39, s62
	s_cselect_b32 s62, s43, s61
	s_cselect_b32 s61, s47, s72
	s_cselect_b32 s60, s55, s71
	s_add_i32 s76, 0, 0x14000
	v_add_u32_e32 v156, s74, v165
	v_add_u32_e32 v166, s76, v165
	ds_read_b128 v[144:147], v156
	ds_read_b128 v[148:151], v156 offset:1024
	ds_read_b128 v[152:155], v156 offset:2048
	ds_read_b128 v[156:159], v156 offset:3072
	ds_read_b128 v[160:163], v166
	ds_read_b128 v[170:173], v166 offset:1024
	ds_read_b128 v[174:177], v166 offset:2048
	ds_read_b128 v[180:183], v166 offset:3072
	v_lshl_add_u64 v[216:217], s[58:59], 0, v[142:143]
	s_add_i32 m0, s8, 0xc000
	ds_read_b128 v[184:187], v178
	ds_read_b128 v[188:191], v178 offset:1024
	ds_read_b128 v[192:195], v178 offset:2048
	ds_read_b128 v[196:199], v178 offset:3072
	ds_read_b128 v[200:203], v178 offset:4096
	ds_read_b128 v[204:207], v178 offset:5120
	ds_read_b128 v[208:211], v178 offset:6144
	ds_read_b128 v[212:215], v178 offset:7168
	global_load_lds_dwordx4 v[216:217], off
	v_lshl_add_u64 v[216:217], s[58:59], 0, v[140:141]
	s_add_i32 m0, s8, 0xe000
	s_nop 0
	global_load_lds_dwordx4 v[216:217], off
	s_waitcnt vmcnt(8) lgkmcnt(0)
	s_barrier
	s_setprio 1
	v_mfma_f32_16x16x32_bf16 v[126:129], v[144:147], v[184:187], v[126:129]
	v_mfma_f32_16x16x32_bf16 v[122:125], v[152:155], v[184:187], v[122:125]
	v_mfma_f32_16x16x32_bf16 v[110:113], v[144:147], v[192:195], v[110:113]
	v_mfma_f32_16x16x32_bf16 v[106:109], v[152:155], v[192:195], v[106:109]
	v_mfma_f32_16x16x32_bf16 v[94:97], v[144:147], v[200:203], v[94:97]
	v_mfma_f32_16x16x32_bf16 v[90:93], v[152:155], v[200:203], v[90:93]
	v_mfma_f32_16x16x32_bf16 v[78:81], v[144:147], v[208:211], v[78:81]
	v_mfma_f32_16x16x32_bf16 v[74:77], v[152:155], v[208:211], v[74:77]
	v_mfma_f32_16x16x32_bf16 v[126:129], v[148:151], v[188:191], v[126:129]
	v_mfma_f32_16x16x32_bf16 v[122:125], v[156:159], v[188:191], v[122:125]
	v_mfma_f32_16x16x32_bf16 v[110:113], v[148:151], v[196:199], v[110:113]
	v_mfma_f32_16x16x32_bf16 v[106:109], v[156:159], v[196:199], v[106:109]
	v_mfma_f32_16x16x32_bf16 v[94:97], v[148:151], v[204:207], v[94:97]
	v_mfma_f32_16x16x32_bf16 v[90:93], v[156:159], v[204:207], v[90:93]
	v_mfma_f32_16x16x32_bf16 v[78:81], v[148:151], v[212:215], v[78:81]
	v_mfma_f32_16x16x32_bf16 v[74:77], v[156:159], v[212:215], v[74:77]
	s_setprio 0
	s_setprio 1
	v_mfma_f32_16x16x32_bf16 v[118:121], v[160:163], v[184:187], v[118:121]
	v_mfma_f32_16x16x32_bf16 v[114:117], v[174:177], v[184:187], v[114:117]
	v_mfma_f32_16x16x32_bf16 v[102:105], v[160:163], v[192:195], v[102:105]
	v_mfma_f32_16x16x32_bf16 v[98:101], v[174:177], v[192:195], v[98:101]
	v_mfma_f32_16x16x32_bf16 v[86:89], v[160:163], v[200:203], v[86:89]
	v_mfma_f32_16x16x32_bf16 v[82:85], v[174:177], v[200:203], v[82:85]
	v_mfma_f32_16x16x32_bf16 v[70:73], v[160:163], v[208:211], v[70:73]
	v_mfma_f32_16x16x32_bf16 v[66:69], v[174:177], v[208:211], v[66:69]
	v_mfma_f32_16x16x32_bf16 v[118:121], v[170:173], v[188:191], v[118:121]
	v_mfma_f32_16x16x32_bf16 v[114:117], v[180:183], v[188:191], v[114:117]
	v_mfma_f32_16x16x32_bf16 v[102:105], v[170:173], v[196:199], v[102:105]
	v_mfma_f32_16x16x32_bf16 v[98:101], v[180:183], v[196:199], v[98:101]
	v_mfma_f32_16x16x32_bf16 v[86:89], v[170:173], v[204:207], v[86:89]
	v_mfma_f32_16x16x32_bf16 v[82:85], v[180:183], v[204:207], v[82:85]
	v_mfma_f32_16x16x32_bf16 v[70:73], v[170:173], v[212:215], v[70:73]
	v_mfma_f32_16x16x32_bf16 v[66:69], v[180:183], v[212:215], v[66:69]
	s_setprio 0
	s_barrier
	s_add_i32 s74, s74, s1
	v_lshl_add_u64 v[216:217], s[60:61], 0, v[130:131]
	s_mov_b32 m0, s74
	ds_read_b128 v[184:187], v178 offset:16384
	ds_read_b128 v[188:191], v178 offset:17408
	ds_read_b128 v[192:195], v178 offset:18432
	ds_read_b128 v[196:199], v178 offset:19456
	ds_read_b128 v[200:203], v178 offset:20480
	ds_read_b128 v[204:207], v178 offset:21504
	ds_read_b128 v[208:211], v178 offset:22528
	ds_read_b128 v[212:215], v178 offset:23552
	global_load_lds_dwordx4 v[216:217], off
	s_add_i32 m0, s74, 0x2000
	s_add_u32 s74, s60, 0x40000
	v_lshl_add_u64 v[218:219], s[60:61], 0, v[132:133]
	s_addc_u32 s75, s61, 0
	s_add_i32 s76, s76, s1
	global_load_lds_dwordx4 v[218:219], off
	v_lshl_add_u64 v[220:221], s[74:75], 0, v[130:131]
	s_mov_b32 m0, s76
	v_lshl_add_u64 v[222:223], s[62:63], 0, v[136:137]
	global_load_lds_dwordx4 v[220:221], off
	v_lshl_add_u64 v[220:221], s[74:75], 0, v[132:133]
	s_add_i32 m0, s76, 0x2000
	s_nop 0
	global_load_lds_dwordx4 v[220:221], off
	v_lshl_add_u64 v[220:221], s[62:63], 0, v[134:135]
	s_mov_b32 m0, s8
	s_nop 0
	global_load_lds_dwordx4 v[220:221], off
	s_mov_b32 m0, s11
	s_nop 0
	global_load_lds_dwordx4 v[222:223], off
	s_waitcnt vmcnt(8) lgkmcnt(0)
	s_barrier
	s_setprio 1
	v_mfma_f32_16x16x32_bf16 v[62:65], v[144:147], v[184:187], v[62:65]
	v_mfma_f32_16x16x32_bf16 v[58:61], v[152:155], v[184:187], v[58:61]
	v_mfma_f32_16x16x32_bf16 v[46:49], v[144:147], v[192:195], v[46:49]
	v_mfma_f32_16x16x32_bf16 v[42:45], v[152:155], v[192:195], v[42:45]
	v_mfma_f32_16x16x32_bf16 v[30:33], v[144:147], v[200:203], v[30:33]
	v_mfma_f32_16x16x32_bf16 v[26:29], v[152:155], v[200:203], v[26:29]
	v_mfma_f32_16x16x32_bf16 v[14:17], v[144:147], v[208:211], v[14:17]
	v_mfma_f32_16x16x32_bf16 v[10:13], v[152:155], v[208:211], v[10:13]
	v_mfma_f32_16x16x32_bf16 v[62:65], v[148:151], v[188:191], v[62:65]
	v_mfma_f32_16x16x32_bf16 v[58:61], v[156:159], v[188:191], v[58:61]
	v_mfma_f32_16x16x32_bf16 v[46:49], v[148:151], v[196:199], v[46:49]
	v_mfma_f32_16x16x32_bf16 v[42:45], v[156:159], v[196:199], v[42:45]
	v_mfma_f32_16x16x32_bf16 v[30:33], v[148:151], v[204:207], v[30:33]
	v_mfma_f32_16x16x32_bf16 v[26:29], v[156:159], v[204:207], v[26:29]
	v_mfma_f32_16x16x32_bf16 v[14:17], v[148:151], v[212:215], v[14:17]
	v_mfma_f32_16x16x32_bf16 v[10:13], v[156:159], v[212:215], v[10:13]
	s_setprio 0
	s_setprio 1
	v_mfma_f32_16x16x32_bf16 v[54:57], v[160:163], v[184:187], v[54:57]
	v_mfma_f32_16x16x32_bf16 v[50:53], v[174:177], v[184:187], v[50:53]
	v_mfma_f32_16x16x32_bf16 v[38:41], v[160:163], v[192:195], v[38:41]
	v_mfma_f32_16x16x32_bf16 v[34:37], v[174:177], v[192:195], v[34:37]
	v_mfma_f32_16x16x32_bf16 v[22:25], v[160:163], v[200:203], v[22:25]
	v_mfma_f32_16x16x32_bf16 v[18:21], v[174:177], v[200:203], v[18:21]
	v_mfma_f32_16x16x32_bf16 v[6:9], v[160:163], v[208:211], v[6:9]
	v_mfma_f32_16x16x32_bf16 v[2:5], v[174:177], v[208:211], v[2:5]
	v_mfma_f32_16x16x32_bf16 v[54:57], v[170:173], v[188:191], v[54:57]
	v_mfma_f32_16x16x32_bf16 v[50:53], v[180:183], v[188:191], v[50:53]
	v_mfma_f32_16x16x32_bf16 v[38:41], v[170:173], v[196:199], v[38:41]
	v_mfma_f32_16x16x32_bf16 v[34:37], v[180:183], v[196:199], v[34:37]
	v_mfma_f32_16x16x32_bf16 v[22:25], v[170:173], v[204:207], v[22:25]
	v_mfma_f32_16x16x32_bf16 v[18:21], v[180:183], v[204:207], v[18:21]
	v_mfma_f32_16x16x32_bf16 v[6:9], v[170:173], v[212:215], v[6:9]
	v_mfma_f32_16x16x32_bf16 v[2:5], v[180:183], v[212:215], v[2:5]
	s_setprio 0
	s_barrier
	s_add_i32 s74, 0, 0x18000
	s_add_i32 s75, 0, 0x1c000
	v_add_u32_e32 v156, s74, v165
	v_add_u32_e32 v166, s75, v165
	ds_read_b128 v[144:147], v156
	ds_read_b128 v[148:151], v156 offset:1024
	ds_read_b128 v[152:155], v156 offset:2048
	ds_read_b128 v[156:159], v156 offset:3072
	ds_read_b128 v[160:163], v166
	ds_read_b128 v[170:173], v166 offset:1024
	ds_read_b128 v[174:177], v166 offset:2048
	ds_read_b128 v[180:183], v166 offset:3072
	s_add_u32 s62, s62, 0x40000
	s_addc_u32 s63, s63, 0
	s_mov_b32 m0, s16
	v_lshl_add_u64 v[232:233], s[62:63], 0, v[134:135]
	ds_read_b128 v[184:187], v178 offset:32768
	ds_read_b128 v[188:191], v178 offset:33792
	ds_read_b128 v[192:195], v178 offset:34816
	ds_read_b128 v[196:199], v178 offset:35840
	ds_read_b128 v[200:203], v178 offset:36864
	ds_read_b128 v[204:207], v178 offset:37888
	ds_read_b128 v[208:211], v178 offset:38912
	ds_read_b128 v[212:215], v178 offset:39936
	global_load_lds_dwordx4 v[232:233], off
	v_lshl_add_u64 v[232:233], s[62:63], 0, v[136:137]
	s_mov_b32 m0, s25
	s_nop 0
	global_load_lds_dwordx4 v[232:233], off
	s_waitcnt vmcnt(8) lgkmcnt(0)
	s_barrier
	s_setprio 1
	v_mfma_f32_16x16x32_bf16 v[126:129], v[144:147], v[184:187], v[126:129]
	v_mfma_f32_16x16x32_bf16 v[122:125], v[152:155], v[184:187], v[122:125]
	v_mfma_f32_16x16x32_bf16 v[110:113], v[144:147], v[192:195], v[110:113]
	v_mfma_f32_16x16x32_bf16 v[106:109], v[152:155], v[192:195], v[106:109]
	v_mfma_f32_16x16x32_bf16 v[94:97], v[144:147], v[200:203], v[94:97]
	v_mfma_f32_16x16x32_bf16 v[90:93], v[152:155], v[200:203], v[90:93]
	v_mfma_f32_16x16x32_bf16 v[78:81], v[144:147], v[208:211], v[78:81]
	v_mfma_f32_16x16x32_bf16 v[74:77], v[152:155], v[208:211], v[74:77]
	v_mfma_f32_16x16x32_bf16 v[126:129], v[148:151], v[188:191], v[126:129]
	v_mfma_f32_16x16x32_bf16 v[122:125], v[156:159], v[188:191], v[122:125]
	v_mfma_f32_16x16x32_bf16 v[110:113], v[148:151], v[196:199], v[110:113]
	v_mfma_f32_16x16x32_bf16 v[106:109], v[156:159], v[196:199], v[106:109]
	v_mfma_f32_16x16x32_bf16 v[94:97], v[148:151], v[204:207], v[94:97]
	v_mfma_f32_16x16x32_bf16 v[90:93], v[156:159], v[204:207], v[90:93]
	v_mfma_f32_16x16x32_bf16 v[78:81], v[148:151], v[212:215], v[78:81]
	v_mfma_f32_16x16x32_bf16 v[74:77], v[156:159], v[212:215], v[74:77]
	s_setprio 0
	s_setprio 1
	v_mfma_f32_16x16x32_bf16 v[118:121], v[160:163], v[184:187], v[118:121]
	v_mfma_f32_16x16x32_bf16 v[114:117], v[174:177], v[184:187], v[114:117]
	v_mfma_f32_16x16x32_bf16 v[102:105], v[160:163], v[192:195], v[102:105]
	v_mfma_f32_16x16x32_bf16 v[98:101], v[174:177], v[192:195], v[98:101]
	v_mfma_f32_16x16x32_bf16 v[86:89], v[160:163], v[200:203], v[86:89]
	v_mfma_f32_16x16x32_bf16 v[82:85], v[174:177], v[200:203], v[82:85]
	v_mfma_f32_16x16x32_bf16 v[70:73], v[160:163], v[208:211], v[70:73]
	v_mfma_f32_16x16x32_bf16 v[66:69], v[174:177], v[208:211], v[66:69]
	v_mfma_f32_16x16x32_bf16 v[118:121], v[170:173], v[188:191], v[118:121]
	v_mfma_f32_16x16x32_bf16 v[114:117], v[180:183], v[188:191], v[114:117]
	v_mfma_f32_16x16x32_bf16 v[102:105], v[170:173], v[196:199], v[102:105]
	v_mfma_f32_16x16x32_bf16 v[98:101], v[180:183], v[196:199], v[98:101]
	v_mfma_f32_16x16x32_bf16 v[86:89], v[170:173], v[204:207], v[86:89]
	v_mfma_f32_16x16x32_bf16 v[82:85], v[180:183], v[204:207], v[82:85]
	v_mfma_f32_16x16x32_bf16 v[70:73], v[170:173], v[212:215], v[70:73]
	v_mfma_f32_16x16x32_bf16 v[66:69], v[180:183], v[212:215], v[66:69]
	s_setprio 0
	s_barrier
	s_add_i32 s62, s74, s1
	v_lshl_add_u64 v[216:217], v[216:217], 0, s[56:57]
	s_mov_b32 m0, s62
	ds_read_b128 v[184:187], v178 offset:49152
	ds_read_b128 v[188:191], v178 offset:50176
	ds_read_b128 v[192:195], v178 offset:51200
	ds_read_b128 v[196:199], v178 offset:52224
	ds_read_b128 v[200:203], v178 offset:53248
	ds_read_b128 v[204:207], v178 offset:54272
	ds_read_b128 v[208:211], v178 offset:55296
	ds_read_b128 v[212:215], v178 offset:56320
	global_load_lds_dwordx4 v[216:217], off
	s_add_i32 m0, s62, 0x2000
	s_add_u32 s60, s60, 0x40080
	v_lshl_add_u64 v[216:217], v[218:219], 0, s[56:57]
	s_addc_u32 s61, s61, 0
	s_add_i32 s62, s75, s1
	global_load_lds_dwordx4 v[216:217], off
	v_lshl_add_u64 v[216:217], s[60:61], 0, v[130:131]
	s_mov_b32 m0, s62
	s_nop 0
	global_load_lds_dwordx4 v[216:217], off
	v_lshl_add_u64 v[216:217], s[60:61], 0, v[132:133]
	s_add_i32 m0, s62, 0x2000
	s_nop 0
	global_load_lds_dwordx4 v[216:217], off
	v_lshl_add_u64 v[216:217], v[220:221], 0, s[56:57]
	s_mov_b32 m0, s64
	s_nop 0
	global_load_lds_dwordx4 v[216:217], off
	v_lshl_add_u64 v[216:217], v[222:223], 0, s[56:57]
	s_mov_b32 m0, s65
	s_nop 0
	global_load_lds_dwordx4 v[216:217], off
	s_waitcnt vmcnt(8) lgkmcnt(0)
	s_barrier
	s_setprio 1
	v_mfma_f32_16x16x32_bf16 v[62:65], v[144:147], v[184:187], v[62:65]
	v_mfma_f32_16x16x32_bf16 v[58:61], v[152:155], v[184:187], v[58:61]
	v_mfma_f32_16x16x32_bf16 v[46:49], v[144:147], v[192:195], v[46:49]
	v_mfma_f32_16x16x32_bf16 v[42:45], v[152:155], v[192:195], v[42:45]
	v_mfma_f32_16x16x32_bf16 v[30:33], v[144:147], v[200:203], v[30:33]
	v_mfma_f32_16x16x32_bf16 v[26:29], v[152:155], v[200:203], v[26:29]
	v_mfma_f32_16x16x32_bf16 v[14:17], v[144:147], v[208:211], v[14:17]
	v_mfma_f32_16x16x32_bf16 v[10:13], v[152:155], v[208:211], v[10:13]
	v_mfma_f32_16x16x32_bf16 v[62:65], v[148:151], v[188:191], v[62:65]
	v_mfma_f32_16x16x32_bf16 v[58:61], v[156:159], v[188:191], v[58:61]
	v_mfma_f32_16x16x32_bf16 v[46:49], v[148:151], v[196:199], v[46:49]
	v_mfma_f32_16x16x32_bf16 v[42:45], v[156:159], v[196:199], v[42:45]
	v_mfma_f32_16x16x32_bf16 v[30:33], v[148:151], v[204:207], v[30:33]
	v_mfma_f32_16x16x32_bf16 v[26:29], v[156:159], v[204:207], v[26:29]
	v_mfma_f32_16x16x32_bf16 v[14:17], v[148:151], v[212:215], v[14:17]
	v_mfma_f32_16x16x32_bf16 v[10:13], v[156:159], v[212:215], v[10:13]
	s_setprio 0
	s_setprio 1
	v_mfma_f32_16x16x32_bf16 v[54:57], v[160:163], v[184:187], v[54:57]
	v_mfma_f32_16x16x32_bf16 v[50:53], v[174:177], v[184:187], v[50:53]
	v_mfma_f32_16x16x32_bf16 v[38:41], v[160:163], v[192:195], v[38:41]
	v_mfma_f32_16x16x32_bf16 v[34:37], v[174:177], v[192:195], v[34:37]
	v_mfma_f32_16x16x32_bf16 v[22:25], v[160:163], v[200:203], v[22:25]
	v_mfma_f32_16x16x32_bf16 v[18:21], v[174:177], v[200:203], v[18:21]
	v_mfma_f32_16x16x32_bf16 v[6:9], v[160:163], v[208:211], v[6:9]
	v_mfma_f32_16x16x32_bf16 v[2:5], v[174:177], v[208:211], v[2:5]
	v_mfma_f32_16x16x32_bf16 v[54:57], v[170:173], v[188:191], v[54:57]
	v_mfma_f32_16x16x32_bf16 v[50:53], v[180:183], v[188:191], v[50:53]
	v_mfma_f32_16x16x32_bf16 v[38:41], v[170:173], v[196:199], v[38:41]
	v_mfma_f32_16x16x32_bf16 v[34:37], v[180:183], v[196:199], v[34:37]
	v_mfma_f32_16x16x32_bf16 v[22:25], v[170:173], v[204:207], v[22:25]
	v_mfma_f32_16x16x32_bf16 v[18:21], v[180:183], v[204:207], v[18:21]
	v_mfma_f32_16x16x32_bf16 v[6:9], v[170:173], v[212:215], v[6:9]
	v_mfma_f32_16x16x32_bf16 v[2:5], v[180:183], v[212:215], v[2:5]
	s_setprio 0
	s_barrier
	s_add_u32 s71, s71, 0x100
	s_addc_u32 s72, s72, 0
	s_add_u32 s58, s58, 0x100
	s_addc_u32 s59, s59, 0
	s_cmp_ge_i32 s73, s0
	s_mov_b32 s60, s73
	s_cbranch_scc0 .LBB0_229

.Lpeelph1f_0:
	s_add_i32 s71, s58, 2
	s_add_u32 s59, s54, 0xfffe0080
	s_addc_u32 s60, s55, -1
	s_add_i32 s72, 0, 0x10000
	s_cmp_eq_u32 s65, s58
	s_cselect_b32 s61, s39, s60
	s_cselect_b32 s60, s41, s59
	s_cselect_b32 s59, s43, s70
	s_cselect_b32 s58, s53, s69
	s_add_i32 s73, 0, 0x14000
	v_add_u32_e32 v2, s72, v198
	v_add_u32_e32 v6, s73, v198
	ds_read_b128 v[26:29], v2
	ds_read_b128 v[30:33], v2 offset:1024
	ds_read_b128 v[18:21], v2 offset:2048
	ds_read_b128 v[22:25], v2 offset:3072
	ds_read_b128 v[10:13], v6
	ds_read_b128 v[14:17], v6 offset:1024
	ds_read_b128 v[2:5], v6 offset:2048
	ds_read_b128 v[6:9], v6 offset:3072
	v_lshl_add_u64 v[170:171], s[54:55], 0, v[186:187]
	s_add_i32 m0, s8, 0xc000
	ds_read_b128 v[188:191], v200
	ds_read_b128 v[192:195], v200 offset:1024
	ds_read_b128 v[202:205], v200 offset:2048
	ds_read_b128 v[206:209], v200 offset:3072
	ds_read_b128 v[210:213], v200 offset:4096
	ds_read_b128 v[214:217], v200 offset:5120
	ds_read_b128 v[236:239], v200 offset:6144
	ds_read_b128 v[240:243], v200 offset:7168
	global_load_lds_dwordx4 v[170:171], off
	v_lshl_add_u64 v[170:171], s[54:55], 0, v[184:185]
	s_add_i32 m0, s8, 0xe000
	s_nop 0
	global_load_lds_dwordx4 v[170:171], off
	s_waitcnt vmcnt(8) lgkmcnt(0)
	s_barrier
	s_setprio 1
	v_mfma_scale_f32_16x16x128_f8f6f4 v[158:161], v[26:33], v[188:195], 0, v196, v169 op_sel_hi:[0,0,0]
	v_mfma_scale_f32_16x16x128_f8f6f4 v[154:157], v[18:25], v[188:195], 0, v196, v169 op_sel_hi:[0,0,0]
	v_mfma_scale_f32_16x16x128_f8f6f4 v[142:145], v[26:33], v[202:209], 0, v196, v169 op_sel_hi:[0,0,0]
	v_mfma_scale_f32_16x16x128_f8f6f4 v[138:141], v[18:25], v[202:209], 0, v196, v169 op_sel_hi:[0,0,0]
	v_mfma_scale_f32_16x16x128_f8f6f4 v[126:129], v[26:33], v[210:217], 0, v196, v169 op_sel_hi:[0,0,0]
	v_mfma_scale_f32_16x16x128_f8f6f4 v[122:125], v[18:25], v[210:217], 0, v196, v169 op_sel_hi:[0,0,0]
	v_mfma_scale_f32_16x16x128_f8f6f4 v[110:113], v[26:33], v[236:243], 0, v196, v169 op_sel_hi:[0,0,0]
	v_mfma_scale_f32_16x16x128_f8f6f4 v[106:109], v[18:25], v[236:243], 0, v196, v169 op_sel_hi:[0,0,0]
	s_setprio 0
	s_setprio 1
	v_mfma_scale_f32_16x16x128_f8f6f4 v[150:153], v[10:17], v[188:195], 0, v196, v169 op_sel_hi:[0,0,0]
	v_mfma_scale_f32_16x16x128_f8f6f4 v[146:149], v[2:9], v[188:195], 0, v196, v169 op_sel_hi:[0,0,0]
	v_mfma_scale_f32_16x16x128_f8f6f4 v[134:137], v[10:17], v[202:209], 0, v196, v169 op_sel_hi:[0,0,0]
	v_mfma_scale_f32_16x16x128_f8f6f4 v[130:133], v[2:9], v[202:209], 0, v196, v169 op_sel_hi:[0,0,0]
	v_mfma_scale_f32_16x16x128_f8f6f4 v[118:121], v[10:17], v[210:217], 0, v196, v169 op_sel_hi:[0,0,0]
	v_mfma_scale_f32_16x16x128_f8f6f4 v[114:117], v[2:9], v[210:217], 0, v196, v169 op_sel_hi:[0,0,0]
	v_mfma_scale_f32_16x16x128_f8f6f4 v[102:105], v[10:17], v[236:243], 0, v196, v169 op_sel_hi:[0,0,0]
	v_mfma_scale_f32_16x16x128_f8f6f4 v[98:101], v[2:9], v[236:243], 0, v196, v169 op_sel_hi:[0,0,0]
	s_setprio 0
	s_barrier
	s_add_i32 s72, s72, s1
	v_lshl_add_u64 v[188:189], s[58:59], 0, v[162:163]
	s_mov_b32 m0, s72
	ds_read_b128 v[202:205], v200 offset:16384
	ds_read_b128 v[206:209], v200 offset:17408
	ds_read_b128 v[210:213], v200 offset:18432
	ds_read_b128 v[214:217], v200 offset:19456
	ds_read_b128 v[236:239], v200 offset:20480
	ds_read_b128 v[240:243], v200 offset:21504
	ds_read_b128 v[244:247], v200 offset:22528
	ds_read_b128 v[248:251], v200 offset:23552
	global_load_lds_dwordx4 v[188:189], off
	s_add_i32 m0, s72, 0x2000
	s_add_u32 s74, s58, 0x20000
	v_lshl_add_u64 v[190:191], s[58:59], 0, v[164:165]
	s_addc_u32 s75, s59, 0
	s_add_i32 s72, s73, s1
	global_load_lds_dwordx4 v[190:191], off
	v_lshl_add_u64 v[170:171], s[74:75], 0, v[162:163]
	s_mov_b32 m0, s72
	v_lshl_add_u64 v[192:193], s[60:61], 0, v[178:179]
	global_load_lds_dwordx4 v[170:171], off
	v_lshl_add_u64 v[170:171], s[74:75], 0, v[164:165]
	s_add_i32 m0, s72, 0x2000
	v_lshl_add_u64 v[194:195], s[60:61], 0, v[180:181]
	global_load_lds_dwordx4 v[170:171], off
	s_mov_b32 m0, s8
	s_nop 0
	global_load_lds_dwordx4 v[192:193], off
	s_mov_b32 m0, s11
	s_nop 0
	global_load_lds_dwordx4 v[194:195], off
	s_waitcnt vmcnt(8) lgkmcnt(0)
	s_barrier
	s_setprio 1
	v_mfma_scale_f32_16x16x128_f8f6f4 v[94:97], v[26:33], v[202:209], 0, v196, v169 op_sel_hi:[0,0,0]
	v_mfma_scale_f32_16x16x128_f8f6f4 v[90:93], v[18:25], v[202:209], 0, v196, v169 op_sel_hi:[0,0,0]
	v_mfma_scale_f32_16x16x128_f8f6f4 v[78:81], v[26:33], v[210:217], 0, v196, v169 op_sel_hi:[0,0,0]
	v_mfma_scale_f32_16x16x128_f8f6f4 v[74:77], v[18:25], v[210:217], 0, v196, v169 op_sel_hi:[0,0,0]
	v_mfma_scale_f32_16x16x128_f8f6f4 v[62:65], v[26:33], v[236:243], 0, v196, v169 op_sel_hi:[0,0,0]
	v_mfma_scale_f32_16x16x128_f8f6f4 v[58:61], v[18:25], v[236:243], 0, v196, v169 op_sel_hi:[0,0,0]
	v_mfma_scale_f32_16x16x128_f8f6f4 v[46:49], v[26:33], v[244:251], 0, v196, v169 op_sel_hi:[0,0,0]
	v_mfma_scale_f32_16x16x128_f8f6f4 v[42:45], v[18:25], v[244:251], 0, v196, v169 op_sel_hi:[0,0,0]
	s_setprio 0
	s_setprio 1
	v_mfma_scale_f32_16x16x128_f8f6f4 v[86:89], v[10:17], v[202:209], 0, v196, v169 op_sel_hi:[0,0,0]
	v_mfma_scale_f32_16x16x128_f8f6f4 v[82:85], v[2:9], v[202:209], 0, v196, v169 op_sel_hi:[0,0,0]
	v_mfma_scale_f32_16x16x128_f8f6f4 v[70:73], v[10:17], v[210:217], 0, v196, v169 op_sel_hi:[0,0,0]
	v_mfma_scale_f32_16x16x128_f8f6f4 v[66:69], v[2:9], v[210:217], 0, v196, v169 op_sel_hi:[0,0,0]
	v_mfma_scale_f32_16x16x128_f8f6f4 v[54:57], v[10:17], v[236:243], 0, v196, v169 op_sel_hi:[0,0,0]
	v_mfma_scale_f32_16x16x128_f8f6f4 v[50:53], v[2:9], v[236:243], 0, v196, v169 op_sel_hi:[0,0,0]
	v_mfma_scale_f32_16x16x128_f8f6f4 v[38:41], v[10:17], v[244:251], 0, v196, v169 op_sel_hi:[0,0,0]
	v_mfma_scale_f32_16x16x128_f8f6f4 v[34:37], v[2:9], v[244:251], 0, v196, v169 op_sel_hi:[0,0,0]
	s_setprio 0
	s_barrier
	s_add_i32 s72, 0, 0x18000
	s_add_i32 s73, 0, 0x1c000
	v_add_u32_e32 v2, s72, v198
	v_add_u32_e32 v6, s73, v198
	ds_read_b128 v[26:29], v2
	ds_read_b128 v[30:33], v2 offset:1024
	ds_read_b128 v[18:21], v2 offset:2048
	ds_read_b128 v[22:25], v2 offset:3072
	ds_read_b128 v[10:13], v6
	ds_read_b128 v[14:17], v6 offset:1024
	ds_read_b128 v[2:5], v6 offset:2048
	ds_read_b128 v[6:9], v6 offset:3072
	s_add_u32 s60, s60, 0x20000
	s_addc_u32 s61, s61, 0
	s_mov_b32 m0, s16
	v_lshl_add_u64 v[170:171], s[60:61], 0, v[178:179]
	ds_read_b128 v[202:205], v200 offset:32768
	ds_read_b128 v[206:209], v200 offset:33792
	ds_read_b128 v[210:213], v200 offset:34816
	ds_read_b128 v[214:217], v200 offset:35840
	ds_read_b128 v[236:239], v200 offset:36864
	ds_read_b128 v[240:243], v200 offset:37888
	ds_read_b128 v[244:247], v200 offset:38912
	ds_read_b128 v[248:251], v200 offset:39936
	global_load_lds_dwordx4 v[170:171], off
	v_lshl_add_u64 v[170:171], s[60:61], 0, v[180:181]
	s_mov_b32 m0, s25
	s_nop 0
	global_load_lds_dwordx4 v[170:171], off
	s_waitcnt vmcnt(8) lgkmcnt(0)
	s_barrier
	s_setprio 1
	v_mfma_scale_f32_16x16x128_f8f6f4 v[158:161], v[26:33], v[202:209], v[158:161], v196, v169 op_sel_hi:[0,0,0]
	v_mfma_scale_f32_16x16x128_f8f6f4 v[154:157], v[18:25], v[202:209], v[154:157], v196, v169 op_sel_hi:[0,0,0]
	v_mfma_scale_f32_16x16x128_f8f6f4 v[142:145], v[26:33], v[210:217], v[142:145], v196, v169 op_sel_hi:[0,0,0]
	v_mfma_scale_f32_16x16x128_f8f6f4 v[138:141], v[18:25], v[210:217], v[138:141], v196, v169 op_sel_hi:[0,0,0]
	v_mfma_scale_f32_16x16x128_f8f6f4 v[126:129], v[26:33], v[236:243], v[126:129], v196, v169 op_sel_hi:[0,0,0]
	v_mfma_scale_f32_16x16x128_f8f6f4 v[122:125], v[18:25], v[236:243], v[122:125], v196, v169 op_sel_hi:[0,0,0]
	v_mfma_scale_f32_16x16x128_f8f6f4 v[110:113], v[26:33], v[244:251], v[110:113], v196, v169 op_sel_hi:[0,0,0]
	v_mfma_scale_f32_16x16x128_f8f6f4 v[106:109], v[18:25], v[244:251], v[106:109], v196, v169 op_sel_hi:[0,0,0]
	s_setprio 0
	s_setprio 1
	v_mfma_scale_f32_16x16x128_f8f6f4 v[150:153], v[10:17], v[202:209], v[150:153], v196, v169 op_sel_hi:[0,0,0]
	v_mfma_scale_f32_16x16x128_f8f6f4 v[146:149], v[2:9], v[202:209], v[146:149], v196, v169 op_sel_hi:[0,0,0]
	v_mfma_scale_f32_16x16x128_f8f6f4 v[134:137], v[10:17], v[210:217], v[134:137], v196, v169 op_sel_hi:[0,0,0]
	v_mfma_scale_f32_16x16x128_f8f6f4 v[130:133], v[2:9], v[210:217], v[130:133], v196, v169 op_sel_hi:[0,0,0]
	v_mfma_scale_f32_16x16x128_f8f6f4 v[118:121], v[10:17], v[236:243], v[118:121], v196, v169 op_sel_hi:[0,0,0]
	v_mfma_scale_f32_16x16x128_f8f6f4 v[114:117], v[2:9], v[236:243], v[114:117], v196, v169 op_sel_hi:[0,0,0]
	v_mfma_scale_f32_16x16x128_f8f6f4 v[102:105], v[10:17], v[244:251], v[102:105], v196, v169 op_sel_hi:[0,0,0]
	v_mfma_scale_f32_16x16x128_f8f6f4 v[98:101], v[2:9], v[244:251], v[98:101], v196, v169 op_sel_hi:[0,0,0]
	s_setprio 0
	s_barrier
	s_add_i32 s60, s72, s1
	v_lshl_add_u64 v[170:171], v[188:189], 0, s[56:57]
	s_mov_b32 m0, s60
	ds_read_b128 v[202:205], v200 offset:49152
	ds_read_b128 v[206:209], v200 offset:50176
	ds_read_b128 v[210:213], v200 offset:51200
	ds_read_b128 v[214:217], v200 offset:52224
	ds_read_b128 v[236:239], v200 offset:53248
	ds_read_b128 v[240:243], v200 offset:54272
	ds_read_b128 v[244:247], v200 offset:55296
	ds_read_b128 v[248:251], v200 offset:56320
	global_load_lds_dwordx4 v[170:171], off
	s_add_i32 m0, s60, 0x2000
	s_add_u32 s58, s58, 0x20080
	v_lshl_add_u64 v[170:171], v[190:191], 0, s[56:57]
	s_addc_u32 s59, s59, 0
	s_add_i32 s60, s73, s1
	global_load_lds_dwordx4 v[170:171], off
	v_lshl_add_u64 v[170:171], s[58:59], 0, v[162:163]
	s_mov_b32 m0, s60
	s_nop 0
	global_load_lds_dwordx4 v[170:171], off
	v_lshl_add_u64 v[170:171], s[58:59], 0, v[164:165]
	s_add_i32 m0, s60, 0x2000
	s_nop 0
	global_load_lds_dwordx4 v[170:171], off
	v_lshl_add_u64 v[170:171], v[192:193], 0, s[56:57]
	s_mov_b32 m0, s62
	s_nop 0
	global_load_lds_dwordx4 v[170:171], off
	v_lshl_add_u64 v[170:171], v[194:195], 0, s[56:57]
	s_mov_b32 m0, s63
	s_nop 0
	global_load_lds_dwordx4 v[170:171], off
	s_waitcnt vmcnt(8) lgkmcnt(0)
	s_barrier
	s_setprio 1
	v_mfma_scale_f32_16x16x128_f8f6f4 v[94:97], v[26:33], v[202:209], v[94:97], v196, v169 op_sel_hi:[0,0,0]
	v_mfma_scale_f32_16x16x128_f8f6f4 v[90:93], v[18:25], v[202:209], v[90:93], v196, v169 op_sel_hi:[0,0,0]
	v_mfma_scale_f32_16x16x128_f8f6f4 v[78:81], v[26:33], v[210:217], v[78:81], v196, v169 op_sel_hi:[0,0,0]
	v_mfma_scale_f32_16x16x128_f8f6f4 v[74:77], v[18:25], v[210:217], v[74:77], v196, v169 op_sel_hi:[0,0,0]
	v_mfma_scale_f32_16x16x128_f8f6f4 v[62:65], v[26:33], v[236:243], v[62:65], v196, v169 op_sel_hi:[0,0,0]
	v_mfma_scale_f32_16x16x128_f8f6f4 v[58:61], v[18:25], v[236:243], v[58:61], v196, v169 op_sel_hi:[0,0,0]
	v_mfma_scale_f32_16x16x128_f8f6f4 v[46:49], v[26:33], v[244:251], v[46:49], v196, v169 op_sel_hi:[0,0,0]
	v_mfma_scale_f32_16x16x128_f8f6f4 v[42:45], v[18:25], v[244:251], v[42:45], v196, v169 op_sel_hi:[0,0,0]
	s_setprio 0
	s_setprio 1
	v_mfma_scale_f32_16x16x128_f8f6f4 v[86:89], v[10:17], v[202:209], v[86:89], v196, v169 op_sel_hi:[0,0,0]
	v_mfma_scale_f32_16x16x128_f8f6f4 v[82:85], v[2:9], v[202:209], v[82:85], v196, v169 op_sel_hi:[0,0,0]
	v_mfma_scale_f32_16x16x128_f8f6f4 v[70:73], v[10:17], v[210:217], v[70:73], v196, v169 op_sel_hi:[0,0,0]
	v_mfma_scale_f32_16x16x128_f8f6f4 v[66:69], v[2:9], v[210:217], v[66:69], v196, v169 op_sel_hi:[0,0,0]
	v_mfma_scale_f32_16x16x128_f8f6f4 v[54:57], v[10:17], v[236:243], v[54:57], v196, v169 op_sel_hi:[0,0,0]
	v_mfma_scale_f32_16x16x128_f8f6f4 v[50:53], v[2:9], v[236:243], v[50:53], v196, v169 op_sel_hi:[0,0,0]
	v_mfma_scale_f32_16x16x128_f8f6f4 v[38:41], v[10:17], v[244:251], v[38:41], v196, v169 op_sel_hi:[0,0,0]
	v_mfma_scale_f32_16x16x128_f8f6f4 v[34:37], v[2:9], v[244:251], v[34:37], v196, v169 op_sel_hi:[0,0,0]
	s_setprio 0
	s_barrier
	s_add_u32 s69, s69, 0x100
	s_addc_u32 s70, s70, 0
	s_add_u32 s54, s54, 0x100
	s_addc_u32 s55, s55, 0
	s_cmp_ge_i32 s71, s0
	s_mov_b32 s58, s71
	s_cbranch_scc0 .LBB0_298
	s_branch .Lpeelexitph1f
.LBB0_298:
	s_add_i32 s71, s58, 2
	s_add_u32 s59, s54, 0xfffe0080
	s_addc_u32 s60, s55, -1
	s_add_i32 s72, 0, 0x10000
	s_cmp_eq_u32 s65, s58
	s_cselect_b32 s61, s39, s60
	s_cselect_b32 s60, s41, s59
	s_cselect_b32 s59, s43, s70
	s_cselect_b32 s58, s53, s69
	s_add_i32 s73, 0, 0x14000
	v_add_u32_e32 v2, s72, v198
	v_add_u32_e32 v6, s73, v198
	ds_read_b128 v[26:29], v2
	ds_read_b128 v[30:33], v2 offset:1024
	ds_read_b128 v[18:21], v2 offset:2048
	ds_read_b128 v[22:25], v2 offset:3072
	ds_read_b128 v[10:13], v6
	ds_read_b128 v[14:17], v6 offset:1024
	ds_read_b128 v[2:5], v6 offset:2048
	ds_read_b128 v[6:9], v6 offset:3072
	v_lshl_add_u64 v[170:171], s[54:55], 0, v[186:187]
	s_add_i32 m0, s8, 0xc000
	ds_read_b128 v[188:191], v200
	ds_read_b128 v[192:195], v200 offset:1024
	ds_read_b128 v[202:205], v200 offset:2048
	ds_read_b128 v[206:209], v200 offset:3072
	ds_read_b128 v[210:213], v200 offset:4096
	ds_read_b128 v[214:217], v200 offset:5120
	ds_read_b128 v[236:239], v200 offset:6144
	ds_read_b128 v[240:243], v200 offset:7168
	global_load_lds_dwordx4 v[170:171], off
	v_lshl_add_u64 v[170:171], s[54:55], 0, v[184:185]
	s_add_i32 m0, s8, 0xe000
	s_nop 0
	global_load_lds_dwordx4 v[170:171], off
	s_waitcnt vmcnt(8) lgkmcnt(0)
	s_barrier
	s_setprio 1
	v_mfma_scale_f32_16x16x128_f8f6f4 v[158:161], v[26:33], v[188:195], v[158:161], v196, v169 op_sel_hi:[0,0,0]
	v_mfma_scale_f32_16x16x128_f8f6f4 v[154:157], v[18:25], v[188:195], v[154:157], v196, v169 op_sel_hi:[0,0,0]
	v_mfma_scale_f32_16x16x128_f8f6f4 v[142:145], v[26:33], v[202:209], v[142:145], v196, v169 op_sel_hi:[0,0,0]
	v_mfma_scale_f32_16x16x128_f8f6f4 v[138:141], v[18:25], v[202:209], v[138:141], v196, v169 op_sel_hi:[0,0,0]
	v_mfma_scale_f32_16x16x128_f8f6f4 v[126:129], v[26:33], v[210:217], v[126:129], v196, v169 op_sel_hi:[0,0,0]
	v_mfma_scale_f32_16x16x128_f8f6f4 v[122:125], v[18:25], v[210:217], v[122:125], v196, v169 op_sel_hi:[0,0,0]
	v_mfma_scale_f32_16x16x128_f8f6f4 v[110:113], v[26:33], v[236:243], v[110:113], v196, v169 op_sel_hi:[0,0,0]
	v_mfma_scale_f32_16x16x128_f8f6f4 v[106:109], v[18:25], v[236:243], v[106:109], v196, v169 op_sel_hi:[0,0,0]
	s_setprio 0
	s_setprio 1
	v_mfma_scale_f32_16x16x128_f8f6f4 v[150:153], v[10:17], v[188:195], v[150:153], v196, v169 op_sel_hi:[0,0,0]
	v_mfma_scale_f32_16x16x128_f8f6f4 v[146:149], v[2:9], v[188:195], v[146:149], v196, v169 op_sel_hi:[0,0,0]
	v_mfma_scale_f32_16x16x128_f8f6f4 v[134:137], v[10:17], v[202:209], v[134:137], v196, v169 op_sel_hi:[0,0,0]
	v_mfma_scale_f32_16x16x128_f8f6f4 v[130:133], v[2:9], v[202:209], v[130:133], v196, v169 op_sel_hi:[0,0,0]
	v_mfma_scale_f32_16x16x128_f8f6f4 v[118:121], v[10:17], v[210:217], v[118:121], v196, v169 op_sel_hi:[0,0,0]
	v_mfma_scale_f32_16x16x128_f8f6f4 v[114:117], v[2:9], v[210:217], v[114:117], v196, v169 op_sel_hi:[0,0,0]
	v_mfma_scale_f32_16x16x128_f8f6f4 v[102:105], v[10:17], v[236:243], v[102:105], v196, v169 op_sel_hi:[0,0,0]
	v_mfma_scale_f32_16x16x128_f8f6f4 v[98:101], v[2:9], v[236:243], v[98:101], v196, v169 op_sel_hi:[0,0,0]
	s_setprio 0
	s_barrier
	s_add_i32 s72, s72, s1
	v_lshl_add_u64 v[188:189], s[58:59], 0, v[162:163]
	s_mov_b32 m0, s72
	ds_read_b128 v[202:205], v200 offset:16384
	ds_read_b128 v[206:209], v200 offset:17408
	ds_read_b128 v[210:213], v200 offset:18432
	ds_read_b128 v[214:217], v200 offset:19456
	ds_read_b128 v[236:239], v200 offset:20480
	ds_read_b128 v[240:243], v200 offset:21504
	ds_read_b128 v[244:247], v200 offset:22528
	ds_read_b128 v[248:251], v200 offset:23552
	global_load_lds_dwordx4 v[188:189], off
	s_add_i32 m0, s72, 0x2000
	s_add_u32 s74, s58, 0x20000
	v_lshl_add_u64 v[190:191], s[58:59], 0, v[164:165]
	s_addc_u32 s75, s59, 0
	s_add_i32 s72, s73, s1
	global_load_lds_dwordx4 v[190:191], off
	v_lshl_add_u64 v[170:171], s[74:75], 0, v[162:163]
	s_mov_b32 m0, s72
	v_lshl_add_u64 v[192:193], s[60:61], 0, v[178:179]
	global_load_lds_dwordx4 v[170:171], off
	v_lshl_add_u64 v[170:171], s[74:75], 0, v[164:165]
	s_add_i32 m0, s72, 0x2000
	v_lshl_add_u64 v[194:195], s[60:61], 0, v[180:181]
	global_load_lds_dwordx4 v[170:171], off
	s_mov_b32 m0, s8
	s_nop 0
	global_load_lds_dwordx4 v[192:193], off
	s_mov_b32 m0, s11
	s_nop 0
	global_load_lds_dwordx4 v[194:195], off
	s_waitcnt vmcnt(8) lgkmcnt(0)
	s_barrier
	s_setprio 1
	v_mfma_scale_f32_16x16x128_f8f6f4 v[94:97], v[26:33], v[202:209], v[94:97], v196, v169 op_sel_hi:[0,0,0]
	v_mfma_scale_f32_16x16x128_f8f6f4 v[90:93], v[18:25], v[202:209], v[90:93], v196, v169 op_sel_hi:[0,0,0]
	v_mfma_scale_f32_16x16x128_f8f6f4 v[78:81], v[26:33], v[210:217], v[78:81], v196, v169 op_sel_hi:[0,0,0]
	v_mfma_scale_f32_16x16x128_f8f6f4 v[74:77], v[18:25], v[210:217], v[74:77], v196, v169 op_sel_hi:[0,0,0]
	v_mfma_scale_f32_16x16x128_f8f6f4 v[62:65], v[26:33], v[236:243], v[62:65], v196, v169 op_sel_hi:[0,0,0]
	v_mfma_scale_f32_16x16x128_f8f6f4 v[58:61], v[18:25], v[236:243], v[58:61], v196, v169 op_sel_hi:[0,0,0]
	v_mfma_scale_f32_16x16x128_f8f6f4 v[46:49], v[26:33], v[244:251], v[46:49], v196, v169 op_sel_hi:[0,0,0]
	v_mfma_scale_f32_16x16x128_f8f6f4 v[42:45], v[18:25], v[244:251], v[42:45], v196, v169 op_sel_hi:[0,0,0]
	s_setprio 0
	s_setprio 1
	v_mfma_scale_f32_16x16x128_f8f6f4 v[86:89], v[10:17], v[202:209], v[86:89], v196, v169 op_sel_hi:[0,0,0]
	v_mfma_scale_f32_16x16x128_f8f6f4 v[82:85], v[2:9], v[202:209], v[82:85], v196, v169 op_sel_hi:[0,0,0]
	v_mfma_scale_f32_16x16x128_f8f6f4 v[70:73], v[10:17], v[210:217], v[70:73], v196, v169 op_sel_hi:[0,0,0]
	v_mfma_scale_f32_16x16x128_f8f6f4 v[66:69], v[2:9], v[210:217], v[66:69], v196, v169 op_sel_hi:[0,0,0]
	v_mfma_scale_f32_16x16x128_f8f6f4 v[54:57], v[10:17], v[236:243], v[54:57], v196, v169 op_sel_hi:[0,0,0]
	v_mfma_scale_f32_16x16x128_f8f6f4 v[50:53], v[2:9], v[236:243], v[50:53], v196, v169 op_sel_hi:[0,0,0]
	v_mfma_scale_f32_16x16x128_f8f6f4 v[38:41], v[10:17], v[244:251], v[38:41], v196, v169 op_sel_hi:[0,0,0]
	v_mfma_scale_f32_16x16x128_f8f6f4 v[34:37], v[2:9], v[244:251], v[34:37], v196, v169 op_sel_hi:[0,0,0]
	s_setprio 0
	s_barrier
	s_add_i32 s72, 0, 0x18000
	s_add_i32 s73, 0, 0x1c000
	v_add_u32_e32 v2, s72, v198
	v_add_u32_e32 v6, s73, v198
	ds_read_b128 v[26:29], v2
	ds_read_b128 v[30:33], v2 offset:1024
	ds_read_b128 v[18:21], v2 offset:2048
	ds_read_b128 v[22:25], v2 offset:3072
	ds_read_b128 v[10:13], v6
	ds_read_b128 v[14:17], v6 offset:1024
	ds_read_b128 v[2:5], v6 offset:2048
	ds_read_b128 v[6:9], v6 offset:3072
	s_add_u32 s60, s60, 0x20000
	s_addc_u32 s61, s61, 0
	s_mov_b32 m0, s16
	v_lshl_add_u64 v[170:171], s[60:61], 0, v[178:179]
	ds_read_b128 v[202:205], v200 offset:32768
	ds_read_b128 v[206:209], v200 offset:33792
	ds_read_b128 v[210:213], v200 offset:34816
	ds_read_b128 v[214:217], v200 offset:35840
	ds_read_b128 v[236:239], v200 offset:36864
	ds_read_b128 v[240:243], v200 offset:37888
	ds_read_b128 v[244:247], v200 offset:38912
	ds_read_b128 v[248:251], v200 offset:39936
	global_load_lds_dwordx4 v[170:171], off
	v_lshl_add_u64 v[170:171], s[60:61], 0, v[180:181]
	s_mov_b32 m0, s25
	s_nop 0
	global_load_lds_dwordx4 v[170:171], off
	s_waitcnt vmcnt(8) lgkmcnt(0)
	s_barrier
	s_setprio 1
	v_mfma_scale_f32_16x16x128_f8f6f4 v[158:161], v[26:33], v[202:209], v[158:161], v196, v169 op_sel_hi:[0,0,0]
	v_mfma_scale_f32_16x16x128_f8f6f4 v[154:157], v[18:25], v[202:209], v[154:157], v196, v169 op_sel_hi:[0,0,0]
	v_mfma_scale_f32_16x16x128_f8f6f4 v[142:145], v[26:33], v[210:217], v[142:145], v196, v169 op_sel_hi:[0,0,0]
	v_mfma_scale_f32_16x16x128_f8f6f4 v[138:141], v[18:25], v[210:217], v[138:141], v196, v169 op_sel_hi:[0,0,0]
	v_mfma_scale_f32_16x16x128_f8f6f4 v[126:129], v[26:33], v[236:243], v[126:129], v196, v169 op_sel_hi:[0,0,0]
	v_mfma_scale_f32_16x16x128_f8f6f4 v[122:125], v[18:25], v[236:243], v[122:125], v196, v169 op_sel_hi:[0,0,0]
	v_mfma_scale_f32_16x16x128_f8f6f4 v[110:113], v[26:33], v[244:251], v[110:113], v196, v169 op_sel_hi:[0,0,0]
	v_mfma_scale_f32_16x16x128_f8f6f4 v[106:109], v[18:25], v[244:251], v[106:109], v196, v169 op_sel_hi:[0,0,0]
	s_setprio 0
	s_setprio 1
	v_mfma_scale_f32_16x16x128_f8f6f4 v[150:153], v[10:17], v[202:209], v[150:153], v196, v169 op_sel_hi:[0,0,0]
	v_mfma_scale_f32_16x16x128_f8f6f4 v[146:149], v[2:9], v[202:209], v[146:149], v196, v169 op_sel_hi:[0,0,0]
	v_mfma_scale_f32_16x16x128_f8f6f4 v[134:137], v[10:17], v[210:217], v[134:137], v196, v169 op_sel_hi:[0,0,0]
	v_mfma_scale_f32_16x16x128_f8f6f4 v[130:133], v[2:9], v[210:217], v[130:133], v196, v169 op_sel_hi:[0,0,0]
	v_mfma_scale_f32_16x16x128_f8f6f4 v[118:121], v[10:17], v[236:243], v[118:121], v196, v169 op_sel_hi:[0,0,0]
	v_mfma_scale_f32_16x16x128_f8f6f4 v[114:117], v[2:9], v[236:243], v[114:117], v196, v169 op_sel_hi:[0,0,0]
	v_mfma_scale_f32_16x16x128_f8f6f4 v[102:105], v[10:17], v[244:251], v[102:105], v196, v169 op_sel_hi:[0,0,0]
	v_mfma_scale_f32_16x16x128_f8f6f4 v[98:101], v[2:9], v[244:251], v[98:101], v196, v169 op_sel_hi:[0,0,0]
	s_setprio 0
	s_barrier
	s_add_i32 s60, s72, s1
	v_lshl_add_u64 v[170:171], v[188:189], 0, s[56:57]
	s_mov_b32 m0, s60
	ds_read_b128 v[202:205], v200 offset:49152
	ds_read_b128 v[206:209], v200 offset:50176
	ds_read_b128 v[210:213], v200 offset:51200
	ds_read_b128 v[214:217], v200 offset:52224
	ds_read_b128 v[236:239], v200 offset:53248
	ds_read_b128 v[240:243], v200 offset:54272
	ds_read_b128 v[244:247], v200 offset:55296
	ds_read_b128 v[248:251], v200 offset:56320
	global_load_lds_dwordx4 v[170:171], off
	s_add_i32 m0, s60, 0x2000
	s_add_u32 s58, s58, 0x20080
	v_lshl_add_u64 v[170:171], v[190:191], 0, s[56:57]
	s_addc_u32 s59, s59, 0
	s_add_i32 s60, s73, s1
	global_load_lds_dwordx4 v[170:171], off
	v_lshl_add_u64 v[170:171], s[58:59], 0, v[162:163]
	s_mov_b32 m0, s60
	s_nop 0
	global_load_lds_dwordx4 v[170:171], off
	v_lshl_add_u64 v[170:171], s[58:59], 0, v[164:165]
	s_add_i32 m0, s60, 0x2000
	s_nop 0
	global_load_lds_dwordx4 v[170:171], off
	v_lshl_add_u64 v[170:171], v[192:193], 0, s[56:57]
	s_mov_b32 m0, s62
	s_nop 0
	global_load_lds_dwordx4 v[170:171], off
	v_lshl_add_u64 v[170:171], v[194:195], 0, s[56:57]
	s_mov_b32 m0, s63
	s_nop 0
	global_load_lds_dwordx4 v[170:171], off
	s_waitcnt vmcnt(8) lgkmcnt(0)
	s_barrier
	s_setprio 1
	v_mfma_scale_f32_16x16x128_f8f6f4 v[94:97], v[26:33], v[202:209], v[94:97], v196, v169 op_sel_hi:[0,0,0]
	v_mfma_scale_f32_16x16x128_f8f6f4 v[90:93], v[18:25], v[202:209], v[90:93], v196, v169 op_sel_hi:[0,0,0]
	v_mfma_scale_f32_16x16x128_f8f6f4 v[78:81], v[26:33], v[210:217], v[78:81], v196, v169 op_sel_hi:[0,0,0]
	v_mfma_scale_f32_16x16x128_f8f6f4 v[74:77], v[18:25], v[210:217], v[74:77], v196, v169 op_sel_hi:[0,0,0]
	v_mfma_scale_f32_16x16x128_f8f6f4 v[62:65], v[26:33], v[236:243], v[62:65], v196, v169 op_sel_hi:[0,0,0]
	v_mfma_scale_f32_16x16x128_f8f6f4 v[58:61], v[18:25], v[236:243], v[58:61], v196, v169 op_sel_hi:[0,0,0]
	v_mfma_scale_f32_16x16x128_f8f6f4 v[46:49], v[26:33], v[244:251], v[46:49], v196, v169 op_sel_hi:[0,0,0]
	v_mfma_scale_f32_16x16x128_f8f6f4 v[42:45], v[18:25], v[244:251], v[42:45], v196, v169 op_sel_hi:[0,0,0]
	s_setprio 0
	s_setprio 1
	v_mfma_scale_f32_16x16x128_f8f6f4 v[86:89], v[10:17], v[202:209], v[86:89], v196, v169 op_sel_hi:[0,0,0]
	v_mfma_scale_f32_16x16x128_f8f6f4 v[82:85], v[2:9], v[202:209], v[82:85], v196, v169 op_sel_hi:[0,0,0]
	v_mfma_scale_f32_16x16x128_f8f6f4 v[70:73], v[10:17], v[210:217], v[70:73], v196, v169 op_sel_hi:[0,0,0]
	v_mfma_scale_f32_16x16x128_f8f6f4 v[66:69], v[2:9], v[210:217], v[66:69], v196, v169 op_sel_hi:[0,0,0]
	v_mfma_scale_f32_16x16x128_f8f6f4 v[54:57], v[10:17], v[236:243], v[54:57], v196, v169 op_sel_hi:[0,0,0]
	v_mfma_scale_f32_16x16x128_f8f6f4 v[50:53], v[2:9], v[236:243], v[50:53], v196, v169 op_sel_hi:[0,0,0]
	v_mfma_scale_f32_16x16x128_f8f6f4 v[38:41], v[10:17], v[244:251], v[38:41], v196, v169 op_sel_hi:[0,0,0]
	v_mfma_scale_f32_16x16x128_f8f6f4 v[34:37], v[2:9], v[244:251], v[34:37], v196, v169 op_sel_hi:[0,0,0]
	s_setprio 0
	s_barrier
	s_add_u32 s69, s69, 0x100
	s_addc_u32 s70, s70, 0
	s_add_u32 s54, s54, 0x100
	s_addc_u32 s55, s55, 0
	s_cmp_ge_i32 s71, s0
	s_mov_b32 s58, s71
	s_cbranch_scc0 .LBB0_298

.Lpeelph3_0:
	s_add_i32 s73, s68, 2
	s_add_u32 s69, s64, 0xfffc0080
	s_addc_u32 s70, s65, -1
	s_add_i32 s74, 0, 0x10000
	s_cmp_eq_u32 s24, s68
	s_cselect_b32 s71, s59, s70
	s_cselect_b32 s70, s58, s69
	s_cselect_b32 s69, s51, s72
	s_cselect_b32 s68, s53, s66
	s_add_i32 s76, 0, 0x14000
	v_add_u32_e32 v152, s74, v220
	v_add_u32_e32 v164, s76, v220
	ds_read_b128 v[106:109], v152
	ds_read_b128 v[110:113], v152 offset:1024
	ds_read_b128 v[114:117], v152 offset:2048
	ds_read_b128 v[152:155], v152 offset:3072
	ds_read_b128 v[156:159], v164
	ds_read_b128 v[160:163], v164 offset:1024
	ds_read_b128 v[170:173], v164 offset:2048
	ds_read_b128 v[174:177], v164 offset:3072
	v_lshl_add_u64 v[164:165], s[64:65], 0, v[150:151]
	s_add_i32 m0, s14, 0xc000
	ds_read_b128 v[178:181], v222
	ds_read_b128 v[182:185], v222 offset:1024
	ds_read_b128 v[186:189], v222 offset:2048
	ds_read_b128 v[190:193], v222 offset:3072
	ds_read_b128 v[194:197], v222 offset:4096
	ds_read_b128 v[198:201], v222 offset:5120
	ds_read_b128 v[202:205], v222 offset:6144
	ds_read_b128 v[206:209], v222 offset:7168
	global_load_lds_dwordx4 v[164:165], off
	v_lshl_add_u64 v[164:165], s[64:65], 0, v[148:149]
	s_add_i32 m0, s14, 0xe000
	s_nop 0
	global_load_lds_dwordx4 v[164:165], off
	s_waitcnt vmcnt(8) lgkmcnt(0)
	s_barrier
	s_setprio 1
	v_mfma_f32_16x16x32_bf16 v[138:141], v[106:109], v[178:181], 0
	v_mfma_f32_16x16x32_bf16 v[62:65], v[114:117], v[178:181], 0
	v_mfma_f32_16x16x32_bf16 v[130:133], v[106:109], v[186:189], 0
	v_mfma_f32_16x16x32_bf16 v[54:57], v[114:117], v[186:189], 0
	v_mfma_f32_16x16x32_bf16 v[122:125], v[106:109], v[194:197], 0
	v_mfma_f32_16x16x32_bf16 v[46:49], v[114:117], v[194:197], 0
	v_mfma_f32_16x16x32_bf16 v[102:105], v[106:109], v[202:205], 0
	v_mfma_f32_16x16x32_bf16 v[38:41], v[114:117], v[202:205], 0
	v_mfma_f32_16x16x32_bf16 v[138:141], v[110:113], v[182:185], v[138:141]
	v_mfma_f32_16x16x32_bf16 v[62:65], v[152:155], v[182:185], v[62:65]
	v_mfma_f32_16x16x32_bf16 v[130:133], v[110:113], v[190:193], v[130:133]
	v_mfma_f32_16x16x32_bf16 v[54:57], v[152:155], v[190:193], v[54:57]
	v_mfma_f32_16x16x32_bf16 v[122:125], v[110:113], v[198:201], v[122:125]
	v_mfma_f32_16x16x32_bf16 v[46:49], v[152:155], v[198:201], v[46:49]
	v_mfma_f32_16x16x32_bf16 v[102:105], v[110:113], v[206:209], v[102:105]
	v_mfma_f32_16x16x32_bf16 v[38:41], v[152:155], v[206:209], v[38:41]
	s_setprio 0
	s_setprio 1
	v_mfma_f32_16x16x32_bf16 v[134:137], v[156:159], v[178:181], 0
	v_mfma_f32_16x16x32_bf16 v[58:61], v[170:173], v[178:181], 0
	v_mfma_f32_16x16x32_bf16 v[126:129], v[156:159], v[186:189], 0
	v_mfma_f32_16x16x32_bf16 v[50:53], v[170:173], v[186:189], 0
	v_mfma_f32_16x16x32_bf16 v[118:121], v[156:159], v[194:197], 0
	v_mfma_f32_16x16x32_bf16 v[42:45], v[170:173], v[194:197], 0
	v_mfma_f32_16x16x32_bf16 v[98:101], v[156:159], v[202:205], 0
	v_mfma_f32_16x16x32_bf16 v[34:37], v[170:173], v[202:205], 0
	v_mfma_f32_16x16x32_bf16 v[134:137], v[160:163], v[182:185], v[134:137]
	v_mfma_f32_16x16x32_bf16 v[58:61], v[174:177], v[182:185], v[58:61]
	v_mfma_f32_16x16x32_bf16 v[126:129], v[160:163], v[190:193], v[126:129]
	v_mfma_f32_16x16x32_bf16 v[50:53], v[174:177], v[190:193], v[50:53]
	v_mfma_f32_16x16x32_bf16 v[118:121], v[160:163], v[198:201], v[118:121]
	v_mfma_f32_16x16x32_bf16 v[42:45], v[174:177], v[198:201], v[42:45]
	v_mfma_f32_16x16x32_bf16 v[98:101], v[160:163], v[206:209], v[98:101]
	v_mfma_f32_16x16x32_bf16 v[34:37], v[174:177], v[206:209], v[34:37]
	s_setprio 0
	s_barrier
	s_add_i32 s74, s74, s13
	v_lshl_add_u64 v[164:165], s[68:69], 0, v[166:167]
	s_mov_b32 m0, s74
	ds_read_b128 v[178:181], v222 offset:16384
	ds_read_b128 v[182:185], v222 offset:17408
	ds_read_b128 v[186:189], v222 offset:18432
	ds_read_b128 v[190:193], v222 offset:19456
	ds_read_b128 v[194:197], v222 offset:20480
	ds_read_b128 v[198:201], v222 offset:21504
	ds_read_b128 v[202:205], v222 offset:22528
	ds_read_b128 v[206:209], v222 offset:23552
	global_load_lds_dwordx4 v[164:165], off
	s_add_i32 m0, s74, 0x2000
	s_add_u32 s74, s68, 0x8000
	v_lshl_add_u64 v[210:211], s[68:69], 0, v[142:143]
	s_addc_u32 s75, s69, 0
	s_add_i32 s76, s76, s13
	global_load_lds_dwordx4 v[210:211], off
	v_lshl_add_u64 v[212:213], s[74:75], 0, v[166:167]
	s_mov_b32 m0, s76
	v_lshl_add_u64 v[214:215], s[70:71], 0, v[146:147]
	global_load_lds_dwordx4 v[212:213], off
	v_lshl_add_u64 v[212:213], s[74:75], 0, v[142:143]
	s_add_i32 m0, s76, 0x2000
	s_nop 0
	global_load_lds_dwordx4 v[212:213], off
	v_lshl_add_u64 v[212:213], s[70:71], 0, v[144:145]
	s_mov_b32 m0, s14
	s_nop 0
	global_load_lds_dwordx4 v[212:213], off
	s_mov_b32 m0, s15
	s_nop 0
	global_load_lds_dwordx4 v[214:215], off
	s_waitcnt vmcnt(8) lgkmcnt(0)
	s_barrier
	s_setprio 1
	v_mfma_f32_16x16x32_bf16 v[94:97], v[106:109], v[178:181], 0
	v_mfma_f32_16x16x32_bf16 v[30:33], v[114:117], v[178:181], 0
	v_mfma_f32_16x16x32_bf16 v[86:89], v[106:109], v[186:189], 0
	v_mfma_f32_16x16x32_bf16 v[22:25], v[114:117], v[186:189], 0
	v_mfma_f32_16x16x32_bf16 v[78:81], v[106:109], v[194:197], 0
	v_mfma_f32_16x16x32_bf16 v[14:17], v[114:117], v[194:197], 0
	v_mfma_f32_16x16x32_bf16 v[70:73], v[106:109], v[202:205], 0
	v_mfma_f32_16x16x32_bf16 v[6:9], v[114:117], v[202:205], 0
	v_mfma_f32_16x16x32_bf16 v[94:97], v[110:113], v[182:185], v[94:97]
	v_mfma_f32_16x16x32_bf16 v[30:33], v[152:155], v[182:185], v[30:33]
	v_mfma_f32_16x16x32_bf16 v[86:89], v[110:113], v[190:193], v[86:89]
	v_mfma_f32_16x16x32_bf16 v[22:25], v[152:155], v[190:193], v[22:25]
	v_mfma_f32_16x16x32_bf16 v[78:81], v[110:113], v[198:201], v[78:81]
	v_mfma_f32_16x16x32_bf16 v[14:17], v[152:155], v[198:201], v[14:17]
	v_mfma_f32_16x16x32_bf16 v[70:73], v[110:113], v[206:209], v[70:73]
	v_mfma_f32_16x16x32_bf16 v[6:9], v[152:155], v[206:209], v[6:9]
	s_setprio 0
	s_setprio 1
	v_mfma_f32_16x16x32_bf16 v[90:93], v[156:159], v[178:181], 0
	v_mfma_f32_16x16x32_bf16 v[26:29], v[170:173], v[178:181], 0
	v_mfma_f32_16x16x32_bf16 v[82:85], v[156:159], v[186:189], 0
	v_mfma_f32_16x16x32_bf16 v[18:21], v[170:173], v[186:189], 0
	v_mfma_f32_16x16x32_bf16 v[74:77], v[156:159], v[194:197], 0
	v_mfma_f32_16x16x32_bf16 v[10:13], v[170:173], v[194:197], 0
	v_mfma_f32_16x16x32_bf16 v[66:69], v[156:159], v[202:205], 0
	v_mfma_f32_16x16x32_bf16 v[2:5], v[170:173], v[202:205], 0
	v_mfma_f32_16x16x32_bf16 v[90:93], v[160:163], v[182:185], v[90:93]
	v_mfma_f32_16x16x32_bf16 v[26:29], v[174:177], v[182:185], v[26:29]
	v_mfma_f32_16x16x32_bf16 v[82:85], v[160:163], v[190:193], v[82:85]
	v_mfma_f32_16x16x32_bf16 v[18:21], v[174:177], v[190:193], v[18:21]
	v_mfma_f32_16x16x32_bf16 v[74:77], v[160:163], v[198:201], v[74:77]
	v_mfma_f32_16x16x32_bf16 v[10:13], v[174:177], v[198:201], v[10:13]
	v_mfma_f32_16x16x32_bf16 v[66:69], v[160:163], v[206:209], v[66:69]
	v_mfma_f32_16x16x32_bf16 v[2:5], v[174:177], v[206:209], v[2:5]
	s_setprio 0
	s_barrier
	s_add_i32 s74, 0, 0x18000
	s_add_i32 s75, 0, 0x1c000
	v_add_u32_e32 v152, s74, v220
	v_add_u32_e32 v174, s75, v220
	ds_read_b128 v[106:109], v152
	ds_read_b128 v[110:113], v152 offset:1024
	ds_read_b128 v[114:117], v152 offset:2048
	ds_read_b128 v[152:155], v152 offset:3072
	ds_read_b128 v[156:159], v174
	ds_read_b128 v[160:163], v174 offset:1024
	ds_read_b128 v[170:173], v174 offset:2048
	ds_read_b128 v[174:177], v174 offset:3072
	s_add_u32 s70, s70, 0x40000
	s_addc_u32 s71, s71, 0
	s_mov_b32 m0, s16
	v_lshl_add_u64 v[216:217], s[70:71], 0, v[144:145]
	ds_read_b128 v[178:181], v222 offset:32768
	ds_read_b128 v[182:185], v222 offset:33792
	ds_read_b128 v[186:189], v222 offset:34816
	ds_read_b128 v[190:193], v222 offset:35840
	ds_read_b128 v[194:197], v222 offset:36864
	ds_read_b128 v[198:201], v222 offset:37888
	ds_read_b128 v[202:205], v222 offset:38912
	ds_read_b128 v[206:209], v222 offset:39936
	global_load_lds_dwordx4 v[216:217], off
	v_lshl_add_u64 v[216:217], s[70:71], 0, v[146:147]
	s_mov_b32 m0, s20
	s_nop 0
	global_load_lds_dwordx4 v[216:217], off
	s_waitcnt vmcnt(8) lgkmcnt(0)
	s_barrier
	s_setprio 1
	v_mfma_f32_16x16x32_bf16 v[138:141], v[106:109], v[178:181], v[138:141]
	v_mfma_f32_16x16x32_bf16 v[62:65], v[114:117], v[178:181], v[62:65]
	v_mfma_f32_16x16x32_bf16 v[130:133], v[106:109], v[186:189], v[130:133]
	v_mfma_f32_16x16x32_bf16 v[54:57], v[114:117], v[186:189], v[54:57]
	v_mfma_f32_16x16x32_bf16 v[122:125], v[106:109], v[194:197], v[122:125]
	v_mfma_f32_16x16x32_bf16 v[46:49], v[114:117], v[194:197], v[46:49]
	v_mfma_f32_16x16x32_bf16 v[102:105], v[106:109], v[202:205], v[102:105]
	v_mfma_f32_16x16x32_bf16 v[38:41], v[114:117], v[202:205], v[38:41]
	v_mfma_f32_16x16x32_bf16 v[138:141], v[110:113], v[182:185], v[138:141]
	v_mfma_f32_16x16x32_bf16 v[62:65], v[152:155], v[182:185], v[62:65]
	v_mfma_f32_16x16x32_bf16 v[130:133], v[110:113], v[190:193], v[130:133]
	v_mfma_f32_16x16x32_bf16 v[54:57], v[152:155], v[190:193], v[54:57]
	v_mfma_f32_16x16x32_bf16 v[122:125], v[110:113], v[198:201], v[122:125]
	v_mfma_f32_16x16x32_bf16 v[46:49], v[152:155], v[198:201], v[46:49]
	v_mfma_f32_16x16x32_bf16 v[102:105], v[110:113], v[206:209], v[102:105]
	v_mfma_f32_16x16x32_bf16 v[38:41], v[152:155], v[206:209], v[38:41]
	s_setprio 0
	s_setprio 1
	v_mfma_f32_16x16x32_bf16 v[134:137], v[156:159], v[178:181], v[134:137]
	v_mfma_f32_16x16x32_bf16 v[58:61], v[170:173], v[178:181], v[58:61]
	v_mfma_f32_16x16x32_bf16 v[126:129], v[156:159], v[186:189], v[126:129]
	v_mfma_f32_16x16x32_bf16 v[50:53], v[170:173], v[186:189], v[50:53]
	v_mfma_f32_16x16x32_bf16 v[118:121], v[156:159], v[194:197], v[118:121]
	v_mfma_f32_16x16x32_bf16 v[42:45], v[170:173], v[194:197], v[42:45]
	v_mfma_f32_16x16x32_bf16 v[98:101], v[156:159], v[202:205], v[98:101]
	v_mfma_f32_16x16x32_bf16 v[34:37], v[170:173], v[202:205], v[34:37]
	v_mfma_f32_16x16x32_bf16 v[134:137], v[160:163], v[182:185], v[134:137]
	v_mfma_f32_16x16x32_bf16 v[58:61], v[174:177], v[182:185], v[58:61]
	v_mfma_f32_16x16x32_bf16 v[126:129], v[160:163], v[190:193], v[126:129]
	v_mfma_f32_16x16x32_bf16 v[50:53], v[174:177], v[190:193], v[50:53]
	v_mfma_f32_16x16x32_bf16 v[118:121], v[160:163], v[198:201], v[118:121]
	v_mfma_f32_16x16x32_bf16 v[42:45], v[174:177], v[198:201], v[42:45]
	v_mfma_f32_16x16x32_bf16 v[98:101], v[160:163], v[206:209], v[98:101]
	v_mfma_f32_16x16x32_bf16 v[34:37], v[174:177], v[206:209], v[34:37]
	s_setprio 0
	s_barrier
	s_add_i32 s70, s74, s13
	v_lshl_add_u64 v[164:165], v[164:165], 0, s[56:57]
	s_mov_b32 m0, s70
	ds_read_b128 v[178:181], v222 offset:49152
	ds_read_b128 v[182:185], v222 offset:50176
	ds_read_b128 v[186:189], v222 offset:51200
	ds_read_b128 v[190:193], v222 offset:52224
	ds_read_b128 v[194:197], v222 offset:53248
	ds_read_b128 v[198:201], v222 offset:54272
	ds_read_b128 v[202:205], v222 offset:55296
	ds_read_b128 v[206:209], v222 offset:56320
	global_load_lds_dwordx4 v[164:165], off
	s_add_i32 m0, s70, 0x2000
	s_add_u32 s68, s68, 0x8080
	v_lshl_add_u64 v[164:165], v[210:211], 0, s[56:57]
	s_addc_u32 s69, s69, 0
	s_add_i32 s70, s75, s13
	global_load_lds_dwordx4 v[164:165], off
	v_lshl_add_u64 v[164:165], s[68:69], 0, v[166:167]
	s_mov_b32 m0, s70
	s_nop 0
	global_load_lds_dwordx4 v[164:165], off
	v_lshl_add_u64 v[164:165], s[68:69], 0, v[142:143]
	s_add_i32 m0, s70, 0x2000
	s_nop 0
	global_load_lds_dwordx4 v[164:165], off
	v_lshl_add_u64 v[164:165], v[212:213], 0, s[56:57]
	s_mov_b32 m0, s21
	s_nop 0
	global_load_lds_dwordx4 v[164:165], off
	v_lshl_add_u64 v[164:165], v[214:215], 0, s[56:57]
	s_mov_b32 m0, s22
	s_nop 0
	global_load_lds_dwordx4 v[164:165], off
	s_waitcnt vmcnt(8) lgkmcnt(0)
	s_barrier
	s_setprio 1
	v_mfma_f32_16x16x32_bf16 v[94:97], v[106:109], v[178:181], v[94:97]
	v_mfma_f32_16x16x32_bf16 v[30:33], v[114:117], v[178:181], v[30:33]
	v_mfma_f32_16x16x32_bf16 v[86:89], v[106:109], v[186:189], v[86:89]
	v_mfma_f32_16x16x32_bf16 v[22:25], v[114:117], v[186:189], v[22:25]
	v_mfma_f32_16x16x32_bf16 v[78:81], v[106:109], v[194:197], v[78:81]
	v_mfma_f32_16x16x32_bf16 v[14:17], v[114:117], v[194:197], v[14:17]
	v_mfma_f32_16x16x32_bf16 v[70:73], v[106:109], v[202:205], v[70:73]
	v_mfma_f32_16x16x32_bf16 v[6:9], v[114:117], v[202:205], v[6:9]
	v_mfma_f32_16x16x32_bf16 v[94:97], v[110:113], v[182:185], v[94:97]
	v_mfma_f32_16x16x32_bf16 v[30:33], v[152:155], v[182:185], v[30:33]
	v_mfma_f32_16x16x32_bf16 v[86:89], v[110:113], v[190:193], v[86:89]
	v_mfma_f32_16x16x32_bf16 v[22:25], v[152:155], v[190:193], v[22:25]
	v_mfma_f32_16x16x32_bf16 v[78:81], v[110:113], v[198:201], v[78:81]
	v_mfma_f32_16x16x32_bf16 v[14:17], v[152:155], v[198:201], v[14:17]
	v_mfma_f32_16x16x32_bf16 v[70:73], v[110:113], v[206:209], v[70:73]
	v_mfma_f32_16x16x32_bf16 v[6:9], v[152:155], v[206:209], v[6:9]
	s_setprio 0
	s_setprio 1
	v_mfma_f32_16x16x32_bf16 v[90:93], v[156:159], v[178:181], v[90:93]
	v_mfma_f32_16x16x32_bf16 v[26:29], v[170:173], v[178:181], v[26:29]
	v_mfma_f32_16x16x32_bf16 v[82:85], v[156:159], v[186:189], v[82:85]
	v_mfma_f32_16x16x32_bf16 v[18:21], v[170:173], v[186:189], v[18:21]
	v_mfma_f32_16x16x32_bf16 v[74:77], v[156:159], v[194:197], v[74:77]
	v_mfma_f32_16x16x32_bf16 v[10:13], v[170:173], v[194:197], v[10:13]
	v_mfma_f32_16x16x32_bf16 v[66:69], v[156:159], v[202:205], v[66:69]
	v_mfma_f32_16x16x32_bf16 v[2:5], v[170:173], v[202:205], v[2:5]
	v_mfma_f32_16x16x32_bf16 v[90:93], v[160:163], v[182:185], v[90:93]
	v_mfma_f32_16x16x32_bf16 v[26:29], v[174:177], v[182:185], v[26:29]
	v_mfma_f32_16x16x32_bf16 v[82:85], v[160:163], v[190:193], v[82:85]
	v_mfma_f32_16x16x32_bf16 v[18:21], v[174:177], v[190:193], v[18:21]
	v_mfma_f32_16x16x32_bf16 v[74:77], v[160:163], v[198:201], v[74:77]
	v_mfma_f32_16x16x32_bf16 v[10:13], v[174:177], v[198:201], v[10:13]
	v_mfma_f32_16x16x32_bf16 v[66:69], v[160:163], v[206:209], v[66:69]
	v_mfma_f32_16x16x32_bf16 v[2:5], v[174:177], v[206:209], v[2:5]
	s_setprio 0
	s_barrier
	s_add_u32 s66, s66, 0x100
	s_addc_u32 s72, s72, 0
	s_add_u32 s64, s64, 0x100
	s_addc_u32 s65, s65, 0
	s_cmp_ge_i32 s73, s1
	s_mov_b32 s68, s73
	s_cbranch_scc0 .LBB0_469
	s_branch .Lpeelexitph3
.LBB0_469:
	s_add_i32 s73, s68, 2
	s_add_u32 s69, s64, 0xfffc0080
	s_addc_u32 s70, s65, -1
	s_add_i32 s74, 0, 0x10000
	s_cmp_eq_u32 s24, s68
	s_cselect_b32 s71, s59, s70
	s_cselect_b32 s70, s58, s69
	s_cselect_b32 s69, s51, s72
	s_cselect_b32 s68, s53, s66
	s_add_i32 s76, 0, 0x14000
	v_add_u32_e32 v152, s74, v220
	v_add_u32_e32 v164, s76, v220
	ds_read_b128 v[106:109], v152
	ds_read_b128 v[110:113], v152 offset:1024
	ds_read_b128 v[114:117], v152 offset:2048
	ds_read_b128 v[152:155], v152 offset:3072
	ds_read_b128 v[156:159], v164
	ds_read_b128 v[160:163], v164 offset:1024
	ds_read_b128 v[170:173], v164 offset:2048
	ds_read_b128 v[174:177], v164 offset:3072
	v_lshl_add_u64 v[164:165], s[64:65], 0, v[150:151]
	s_add_i32 m0, s14, 0xc000
	ds_read_b128 v[178:181], v222
	ds_read_b128 v[182:185], v222 offset:1024
	ds_read_b128 v[186:189], v222 offset:2048
	ds_read_b128 v[190:193], v222 offset:3072
	ds_read_b128 v[194:197], v222 offset:4096
	ds_read_b128 v[198:201], v222 offset:5120
	ds_read_b128 v[202:205], v222 offset:6144
	ds_read_b128 v[206:209], v222 offset:7168
	global_load_lds_dwordx4 v[164:165], off
	v_lshl_add_u64 v[164:165], s[64:65], 0, v[148:149]
	s_add_i32 m0, s14, 0xe000
	s_nop 0
	global_load_lds_dwordx4 v[164:165], off
	s_waitcnt vmcnt(8) lgkmcnt(0)
	s_barrier
	s_setprio 1
	v_mfma_f32_16x16x32_bf16 v[138:141], v[106:109], v[178:181], v[138:141]
	v_mfma_f32_16x16x32_bf16 v[62:65], v[114:117], v[178:181], v[62:65]
	v_mfma_f32_16x16x32_bf16 v[130:133], v[106:109], v[186:189], v[130:133]
	v_mfma_f32_16x16x32_bf16 v[54:57], v[114:117], v[186:189], v[54:57]
	v_mfma_f32_16x16x32_bf16 v[122:125], v[106:109], v[194:197], v[122:125]
	v_mfma_f32_16x16x32_bf16 v[46:49], v[114:117], v[194:197], v[46:49]
	v_mfma_f32_16x16x32_bf16 v[102:105], v[106:109], v[202:205], v[102:105]
	v_mfma_f32_16x16x32_bf16 v[38:41], v[114:117], v[202:205], v[38:41]
	v_mfma_f32_16x16x32_bf16 v[138:141], v[110:113], v[182:185], v[138:141]
	v_mfma_f32_16x16x32_bf16 v[62:65], v[152:155], v[182:185], v[62:65]
	v_mfma_f32_16x16x32_bf16 v[130:133], v[110:113], v[190:193], v[130:133]
	v_mfma_f32_16x16x32_bf16 v[54:57], v[152:155], v[190:193], v[54:57]
	v_mfma_f32_16x16x32_bf16 v[122:125], v[110:113], v[198:201], v[122:125]
	v_mfma_f32_16x16x32_bf16 v[46:49], v[152:155], v[198:201], v[46:49]
	v_mfma_f32_16x16x32_bf16 v[102:105], v[110:113], v[206:209], v[102:105]
	v_mfma_f32_16x16x32_bf16 v[38:41], v[152:155], v[206:209], v[38:41]
	s_setprio 0
	s_setprio 1
	v_mfma_f32_16x16x32_bf16 v[134:137], v[156:159], v[178:181], v[134:137]
	v_mfma_f32_16x16x32_bf16 v[58:61], v[170:173], v[178:181], v[58:61]
	v_mfma_f32_16x16x32_bf16 v[126:129], v[156:159], v[186:189], v[126:129]
	v_mfma_f32_16x16x32_bf16 v[50:53], v[170:173], v[186:189], v[50:53]
	v_mfma_f32_16x16x32_bf16 v[118:121], v[156:159], v[194:197], v[118:121]
	v_mfma_f32_16x16x32_bf16 v[42:45], v[170:173], v[194:197], v[42:45]
	v_mfma_f32_16x16x32_bf16 v[98:101], v[156:159], v[202:205], v[98:101]
	v_mfma_f32_16x16x32_bf16 v[34:37], v[170:173], v[202:205], v[34:37]
	v_mfma_f32_16x16x32_bf16 v[134:137], v[160:163], v[182:185], v[134:137]
	v_mfma_f32_16x16x32_bf16 v[58:61], v[174:177], v[182:185], v[58:61]
	v_mfma_f32_16x16x32_bf16 v[126:129], v[160:163], v[190:193], v[126:129]
	v_mfma_f32_16x16x32_bf16 v[50:53], v[174:177], v[190:193], v[50:53]
	v_mfma_f32_16x16x32_bf16 v[118:121], v[160:163], v[198:201], v[118:121]
	v_mfma_f32_16x16x32_bf16 v[42:45], v[174:177], v[198:201], v[42:45]
	v_mfma_f32_16x16x32_bf16 v[98:101], v[160:163], v[206:209], v[98:101]
	v_mfma_f32_16x16x32_bf16 v[34:37], v[174:177], v[206:209], v[34:37]
	s_setprio 0
	s_barrier
	s_add_i32 s74, s74, s13
	v_lshl_add_u64 v[164:165], s[68:69], 0, v[166:167]
	s_mov_b32 m0, s74
	ds_read_b128 v[178:181], v222 offset:16384
	ds_read_b128 v[182:185], v222 offset:17408
	ds_read_b128 v[186:189], v222 offset:18432
	ds_read_b128 v[190:193], v222 offset:19456
	ds_read_b128 v[194:197], v222 offset:20480
	ds_read_b128 v[198:201], v222 offset:21504
	ds_read_b128 v[202:205], v222 offset:22528
	ds_read_b128 v[206:209], v222 offset:23552
	global_load_lds_dwordx4 v[164:165], off
	s_add_i32 m0, s74, 0x2000
	s_add_u32 s74, s68, 0x8000
	v_lshl_add_u64 v[210:211], s[68:69], 0, v[142:143]
	s_addc_u32 s75, s69, 0
	s_add_i32 s76, s76, s13
	global_load_lds_dwordx4 v[210:211], off
	v_lshl_add_u64 v[212:213], s[74:75], 0, v[166:167]
	s_mov_b32 m0, s76
	v_lshl_add_u64 v[214:215], s[70:71], 0, v[146:147]
	global_load_lds_dwordx4 v[212:213], off
	v_lshl_add_u64 v[212:213], s[74:75], 0, v[142:143]
	s_add_i32 m0, s76, 0x2000
	s_nop 0
	global_load_lds_dwordx4 v[212:213], off
	v_lshl_add_u64 v[212:213], s[70:71], 0, v[144:145]
	s_mov_b32 m0, s14
	s_nop 0
	global_load_lds_dwordx4 v[212:213], off
	s_mov_b32 m0, s15
	s_nop 0
	global_load_lds_dwordx4 v[214:215], off
	s_waitcnt vmcnt(8) lgkmcnt(0)
	s_barrier
	s_setprio 1
	v_mfma_f32_16x16x32_bf16 v[94:97], v[106:109], v[178:181], v[94:97]
	v_mfma_f32_16x16x32_bf16 v[30:33], v[114:117], v[178:181], v[30:33]
	v_mfma_f32_16x16x32_bf16 v[86:89], v[106:109], v[186:189], v[86:89]
	v_mfma_f32_16x16x32_bf16 v[22:25], v[114:117], v[186:189], v[22:25]
	v_mfma_f32_16x16x32_bf16 v[78:81], v[106:109], v[194:197], v[78:81]
	v_mfma_f32_16x16x32_bf16 v[14:17], v[114:117], v[194:197], v[14:17]
	v_mfma_f32_16x16x32_bf16 v[70:73], v[106:109], v[202:205], v[70:73]
	v_mfma_f32_16x16x32_bf16 v[6:9], v[114:117], v[202:205], v[6:9]
	v_mfma_f32_16x16x32_bf16 v[94:97], v[110:113], v[182:185], v[94:97]
	v_mfma_f32_16x16x32_bf16 v[30:33], v[152:155], v[182:185], v[30:33]
	v_mfma_f32_16x16x32_bf16 v[86:89], v[110:113], v[190:193], v[86:89]
	v_mfma_f32_16x16x32_bf16 v[22:25], v[152:155], v[190:193], v[22:25]
	v_mfma_f32_16x16x32_bf16 v[78:81], v[110:113], v[198:201], v[78:81]
	v_mfma_f32_16x16x32_bf16 v[14:17], v[152:155], v[198:201], v[14:17]
	v_mfma_f32_16x16x32_bf16 v[70:73], v[110:113], v[206:209], v[70:73]
	v_mfma_f32_16x16x32_bf16 v[6:9], v[152:155], v[206:209], v[6:9]
	s_setprio 0
	s_setprio 1
	v_mfma_f32_16x16x32_bf16 v[90:93], v[156:159], v[178:181], v[90:93]
	v_mfma_f32_16x16x32_bf16 v[26:29], v[170:173], v[178:181], v[26:29]
	v_mfma_f32_16x16x32_bf16 v[82:85], v[156:159], v[186:189], v[82:85]
	v_mfma_f32_16x16x32_bf16 v[18:21], v[170:173], v[186:189], v[18:21]
	v_mfma_f32_16x16x32_bf16 v[74:77], v[156:159], v[194:197], v[74:77]
	v_mfma_f32_16x16x32_bf16 v[10:13], v[170:173], v[194:197], v[10:13]
	v_mfma_f32_16x16x32_bf16 v[66:69], v[156:159], v[202:205], v[66:69]
	v_mfma_f32_16x16x32_bf16 v[2:5], v[170:173], v[202:205], v[2:5]
	v_mfma_f32_16x16x32_bf16 v[90:93], v[160:163], v[182:185], v[90:93]
	v_mfma_f32_16x16x32_bf16 v[26:29], v[174:177], v[182:185], v[26:29]
	v_mfma_f32_16x16x32_bf16 v[82:85], v[160:163], v[190:193], v[82:85]
	v_mfma_f32_16x16x32_bf16 v[18:21], v[174:177], v[190:193], v[18:21]
	v_mfma_f32_16x16x32_bf16 v[74:77], v[160:163], v[198:201], v[74:77]
	v_mfma_f32_16x16x32_bf16 v[10:13], v[174:177], v[198:201], v[10:13]
	v_mfma_f32_16x16x32_bf16 v[66:69], v[160:163], v[206:209], v[66:69]
	v_mfma_f32_16x16x32_bf16 v[2:5], v[174:177], v[206:209], v[2:5]
	s_setprio 0
	s_barrier
	s_add_i32 s74, 0, 0x18000
	s_add_i32 s75, 0, 0x1c000
	v_add_u32_e32 v152, s74, v220
	v_add_u32_e32 v174, s75, v220
	ds_read_b128 v[106:109], v152
	ds_read_b128 v[110:113], v152 offset:1024
	ds_read_b128 v[114:117], v152 offset:2048
	ds_read_b128 v[152:155], v152 offset:3072
	ds_read_b128 v[156:159], v174
	ds_read_b128 v[160:163], v174 offset:1024
	ds_read_b128 v[170:173], v174 offset:2048
	ds_read_b128 v[174:177], v174 offset:3072
	s_add_u32 s70, s70, 0x40000
	s_addc_u32 s71, s71, 0
	s_mov_b32 m0, s16
	v_lshl_add_u64 v[216:217], s[70:71], 0, v[144:145]
	ds_read_b128 v[178:181], v222 offset:32768
	ds_read_b128 v[182:185], v222 offset:33792
	ds_read_b128 v[186:189], v222 offset:34816
	ds_read_b128 v[190:193], v222 offset:35840
	ds_read_b128 v[194:197], v222 offset:36864
	ds_read_b128 v[198:201], v222 offset:37888
	ds_read_b128 v[202:205], v222 offset:38912
	ds_read_b128 v[206:209], v222 offset:39936
	global_load_lds_dwordx4 v[216:217], off
	v_lshl_add_u64 v[216:217], s[70:71], 0, v[146:147]
	s_mov_b32 m0, s20
	s_nop 0
	global_load_lds_dwordx4 v[216:217], off
	s_waitcnt vmcnt(8) lgkmcnt(0)
	s_barrier
	s_setprio 1
	v_mfma_f32_16x16x32_bf16 v[138:141], v[106:109], v[178:181], v[138:141]
	v_mfma_f32_16x16x32_bf16 v[62:65], v[114:117], v[178:181], v[62:65]
	v_mfma_f32_16x16x32_bf16 v[130:133], v[106:109], v[186:189], v[130:133]
	v_mfma_f32_16x16x32_bf16 v[54:57], v[114:117], v[186:189], v[54:57]
	v_mfma_f32_16x16x32_bf16 v[122:125], v[106:109], v[194:197], v[122:125]
	v_mfma_f32_16x16x32_bf16 v[46:49], v[114:117], v[194:197], v[46:49]
	v_mfma_f32_16x16x32_bf16 v[102:105], v[106:109], v[202:205], v[102:105]
	v_mfma_f32_16x16x32_bf16 v[38:41], v[114:117], v[202:205], v[38:41]
	v_mfma_f32_16x16x32_bf16 v[138:141], v[110:113], v[182:185], v[138:141]
	v_mfma_f32_16x16x32_bf16 v[62:65], v[152:155], v[182:185], v[62:65]
	v_mfma_f32_16x16x32_bf16 v[130:133], v[110:113], v[190:193], v[130:133]
	v_mfma_f32_16x16x32_bf16 v[54:57], v[152:155], v[190:193], v[54:57]
	v_mfma_f32_16x16x32_bf16 v[122:125], v[110:113], v[198:201], v[122:125]
	v_mfma_f32_16x16x32_bf16 v[46:49], v[152:155], v[198:201], v[46:49]
	v_mfma_f32_16x16x32_bf16 v[102:105], v[110:113], v[206:209], v[102:105]
	v_mfma_f32_16x16x32_bf16 v[38:41], v[152:155], v[206:209], v[38:41]
	s_setprio 0
	s_setprio 1
	v_mfma_f32_16x16x32_bf16 v[134:137], v[156:159], v[178:181], v[134:137]
	v_mfma_f32_16x16x32_bf16 v[58:61], v[170:173], v[178:181], v[58:61]
	v_mfma_f32_16x16x32_bf16 v[126:129], v[156:159], v[186:189], v[126:129]
	v_mfma_f32_16x16x32_bf16 v[50:53], v[170:173], v[186:189], v[50:53]
	v_mfma_f32_16x16x32_bf16 v[118:121], v[156:159], v[194:197], v[118:121]
	v_mfma_f32_16x16x32_bf16 v[42:45], v[170:173], v[194:197], v[42:45]
	v_mfma_f32_16x16x32_bf16 v[98:101], v[156:159], v[202:205], v[98:101]
	v_mfma_f32_16x16x32_bf16 v[34:37], v[170:173], v[202:205], v[34:37]
	v_mfma_f32_16x16x32_bf16 v[134:137], v[160:163], v[182:185], v[134:137]
	v_mfma_f32_16x16x32_bf16 v[58:61], v[174:177], v[182:185], v[58:61]
	v_mfma_f32_16x16x32_bf16 v[126:129], v[160:163], v[190:193], v[126:129]
	v_mfma_f32_16x16x32_bf16 v[50:53], v[174:177], v[190:193], v[50:53]
	v_mfma_f32_16x16x32_bf16 v[118:121], v[160:163], v[198:201], v[118:121]
	v_mfma_f32_16x16x32_bf16 v[42:45], v[174:177], v[198:201], v[42:45]
	v_mfma_f32_16x16x32_bf16 v[98:101], v[160:163], v[206:209], v[98:101]
	v_mfma_f32_16x16x32_bf16 v[34:37], v[174:177], v[206:209], v[34:37]
	s_setprio 0
	s_barrier
	s_add_i32 s70, s74, s13
	v_lshl_add_u64 v[164:165], v[164:165], 0, s[56:57]
	s_mov_b32 m0, s70
	ds_read_b128 v[178:181], v222 offset:49152
	ds_read_b128 v[182:185], v222 offset:50176
	ds_read_b128 v[186:189], v222 offset:51200
	ds_read_b128 v[190:193], v222 offset:52224
	ds_read_b128 v[194:197], v222 offset:53248
	ds_read_b128 v[198:201], v222 offset:54272
	ds_read_b128 v[202:205], v222 offset:55296
	ds_read_b128 v[206:209], v222 offset:56320
	global_load_lds_dwordx4 v[164:165], off
	s_add_i32 m0, s70, 0x2000
	s_add_u32 s68, s68, 0x8080
	v_lshl_add_u64 v[164:165], v[210:211], 0, s[56:57]
	s_addc_u32 s69, s69, 0
	s_add_i32 s70, s75, s13
	global_load_lds_dwordx4 v[164:165], off
	v_lshl_add_u64 v[164:165], s[68:69], 0, v[166:167]
	s_mov_b32 m0, s70
	s_nop 0
	global_load_lds_dwordx4 v[164:165], off
	v_lshl_add_u64 v[164:165], s[68:69], 0, v[142:143]
	s_add_i32 m0, s70, 0x2000
	s_nop 0
	global_load_lds_dwordx4 v[164:165], off
	v_lshl_add_u64 v[164:165], v[212:213], 0, s[56:57]
	s_mov_b32 m0, s21
	s_nop 0
	global_load_lds_dwordx4 v[164:165], off
	v_lshl_add_u64 v[164:165], v[214:215], 0, s[56:57]
	s_mov_b32 m0, s22
	s_nop 0
	global_load_lds_dwordx4 v[164:165], off
	s_waitcnt vmcnt(8) lgkmcnt(0)
	s_barrier
	s_setprio 1
	v_mfma_f32_16x16x32_bf16 v[94:97], v[106:109], v[178:181], v[94:97]
	v_mfma_f32_16x16x32_bf16 v[30:33], v[114:117], v[178:181], v[30:33]
	v_mfma_f32_16x16x32_bf16 v[86:89], v[106:109], v[186:189], v[86:89]
	v_mfma_f32_16x16x32_bf16 v[22:25], v[114:117], v[186:189], v[22:25]
	v_mfma_f32_16x16x32_bf16 v[78:81], v[106:109], v[194:197], v[78:81]
	v_mfma_f32_16x16x32_bf16 v[14:17], v[114:117], v[194:197], v[14:17]
	v_mfma_f32_16x16x32_bf16 v[70:73], v[106:109], v[202:205], v[70:73]
	v_mfma_f32_16x16x32_bf16 v[6:9], v[114:117], v[202:205], v[6:9]
	v_mfma_f32_16x16x32_bf16 v[94:97], v[110:113], v[182:185], v[94:97]
	v_mfma_f32_16x16x32_bf16 v[30:33], v[152:155], v[182:185], v[30:33]
	v_mfma_f32_16x16x32_bf16 v[86:89], v[110:113], v[190:193], v[86:89]
	v_mfma_f32_16x16x32_bf16 v[22:25], v[152:155], v[190:193], v[22:25]
	v_mfma_f32_16x16x32_bf16 v[78:81], v[110:113], v[198:201], v[78:81]
	v_mfma_f32_16x16x32_bf16 v[14:17], v[152:155], v[198:201], v[14:17]
	v_mfma_f32_16x16x32_bf16 v[70:73], v[110:113], v[206:209], v[70:73]
	v_mfma_f32_16x16x32_bf16 v[6:9], v[152:155], v[206:209], v[6:9]
	s_setprio 0
	s_setprio 1
	v_mfma_f32_16x16x32_bf16 v[90:93], v[156:159], v[178:181], v[90:93]
	v_mfma_f32_16x16x32_bf16 v[26:29], v[170:173], v[178:181], v[26:29]
	v_mfma_f32_16x16x32_bf16 v[82:85], v[156:159], v[186:189], v[82:85]
	v_mfma_f32_16x16x32_bf16 v[18:21], v[170:173], v[186:189], v[18:21]
	v_mfma_f32_16x16x32_bf16 v[74:77], v[156:159], v[194:197], v[74:77]
	v_mfma_f32_16x16x32_bf16 v[10:13], v[170:173], v[194:197], v[10:13]
	v_mfma_f32_16x16x32_bf16 v[66:69], v[156:159], v[202:205], v[66:69]
	v_mfma_f32_16x16x32_bf16 v[2:5], v[170:173], v[202:205], v[2:5]
	v_mfma_f32_16x16x32_bf16 v[90:93], v[160:163], v[182:185], v[90:93]
	v_mfma_f32_16x16x32_bf16 v[26:29], v[174:177], v[182:185], v[26:29]
	v_mfma_f32_16x16x32_bf16 v[82:85], v[160:163], v[190:193], v[82:85]
	v_mfma_f32_16x16x32_bf16 v[18:21], v[174:177], v[190:193], v[18:21]
	v_mfma_f32_16x16x32_bf16 v[74:77], v[160:163], v[198:201], v[74:77]
	v_mfma_f32_16x16x32_bf16 v[10:13], v[174:177], v[198:201], v[10:13]
	v_mfma_f32_16x16x32_bf16 v[66:69], v[160:163], v[206:209], v[66:69]
	v_mfma_f32_16x16x32_bf16 v[2:5], v[174:177], v[206:209], v[2:5]
	s_setprio 0
	s_barrier
	s_add_u32 s66, s66, 0x100
	s_addc_u32 s72, s72, 0
	s_add_u32 s64, s64, 0x100
	s_addc_u32 s65, s65, 0
	s_cmp_ge_i32 s73, s1
	s_mov_b32 s68, s73
	s_cbranch_scc0 .LBB0_469

.Lpeelph6_0:
	s_add_i32 s84, s68, 2
	s_add_u32 s69, s74, 0xfffc0080
	s_addc_u32 s70, s75, -1
	s_add_i32 s88, 0, 0x10000
	s_cmp_eq_u32 s72, s68
	s_cselect_b32 s71, s29, s70
	s_cselect_b32 s70, s43, s69
	s_cselect_b32 s69, s55, s79
	s_cselect_b32 s68, s59, s77
	s_add_i32 s92, 0, 0x14000
	v_add_u32_e32 v78, s88, v204
	v_add_u32_e32 v170, s92, v204
	ds_read_b128 v[58:61], v78
	ds_read_b128 v[62:65], v78 offset:1024
	ds_read_b128 v[74:77], v78 offset:2048
	ds_read_b128 v[78:81], v78 offset:3072
	ds_read_b128 v[146:149], v170
	ds_read_b128 v[150:153], v170 offset:1024
	ds_read_b128 v[154:157], v170 offset:2048
	ds_read_b128 v[170:173], v170 offset:3072
	v_lshl_add_u64 v[202:203], s[74:75], 0, v[180:181]
	s_add_i32 m0, s15, 0xc000
	ds_read_b128 v[174:177], v208
	ds_read_b128 v[182:185], v208 offset:1024
	ds_read_b128 v[186:189], v208 offset:2048
	ds_read_b128 v[190:193], v208 offset:3072
	ds_read_b128 v[194:197], v208 offset:4096
	ds_read_b128 v[198:201], v208 offset:5120
	ds_read_b128 v[210:213], v208 offset:6144
	ds_read_b128 v[214:217], v208 offset:7168
	global_load_lds_dwordx4 v[202:203], off
	v_lshl_add_u64 v[202:203], s[74:75], 0, v[178:179]
	s_add_i32 m0, s15, 0xe000
	s_nop 0
	global_load_lds_dwordx4 v[202:203], off
	s_waitcnt vmcnt(8) lgkmcnt(0)
	s_barrier
	s_setprio 1
	v_mfma_f32_16x16x32_bf16 v[142:145], v[58:61], v[174:177], 0
	v_mfma_f32_16x16x32_bf16 v[138:141], v[74:77], v[174:177], 0
	v_mfma_f32_16x16x32_bf16 v[126:129], v[58:61], v[186:189], 0
	v_mfma_f32_16x16x32_bf16 v[122:125], v[74:77], v[186:189], 0
	v_mfma_f32_16x16x32_bf16 v[110:113], v[58:61], v[194:197], 0
	v_mfma_f32_16x16x32_bf16 v[106:109], v[74:77], v[194:197], 0
	v_mfma_f32_16x16x32_bf16 v[94:97], v[58:61], v[210:213], 0
	v_mfma_f32_16x16x32_bf16 v[90:93], v[74:77], v[210:213], 0
	v_mfma_f32_16x16x32_bf16 v[142:145], v[62:65], v[182:185], v[142:145]
	v_mfma_f32_16x16x32_bf16 v[138:141], v[78:81], v[182:185], v[138:141]
	v_mfma_f32_16x16x32_bf16 v[126:129], v[62:65], v[190:193], v[126:129]
	v_mfma_f32_16x16x32_bf16 v[122:125], v[78:81], v[190:193], v[122:125]
	v_mfma_f32_16x16x32_bf16 v[110:113], v[62:65], v[198:201], v[110:113]
	v_mfma_f32_16x16x32_bf16 v[106:109], v[78:81], v[198:201], v[106:109]
	v_mfma_f32_16x16x32_bf16 v[94:97], v[62:65], v[214:217], v[94:97]
	v_mfma_f32_16x16x32_bf16 v[90:93], v[78:81], v[214:217], v[90:93]
	s_setprio 0
	s_setprio 1
	v_mfma_f32_16x16x32_bf16 v[134:137], v[146:149], v[174:177], 0
	v_mfma_f32_16x16x32_bf16 v[130:133], v[154:157], v[174:177], 0
	v_mfma_f32_16x16x32_bf16 v[118:121], v[146:149], v[186:189], 0
	v_mfma_f32_16x16x32_bf16 v[114:117], v[154:157], v[186:189], 0
	v_mfma_f32_16x16x32_bf16 v[102:105], v[146:149], v[194:197], 0
	v_mfma_f32_16x16x32_bf16 v[98:101], v[154:157], v[194:197], 0
	v_mfma_f32_16x16x32_bf16 v[86:89], v[146:149], v[210:213], 0
	v_mfma_f32_16x16x32_bf16 v[82:85], v[154:157], v[210:213], 0
	v_mfma_f32_16x16x32_bf16 v[134:137], v[150:153], v[182:185], v[134:137]
	v_mfma_f32_16x16x32_bf16 v[130:133], v[170:173], v[182:185], v[130:133]
	v_mfma_f32_16x16x32_bf16 v[118:121], v[150:153], v[190:193], v[118:121]
	v_mfma_f32_16x16x32_bf16 v[114:117], v[170:173], v[190:193], v[114:117]
	v_mfma_f32_16x16x32_bf16 v[102:105], v[150:153], v[198:201], v[102:105]
	v_mfma_f32_16x16x32_bf16 v[98:101], v[170:173], v[198:201], v[98:101]
	v_mfma_f32_16x16x32_bf16 v[86:89], v[150:153], v[214:217], v[86:89]
	v_mfma_f32_16x16x32_bf16 v[82:85], v[170:173], v[214:217], v[82:85]
	s_setprio 0
	s_barrier
	s_add_i32 s88, s88, s14
	v_lshl_add_u64 v[202:203], s[68:69], 0, v[166:167]
	s_mov_b32 m0, s88
	ds_read_b128 v[174:177], v208 offset:16384
	ds_read_b128 v[182:185], v208 offset:17408
	ds_read_b128 v[186:189], v208 offset:18432
	ds_read_b128 v[190:193], v208 offset:19456
	ds_read_b128 v[194:197], v208 offset:20480
	ds_read_b128 v[198:201], v208 offset:21504
	ds_read_b128 v[210:213], v208 offset:22528
	ds_read_b128 v[214:217], v208 offset:23552
	global_load_lds_dwordx4 v[202:203], off
	s_add_i32 m0, s88, 0x2000
	s_add_u32 s90, s68, 0x40000
	v_lshl_add_u64 v[218:219], s[68:69], 0, v[158:159]
	s_addc_u32 s91, s69, 0
	s_add_i32 s88, s92, s14
	global_load_lds_dwordx4 v[218:219], off
	v_lshl_add_u64 v[220:221], s[90:91], 0, v[166:167]
	s_mov_b32 m0, s88
	v_lshl_add_u64 v[222:223], s[70:71], 0, v[162:163]
	global_load_lds_dwordx4 v[220:221], off
	v_lshl_add_u64 v[220:221], s[90:91], 0, v[158:159]
	s_add_i32 m0, s88, 0x2000
	s_nop 0
	global_load_lds_dwordx4 v[220:221], off
	v_lshl_add_u64 v[220:221], s[70:71], 0, v[160:161]
	s_mov_b32 m0, s15
	s_nop 0
	global_load_lds_dwordx4 v[220:221], off
	s_mov_b32 m0, s16
	s_nop 0
	global_load_lds_dwordx4 v[222:223], off
	s_waitcnt vmcnt(8) lgkmcnt(0)
	s_barrier
	s_setprio 1
	v_mfma_f32_16x16x32_bf16 v[70:73], v[58:61], v[174:177], 0
	v_mfma_f32_16x16x32_bf16 v[66:69], v[74:77], v[174:177], 0
	v_mfma_f32_16x16x32_bf16 v[46:49], v[58:61], v[186:189], 0
	v_mfma_f32_16x16x32_bf16 v[42:45], v[74:77], v[186:189], 0
	v_mfma_f32_16x16x32_bf16 v[30:33], v[58:61], v[194:197], 0
	v_mfma_f32_16x16x32_bf16 v[26:29], v[74:77], v[194:197], 0
	v_mfma_f32_16x16x32_bf16 v[14:17], v[58:61], v[210:213], 0
	v_mfma_f32_16x16x32_bf16 v[10:13], v[74:77], v[210:213], 0
	v_mfma_f32_16x16x32_bf16 v[70:73], v[62:65], v[182:185], v[70:73]
	v_mfma_f32_16x16x32_bf16 v[66:69], v[78:81], v[182:185], v[66:69]
	v_mfma_f32_16x16x32_bf16 v[46:49], v[62:65], v[190:193], v[46:49]
	v_mfma_f32_16x16x32_bf16 v[42:45], v[78:81], v[190:193], v[42:45]
	v_mfma_f32_16x16x32_bf16 v[30:33], v[62:65], v[198:201], v[30:33]
	v_mfma_f32_16x16x32_bf16 v[26:29], v[78:81], v[198:201], v[26:29]
	v_mfma_f32_16x16x32_bf16 v[14:17], v[62:65], v[214:217], v[14:17]
	v_mfma_f32_16x16x32_bf16 v[10:13], v[78:81], v[214:217], v[10:13]
	s_setprio 0
	s_setprio 1
	v_mfma_f32_16x16x32_bf16 v[54:57], v[146:149], v[174:177], 0
	v_mfma_f32_16x16x32_bf16 v[50:53], v[154:157], v[174:177], 0
	v_mfma_f32_16x16x32_bf16 v[38:41], v[146:149], v[186:189], 0
	v_mfma_f32_16x16x32_bf16 v[34:37], v[154:157], v[186:189], 0
	v_mfma_f32_16x16x32_bf16 v[22:25], v[146:149], v[194:197], 0
	v_mfma_f32_16x16x32_bf16 v[18:21], v[154:157], v[194:197], 0
	v_mfma_f32_16x16x32_bf16 v[6:9], v[146:149], v[210:213], 0
	v_mfma_f32_16x16x32_bf16 v[2:5], v[154:157], v[210:213], 0
	v_mfma_f32_16x16x32_bf16 v[54:57], v[150:153], v[182:185], v[54:57]
	v_mfma_f32_16x16x32_bf16 v[50:53], v[170:173], v[182:185], v[50:53]
	v_mfma_f32_16x16x32_bf16 v[38:41], v[150:153], v[190:193], v[38:41]
	v_mfma_f32_16x16x32_bf16 v[34:37], v[170:173], v[190:193], v[34:37]
	v_mfma_f32_16x16x32_bf16 v[22:25], v[150:153], v[198:201], v[22:25]
	v_mfma_f32_16x16x32_bf16 v[18:21], v[170:173], v[198:201], v[18:21]
	v_mfma_f32_16x16x32_bf16 v[6:9], v[150:153], v[214:217], v[6:9]
	v_mfma_f32_16x16x32_bf16 v[2:5], v[170:173], v[214:217], v[2:5]
	s_setprio 0
	s_barrier
	s_add_i32 s88, 0, 0x18000
	s_add_i32 s90, 0, 0x1c000
	v_add_u32_e32 v78, s88, v204
	v_add_u32_e32 v170, s90, v204
	ds_read_b128 v[58:61], v78
	ds_read_b128 v[62:65], v78 offset:1024
	ds_read_b128 v[74:77], v78 offset:2048
	ds_read_b128 v[78:81], v78 offset:3072
	ds_read_b128 v[146:149], v170
	ds_read_b128 v[150:153], v170 offset:1024
	ds_read_b128 v[154:157], v170 offset:2048
	ds_read_b128 v[170:173], v170 offset:3072
	s_add_u32 s70, s70, 0x40000
	s_addc_u32 s71, s71, 0
	s_mov_b32 m0, s20
	v_lshl_add_u64 v[232:233], s[70:71], 0, v[160:161]
	ds_read_b128 v[174:177], v208 offset:32768
	ds_read_b128 v[182:185], v208 offset:33792
	ds_read_b128 v[186:189], v208 offset:34816
	ds_read_b128 v[190:193], v208 offset:35840
	ds_read_b128 v[194:197], v208 offset:36864
	ds_read_b128 v[198:201], v208 offset:37888
	ds_read_b128 v[210:213], v208 offset:38912
	ds_read_b128 v[214:217], v208 offset:39936
	global_load_lds_dwordx4 v[232:233], off
	v_lshl_add_u64 v[232:233], s[70:71], 0, v[162:163]
	s_mov_b32 m0, s21
	s_nop 0
	global_load_lds_dwordx4 v[232:233], off
	s_waitcnt vmcnt(8) lgkmcnt(0)
	s_barrier
	s_setprio 1
	v_mfma_f32_16x16x32_bf16 v[142:145], v[58:61], v[174:177], v[142:145]
	v_mfma_f32_16x16x32_bf16 v[138:141], v[74:77], v[174:177], v[138:141]
	v_mfma_f32_16x16x32_bf16 v[126:129], v[58:61], v[186:189], v[126:129]
	v_mfma_f32_16x16x32_bf16 v[122:125], v[74:77], v[186:189], v[122:125]
	v_mfma_f32_16x16x32_bf16 v[110:113], v[58:61], v[194:197], v[110:113]
	v_mfma_f32_16x16x32_bf16 v[106:109], v[74:77], v[194:197], v[106:109]
	v_mfma_f32_16x16x32_bf16 v[94:97], v[58:61], v[210:213], v[94:97]
	v_mfma_f32_16x16x32_bf16 v[90:93], v[74:77], v[210:213], v[90:93]
	v_mfma_f32_16x16x32_bf16 v[142:145], v[62:65], v[182:185], v[142:145]
	v_mfma_f32_16x16x32_bf16 v[138:141], v[78:81], v[182:185], v[138:141]
	v_mfma_f32_16x16x32_bf16 v[126:129], v[62:65], v[190:193], v[126:129]
	v_mfma_f32_16x16x32_bf16 v[122:125], v[78:81], v[190:193], v[122:125]
	v_mfma_f32_16x16x32_bf16 v[110:113], v[62:65], v[198:201], v[110:113]
	v_mfma_f32_16x16x32_bf16 v[106:109], v[78:81], v[198:201], v[106:109]
	v_mfma_f32_16x16x32_bf16 v[94:97], v[62:65], v[214:217], v[94:97]
	v_mfma_f32_16x16x32_bf16 v[90:93], v[78:81], v[214:217], v[90:93]
	s_setprio 0
	s_setprio 1
	v_mfma_f32_16x16x32_bf16 v[134:137], v[146:149], v[174:177], v[134:137]
	v_mfma_f32_16x16x32_bf16 v[130:133], v[154:157], v[174:177], v[130:133]
	v_mfma_f32_16x16x32_bf16 v[118:121], v[146:149], v[186:189], v[118:121]
	v_mfma_f32_16x16x32_bf16 v[114:117], v[154:157], v[186:189], v[114:117]
	v_mfma_f32_16x16x32_bf16 v[102:105], v[146:149], v[194:197], v[102:105]
	v_mfma_f32_16x16x32_bf16 v[98:101], v[154:157], v[194:197], v[98:101]
	v_mfma_f32_16x16x32_bf16 v[86:89], v[146:149], v[210:213], v[86:89]
	v_mfma_f32_16x16x32_bf16 v[82:85], v[154:157], v[210:213], v[82:85]
	v_mfma_f32_16x16x32_bf16 v[134:137], v[150:153], v[182:185], v[134:137]
	v_mfma_f32_16x16x32_bf16 v[130:133], v[170:173], v[182:185], v[130:133]
	v_mfma_f32_16x16x32_bf16 v[118:121], v[150:153], v[190:193], v[118:121]
	v_mfma_f32_16x16x32_bf16 v[114:117], v[170:173], v[190:193], v[114:117]
	v_mfma_f32_16x16x32_bf16 v[102:105], v[150:153], v[198:201], v[102:105]
	v_mfma_f32_16x16x32_bf16 v[98:101], v[170:173], v[198:201], v[98:101]
	v_mfma_f32_16x16x32_bf16 v[86:89], v[150:153], v[214:217], v[86:89]
	v_mfma_f32_16x16x32_bf16 v[82:85], v[170:173], v[214:217], v[82:85]
	s_setprio 0
	s_barrier
	s_add_i32 s70, s88, s14
	v_lshl_add_u64 v[202:203], v[202:203], 0, s[56:57]
	s_mov_b32 m0, s70
	ds_read_b128 v[174:177], v208 offset:49152
	ds_read_b128 v[182:185], v208 offset:50176
	ds_read_b128 v[186:189], v208 offset:51200
	ds_read_b128 v[190:193], v208 offset:52224
	ds_read_b128 v[194:197], v208 offset:53248
	ds_read_b128 v[198:201], v208 offset:54272
	ds_read_b128 v[210:213], v208 offset:55296
	ds_read_b128 v[214:217], v208 offset:56320
	global_load_lds_dwordx4 v[202:203], off
	s_add_i32 m0, s70, 0x2000
	s_add_u32 s68, s68, 0x40080
	v_lshl_add_u64 v[202:203], v[218:219], 0, s[56:57]
	s_addc_u32 s69, s69, 0
	s_add_i32 s70, s90, s14
	global_load_lds_dwordx4 v[202:203], off
	v_lshl_add_u64 v[202:203], s[68:69], 0, v[166:167]
	s_mov_b32 m0, s70
	s_nop 0
	global_load_lds_dwordx4 v[202:203], off
	v_lshl_add_u64 v[202:203], s[68:69], 0, v[158:159]
	s_add_i32 m0, s70, 0x2000
	s_nop 0
	global_load_lds_dwordx4 v[202:203], off
	v_lshl_add_u64 v[202:203], v[220:221], 0, s[56:57]
	s_mov_b32 m0, s24
	s_nop 0
	global_load_lds_dwordx4 v[202:203], off
	v_lshl_add_u64 v[202:203], v[222:223], 0, s[56:57]
	s_mov_b32 m0, s25
	s_nop 0
	global_load_lds_dwordx4 v[202:203], off
	s_waitcnt vmcnt(8) lgkmcnt(0)
	s_barrier
	s_setprio 1
	v_mfma_f32_16x16x32_bf16 v[70:73], v[58:61], v[174:177], v[70:73]
	v_mfma_f32_16x16x32_bf16 v[66:69], v[74:77], v[174:177], v[66:69]
	v_mfma_f32_16x16x32_bf16 v[46:49], v[58:61], v[186:189], v[46:49]
	v_mfma_f32_16x16x32_bf16 v[42:45], v[74:77], v[186:189], v[42:45]
	v_mfma_f32_16x16x32_bf16 v[30:33], v[58:61], v[194:197], v[30:33]
	v_mfma_f32_16x16x32_bf16 v[26:29], v[74:77], v[194:197], v[26:29]
	v_mfma_f32_16x16x32_bf16 v[14:17], v[58:61], v[210:213], v[14:17]
	v_mfma_f32_16x16x32_bf16 v[10:13], v[74:77], v[210:213], v[10:13]
	v_mfma_f32_16x16x32_bf16 v[70:73], v[62:65], v[182:185], v[70:73]
	v_mfma_f32_16x16x32_bf16 v[66:69], v[78:81], v[182:185], v[66:69]
	v_mfma_f32_16x16x32_bf16 v[46:49], v[62:65], v[190:193], v[46:49]
	v_mfma_f32_16x16x32_bf16 v[42:45], v[78:81], v[190:193], v[42:45]
	v_mfma_f32_16x16x32_bf16 v[30:33], v[62:65], v[198:201], v[30:33]
	v_mfma_f32_16x16x32_bf16 v[26:29], v[78:81], v[198:201], v[26:29]
	v_mfma_f32_16x16x32_bf16 v[14:17], v[62:65], v[214:217], v[14:17]
	v_mfma_f32_16x16x32_bf16 v[10:13], v[78:81], v[214:217], v[10:13]
	s_setprio 0
	s_setprio 1
	v_mfma_f32_16x16x32_bf16 v[54:57], v[146:149], v[174:177], v[54:57]
	v_mfma_f32_16x16x32_bf16 v[50:53], v[154:157], v[174:177], v[50:53]
	v_mfma_f32_16x16x32_bf16 v[38:41], v[146:149], v[186:189], v[38:41]
	v_mfma_f32_16x16x32_bf16 v[34:37], v[154:157], v[186:189], v[34:37]
	v_mfma_f32_16x16x32_bf16 v[22:25], v[146:149], v[194:197], v[22:25]
	v_mfma_f32_16x16x32_bf16 v[18:21], v[154:157], v[194:197], v[18:21]
	v_mfma_f32_16x16x32_bf16 v[6:9], v[146:149], v[210:213], v[6:9]
	v_mfma_f32_16x16x32_bf16 v[2:5], v[154:157], v[210:213], v[2:5]
	v_mfma_f32_16x16x32_bf16 v[54:57], v[150:153], v[182:185], v[54:57]
	v_mfma_f32_16x16x32_bf16 v[50:53], v[170:173], v[182:185], v[50:53]
	v_mfma_f32_16x16x32_bf16 v[38:41], v[150:153], v[190:193], v[38:41]
	v_mfma_f32_16x16x32_bf16 v[34:37], v[170:173], v[190:193], v[34:37]
	v_mfma_f32_16x16x32_bf16 v[22:25], v[150:153], v[198:201], v[22:25]
	v_mfma_f32_16x16x32_bf16 v[18:21], v[170:173], v[198:201], v[18:21]
	v_mfma_f32_16x16x32_bf16 v[6:9], v[150:153], v[214:217], v[6:9]
	v_mfma_f32_16x16x32_bf16 v[2:5], v[170:173], v[214:217], v[2:5]
	s_setprio 0
	s_barrier
	s_add_u32 s77, s77, 0x100
	s_addc_u32 s79, s79, 0
	s_add_u32 s74, s74, 0x100
	s_addc_u32 s75, s75, 0
	s_cmp_ge_i32 s84, s1
	s_mov_b32 s68, s84
	s_cbranch_scc0 .LBB0_664
	s_branch .Lpeelexitph6
.LBB0_664:
	s_add_i32 s84, s68, 2
	s_add_u32 s69, s74, 0xfffc0080
	s_addc_u32 s70, s75, -1
	s_add_i32 s88, 0, 0x10000
	s_cmp_eq_u32 s72, s68
	s_cselect_b32 s71, s29, s70
	s_cselect_b32 s70, s43, s69
	s_cselect_b32 s69, s55, s79
	s_cselect_b32 s68, s59, s77
	s_add_i32 s92, 0, 0x14000
	v_add_u32_e32 v78, s88, v204
	v_add_u32_e32 v170, s92, v204
	ds_read_b128 v[58:61], v78
	ds_read_b128 v[62:65], v78 offset:1024
	ds_read_b128 v[74:77], v78 offset:2048
	ds_read_b128 v[78:81], v78 offset:3072
	ds_read_b128 v[146:149], v170
	ds_read_b128 v[150:153], v170 offset:1024
	ds_read_b128 v[154:157], v170 offset:2048
	ds_read_b128 v[170:173], v170 offset:3072
	v_lshl_add_u64 v[202:203], s[74:75], 0, v[180:181]
	s_add_i32 m0, s15, 0xc000
	ds_read_b128 v[174:177], v208
	ds_read_b128 v[182:185], v208 offset:1024
	ds_read_b128 v[186:189], v208 offset:2048
	ds_read_b128 v[190:193], v208 offset:3072
	ds_read_b128 v[194:197], v208 offset:4096
	ds_read_b128 v[198:201], v208 offset:5120
	ds_read_b128 v[210:213], v208 offset:6144
	ds_read_b128 v[214:217], v208 offset:7168
	global_load_lds_dwordx4 v[202:203], off
	v_lshl_add_u64 v[202:203], s[74:75], 0, v[178:179]
	s_add_i32 m0, s15, 0xe000
	s_nop 0
	global_load_lds_dwordx4 v[202:203], off
	s_waitcnt vmcnt(8) lgkmcnt(0)
	s_barrier
	s_setprio 1
	v_mfma_f32_16x16x32_bf16 v[142:145], v[58:61], v[174:177], v[142:145]
	v_mfma_f32_16x16x32_bf16 v[138:141], v[74:77], v[174:177], v[138:141]
	v_mfma_f32_16x16x32_bf16 v[126:129], v[58:61], v[186:189], v[126:129]
	v_mfma_f32_16x16x32_bf16 v[122:125], v[74:77], v[186:189], v[122:125]
	v_mfma_f32_16x16x32_bf16 v[110:113], v[58:61], v[194:197], v[110:113]
	v_mfma_f32_16x16x32_bf16 v[106:109], v[74:77], v[194:197], v[106:109]
	v_mfma_f32_16x16x32_bf16 v[94:97], v[58:61], v[210:213], v[94:97]
	v_mfma_f32_16x16x32_bf16 v[90:93], v[74:77], v[210:213], v[90:93]
	v_mfma_f32_16x16x32_bf16 v[142:145], v[62:65], v[182:185], v[142:145]
	v_mfma_f32_16x16x32_bf16 v[138:141], v[78:81], v[182:185], v[138:141]
	v_mfma_f32_16x16x32_bf16 v[126:129], v[62:65], v[190:193], v[126:129]
	v_mfma_f32_16x16x32_bf16 v[122:125], v[78:81], v[190:193], v[122:125]
	v_mfma_f32_16x16x32_bf16 v[110:113], v[62:65], v[198:201], v[110:113]
	v_mfma_f32_16x16x32_bf16 v[106:109], v[78:81], v[198:201], v[106:109]
	v_mfma_f32_16x16x32_bf16 v[94:97], v[62:65], v[214:217], v[94:97]
	v_mfma_f32_16x16x32_bf16 v[90:93], v[78:81], v[214:217], v[90:93]
	s_setprio 0
	s_setprio 1
	v_mfma_f32_16x16x32_bf16 v[134:137], v[146:149], v[174:177], v[134:137]
	v_mfma_f32_16x16x32_bf16 v[130:133], v[154:157], v[174:177], v[130:133]
	v_mfma_f32_16x16x32_bf16 v[118:121], v[146:149], v[186:189], v[118:121]
	v_mfma_f32_16x16x32_bf16 v[114:117], v[154:157], v[186:189], v[114:117]
	v_mfma_f32_16x16x32_bf16 v[102:105], v[146:149], v[194:197], v[102:105]
	v_mfma_f32_16x16x32_bf16 v[98:101], v[154:157], v[194:197], v[98:101]
	v_mfma_f32_16x16x32_bf16 v[86:89], v[146:149], v[210:213], v[86:89]
	v_mfma_f32_16x16x32_bf16 v[82:85], v[154:157], v[210:213], v[82:85]
	v_mfma_f32_16x16x32_bf16 v[134:137], v[150:153], v[182:185], v[134:137]
	v_mfma_f32_16x16x32_bf16 v[130:133], v[170:173], v[182:185], v[130:133]
	v_mfma_f32_16x16x32_bf16 v[118:121], v[150:153], v[190:193], v[118:121]
	v_mfma_f32_16x16x32_bf16 v[114:117], v[170:173], v[190:193], v[114:117]
	v_mfma_f32_16x16x32_bf16 v[102:105], v[150:153], v[198:201], v[102:105]
	v_mfma_f32_16x16x32_bf16 v[98:101], v[170:173], v[198:201], v[98:101]
	v_mfma_f32_16x16x32_bf16 v[86:89], v[150:153], v[214:217], v[86:89]
	v_mfma_f32_16x16x32_bf16 v[82:85], v[170:173], v[214:217], v[82:85]
	s_setprio 0
	s_barrier
	s_add_i32 s88, s88, s14
	v_lshl_add_u64 v[202:203], s[68:69], 0, v[166:167]
	s_mov_b32 m0, s88
	ds_read_b128 v[174:177], v208 offset:16384
	ds_read_b128 v[182:185], v208 offset:17408
	ds_read_b128 v[186:189], v208 offset:18432
	ds_read_b128 v[190:193], v208 offset:19456
	ds_read_b128 v[194:197], v208 offset:20480
	ds_read_b128 v[198:201], v208 offset:21504
	ds_read_b128 v[210:213], v208 offset:22528
	ds_read_b128 v[214:217], v208 offset:23552
	global_load_lds_dwordx4 v[202:203], off
	s_add_i32 m0, s88, 0x2000
	s_add_u32 s90, s68, 0x40000
	v_lshl_add_u64 v[218:219], s[68:69], 0, v[158:159]
	s_addc_u32 s91, s69, 0
	s_add_i32 s88, s92, s14
	global_load_lds_dwordx4 v[218:219], off
	v_lshl_add_u64 v[220:221], s[90:91], 0, v[166:167]
	s_mov_b32 m0, s88
	v_lshl_add_u64 v[222:223], s[70:71], 0, v[162:163]
	global_load_lds_dwordx4 v[220:221], off
	v_lshl_add_u64 v[220:221], s[90:91], 0, v[158:159]
	s_add_i32 m0, s88, 0x2000
	s_nop 0
	global_load_lds_dwordx4 v[220:221], off
	v_lshl_add_u64 v[220:221], s[70:71], 0, v[160:161]
	s_mov_b32 m0, s15
	s_nop 0
	global_load_lds_dwordx4 v[220:221], off
	s_mov_b32 m0, s16
	s_nop 0
	global_load_lds_dwordx4 v[222:223], off
	s_waitcnt vmcnt(8) lgkmcnt(0)
	s_barrier
	s_setprio 1
	v_mfma_f32_16x16x32_bf16 v[70:73], v[58:61], v[174:177], v[70:73]
	v_mfma_f32_16x16x32_bf16 v[66:69], v[74:77], v[174:177], v[66:69]
	v_mfma_f32_16x16x32_bf16 v[46:49], v[58:61], v[186:189], v[46:49]
	v_mfma_f32_16x16x32_bf16 v[42:45], v[74:77], v[186:189], v[42:45]
	v_mfma_f32_16x16x32_bf16 v[30:33], v[58:61], v[194:197], v[30:33]
	v_mfma_f32_16x16x32_bf16 v[26:29], v[74:77], v[194:197], v[26:29]
	v_mfma_f32_16x16x32_bf16 v[14:17], v[58:61], v[210:213], v[14:17]
	v_mfma_f32_16x16x32_bf16 v[10:13], v[74:77], v[210:213], v[10:13]
	v_mfma_f32_16x16x32_bf16 v[70:73], v[62:65], v[182:185], v[70:73]
	v_mfma_f32_16x16x32_bf16 v[66:69], v[78:81], v[182:185], v[66:69]
	v_mfma_f32_16x16x32_bf16 v[46:49], v[62:65], v[190:193], v[46:49]
	v_mfma_f32_16x16x32_bf16 v[42:45], v[78:81], v[190:193], v[42:45]
	v_mfma_f32_16x16x32_bf16 v[30:33], v[62:65], v[198:201], v[30:33]
	v_mfma_f32_16x16x32_bf16 v[26:29], v[78:81], v[198:201], v[26:29]
	v_mfma_f32_16x16x32_bf16 v[14:17], v[62:65], v[214:217], v[14:17]
	v_mfma_f32_16x16x32_bf16 v[10:13], v[78:81], v[214:217], v[10:13]
	s_setprio 0
	s_setprio 1
	v_mfma_f32_16x16x32_bf16 v[54:57], v[146:149], v[174:177], v[54:57]
	v_mfma_f32_16x16x32_bf16 v[50:53], v[154:157], v[174:177], v[50:53]
	v_mfma_f32_16x16x32_bf16 v[38:41], v[146:149], v[186:189], v[38:41]
	v_mfma_f32_16x16x32_bf16 v[34:37], v[154:157], v[186:189], v[34:37]
	v_mfma_f32_16x16x32_bf16 v[22:25], v[146:149], v[194:197], v[22:25]
	v_mfma_f32_16x16x32_bf16 v[18:21], v[154:157], v[194:197], v[18:21]
	v_mfma_f32_16x16x32_bf16 v[6:9], v[146:149], v[210:213], v[6:9]
	v_mfma_f32_16x16x32_bf16 v[2:5], v[154:157], v[210:213], v[2:5]
	v_mfma_f32_16x16x32_bf16 v[54:57], v[150:153], v[182:185], v[54:57]
	v_mfma_f32_16x16x32_bf16 v[50:53], v[170:173], v[182:185], v[50:53]
	v_mfma_f32_16x16x32_bf16 v[38:41], v[150:153], v[190:193], v[38:41]
	v_mfma_f32_16x16x32_bf16 v[34:37], v[170:173], v[190:193], v[34:37]
	v_mfma_f32_16x16x32_bf16 v[22:25], v[150:153], v[198:201], v[22:25]
	v_mfma_f32_16x16x32_bf16 v[18:21], v[170:173], v[198:201], v[18:21]
	v_mfma_f32_16x16x32_bf16 v[6:9], v[150:153], v[214:217], v[6:9]
	v_mfma_f32_16x16x32_bf16 v[2:5], v[170:173], v[214:217], v[2:5]
	s_setprio 0
	s_barrier
	s_add_i32 s88, 0, 0x18000
	s_add_i32 s90, 0, 0x1c000
	v_add_u32_e32 v78, s88, v204
	v_add_u32_e32 v170, s90, v204
	ds_read_b128 v[58:61], v78
	ds_read_b128 v[62:65], v78 offset:1024
	ds_read_b128 v[74:77], v78 offset:2048
	ds_read_b128 v[78:81], v78 offset:3072
	ds_read_b128 v[146:149], v170
	ds_read_b128 v[150:153], v170 offset:1024
	ds_read_b128 v[154:157], v170 offset:2048
	ds_read_b128 v[170:173], v170 offset:3072
	s_add_u32 s70, s70, 0x40000
	s_addc_u32 s71, s71, 0
	s_mov_b32 m0, s20
	v_lshl_add_u64 v[232:233], s[70:71], 0, v[160:161]
	ds_read_b128 v[174:177], v208 offset:32768
	ds_read_b128 v[182:185], v208 offset:33792
	ds_read_b128 v[186:189], v208 offset:34816
	ds_read_b128 v[190:193], v208 offset:35840
	ds_read_b128 v[194:197], v208 offset:36864
	ds_read_b128 v[198:201], v208 offset:37888
	ds_read_b128 v[210:213], v208 offset:38912
	ds_read_b128 v[214:217], v208 offset:39936
	global_load_lds_dwordx4 v[232:233], off
	v_lshl_add_u64 v[232:233], s[70:71], 0, v[162:163]
	s_mov_b32 m0, s21
	s_nop 0
	global_load_lds_dwordx4 v[232:233], off
	s_waitcnt vmcnt(8) lgkmcnt(0)
	s_barrier
	s_setprio 1
	v_mfma_f32_16x16x32_bf16 v[142:145], v[58:61], v[174:177], v[142:145]
	v_mfma_f32_16x16x32_bf16 v[138:141], v[74:77], v[174:177], v[138:141]
	v_mfma_f32_16x16x32_bf16 v[126:129], v[58:61], v[186:189], v[126:129]
	v_mfma_f32_16x16x32_bf16 v[122:125], v[74:77], v[186:189], v[122:125]
	v_mfma_f32_16x16x32_bf16 v[110:113], v[58:61], v[194:197], v[110:113]
	v_mfma_f32_16x16x32_bf16 v[106:109], v[74:77], v[194:197], v[106:109]
	v_mfma_f32_16x16x32_bf16 v[94:97], v[58:61], v[210:213], v[94:97]
	v_mfma_f32_16x16x32_bf16 v[90:93], v[74:77], v[210:213], v[90:93]
	v_mfma_f32_16x16x32_bf16 v[142:145], v[62:65], v[182:185], v[142:145]
	v_mfma_f32_16x16x32_bf16 v[138:141], v[78:81], v[182:185], v[138:141]
	v_mfma_f32_16x16x32_bf16 v[126:129], v[62:65], v[190:193], v[126:129]
	v_mfma_f32_16x16x32_bf16 v[122:125], v[78:81], v[190:193], v[122:125]
	v_mfma_f32_16x16x32_bf16 v[110:113], v[62:65], v[198:201], v[110:113]
	v_mfma_f32_16x16x32_bf16 v[106:109], v[78:81], v[198:201], v[106:109]
	v_mfma_f32_16x16x32_bf16 v[94:97], v[62:65], v[214:217], v[94:97]
	v_mfma_f32_16x16x32_bf16 v[90:93], v[78:81], v[214:217], v[90:93]
	s_setprio 0
	s_setprio 1
	v_mfma_f32_16x16x32_bf16 v[134:137], v[146:149], v[174:177], v[134:137]
	v_mfma_f32_16x16x32_bf16 v[130:133], v[154:157], v[174:177], v[130:133]
	v_mfma_f32_16x16x32_bf16 v[118:121], v[146:149], v[186:189], v[118:121]
	v_mfma_f32_16x16x32_bf16 v[114:117], v[154:157], v[186:189], v[114:117]
	v_mfma_f32_16x16x32_bf16 v[102:105], v[146:149], v[194:197], v[102:105]
	v_mfma_f32_16x16x32_bf16 v[98:101], v[154:157], v[194:197], v[98:101]
	v_mfma_f32_16x16x32_bf16 v[86:89], v[146:149], v[210:213], v[86:89]
	v_mfma_f32_16x16x32_bf16 v[82:85], v[154:157], v[210:213], v[82:85]
	v_mfma_f32_16x16x32_bf16 v[134:137], v[150:153], v[182:185], v[134:137]
	v_mfma_f32_16x16x32_bf16 v[130:133], v[170:173], v[182:185], v[130:133]
	v_mfma_f32_16x16x32_bf16 v[118:121], v[150:153], v[190:193], v[118:121]
	v_mfma_f32_16x16x32_bf16 v[114:117], v[170:173], v[190:193], v[114:117]
	v_mfma_f32_16x16x32_bf16 v[102:105], v[150:153], v[198:201], v[102:105]
	v_mfma_f32_16x16x32_bf16 v[98:101], v[170:173], v[198:201], v[98:101]
	v_mfma_f32_16x16x32_bf16 v[86:89], v[150:153], v[214:217], v[86:89]
	v_mfma_f32_16x16x32_bf16 v[82:85], v[170:173], v[214:217], v[82:85]
	s_setprio 0
	s_barrier
	s_add_i32 s70, s88, s14
	v_lshl_add_u64 v[202:203], v[202:203], 0, s[56:57]
	s_mov_b32 m0, s70
	ds_read_b128 v[174:177], v208 offset:49152
	ds_read_b128 v[182:185], v208 offset:50176
	ds_read_b128 v[186:189], v208 offset:51200
	ds_read_b128 v[190:193], v208 offset:52224
	ds_read_b128 v[194:197], v208 offset:53248
	ds_read_b128 v[198:201], v208 offset:54272
	ds_read_b128 v[210:213], v208 offset:55296
	ds_read_b128 v[214:217], v208 offset:56320
	global_load_lds_dwordx4 v[202:203], off
	s_add_i32 m0, s70, 0x2000
	s_add_u32 s68, s68, 0x40080
	v_lshl_add_u64 v[202:203], v[218:219], 0, s[56:57]
	s_addc_u32 s69, s69, 0
	s_add_i32 s70, s90, s14
	global_load_lds_dwordx4 v[202:203], off
	v_lshl_add_u64 v[202:203], s[68:69], 0, v[166:167]
	s_mov_b32 m0, s70
	s_nop 0
	global_load_lds_dwordx4 v[202:203], off
	v_lshl_add_u64 v[202:203], s[68:69], 0, v[158:159]
	s_add_i32 m0, s70, 0x2000
	s_nop 0
	global_load_lds_dwordx4 v[202:203], off
	v_lshl_add_u64 v[202:203], v[220:221], 0, s[56:57]
	s_mov_b32 m0, s24
	s_nop 0
	global_load_lds_dwordx4 v[202:203], off
	v_lshl_add_u64 v[202:203], v[222:223], 0, s[56:57]
	s_mov_b32 m0, s25
	s_nop 0
	global_load_lds_dwordx4 v[202:203], off
	s_waitcnt vmcnt(8) lgkmcnt(0)
	s_barrier
	s_setprio 1
	v_mfma_f32_16x16x32_bf16 v[70:73], v[58:61], v[174:177], v[70:73]
	v_mfma_f32_16x16x32_bf16 v[66:69], v[74:77], v[174:177], v[66:69]
	v_mfma_f32_16x16x32_bf16 v[46:49], v[58:61], v[186:189], v[46:49]
	v_mfma_f32_16x16x32_bf16 v[42:45], v[74:77], v[186:189], v[42:45]
	v_mfma_f32_16x16x32_bf16 v[30:33], v[58:61], v[194:197], v[30:33]
	v_mfma_f32_16x16x32_bf16 v[26:29], v[74:77], v[194:197], v[26:29]
	v_mfma_f32_16x16x32_bf16 v[14:17], v[58:61], v[210:213], v[14:17]
	v_mfma_f32_16x16x32_bf16 v[10:13], v[74:77], v[210:213], v[10:13]
	v_mfma_f32_16x16x32_bf16 v[70:73], v[62:65], v[182:185], v[70:73]
	v_mfma_f32_16x16x32_bf16 v[66:69], v[78:81], v[182:185], v[66:69]
	v_mfma_f32_16x16x32_bf16 v[46:49], v[62:65], v[190:193], v[46:49]
	v_mfma_f32_16x16x32_bf16 v[42:45], v[78:81], v[190:193], v[42:45]
	v_mfma_f32_16x16x32_bf16 v[30:33], v[62:65], v[198:201], v[30:33]
	v_mfma_f32_16x16x32_bf16 v[26:29], v[78:81], v[198:201], v[26:29]
	v_mfma_f32_16x16x32_bf16 v[14:17], v[62:65], v[214:217], v[14:17]
	v_mfma_f32_16x16x32_bf16 v[10:13], v[78:81], v[214:217], v[10:13]
	s_setprio 0
	s_setprio 1
	v_mfma_f32_16x16x32_bf16 v[54:57], v[146:149], v[174:177], v[54:57]
	v_mfma_f32_16x16x32_bf16 v[50:53], v[154:157], v[174:177], v[50:53]
	v_mfma_f32_16x16x32_bf16 v[38:41], v[146:149], v[186:189], v[38:41]
	v_mfma_f32_16x16x32_bf16 v[34:37], v[154:157], v[186:189], v[34:37]
	v_mfma_f32_16x16x32_bf16 v[22:25], v[146:149], v[194:197], v[22:25]
	v_mfma_f32_16x16x32_bf16 v[18:21], v[154:157], v[194:197], v[18:21]
	v_mfma_f32_16x16x32_bf16 v[6:9], v[146:149], v[210:213], v[6:9]
	v_mfma_f32_16x16x32_bf16 v[2:5], v[154:157], v[210:213], v[2:5]
	v_mfma_f32_16x16x32_bf16 v[54:57], v[150:153], v[182:185], v[54:57]
	v_mfma_f32_16x16x32_bf16 v[50:53], v[170:173], v[182:185], v[50:53]
	v_mfma_f32_16x16x32_bf16 v[38:41], v[150:153], v[190:193], v[38:41]
	v_mfma_f32_16x16x32_bf16 v[34:37], v[170:173], v[190:193], v[34:37]
	v_mfma_f32_16x16x32_bf16 v[22:25], v[150:153], v[198:201], v[22:25]
	v_mfma_f32_16x16x32_bf16 v[18:21], v[170:173], v[198:201], v[18:21]
	v_mfma_f32_16x16x32_bf16 v[6:9], v[150:153], v[214:217], v[6:9]
	v_mfma_f32_16x16x32_bf16 v[2:5], v[170:173], v[214:217], v[2:5]
	s_setprio 0
	s_barrier
	s_add_u32 s77, s77, 0x100
	s_addc_u32 s79, s79, 0
	s_add_u32 s74, s74, 0x100
	s_addc_u32 s75, s75, 0
	s_cmp_ge_i32 s84, s1
	s_mov_b32 s68, s84
	s_cbranch_scc0 .LBB0_664

.Lpeelph7b_0:
	s_add_i32 s69, s58, 2
	s_add_u32 s59, s54, 0xfffc0080
	s_addc_u32 s60, s55, -1
	s_add_i32 s70, 0, 0x10000
	s_cmp_eq_u32 s53, s58
	s_cselect_b32 s61, s43, s60
	s_cselect_b32 s60, s45, s59
	v_add_u32_e32 v146, s70, v151
	s_cselect_b32 s59, s64, s68
	s_cselect_b32 s58, s65, s66
	s_add_i32 s72, 0, 0x14000
	ds_read_b128 v[142:145], v146
	ds_read_b128 v[156:159], v146 offset:1024
	ds_read_b128 v[160:163], v146 offset:2048
	ds_read_b128 v[170:173], v146 offset:3072
	v_add_u32_e32 v146, s72, v151
	ds_read_b128 v[174:177], v146
	ds_read_b128 v[178:181], v146 offset:1024
	ds_read_b128 v[182:185], v146 offset:2048
	ds_read_b128 v[186:189], v146 offset:3072
	v_lshl_add_u64 v[146:147], s[54:55], 0, v[140:141]
	s_add_i32 m0, s16, 0xc000
	ds_read_b128 v[190:193], v154
	ds_read_b128 v[194:197], v154 offset:1024
	ds_read_b128 v[198:201], v154 offset:2048
	ds_read_b128 v[202:205], v154 offset:3072
	ds_read_b128 v[206:209], v154 offset:4096
	ds_read_b128 v[210:213], v154 offset:5120
	ds_read_b128 v[214:217], v154 offset:6144
	ds_read_b128 v[218:221], v154 offset:7168
	global_load_lds_dwordx4 v[146:147], off
	v_lshl_add_u64 v[146:147], s[54:55], 0, v[138:139]
	s_add_i32 m0, s16, 0xe000
	s_nop 0
	global_load_lds_dwordx4 v[146:147], off
	s_waitcnt vmcnt(8) lgkmcnt(0)
	s_barrier
	s_setprio 1
	v_mfma_f32_16x16x32_bf16 v[126:129], v[142:145], v[190:193], 0
	v_mfma_f32_16x16x32_bf16 v[118:121], v[160:163], v[190:193], 0
	v_mfma_f32_16x16x32_bf16 v[110:113], v[142:145], v[198:201], 0
	v_mfma_f32_16x16x32_bf16 v[102:105], v[160:163], v[198:201], 0
	v_mfma_f32_16x16x32_bf16 v[94:97], v[142:145], v[206:209], 0
	v_mfma_f32_16x16x32_bf16 v[86:89], v[160:163], v[206:209], 0
	v_mfma_f32_16x16x32_bf16 v[78:81], v[142:145], v[214:217], 0
	v_mfma_f32_16x16x32_bf16 v[70:73], v[160:163], v[214:217], 0
	v_mfma_f32_16x16x32_bf16 v[126:129], v[156:159], v[194:197], v[126:129]
	v_mfma_f32_16x16x32_bf16 v[118:121], v[170:173], v[194:197], v[118:121]
	v_mfma_f32_16x16x32_bf16 v[110:113], v[156:159], v[202:205], v[110:113]
	v_mfma_f32_16x16x32_bf16 v[102:105], v[170:173], v[202:205], v[102:105]
	v_mfma_f32_16x16x32_bf16 v[94:97], v[156:159], v[210:213], v[94:97]
	v_mfma_f32_16x16x32_bf16 v[86:89], v[170:173], v[210:213], v[86:89]
	v_mfma_f32_16x16x32_bf16 v[78:81], v[156:159], v[218:221], v[78:81]
	v_mfma_f32_16x16x32_bf16 v[70:73], v[170:173], v[218:221], v[70:73]
	s_setprio 0
	s_setprio 1
	v_mfma_f32_16x16x32_bf16 v[122:125], v[174:177], v[190:193], 0
	v_mfma_f32_16x16x32_bf16 v[114:117], v[182:185], v[190:193], 0
	v_mfma_f32_16x16x32_bf16 v[106:109], v[174:177], v[198:201], 0
	v_mfma_f32_16x16x32_bf16 v[98:101], v[182:185], v[198:201], 0
	v_mfma_f32_16x16x32_bf16 v[90:93], v[174:177], v[206:209], 0
	v_mfma_f32_16x16x32_bf16 v[82:85], v[182:185], v[206:209], 0
	v_mfma_f32_16x16x32_bf16 v[74:77], v[174:177], v[214:217], 0
	v_mfma_f32_16x16x32_bf16 v[66:69], v[182:185], v[214:217], 0
	v_mfma_f32_16x16x32_bf16 v[122:125], v[178:181], v[194:197], v[122:125]
	v_mfma_f32_16x16x32_bf16 v[114:117], v[186:189], v[194:197], v[114:117]
	v_mfma_f32_16x16x32_bf16 v[106:109], v[178:181], v[202:205], v[106:109]
	v_mfma_f32_16x16x32_bf16 v[98:101], v[186:189], v[202:205], v[98:101]
	v_mfma_f32_16x16x32_bf16 v[90:93], v[178:181], v[210:213], v[90:93]
	v_mfma_f32_16x16x32_bf16 v[82:85], v[186:189], v[210:213], v[82:85]
	v_mfma_f32_16x16x32_bf16 v[74:77], v[178:181], v[218:221], v[74:77]
	v_mfma_f32_16x16x32_bf16 v[66:69], v[186:189], v[218:221], v[66:69]
	s_setprio 0
	s_barrier
	s_add_i32 s70, s70, s14
	v_lshl_add_u64 v[146:147], s[58:59], 0, v[166:167]
	s_mov_b32 m0, s70
	ds_read_b128 v[190:193], v154 offset:16384
	ds_read_b128 v[194:197], v154 offset:17408
	ds_read_b128 v[198:201], v154 offset:18432
	ds_read_b128 v[202:205], v154 offset:19456
	ds_read_b128 v[206:209], v154 offset:20480
	ds_read_b128 v[210:213], v154 offset:21504
	ds_read_b128 v[214:217], v154 offset:22528
	ds_read_b128 v[218:221], v154 offset:23552
	global_load_lds_dwordx4 v[146:147], off
	s_add_i32 m0, s70, 0x2000
	s_add_u32 s70, s58, 0x40000
	v_lshl_add_u64 v[164:165], s[58:59], 0, v[134:135]
	s_addc_u32 s71, s59, 0
	s_add_i32 s72, s72, s14
	global_load_lds_dwordx4 v[164:165], off
	v_lshl_add_u64 v[222:223], s[70:71], 0, v[166:167]
	s_mov_b32 m0, s72
	v_lshl_add_u64 v[232:233], s[60:61], 0, v[130:131]
	global_load_lds_dwordx4 v[222:223], off
	v_lshl_add_u64 v[222:223], s[70:71], 0, v[134:135]
	s_add_i32 m0, s72, 0x2000
	s_nop 0
	global_load_lds_dwordx4 v[222:223], off
	v_lshl_add_u64 v[222:223], s[60:61], 0, v[132:133]
	s_mov_b32 m0, s16
	s_nop 0
	global_load_lds_dwordx4 v[222:223], off
	s_mov_b32 m0, s20
	s_nop 0
	global_load_lds_dwordx4 v[232:233], off
	s_waitcnt vmcnt(8) lgkmcnt(0)
	s_barrier
	s_setprio 1
	v_mfma_f32_16x16x32_bf16 v[62:65], v[142:145], v[190:193], 0
	v_mfma_f32_16x16x32_bf16 v[54:57], v[160:163], v[190:193], 0
	v_mfma_f32_16x16x32_bf16 v[46:49], v[142:145], v[198:201], 0
	v_mfma_f32_16x16x32_bf16 v[38:41], v[160:163], v[198:201], 0
	v_mfma_f32_16x16x32_bf16 v[30:33], v[142:145], v[206:209], 0
	v_mfma_f32_16x16x32_bf16 v[22:25], v[160:163], v[206:209], 0
	v_mfma_f32_16x16x32_bf16 v[14:17], v[142:145], v[214:217], 0
	v_mfma_f32_16x16x32_bf16 v[6:9], v[160:163], v[214:217], 0
	v_mfma_f32_16x16x32_bf16 v[62:65], v[156:159], v[194:197], v[62:65]
	v_mfma_f32_16x16x32_bf16 v[54:57], v[170:173], v[194:197], v[54:57]
	v_mfma_f32_16x16x32_bf16 v[46:49], v[156:159], v[202:205], v[46:49]
	v_mfma_f32_16x16x32_bf16 v[38:41], v[170:173], v[202:205], v[38:41]
	v_mfma_f32_16x16x32_bf16 v[30:33], v[156:159], v[210:213], v[30:33]
	v_mfma_f32_16x16x32_bf16 v[22:25], v[170:173], v[210:213], v[22:25]
	v_mfma_f32_16x16x32_bf16 v[14:17], v[156:159], v[218:221], v[14:17]
	v_mfma_f32_16x16x32_bf16 v[6:9], v[170:173], v[218:221], v[6:9]
	s_setprio 0
	s_setprio 1
	v_mfma_f32_16x16x32_bf16 v[58:61], v[174:177], v[190:193], 0
	v_mfma_f32_16x16x32_bf16 v[50:53], v[182:185], v[190:193], 0
	v_mfma_f32_16x16x32_bf16 v[42:45], v[174:177], v[198:201], 0
	v_mfma_f32_16x16x32_bf16 v[34:37], v[182:185], v[198:201], 0
	v_mfma_f32_16x16x32_bf16 v[26:29], v[174:177], v[206:209], 0
	v_mfma_f32_16x16x32_bf16 v[18:21], v[182:185], v[206:209], 0
	v_mfma_f32_16x16x32_bf16 v[10:13], v[174:177], v[214:217], 0
	v_mfma_f32_16x16x32_bf16 v[2:5], v[182:185], v[214:217], 0
	v_mfma_f32_16x16x32_bf16 v[58:61], v[178:181], v[194:197], v[58:61]
	v_mfma_f32_16x16x32_bf16 v[50:53], v[186:189], v[194:197], v[50:53]
	v_mfma_f32_16x16x32_bf16 v[42:45], v[178:181], v[202:205], v[42:45]
	v_mfma_f32_16x16x32_bf16 v[34:37], v[186:189], v[202:205], v[34:37]
	v_mfma_f32_16x16x32_bf16 v[26:29], v[178:181], v[210:213], v[26:29]
	v_mfma_f32_16x16x32_bf16 v[18:21], v[186:189], v[210:213], v[18:21]
	v_mfma_f32_16x16x32_bf16 v[10:13], v[178:181], v[218:221], v[10:13]
	v_mfma_f32_16x16x32_bf16 v[2:5], v[186:189], v[218:221], v[2:5]
	s_setprio 0
	s_barrier
	s_add_i32 s70, 0, 0x18000
	v_add_u32_e32 v148, s70, v151
	s_add_i32 s71, 0, 0x1c000
	ds_read_b128 v[142:145], v148
	ds_read_b128 v[156:159], v148 offset:1024
	ds_read_b128 v[160:163], v148 offset:2048
	ds_read_b128 v[170:173], v148 offset:3072
	v_add_u32_e32 v148, s71, v151
	ds_read_b128 v[174:177], v148
	ds_read_b128 v[178:181], v148 offset:1024
	ds_read_b128 v[182:185], v148 offset:2048
	ds_read_b128 v[186:189], v148 offset:3072
	s_add_u32 s60, s60, 0x40000
	s_addc_u32 s61, s61, 0
	s_mov_b32 m0, s21
	v_lshl_add_u64 v[234:235], s[60:61], 0, v[132:133]
	ds_read_b128 v[190:193], v154 offset:32768
	ds_read_b128 v[194:197], v154 offset:33792
	ds_read_b128 v[198:201], v154 offset:34816
	ds_read_b128 v[202:205], v154 offset:35840
	ds_read_b128 v[206:209], v154 offset:36864
	ds_read_b128 v[210:213], v154 offset:37888
	ds_read_b128 v[214:217], v154 offset:38912
	ds_read_b128 v[218:221], v154 offset:39936
	global_load_lds_dwordx4 v[234:235], off
	v_lshl_add_u64 v[234:235], s[60:61], 0, v[130:131]
	s_mov_b32 m0, s22
	s_nop 0
	global_load_lds_dwordx4 v[234:235], off
	s_waitcnt vmcnt(8) lgkmcnt(0)
	s_barrier
	s_setprio 1
	v_mfma_f32_16x16x32_bf16 v[126:129], v[142:145], v[190:193], v[126:129]
	v_mfma_f32_16x16x32_bf16 v[118:121], v[160:163], v[190:193], v[118:121]
	v_mfma_f32_16x16x32_bf16 v[110:113], v[142:145], v[198:201], v[110:113]
	v_mfma_f32_16x16x32_bf16 v[102:105], v[160:163], v[198:201], v[102:105]
	v_mfma_f32_16x16x32_bf16 v[94:97], v[142:145], v[206:209], v[94:97]
	v_mfma_f32_16x16x32_bf16 v[86:89], v[160:163], v[206:209], v[86:89]
	v_mfma_f32_16x16x32_bf16 v[78:81], v[142:145], v[214:217], v[78:81]
	v_mfma_f32_16x16x32_bf16 v[70:73], v[160:163], v[214:217], v[70:73]
	v_mfma_f32_16x16x32_bf16 v[126:129], v[156:159], v[194:197], v[126:129]
	v_mfma_f32_16x16x32_bf16 v[118:121], v[170:173], v[194:197], v[118:121]
	v_mfma_f32_16x16x32_bf16 v[110:113], v[156:159], v[202:205], v[110:113]
	v_mfma_f32_16x16x32_bf16 v[102:105], v[170:173], v[202:205], v[102:105]
	v_mfma_f32_16x16x32_bf16 v[94:97], v[156:159], v[210:213], v[94:97]
	v_mfma_f32_16x16x32_bf16 v[86:89], v[170:173], v[210:213], v[86:89]
	v_mfma_f32_16x16x32_bf16 v[78:81], v[156:159], v[218:221], v[78:81]
	v_mfma_f32_16x16x32_bf16 v[70:73], v[170:173], v[218:221], v[70:73]
	s_setprio 0
	s_setprio 1
	v_mfma_f32_16x16x32_bf16 v[122:125], v[174:177], v[190:193], v[122:125]
	v_mfma_f32_16x16x32_bf16 v[114:117], v[182:185], v[190:193], v[114:117]
	v_mfma_f32_16x16x32_bf16 v[106:109], v[174:177], v[198:201], v[106:109]
	v_mfma_f32_16x16x32_bf16 v[98:101], v[182:185], v[198:201], v[98:101]
	v_mfma_f32_16x16x32_bf16 v[90:93], v[174:177], v[206:209], v[90:93]
	v_mfma_f32_16x16x32_bf16 v[82:85], v[182:185], v[206:209], v[82:85]
	v_mfma_f32_16x16x32_bf16 v[74:77], v[174:177], v[214:217], v[74:77]
	v_mfma_f32_16x16x32_bf16 v[66:69], v[182:185], v[214:217], v[66:69]
	v_mfma_f32_16x16x32_bf16 v[122:125], v[178:181], v[194:197], v[122:125]
	v_mfma_f32_16x16x32_bf16 v[114:117], v[186:189], v[194:197], v[114:117]
	v_mfma_f32_16x16x32_bf16 v[106:109], v[178:181], v[202:205], v[106:109]
	v_mfma_f32_16x16x32_bf16 v[98:101], v[186:189], v[202:205], v[98:101]
	v_mfma_f32_16x16x32_bf16 v[90:93], v[178:181], v[210:213], v[90:93]
	v_mfma_f32_16x16x32_bf16 v[82:85], v[186:189], v[210:213], v[82:85]
	v_mfma_f32_16x16x32_bf16 v[74:77], v[178:181], v[218:221], v[74:77]
	v_mfma_f32_16x16x32_bf16 v[66:69], v[186:189], v[218:221], v[66:69]
	s_setprio 0
	s_barrier
	s_add_i32 s60, s70, s14
	v_lshl_add_u64 v[146:147], v[146:147], 0, s[56:57]
	s_mov_b32 m0, s60
	ds_read_b128 v[190:193], v154 offset:49152
	ds_read_b128 v[194:197], v154 offset:50176
	ds_read_b128 v[198:201], v154 offset:51200
	ds_read_b128 v[202:205], v154 offset:52224
	ds_read_b128 v[206:209], v154 offset:53248
	ds_read_b128 v[210:213], v154 offset:54272
	ds_read_b128 v[214:217], v154 offset:55296
	ds_read_b128 v[218:221], v154 offset:56320
	global_load_lds_dwordx4 v[146:147], off
	s_add_i32 m0, s60, 0x2000
	s_add_u32 s58, s58, 0x40080
	v_lshl_add_u64 v[146:147], v[164:165], 0, s[56:57]
	s_addc_u32 s59, s59, 0
	s_add_i32 s60, s71, s14
	global_load_lds_dwordx4 v[146:147], off
	v_lshl_add_u64 v[146:147], s[58:59], 0, v[166:167]
	s_mov_b32 m0, s60
	s_nop 0
	global_load_lds_dwordx4 v[146:147], off
	v_lshl_add_u64 v[146:147], s[58:59], 0, v[134:135]
	s_add_i32 m0, s60, 0x2000
	s_nop 0
	global_load_lds_dwordx4 v[146:147], off
	v_lshl_add_u64 v[146:147], v[222:223], 0, s[56:57]
	s_mov_b32 m0, s23
	s_nop 0
	global_load_lds_dwordx4 v[146:147], off
	v_lshl_add_u64 v[146:147], v[232:233], 0, s[56:57]
	s_mov_b32 m0, s24
	s_nop 0
	global_load_lds_dwordx4 v[146:147], off
	s_waitcnt vmcnt(8) lgkmcnt(0)
	s_barrier
	s_setprio 1
	v_mfma_f32_16x16x32_bf16 v[62:65], v[142:145], v[190:193], v[62:65]
	v_mfma_f32_16x16x32_bf16 v[54:57], v[160:163], v[190:193], v[54:57]
	v_mfma_f32_16x16x32_bf16 v[46:49], v[142:145], v[198:201], v[46:49]
	v_mfma_f32_16x16x32_bf16 v[38:41], v[160:163], v[198:201], v[38:41]
	v_mfma_f32_16x16x32_bf16 v[30:33], v[142:145], v[206:209], v[30:33]
	v_mfma_f32_16x16x32_bf16 v[22:25], v[160:163], v[206:209], v[22:25]
	v_mfma_f32_16x16x32_bf16 v[14:17], v[142:145], v[214:217], v[14:17]
	v_mfma_f32_16x16x32_bf16 v[6:9], v[160:163], v[214:217], v[6:9]
	v_mfma_f32_16x16x32_bf16 v[62:65], v[156:159], v[194:197], v[62:65]
	v_mfma_f32_16x16x32_bf16 v[54:57], v[170:173], v[194:197], v[54:57]
	v_mfma_f32_16x16x32_bf16 v[46:49], v[156:159], v[202:205], v[46:49]
	v_mfma_f32_16x16x32_bf16 v[38:41], v[170:173], v[202:205], v[38:41]
	v_mfma_f32_16x16x32_bf16 v[30:33], v[156:159], v[210:213], v[30:33]
	v_mfma_f32_16x16x32_bf16 v[22:25], v[170:173], v[210:213], v[22:25]
	v_mfma_f32_16x16x32_bf16 v[14:17], v[156:159], v[218:221], v[14:17]
	v_mfma_f32_16x16x32_bf16 v[6:9], v[170:173], v[218:221], v[6:9]
	s_setprio 0
	s_setprio 1
	v_mfma_f32_16x16x32_bf16 v[58:61], v[174:177], v[190:193], v[58:61]
	v_mfma_f32_16x16x32_bf16 v[50:53], v[182:185], v[190:193], v[50:53]
	v_mfma_f32_16x16x32_bf16 v[42:45], v[174:177], v[198:201], v[42:45]
	v_mfma_f32_16x16x32_bf16 v[34:37], v[182:185], v[198:201], v[34:37]
	v_mfma_f32_16x16x32_bf16 v[26:29], v[174:177], v[206:209], v[26:29]
	v_mfma_f32_16x16x32_bf16 v[18:21], v[182:185], v[206:209], v[18:21]
	v_mfma_f32_16x16x32_bf16 v[10:13], v[174:177], v[214:217], v[10:13]
	v_mfma_f32_16x16x32_bf16 v[2:5], v[182:185], v[214:217], v[2:5]
	v_mfma_f32_16x16x32_bf16 v[58:61], v[178:181], v[194:197], v[58:61]
	v_mfma_f32_16x16x32_bf16 v[50:53], v[186:189], v[194:197], v[50:53]
	v_mfma_f32_16x16x32_bf16 v[42:45], v[178:181], v[202:205], v[42:45]
	v_mfma_f32_16x16x32_bf16 v[34:37], v[186:189], v[202:205], v[34:37]
	v_mfma_f32_16x16x32_bf16 v[26:29], v[178:181], v[210:213], v[26:29]
	v_mfma_f32_16x16x32_bf16 v[18:21], v[186:189], v[210:213], v[18:21]
	v_mfma_f32_16x16x32_bf16 v[10:13], v[178:181], v[218:221], v[10:13]
	v_mfma_f32_16x16x32_bf16 v[2:5], v[186:189], v[218:221], v[2:5]
	s_setprio 0
	s_barrier
	s_add_u32 s66, s66, 0x100
	s_addc_u32 s68, s68, 0
	s_add_u32 s54, s54, 0x100
	s_addc_u32 s55, s55, 0
	s_cmp_ge_i32 s69, s13
	s_mov_b32 s58, s69
	s_cbranch_scc0 .LBB0_817
	s_branch .Lpeelexitph7b
.LBB0_817:
	s_add_i32 s69, s58, 2
	s_add_u32 s59, s54, 0xfffc0080
	s_addc_u32 s60, s55, -1
	s_add_i32 s70, 0, 0x10000
	s_cmp_eq_u32 s53, s58
	s_cselect_b32 s61, s43, s60
	s_cselect_b32 s60, s45, s59
	v_add_u32_e32 v146, s70, v151
	s_cselect_b32 s59, s64, s68
	s_cselect_b32 s58, s65, s66
	s_add_i32 s72, 0, 0x14000
	ds_read_b128 v[142:145], v146
	ds_read_b128 v[156:159], v146 offset:1024
	ds_read_b128 v[160:163], v146 offset:2048
	ds_read_b128 v[170:173], v146 offset:3072
	v_add_u32_e32 v146, s72, v151
	ds_read_b128 v[174:177], v146
	ds_read_b128 v[178:181], v146 offset:1024
	ds_read_b128 v[182:185], v146 offset:2048
	ds_read_b128 v[186:189], v146 offset:3072
	v_lshl_add_u64 v[146:147], s[54:55], 0, v[140:141]
	s_add_i32 m0, s16, 0xc000
	ds_read_b128 v[190:193], v154
	ds_read_b128 v[194:197], v154 offset:1024
	ds_read_b128 v[198:201], v154 offset:2048
	ds_read_b128 v[202:205], v154 offset:3072
	ds_read_b128 v[206:209], v154 offset:4096
	ds_read_b128 v[210:213], v154 offset:5120
	ds_read_b128 v[214:217], v154 offset:6144
	ds_read_b128 v[218:221], v154 offset:7168
	global_load_lds_dwordx4 v[146:147], off
	v_lshl_add_u64 v[146:147], s[54:55], 0, v[138:139]
	s_add_i32 m0, s16, 0xe000
	s_nop 0
	global_load_lds_dwordx4 v[146:147], off
	s_waitcnt vmcnt(8) lgkmcnt(0)
	s_barrier
	s_setprio 1
	v_mfma_f32_16x16x32_bf16 v[126:129], v[142:145], v[190:193], v[126:129]
	v_mfma_f32_16x16x32_bf16 v[118:121], v[160:163], v[190:193], v[118:121]
	v_mfma_f32_16x16x32_bf16 v[110:113], v[142:145], v[198:201], v[110:113]
	v_mfma_f32_16x16x32_bf16 v[102:105], v[160:163], v[198:201], v[102:105]
	v_mfma_f32_16x16x32_bf16 v[94:97], v[142:145], v[206:209], v[94:97]
	v_mfma_f32_16x16x32_bf16 v[86:89], v[160:163], v[206:209], v[86:89]
	v_mfma_f32_16x16x32_bf16 v[78:81], v[142:145], v[214:217], v[78:81]
	v_mfma_f32_16x16x32_bf16 v[70:73], v[160:163], v[214:217], v[70:73]
	v_mfma_f32_16x16x32_bf16 v[126:129], v[156:159], v[194:197], v[126:129]
	v_mfma_f32_16x16x32_bf16 v[118:121], v[170:173], v[194:197], v[118:121]
	v_mfma_f32_16x16x32_bf16 v[110:113], v[156:159], v[202:205], v[110:113]
	v_mfma_f32_16x16x32_bf16 v[102:105], v[170:173], v[202:205], v[102:105]
	v_mfma_f32_16x16x32_bf16 v[94:97], v[156:159], v[210:213], v[94:97]
	v_mfma_f32_16x16x32_bf16 v[86:89], v[170:173], v[210:213], v[86:89]
	v_mfma_f32_16x16x32_bf16 v[78:81], v[156:159], v[218:221], v[78:81]
	v_mfma_f32_16x16x32_bf16 v[70:73], v[170:173], v[218:221], v[70:73]
	s_setprio 0
	s_setprio 1
	v_mfma_f32_16x16x32_bf16 v[122:125], v[174:177], v[190:193], v[122:125]
	v_mfma_f32_16x16x32_bf16 v[114:117], v[182:185], v[190:193], v[114:117]
	v_mfma_f32_16x16x32_bf16 v[106:109], v[174:177], v[198:201], v[106:109]
	v_mfma_f32_16x16x32_bf16 v[98:101], v[182:185], v[198:201], v[98:101]
	v_mfma_f32_16x16x32_bf16 v[90:93], v[174:177], v[206:209], v[90:93]
	v_mfma_f32_16x16x32_bf16 v[82:85], v[182:185], v[206:209], v[82:85]
	v_mfma_f32_16x16x32_bf16 v[74:77], v[174:177], v[214:217], v[74:77]
	v_mfma_f32_16x16x32_bf16 v[66:69], v[182:185], v[214:217], v[66:69]
	v_mfma_f32_16x16x32_bf16 v[122:125], v[178:181], v[194:197], v[122:125]
	v_mfma_f32_16x16x32_bf16 v[114:117], v[186:189], v[194:197], v[114:117]
	v_mfma_f32_16x16x32_bf16 v[106:109], v[178:181], v[202:205], v[106:109]
	v_mfma_f32_16x16x32_bf16 v[98:101], v[186:189], v[202:205], v[98:101]
	v_mfma_f32_16x16x32_bf16 v[90:93], v[178:181], v[210:213], v[90:93]
	v_mfma_f32_16x16x32_bf16 v[82:85], v[186:189], v[210:213], v[82:85]
	v_mfma_f32_16x16x32_bf16 v[74:77], v[178:181], v[218:221], v[74:77]
	v_mfma_f32_16x16x32_bf16 v[66:69], v[186:189], v[218:221], v[66:69]
	s_setprio 0
	s_barrier
	s_add_i32 s70, s70, s14
	v_lshl_add_u64 v[146:147], s[58:59], 0, v[166:167]
	s_mov_b32 m0, s70
	ds_read_b128 v[190:193], v154 offset:16384
	ds_read_b128 v[194:197], v154 offset:17408
	ds_read_b128 v[198:201], v154 offset:18432
	ds_read_b128 v[202:205], v154 offset:19456
	ds_read_b128 v[206:209], v154 offset:20480
	ds_read_b128 v[210:213], v154 offset:21504
	ds_read_b128 v[214:217], v154 offset:22528
	ds_read_b128 v[218:221], v154 offset:23552
	global_load_lds_dwordx4 v[146:147], off
	s_add_i32 m0, s70, 0x2000
	s_add_u32 s70, s58, 0x40000
	v_lshl_add_u64 v[164:165], s[58:59], 0, v[134:135]
	s_addc_u32 s71, s59, 0
	s_add_i32 s72, s72, s14
	global_load_lds_dwordx4 v[164:165], off
	v_lshl_add_u64 v[222:223], s[70:71], 0, v[166:167]
	s_mov_b32 m0, s72
	v_lshl_add_u64 v[232:233], s[60:61], 0, v[130:131]
	global_load_lds_dwordx4 v[222:223], off
	v_lshl_add_u64 v[222:223], s[70:71], 0, v[134:135]
	s_add_i32 m0, s72, 0x2000
	s_nop 0
	global_load_lds_dwordx4 v[222:223], off
	v_lshl_add_u64 v[222:223], s[60:61], 0, v[132:133]
	s_mov_b32 m0, s16
	s_nop 0
	global_load_lds_dwordx4 v[222:223], off
	s_mov_b32 m0, s20
	s_nop 0
	global_load_lds_dwordx4 v[232:233], off
	s_waitcnt vmcnt(8) lgkmcnt(0)
	s_barrier
	s_setprio 1
	v_mfma_f32_16x16x32_bf16 v[62:65], v[142:145], v[190:193], v[62:65]
	v_mfma_f32_16x16x32_bf16 v[54:57], v[160:163], v[190:193], v[54:57]
	v_mfma_f32_16x16x32_bf16 v[46:49], v[142:145], v[198:201], v[46:49]
	v_mfma_f32_16x16x32_bf16 v[38:41], v[160:163], v[198:201], v[38:41]
	v_mfma_f32_16x16x32_bf16 v[30:33], v[142:145], v[206:209], v[30:33]
	v_mfma_f32_16x16x32_bf16 v[22:25], v[160:163], v[206:209], v[22:25]
	v_mfma_f32_16x16x32_bf16 v[14:17], v[142:145], v[214:217], v[14:17]
	v_mfma_f32_16x16x32_bf16 v[6:9], v[160:163], v[214:217], v[6:9]
	v_mfma_f32_16x16x32_bf16 v[62:65], v[156:159], v[194:197], v[62:65]
	v_mfma_f32_16x16x32_bf16 v[54:57], v[170:173], v[194:197], v[54:57]
	v_mfma_f32_16x16x32_bf16 v[46:49], v[156:159], v[202:205], v[46:49]
	v_mfma_f32_16x16x32_bf16 v[38:41], v[170:173], v[202:205], v[38:41]
	v_mfma_f32_16x16x32_bf16 v[30:33], v[156:159], v[210:213], v[30:33]
	v_mfma_f32_16x16x32_bf16 v[22:25], v[170:173], v[210:213], v[22:25]
	v_mfma_f32_16x16x32_bf16 v[14:17], v[156:159], v[218:221], v[14:17]
	v_mfma_f32_16x16x32_bf16 v[6:9], v[170:173], v[218:221], v[6:9]
	s_setprio 0
	s_setprio 1
	v_mfma_f32_16x16x32_bf16 v[58:61], v[174:177], v[190:193], v[58:61]
	v_mfma_f32_16x16x32_bf16 v[50:53], v[182:185], v[190:193], v[50:53]
	v_mfma_f32_16x16x32_bf16 v[42:45], v[174:177], v[198:201], v[42:45]
	v_mfma_f32_16x16x32_bf16 v[34:37], v[182:185], v[198:201], v[34:37]
	v_mfma_f32_16x16x32_bf16 v[26:29], v[174:177], v[206:209], v[26:29]
	v_mfma_f32_16x16x32_bf16 v[18:21], v[182:185], v[206:209], v[18:21]
	v_mfma_f32_16x16x32_bf16 v[10:13], v[174:177], v[214:217], v[10:13]
	v_mfma_f32_16x16x32_bf16 v[2:5], v[182:185], v[214:217], v[2:5]
	v_mfma_f32_16x16x32_bf16 v[58:61], v[178:181], v[194:197], v[58:61]
	v_mfma_f32_16x16x32_bf16 v[50:53], v[186:189], v[194:197], v[50:53]
	v_mfma_f32_16x16x32_bf16 v[42:45], v[178:181], v[202:205], v[42:45]
	v_mfma_f32_16x16x32_bf16 v[34:37], v[186:189], v[202:205], v[34:37]
	v_mfma_f32_16x16x32_bf16 v[26:29], v[178:181], v[210:213], v[26:29]
	v_mfma_f32_16x16x32_bf16 v[18:21], v[186:189], v[210:213], v[18:21]
	v_mfma_f32_16x16x32_bf16 v[10:13], v[178:181], v[218:221], v[10:13]
	v_mfma_f32_16x16x32_bf16 v[2:5], v[186:189], v[218:221], v[2:5]
	s_setprio 0
	s_barrier
	s_add_i32 s70, 0, 0x18000
	v_add_u32_e32 v148, s70, v151
	s_add_i32 s71, 0, 0x1c000
	ds_read_b128 v[142:145], v148
	ds_read_b128 v[156:159], v148 offset:1024
	ds_read_b128 v[160:163], v148 offset:2048
	ds_read_b128 v[170:173], v148 offset:3072
	v_add_u32_e32 v148, s71, v151
	ds_read_b128 v[174:177], v148
	ds_read_b128 v[178:181], v148 offset:1024
	ds_read_b128 v[182:185], v148 offset:2048
	ds_read_b128 v[186:189], v148 offset:3072
	s_add_u32 s60, s60, 0x40000
	s_addc_u32 s61, s61, 0
	s_mov_b32 m0, s21
	v_lshl_add_u64 v[234:235], s[60:61], 0, v[132:133]
	ds_read_b128 v[190:193], v154 offset:32768
	ds_read_b128 v[194:197], v154 offset:33792
	ds_read_b128 v[198:201], v154 offset:34816
	ds_read_b128 v[202:205], v154 offset:35840
	ds_read_b128 v[206:209], v154 offset:36864
	ds_read_b128 v[210:213], v154 offset:37888
	ds_read_b128 v[214:217], v154 offset:38912
	ds_read_b128 v[218:221], v154 offset:39936
	global_load_lds_dwordx4 v[234:235], off
	v_lshl_add_u64 v[234:235], s[60:61], 0, v[130:131]
	s_mov_b32 m0, s22
	s_nop 0
	global_load_lds_dwordx4 v[234:235], off
	s_waitcnt vmcnt(8) lgkmcnt(0)
	s_barrier
	s_setprio 1
	v_mfma_f32_16x16x32_bf16 v[126:129], v[142:145], v[190:193], v[126:129]
	v_mfma_f32_16x16x32_bf16 v[118:121], v[160:163], v[190:193], v[118:121]
	v_mfma_f32_16x16x32_bf16 v[110:113], v[142:145], v[198:201], v[110:113]
	v_mfma_f32_16x16x32_bf16 v[102:105], v[160:163], v[198:201], v[102:105]
	v_mfma_f32_16x16x32_bf16 v[94:97], v[142:145], v[206:209], v[94:97]
	v_mfma_f32_16x16x32_bf16 v[86:89], v[160:163], v[206:209], v[86:89]
	v_mfma_f32_16x16x32_bf16 v[78:81], v[142:145], v[214:217], v[78:81]
	v_mfma_f32_16x16x32_bf16 v[70:73], v[160:163], v[214:217], v[70:73]
	v_mfma_f32_16x16x32_bf16 v[126:129], v[156:159], v[194:197], v[126:129]
	v_mfma_f32_16x16x32_bf16 v[118:121], v[170:173], v[194:197], v[118:121]
	v_mfma_f32_16x16x32_bf16 v[110:113], v[156:159], v[202:205], v[110:113]
	v_mfma_f32_16x16x32_bf16 v[102:105], v[170:173], v[202:205], v[102:105]
	v_mfma_f32_16x16x32_bf16 v[94:97], v[156:159], v[210:213], v[94:97]
	v_mfma_f32_16x16x32_bf16 v[86:89], v[170:173], v[210:213], v[86:89]
	v_mfma_f32_16x16x32_bf16 v[78:81], v[156:159], v[218:221], v[78:81]
	v_mfma_f32_16x16x32_bf16 v[70:73], v[170:173], v[218:221], v[70:73]
	s_setprio 0
	s_setprio 1
	v_mfma_f32_16x16x32_bf16 v[122:125], v[174:177], v[190:193], v[122:125]
	v_mfma_f32_16x16x32_bf16 v[114:117], v[182:185], v[190:193], v[114:117]
	v_mfma_f32_16x16x32_bf16 v[106:109], v[174:177], v[198:201], v[106:109]
	v_mfma_f32_16x16x32_bf16 v[98:101], v[182:185], v[198:201], v[98:101]
	v_mfma_f32_16x16x32_bf16 v[90:93], v[174:177], v[206:209], v[90:93]
	v_mfma_f32_16x16x32_bf16 v[82:85], v[182:185], v[206:209], v[82:85]
	v_mfma_f32_16x16x32_bf16 v[74:77], v[174:177], v[214:217], v[74:77]
	v_mfma_f32_16x16x32_bf16 v[66:69], v[182:185], v[214:217], v[66:69]
	v_mfma_f32_16x16x32_bf16 v[122:125], v[178:181], v[194:197], v[122:125]
	v_mfma_f32_16x16x32_bf16 v[114:117], v[186:189], v[194:197], v[114:117]
	v_mfma_f32_16x16x32_bf16 v[106:109], v[178:181], v[202:205], v[106:109]
	v_mfma_f32_16x16x32_bf16 v[98:101], v[186:189], v[202:205], v[98:101]
	v_mfma_f32_16x16x32_bf16 v[90:93], v[178:181], v[210:213], v[90:93]
	v_mfma_f32_16x16x32_bf16 v[82:85], v[186:189], v[210:213], v[82:85]
	v_mfma_f32_16x16x32_bf16 v[74:77], v[178:181], v[218:221], v[74:77]
	v_mfma_f32_16x16x32_bf16 v[66:69], v[186:189], v[218:221], v[66:69]
	s_setprio 0
	s_barrier
	s_add_i32 s60, s70, s14
	v_lshl_add_u64 v[146:147], v[146:147], 0, s[56:57]
	s_mov_b32 m0, s60
	ds_read_b128 v[190:193], v154 offset:49152
	ds_read_b128 v[194:197], v154 offset:50176
	ds_read_b128 v[198:201], v154 offset:51200
	ds_read_b128 v[202:205], v154 offset:52224
	ds_read_b128 v[206:209], v154 offset:53248
	ds_read_b128 v[210:213], v154 offset:54272
	ds_read_b128 v[214:217], v154 offset:55296
	ds_read_b128 v[218:221], v154 offset:56320
	global_load_lds_dwordx4 v[146:147], off
	s_add_i32 m0, s60, 0x2000
	s_add_u32 s58, s58, 0x40080
	v_lshl_add_u64 v[146:147], v[164:165], 0, s[56:57]
	s_addc_u32 s59, s59, 0
	s_add_i32 s60, s71, s14
	global_load_lds_dwordx4 v[146:147], off
	v_lshl_add_u64 v[146:147], s[58:59], 0, v[166:167]
	s_mov_b32 m0, s60
	s_nop 0
	global_load_lds_dwordx4 v[146:147], off
	v_lshl_add_u64 v[146:147], s[58:59], 0, v[134:135]
	s_add_i32 m0, s60, 0x2000
	s_nop 0
	global_load_lds_dwordx4 v[146:147], off
	v_lshl_add_u64 v[146:147], v[222:223], 0, s[56:57]
	s_mov_b32 m0, s23
	s_nop 0
	global_load_lds_dwordx4 v[146:147], off
	v_lshl_add_u64 v[146:147], v[232:233], 0, s[56:57]
	s_mov_b32 m0, s24
	s_nop 0
	global_load_lds_dwordx4 v[146:147], off
	s_waitcnt vmcnt(8) lgkmcnt(0)
	s_barrier
	s_setprio 1
	v_mfma_f32_16x16x32_bf16 v[62:65], v[142:145], v[190:193], v[62:65]
	v_mfma_f32_16x16x32_bf16 v[54:57], v[160:163], v[190:193], v[54:57]
	v_mfma_f32_16x16x32_bf16 v[46:49], v[142:145], v[198:201], v[46:49]
	v_mfma_f32_16x16x32_bf16 v[38:41], v[160:163], v[198:201], v[38:41]
	v_mfma_f32_16x16x32_bf16 v[30:33], v[142:145], v[206:209], v[30:33]
	v_mfma_f32_16x16x32_bf16 v[22:25], v[160:163], v[206:209], v[22:25]
	v_mfma_f32_16x16x32_bf16 v[14:17], v[142:145], v[214:217], v[14:17]
	v_mfma_f32_16x16x32_bf16 v[6:9], v[160:163], v[214:217], v[6:9]
	v_mfma_f32_16x16x32_bf16 v[62:65], v[156:159], v[194:197], v[62:65]
	v_mfma_f32_16x16x32_bf16 v[54:57], v[170:173], v[194:197], v[54:57]
	v_mfma_f32_16x16x32_bf16 v[46:49], v[156:159], v[202:205], v[46:49]
	v_mfma_f32_16x16x32_bf16 v[38:41], v[170:173], v[202:205], v[38:41]
	v_mfma_f32_16x16x32_bf16 v[30:33], v[156:159], v[210:213], v[30:33]
	v_mfma_f32_16x16x32_bf16 v[22:25], v[170:173], v[210:213], v[22:25]
	v_mfma_f32_16x16x32_bf16 v[14:17], v[156:159], v[218:221], v[14:17]
	v_mfma_f32_16x16x32_bf16 v[6:9], v[170:173], v[218:221], v[6:9]
	s_setprio 0
	s_setprio 1
	v_mfma_f32_16x16x32_bf16 v[58:61], v[174:177], v[190:193], v[58:61]
	v_mfma_f32_16x16x32_bf16 v[50:53], v[182:185], v[190:193], v[50:53]
	v_mfma_f32_16x16x32_bf16 v[42:45], v[174:177], v[198:201], v[42:45]
	v_mfma_f32_16x16x32_bf16 v[34:37], v[182:185], v[198:201], v[34:37]
	v_mfma_f32_16x16x32_bf16 v[26:29], v[174:177], v[206:209], v[26:29]
	v_mfma_f32_16x16x32_bf16 v[18:21], v[182:185], v[206:209], v[18:21]
	v_mfma_f32_16x16x32_bf16 v[10:13], v[174:177], v[214:217], v[10:13]
	v_mfma_f32_16x16x32_bf16 v[2:5], v[182:185], v[214:217], v[2:5]
	v_mfma_f32_16x16x32_bf16 v[58:61], v[178:181], v[194:197], v[58:61]
	v_mfma_f32_16x16x32_bf16 v[50:53], v[186:189], v[194:197], v[50:53]
	v_mfma_f32_16x16x32_bf16 v[42:45], v[178:181], v[202:205], v[42:45]
	v_mfma_f32_16x16x32_bf16 v[34:37], v[186:189], v[202:205], v[34:37]
	v_mfma_f32_16x16x32_bf16 v[26:29], v[178:181], v[210:213], v[26:29]
	v_mfma_f32_16x16x32_bf16 v[18:21], v[186:189], v[210:213], v[18:21]
	v_mfma_f32_16x16x32_bf16 v[10:13], v[178:181], v[218:221], v[10:13]
	v_mfma_f32_16x16x32_bf16 v[2:5], v[186:189], v[218:221], v[2:5]
	s_setprio 0
	s_barrier
	s_add_u32 s66, s66, 0x100
	s_addc_u32 s68, s68, 0
	s_add_u32 s54, s54, 0x100
	s_addc_u32 s55, s55, 0
	s_cmp_ge_i32 s69, s13
	s_mov_b32 s58, s69
	s_cbranch_scc0 .LBB0_817

.Lpeelph7f_0:
	s_add_i32 s66, s54, 2
	s_add_u32 s55, s52, 0xfffe0080
	s_addc_u32 s58, s53, -1
	s_add_i32 s68, 0, 0x10000
	s_cmp_eq_u32 s51, s54
	s_cselect_b32 s59, s41, s58
	s_cselect_b32 s58, s43, s55
	s_cselect_b32 s55, s62, s65
	s_cselect_b32 s54, s63, s64
	s_add_i32 s69, 0, 0x14000
	v_add_u32_e32 v2, s68, v196
	v_add_u32_e32 v6, s69, v196
	ds_read_b128 v[26:29], v2
	ds_read_b128 v[30:33], v2 offset:1024
	ds_read_b128 v[18:21], v2 offset:2048
	ds_read_b128 v[22:25], v2 offset:3072
	ds_read_b128 v[10:13], v6
	ds_read_b128 v[14:17], v6 offset:1024
	ds_read_b128 v[2:5], v6 offset:2048
	ds_read_b128 v[6:9], v6 offset:3072
	v_lshl_add_u64 v[170:171], s[52:53], 0, v[184:185]
	s_add_i32 m0, s16, 0xc000
	ds_read_b128 v[186:189], v198
	ds_read_b128 v[190:193], v198 offset:1024
	ds_read_b128 v[200:203], v198 offset:2048
	ds_read_b128 v[204:207], v198 offset:3072
	ds_read_b128 v[208:211], v198 offset:4096
	ds_read_b128 v[212:215], v198 offset:5120
	ds_read_b128 v[216:219], v198 offset:6144
	ds_read_b128 v[220:223], v198 offset:7168
	global_load_lds_dwordx4 v[170:171], off
	v_lshl_add_u64 v[170:171], s[52:53], 0, v[182:183]
	s_add_i32 m0, s16, 0xe000
	s_nop 0
	global_load_lds_dwordx4 v[170:171], off
	s_waitcnt vmcnt(8) lgkmcnt(0)
	s_barrier
	s_setprio 1
	v_mfma_scale_f32_16x16x128_f8f6f4 v[158:161], v[26:33], v[186:193], 0, v194, v169 op_sel_hi:[0,0,0]
	v_mfma_scale_f32_16x16x128_f8f6f4 v[150:153], v[18:25], v[186:193], 0, v194, v169 op_sel_hi:[0,0,0]
	v_mfma_scale_f32_16x16x128_f8f6f4 v[142:145], v[26:33], v[200:207], 0, v194, v169 op_sel_hi:[0,0,0]
	v_mfma_scale_f32_16x16x128_f8f6f4 v[134:137], v[18:25], v[200:207], 0, v194, v169 op_sel_hi:[0,0,0]
	v_mfma_scale_f32_16x16x128_f8f6f4 v[126:129], v[26:33], v[208:215], 0, v194, v169 op_sel_hi:[0,0,0]
	v_mfma_scale_f32_16x16x128_f8f6f4 v[118:121], v[18:25], v[208:215], 0, v194, v169 op_sel_hi:[0,0,0]
	v_mfma_scale_f32_16x16x128_f8f6f4 v[110:113], v[26:33], v[216:223], 0, v194, v169 op_sel_hi:[0,0,0]
	v_mfma_scale_f32_16x16x128_f8f6f4 v[102:105], v[18:25], v[216:223], 0, v194, v169 op_sel_hi:[0,0,0]
	s_setprio 0
	s_setprio 1
	v_mfma_scale_f32_16x16x128_f8f6f4 v[154:157], v[10:17], v[186:193], 0, v194, v169 op_sel_hi:[0,0,0]
	v_mfma_scale_f32_16x16x128_f8f6f4 v[146:149], v[2:9], v[186:193], 0, v194, v169 op_sel_hi:[0,0,0]
	v_mfma_scale_f32_16x16x128_f8f6f4 v[138:141], v[10:17], v[200:207], 0, v194, v169 op_sel_hi:[0,0,0]
	v_mfma_scale_f32_16x16x128_f8f6f4 v[130:133], v[2:9], v[200:207], 0, v194, v169 op_sel_hi:[0,0,0]
	v_mfma_scale_f32_16x16x128_f8f6f4 v[122:125], v[10:17], v[208:215], 0, v194, v169 op_sel_hi:[0,0,0]
	v_mfma_scale_f32_16x16x128_f8f6f4 v[114:117], v[2:9], v[208:215], 0, v194, v169 op_sel_hi:[0,0,0]
	v_mfma_scale_f32_16x16x128_f8f6f4 v[106:109], v[10:17], v[216:223], 0, v194, v169 op_sel_hi:[0,0,0]
	v_mfma_scale_f32_16x16x128_f8f6f4 v[98:101], v[2:9], v[216:223], 0, v194, v169 op_sel_hi:[0,0,0]
	s_setprio 0
	s_barrier
	s_add_i32 s68, s68, s14
	v_lshl_add_u64 v[186:187], s[54:55], 0, v[166:167]
	s_mov_b32 m0, s68
	ds_read_b128 v[200:203], v198 offset:16384
	ds_read_b128 v[204:207], v198 offset:17408
	ds_read_b128 v[208:211], v198 offset:18432
	ds_read_b128 v[212:215], v198 offset:19456
	ds_read_b128 v[216:219], v198 offset:20480
	ds_read_b128 v[220:223], v198 offset:21504
	ds_read_b128 v[236:239], v198 offset:22528
	ds_read_b128 v[240:243], v198 offset:23552
	global_load_lds_dwordx4 v[186:187], off
	s_add_i32 m0, s68, 0x2000
	s_add_u32 s70, s54, 0x20000
	v_lshl_add_u64 v[188:189], s[54:55], 0, v[178:179]
	s_addc_u32 s71, s55, 0
	s_add_i32 s68, s69, s14
	global_load_lds_dwordx4 v[188:189], off
	v_lshl_add_u64 v[170:171], s[70:71], 0, v[166:167]
	s_mov_b32 m0, s68
	v_lshl_add_u64 v[190:191], s[58:59], 0, v[164:165]
	global_load_lds_dwordx4 v[170:171], off
	v_lshl_add_u64 v[170:171], s[70:71], 0, v[178:179]
	s_add_i32 m0, s68, 0x2000
	v_lshl_add_u64 v[192:193], s[58:59], 0, v[162:163]
	global_load_lds_dwordx4 v[170:171], off
	s_mov_b32 m0, s16
	s_nop 0
	global_load_lds_dwordx4 v[190:191], off
	s_mov_b32 m0, s20
	s_nop 0
	global_load_lds_dwordx4 v[192:193], off
	s_waitcnt vmcnt(8) lgkmcnt(0)
	s_barrier
	s_setprio 1
	v_mfma_scale_f32_16x16x128_f8f6f4 v[94:97], v[26:33], v[200:207], 0, v194, v169 op_sel_hi:[0,0,0]
	v_mfma_scale_f32_16x16x128_f8f6f4 v[86:89], v[18:25], v[200:207], 0, v194, v169 op_sel_hi:[0,0,0]
	v_mfma_scale_f32_16x16x128_f8f6f4 v[78:81], v[26:33], v[208:215], 0, v194, v169 op_sel_hi:[0,0,0]
	v_mfma_scale_f32_16x16x128_f8f6f4 v[70:73], v[18:25], v[208:215], 0, v194, v169 op_sel_hi:[0,0,0]
	v_mfma_scale_f32_16x16x128_f8f6f4 v[62:65], v[26:33], v[216:223], 0, v194, v169 op_sel_hi:[0,0,0]
	v_mfma_scale_f32_16x16x128_f8f6f4 v[54:57], v[18:25], v[216:223], 0, v194, v169 op_sel_hi:[0,0,0]
	v_mfma_scale_f32_16x16x128_f8f6f4 v[46:49], v[26:33], v[236:243], 0, v194, v169 op_sel_hi:[0,0,0]
	v_mfma_scale_f32_16x16x128_f8f6f4 v[38:41], v[18:25], v[236:243], 0, v194, v169 op_sel_hi:[0,0,0]
	s_setprio 0
	s_setprio 1
	v_mfma_scale_f32_16x16x128_f8f6f4 v[90:93], v[10:17], v[200:207], 0, v194, v169 op_sel_hi:[0,0,0]
	v_mfma_scale_f32_16x16x128_f8f6f4 v[82:85], v[2:9], v[200:207], 0, v194, v169 op_sel_hi:[0,0,0]
	v_mfma_scale_f32_16x16x128_f8f6f4 v[74:77], v[10:17], v[208:215], 0, v194, v169 op_sel_hi:[0,0,0]
	v_mfma_scale_f32_16x16x128_f8f6f4 v[66:69], v[2:9], v[208:215], 0, v194, v169 op_sel_hi:[0,0,0]
	v_mfma_scale_f32_16x16x128_f8f6f4 v[58:61], v[10:17], v[216:223], 0, v194, v169 op_sel_hi:[0,0,0]
	v_mfma_scale_f32_16x16x128_f8f6f4 v[50:53], v[2:9], v[216:223], 0, v194, v169 op_sel_hi:[0,0,0]
	v_mfma_scale_f32_16x16x128_f8f6f4 v[42:45], v[10:17], v[236:243], 0, v194, v169 op_sel_hi:[0,0,0]
	v_mfma_scale_f32_16x16x128_f8f6f4 v[34:37], v[2:9], v[236:243], 0, v194, v169 op_sel_hi:[0,0,0]
	s_setprio 0
	s_barrier
	s_add_i32 s68, 0, 0x18000
	s_add_i32 s69, 0, 0x1c000
	v_add_u32_e32 v2, s68, v196
	v_add_u32_e32 v6, s69, v196
	ds_read_b128 v[26:29], v2
	ds_read_b128 v[30:33], v2 offset:1024
	ds_read_b128 v[18:21], v2 offset:2048
	ds_read_b128 v[22:25], v2 offset:3072
	ds_read_b128 v[10:13], v6
	ds_read_b128 v[14:17], v6 offset:1024
	ds_read_b128 v[2:5], v6 offset:2048
	ds_read_b128 v[6:9], v6 offset:3072
	s_add_u32 s58, s58, 0x20000
	s_addc_u32 s59, s59, 0
	s_mov_b32 m0, s21
	v_lshl_add_u64 v[170:171], s[58:59], 0, v[164:165]
	ds_read_b128 v[200:203], v198 offset:32768
	ds_read_b128 v[204:207], v198 offset:33792
	ds_read_b128 v[208:211], v198 offset:34816
	ds_read_b128 v[212:215], v198 offset:35840
	ds_read_b128 v[216:219], v198 offset:36864
	ds_read_b128 v[220:223], v198 offset:37888
	ds_read_b128 v[236:239], v198 offset:38912
	ds_read_b128 v[240:243], v198 offset:39936
	global_load_lds_dwordx4 v[170:171], off
	v_lshl_add_u64 v[170:171], s[58:59], 0, v[162:163]
	s_mov_b32 m0, s22
	s_nop 0
	global_load_lds_dwordx4 v[170:171], off
	s_waitcnt vmcnt(8) lgkmcnt(0)
	s_barrier
	s_setprio 1
	v_mfma_scale_f32_16x16x128_f8f6f4 v[158:161], v[26:33], v[200:207], v[158:161], v194, v169 op_sel_hi:[0,0,0]
	v_mfma_scale_f32_16x16x128_f8f6f4 v[150:153], v[18:25], v[200:207], v[150:153], v194, v169 op_sel_hi:[0,0,0]
	v_mfma_scale_f32_16x16x128_f8f6f4 v[142:145], v[26:33], v[208:215], v[142:145], v194, v169 op_sel_hi:[0,0,0]
	v_mfma_scale_f32_16x16x128_f8f6f4 v[134:137], v[18:25], v[208:215], v[134:137], v194, v169 op_sel_hi:[0,0,0]
	v_mfma_scale_f32_16x16x128_f8f6f4 v[126:129], v[26:33], v[216:223], v[126:129], v194, v169 op_sel_hi:[0,0,0]
	v_mfma_scale_f32_16x16x128_f8f6f4 v[118:121], v[18:25], v[216:223], v[118:121], v194, v169 op_sel_hi:[0,0,0]
	v_mfma_scale_f32_16x16x128_f8f6f4 v[110:113], v[26:33], v[236:243], v[110:113], v194, v169 op_sel_hi:[0,0,0]
	v_mfma_scale_f32_16x16x128_f8f6f4 v[102:105], v[18:25], v[236:243], v[102:105], v194, v169 op_sel_hi:[0,0,0]
	s_setprio 0
	s_setprio 1
	v_mfma_scale_f32_16x16x128_f8f6f4 v[154:157], v[10:17], v[200:207], v[154:157], v194, v169 op_sel_hi:[0,0,0]
	v_mfma_scale_f32_16x16x128_f8f6f4 v[146:149], v[2:9], v[200:207], v[146:149], v194, v169 op_sel_hi:[0,0,0]
	v_mfma_scale_f32_16x16x128_f8f6f4 v[138:141], v[10:17], v[208:215], v[138:141], v194, v169 op_sel_hi:[0,0,0]
	v_mfma_scale_f32_16x16x128_f8f6f4 v[130:133], v[2:9], v[208:215], v[130:133], v194, v169 op_sel_hi:[0,0,0]
	v_mfma_scale_f32_16x16x128_f8f6f4 v[122:125], v[10:17], v[216:223], v[122:125], v194, v169 op_sel_hi:[0,0,0]
	v_mfma_scale_f32_16x16x128_f8f6f4 v[114:117], v[2:9], v[216:223], v[114:117], v194, v169 op_sel_hi:[0,0,0]
	v_mfma_scale_f32_16x16x128_f8f6f4 v[106:109], v[10:17], v[236:243], v[106:109], v194, v169 op_sel_hi:[0,0,0]
	v_mfma_scale_f32_16x16x128_f8f6f4 v[98:101], v[2:9], v[236:243], v[98:101], v194, v169 op_sel_hi:[0,0,0]
	s_setprio 0
	s_barrier
	s_add_i32 s58, s68, s14
	v_lshl_add_u64 v[170:171], v[186:187], 0, s[56:57]
	s_mov_b32 m0, s58
	ds_read_b128 v[200:203], v198 offset:49152
	ds_read_b128 v[204:207], v198 offset:50176
	ds_read_b128 v[208:211], v198 offset:51200
	ds_read_b128 v[212:215], v198 offset:52224
	ds_read_b128 v[216:219], v198 offset:53248
	ds_read_b128 v[220:223], v198 offset:54272
	ds_read_b128 v[236:239], v198 offset:55296
	ds_read_b128 v[240:243], v198 offset:56320
	global_load_lds_dwordx4 v[170:171], off
	s_add_i32 m0, s58, 0x2000
	s_add_u32 s54, s54, 0x20080
	v_lshl_add_u64 v[170:171], v[188:189], 0, s[56:57]
	s_addc_u32 s55, s55, 0
	s_add_i32 s58, s69, s14
	global_load_lds_dwordx4 v[170:171], off
	v_lshl_add_u64 v[170:171], s[54:55], 0, v[166:167]
	s_mov_b32 m0, s58
	s_nop 0
	global_load_lds_dwordx4 v[170:171], off
	v_lshl_add_u64 v[170:171], s[54:55], 0, v[178:179]
	s_add_i32 m0, s58, 0x2000
	s_nop 0
	global_load_lds_dwordx4 v[170:171], off
	v_lshl_add_u64 v[170:171], v[190:191], 0, s[56:57]
	s_mov_b32 m0, s23
	s_nop 0
	global_load_lds_dwordx4 v[170:171], off
	v_lshl_add_u64 v[170:171], v[192:193], 0, s[56:57]
	s_mov_b32 m0, s24
	s_nop 0
	global_load_lds_dwordx4 v[170:171], off
	s_waitcnt vmcnt(8) lgkmcnt(0)
	s_barrier
	s_setprio 1
	v_mfma_scale_f32_16x16x128_f8f6f4 v[94:97], v[26:33], v[200:207], v[94:97], v194, v169 op_sel_hi:[0,0,0]
	v_mfma_scale_f32_16x16x128_f8f6f4 v[86:89], v[18:25], v[200:207], v[86:89], v194, v169 op_sel_hi:[0,0,0]
	v_mfma_scale_f32_16x16x128_f8f6f4 v[78:81], v[26:33], v[208:215], v[78:81], v194, v169 op_sel_hi:[0,0,0]
	v_mfma_scale_f32_16x16x128_f8f6f4 v[70:73], v[18:25], v[208:215], v[70:73], v194, v169 op_sel_hi:[0,0,0]
	v_mfma_scale_f32_16x16x128_f8f6f4 v[62:65], v[26:33], v[216:223], v[62:65], v194, v169 op_sel_hi:[0,0,0]
	v_mfma_scale_f32_16x16x128_f8f6f4 v[54:57], v[18:25], v[216:223], v[54:57], v194, v169 op_sel_hi:[0,0,0]
	v_mfma_scale_f32_16x16x128_f8f6f4 v[46:49], v[26:33], v[236:243], v[46:49], v194, v169 op_sel_hi:[0,0,0]
	v_mfma_scale_f32_16x16x128_f8f6f4 v[38:41], v[18:25], v[236:243], v[38:41], v194, v169 op_sel_hi:[0,0,0]
	s_setprio 0
	s_setprio 1
	v_mfma_scale_f32_16x16x128_f8f6f4 v[90:93], v[10:17], v[200:207], v[90:93], v194, v169 op_sel_hi:[0,0,0]
	v_mfma_scale_f32_16x16x128_f8f6f4 v[82:85], v[2:9], v[200:207], v[82:85], v194, v169 op_sel_hi:[0,0,0]
	v_mfma_scale_f32_16x16x128_f8f6f4 v[74:77], v[10:17], v[208:215], v[74:77], v194, v169 op_sel_hi:[0,0,0]
	v_mfma_scale_f32_16x16x128_f8f6f4 v[66:69], v[2:9], v[208:215], v[66:69], v194, v169 op_sel_hi:[0,0,0]
	v_mfma_scale_f32_16x16x128_f8f6f4 v[58:61], v[10:17], v[216:223], v[58:61], v194, v169 op_sel_hi:[0,0,0]
	v_mfma_scale_f32_16x16x128_f8f6f4 v[50:53], v[2:9], v[216:223], v[50:53], v194, v169 op_sel_hi:[0,0,0]
	v_mfma_scale_f32_16x16x128_f8f6f4 v[42:45], v[10:17], v[236:243], v[42:45], v194, v169 op_sel_hi:[0,0,0]
	v_mfma_scale_f32_16x16x128_f8f6f4 v[34:37], v[2:9], v[236:243], v[34:37], v194, v169 op_sel_hi:[0,0,0]
	s_setprio 0
	s_barrier
	s_add_u32 s64, s64, 0x100
	s_addc_u32 s65, s65, 0
	s_add_u32 s52, s52, 0x100
	s_addc_u32 s53, s53, 0
	s_cmp_ge_i32 s66, s13
	s_mov_b32 s54, s66
	s_cbranch_scc0 .LBB0_842
	s_branch .Lpeelexitph7f
.LBB0_842:
	s_add_i32 s66, s54, 2
	s_add_u32 s55, s52, 0xfffe0080
	s_addc_u32 s58, s53, -1
	s_add_i32 s68, 0, 0x10000
	s_cmp_eq_u32 s51, s54
	s_cselect_b32 s59, s41, s58
	s_cselect_b32 s58, s43, s55
	s_cselect_b32 s55, s62, s65
	s_cselect_b32 s54, s63, s64
	s_add_i32 s69, 0, 0x14000
	v_add_u32_e32 v2, s68, v196
	v_add_u32_e32 v6, s69, v196
	ds_read_b128 v[26:29], v2
	ds_read_b128 v[30:33], v2 offset:1024
	ds_read_b128 v[18:21], v2 offset:2048
	ds_read_b128 v[22:25], v2 offset:3072
	ds_read_b128 v[10:13], v6
	ds_read_b128 v[14:17], v6 offset:1024
	ds_read_b128 v[2:5], v6 offset:2048
	ds_read_b128 v[6:9], v6 offset:3072
	v_lshl_add_u64 v[170:171], s[52:53], 0, v[184:185]
	s_add_i32 m0, s16, 0xc000
	ds_read_b128 v[186:189], v198
	ds_read_b128 v[190:193], v198 offset:1024
	ds_read_b128 v[200:203], v198 offset:2048
	ds_read_b128 v[204:207], v198 offset:3072
	ds_read_b128 v[208:211], v198 offset:4096
	ds_read_b128 v[212:215], v198 offset:5120
	ds_read_b128 v[216:219], v198 offset:6144
	ds_read_b128 v[220:223], v198 offset:7168
	global_load_lds_dwordx4 v[170:171], off
	v_lshl_add_u64 v[170:171], s[52:53], 0, v[182:183]
	s_add_i32 m0, s16, 0xe000
	s_nop 0
	global_load_lds_dwordx4 v[170:171], off
	s_waitcnt vmcnt(8) lgkmcnt(0)
	s_barrier
	s_setprio 1
	v_mfma_scale_f32_16x16x128_f8f6f4 v[158:161], v[26:33], v[186:193], v[158:161], v194, v169 op_sel_hi:[0,0,0]
	v_mfma_scale_f32_16x16x128_f8f6f4 v[150:153], v[18:25], v[186:193], v[150:153], v194, v169 op_sel_hi:[0,0,0]
	v_mfma_scale_f32_16x16x128_f8f6f4 v[142:145], v[26:33], v[200:207], v[142:145], v194, v169 op_sel_hi:[0,0,0]
	v_mfma_scale_f32_16x16x128_f8f6f4 v[134:137], v[18:25], v[200:207], v[134:137], v194, v169 op_sel_hi:[0,0,0]
	v_mfma_scale_f32_16x16x128_f8f6f4 v[126:129], v[26:33], v[208:215], v[126:129], v194, v169 op_sel_hi:[0,0,0]
	v_mfma_scale_f32_16x16x128_f8f6f4 v[118:121], v[18:25], v[208:215], v[118:121], v194, v169 op_sel_hi:[0,0,0]
	v_mfma_scale_f32_16x16x128_f8f6f4 v[110:113], v[26:33], v[216:223], v[110:113], v194, v169 op_sel_hi:[0,0,0]
	v_mfma_scale_f32_16x16x128_f8f6f4 v[102:105], v[18:25], v[216:223], v[102:105], v194, v169 op_sel_hi:[0,0,0]
	s_setprio 0
	s_setprio 1
	v_mfma_scale_f32_16x16x128_f8f6f4 v[154:157], v[10:17], v[186:193], v[154:157], v194, v169 op_sel_hi:[0,0,0]
	v_mfma_scale_f32_16x16x128_f8f6f4 v[146:149], v[2:9], v[186:193], v[146:149], v194, v169 op_sel_hi:[0,0,0]
	v_mfma_scale_f32_16x16x128_f8f6f4 v[138:141], v[10:17], v[200:207], v[138:141], v194, v169 op_sel_hi:[0,0,0]
	v_mfma_scale_f32_16x16x128_f8f6f4 v[130:133], v[2:9], v[200:207], v[130:133], v194, v169 op_sel_hi:[0,0,0]
	v_mfma_scale_f32_16x16x128_f8f6f4 v[122:125], v[10:17], v[208:215], v[122:125], v194, v169 op_sel_hi:[0,0,0]
	v_mfma_scale_f32_16x16x128_f8f6f4 v[114:117], v[2:9], v[208:215], v[114:117], v194, v169 op_sel_hi:[0,0,0]
	v_mfma_scale_f32_16x16x128_f8f6f4 v[106:109], v[10:17], v[216:223], v[106:109], v194, v169 op_sel_hi:[0,0,0]
	v_mfma_scale_f32_16x16x128_f8f6f4 v[98:101], v[2:9], v[216:223], v[98:101], v194, v169 op_sel_hi:[0,0,0]
	s_setprio 0
	s_barrier
	s_add_i32 s68, s68, s14
	v_lshl_add_u64 v[186:187], s[54:55], 0, v[166:167]
	s_mov_b32 m0, s68
	ds_read_b128 v[200:203], v198 offset:16384
	ds_read_b128 v[204:207], v198 offset:17408
	ds_read_b128 v[208:211], v198 offset:18432
	ds_read_b128 v[212:215], v198 offset:19456
	ds_read_b128 v[216:219], v198 offset:20480
	ds_read_b128 v[220:223], v198 offset:21504
	ds_read_b128 v[236:239], v198 offset:22528
	ds_read_b128 v[240:243], v198 offset:23552
	global_load_lds_dwordx4 v[186:187], off
	s_add_i32 m0, s68, 0x2000
	s_add_u32 s70, s54, 0x20000
	v_lshl_add_u64 v[188:189], s[54:55], 0, v[178:179]
	s_addc_u32 s71, s55, 0
	s_add_i32 s68, s69, s14
	global_load_lds_dwordx4 v[188:189], off
	v_lshl_add_u64 v[170:171], s[70:71], 0, v[166:167]
	s_mov_b32 m0, s68
	v_lshl_add_u64 v[190:191], s[58:59], 0, v[164:165]
	global_load_lds_dwordx4 v[170:171], off
	v_lshl_add_u64 v[170:171], s[70:71], 0, v[178:179]
	s_add_i32 m0, s68, 0x2000
	v_lshl_add_u64 v[192:193], s[58:59], 0, v[162:163]
	global_load_lds_dwordx4 v[170:171], off
	s_mov_b32 m0, s16
	s_nop 0
	global_load_lds_dwordx4 v[190:191], off
	s_mov_b32 m0, s20
	s_nop 0
	global_load_lds_dwordx4 v[192:193], off
	s_waitcnt vmcnt(8) lgkmcnt(0)
	s_barrier
	s_setprio 1
	v_mfma_scale_f32_16x16x128_f8f6f4 v[94:97], v[26:33], v[200:207], v[94:97], v194, v169 op_sel_hi:[0,0,0]
	v_mfma_scale_f32_16x16x128_f8f6f4 v[86:89], v[18:25], v[200:207], v[86:89], v194, v169 op_sel_hi:[0,0,0]
	v_mfma_scale_f32_16x16x128_f8f6f4 v[78:81], v[26:33], v[208:215], v[78:81], v194, v169 op_sel_hi:[0,0,0]
	v_mfma_scale_f32_16x16x128_f8f6f4 v[70:73], v[18:25], v[208:215], v[70:73], v194, v169 op_sel_hi:[0,0,0]
	v_mfma_scale_f32_16x16x128_f8f6f4 v[62:65], v[26:33], v[216:223], v[62:65], v194, v169 op_sel_hi:[0,0,0]
	v_mfma_scale_f32_16x16x128_f8f6f4 v[54:57], v[18:25], v[216:223], v[54:57], v194, v169 op_sel_hi:[0,0,0]
	v_mfma_scale_f32_16x16x128_f8f6f4 v[46:49], v[26:33], v[236:243], v[46:49], v194, v169 op_sel_hi:[0,0,0]
	v_mfma_scale_f32_16x16x128_f8f6f4 v[38:41], v[18:25], v[236:243], v[38:41], v194, v169 op_sel_hi:[0,0,0]
	s_setprio 0
	s_setprio 1
	v_mfma_scale_f32_16x16x128_f8f6f4 v[90:93], v[10:17], v[200:207], v[90:93], v194, v169 op_sel_hi:[0,0,0]
	v_mfma_scale_f32_16x16x128_f8f6f4 v[82:85], v[2:9], v[200:207], v[82:85], v194, v169 op_sel_hi:[0,0,0]
	v_mfma_scale_f32_16x16x128_f8f6f4 v[74:77], v[10:17], v[208:215], v[74:77], v194, v169 op_sel_hi:[0,0,0]
	v_mfma_scale_f32_16x16x128_f8f6f4 v[66:69], v[2:9], v[208:215], v[66:69], v194, v169 op_sel_hi:[0,0,0]
	v_mfma_scale_f32_16x16x128_f8f6f4 v[58:61], v[10:17], v[216:223], v[58:61], v194, v169 op_sel_hi:[0,0,0]
	v_mfma_scale_f32_16x16x128_f8f6f4 v[50:53], v[2:9], v[216:223], v[50:53], v194, v169 op_sel_hi:[0,0,0]
	v_mfma_scale_f32_16x16x128_f8f6f4 v[42:45], v[10:17], v[236:243], v[42:45], v194, v169 op_sel_hi:[0,0,0]
	v_mfma_scale_f32_16x16x128_f8f6f4 v[34:37], v[2:9], v[236:243], v[34:37], v194, v169 op_sel_hi:[0,0,0]
	s_setprio 0
	s_barrier
	s_add_i32 s68, 0, 0x18000
	s_add_i32 s69, 0, 0x1c000
	v_add_u32_e32 v2, s68, v196
	v_add_u32_e32 v6, s69, v196
	ds_read_b128 v[26:29], v2
	ds_read_b128 v[30:33], v2 offset:1024
	ds_read_b128 v[18:21], v2 offset:2048
	ds_read_b128 v[22:25], v2 offset:3072
	ds_read_b128 v[10:13], v6
	ds_read_b128 v[14:17], v6 offset:1024
	ds_read_b128 v[2:5], v6 offset:2048
	ds_read_b128 v[6:9], v6 offset:3072
	s_add_u32 s58, s58, 0x20000
	s_addc_u32 s59, s59, 0
	s_mov_b32 m0, s21
	v_lshl_add_u64 v[170:171], s[58:59], 0, v[164:165]
	ds_read_b128 v[200:203], v198 offset:32768
	ds_read_b128 v[204:207], v198 offset:33792
	ds_read_b128 v[208:211], v198 offset:34816
	ds_read_b128 v[212:215], v198 offset:35840
	ds_read_b128 v[216:219], v198 offset:36864
	ds_read_b128 v[220:223], v198 offset:37888
	ds_read_b128 v[236:239], v198 offset:38912
	ds_read_b128 v[240:243], v198 offset:39936
	global_load_lds_dwordx4 v[170:171], off
	v_lshl_add_u64 v[170:171], s[58:59], 0, v[162:163]
	s_mov_b32 m0, s22
	s_nop 0
	global_load_lds_dwordx4 v[170:171], off
	s_waitcnt vmcnt(8) lgkmcnt(0)
	s_barrier
	s_setprio 1
	v_mfma_scale_f32_16x16x128_f8f6f4 v[158:161], v[26:33], v[200:207], v[158:161], v194, v169 op_sel_hi:[0,0,0]
	v_mfma_scale_f32_16x16x128_f8f6f4 v[150:153], v[18:25], v[200:207], v[150:153], v194, v169 op_sel_hi:[0,0,0]
	v_mfma_scale_f32_16x16x128_f8f6f4 v[142:145], v[26:33], v[208:215], v[142:145], v194, v169 op_sel_hi:[0,0,0]
	v_mfma_scale_f32_16x16x128_f8f6f4 v[134:137], v[18:25], v[208:215], v[134:137], v194, v169 op_sel_hi:[0,0,0]
	v_mfma_scale_f32_16x16x128_f8f6f4 v[126:129], v[26:33], v[216:223], v[126:129], v194, v169 op_sel_hi:[0,0,0]
	v_mfma_scale_f32_16x16x128_f8f6f4 v[118:121], v[18:25], v[216:223], v[118:121], v194, v169 op_sel_hi:[0,0,0]
	v_mfma_scale_f32_16x16x128_f8f6f4 v[110:113], v[26:33], v[236:243], v[110:113], v194, v169 op_sel_hi:[0,0,0]
	v_mfma_scale_f32_16x16x128_f8f6f4 v[102:105], v[18:25], v[236:243], v[102:105], v194, v169 op_sel_hi:[0,0,0]
	s_setprio 0
	s_setprio 1
	v_mfma_scale_f32_16x16x128_f8f6f4 v[154:157], v[10:17], v[200:207], v[154:157], v194, v169 op_sel_hi:[0,0,0]
	v_mfma_scale_f32_16x16x128_f8f6f4 v[146:149], v[2:9], v[200:207], v[146:149], v194, v169 op_sel_hi:[0,0,0]
	v_mfma_scale_f32_16x16x128_f8f6f4 v[138:141], v[10:17], v[208:215], v[138:141], v194, v169 op_sel_hi:[0,0,0]
	v_mfma_scale_f32_16x16x128_f8f6f4 v[130:133], v[2:9], v[208:215], v[130:133], v194, v169 op_sel_hi:[0,0,0]
	v_mfma_scale_f32_16x16x128_f8f6f4 v[122:125], v[10:17], v[216:223], v[122:125], v194, v169 op_sel_hi:[0,0,0]
	v_mfma_scale_f32_16x16x128_f8f6f4 v[114:117], v[2:9], v[216:223], v[114:117], v194, v169 op_sel_hi:[0,0,0]
	v_mfma_scale_f32_16x16x128_f8f6f4 v[106:109], v[10:17], v[236:243], v[106:109], v194, v169 op_sel_hi:[0,0,0]
	v_mfma_scale_f32_16x16x128_f8f6f4 v[98:101], v[2:9], v[236:243], v[98:101], v194, v169 op_sel_hi:[0,0,0]
	s_setprio 0
	s_barrier
	s_add_i32 s58, s68, s14
	v_lshl_add_u64 v[170:171], v[186:187], 0, s[56:57]
	s_mov_b32 m0, s58
	ds_read_b128 v[200:203], v198 offset:49152
	ds_read_b128 v[204:207], v198 offset:50176
	ds_read_b128 v[208:211], v198 offset:51200
	ds_read_b128 v[212:215], v198 offset:52224
	ds_read_b128 v[216:219], v198 offset:53248
	ds_read_b128 v[220:223], v198 offset:54272
	ds_read_b128 v[236:239], v198 offset:55296
	ds_read_b128 v[240:243], v198 offset:56320
	global_load_lds_dwordx4 v[170:171], off
	s_add_i32 m0, s58, 0x2000
	s_add_u32 s54, s54, 0x20080
	v_lshl_add_u64 v[170:171], v[188:189], 0, s[56:57]
	s_addc_u32 s55, s55, 0
	s_add_i32 s58, s69, s14
	global_load_lds_dwordx4 v[170:171], off
	v_lshl_add_u64 v[170:171], s[54:55], 0, v[166:167]
	s_mov_b32 m0, s58
	s_nop 0
	global_load_lds_dwordx4 v[170:171], off
	v_lshl_add_u64 v[170:171], s[54:55], 0, v[178:179]
	s_add_i32 m0, s58, 0x2000
	s_nop 0
	global_load_lds_dwordx4 v[170:171], off
	v_lshl_add_u64 v[170:171], v[190:191], 0, s[56:57]
	s_mov_b32 m0, s23
	s_nop 0
	global_load_lds_dwordx4 v[170:171], off
	v_lshl_add_u64 v[170:171], v[192:193], 0, s[56:57]
	s_mov_b32 m0, s24
	s_nop 0
	global_load_lds_dwordx4 v[170:171], off
	s_waitcnt vmcnt(8) lgkmcnt(0)
	s_barrier
	s_setprio 1
	v_mfma_scale_f32_16x16x128_f8f6f4 v[94:97], v[26:33], v[200:207], v[94:97], v194, v169 op_sel_hi:[0,0,0]
	v_mfma_scale_f32_16x16x128_f8f6f4 v[86:89], v[18:25], v[200:207], v[86:89], v194, v169 op_sel_hi:[0,0,0]
	v_mfma_scale_f32_16x16x128_f8f6f4 v[78:81], v[26:33], v[208:215], v[78:81], v194, v169 op_sel_hi:[0,0,0]
	v_mfma_scale_f32_16x16x128_f8f6f4 v[70:73], v[18:25], v[208:215], v[70:73], v194, v169 op_sel_hi:[0,0,0]
	v_mfma_scale_f32_16x16x128_f8f6f4 v[62:65], v[26:33], v[216:223], v[62:65], v194, v169 op_sel_hi:[0,0,0]
	v_mfma_scale_f32_16x16x128_f8f6f4 v[54:57], v[18:25], v[216:223], v[54:57], v194, v169 op_sel_hi:[0,0,0]
	v_mfma_scale_f32_16x16x128_f8f6f4 v[46:49], v[26:33], v[236:243], v[46:49], v194, v169 op_sel_hi:[0,0,0]
	v_mfma_scale_f32_16x16x128_f8f6f4 v[38:41], v[18:25], v[236:243], v[38:41], v194, v169 op_sel_hi:[0,0,0]
	s_setprio 0
	s_setprio 1
	v_mfma_scale_f32_16x16x128_f8f6f4 v[90:93], v[10:17], v[200:207], v[90:93], v194, v169 op_sel_hi:[0,0,0]
	v_mfma_scale_f32_16x16x128_f8f6f4 v[82:85], v[2:9], v[200:207], v[82:85], v194, v169 op_sel_hi:[0,0,0]
	v_mfma_scale_f32_16x16x128_f8f6f4 v[74:77], v[10:17], v[208:215], v[74:77], v194, v169 op_sel_hi:[0,0,0]
	v_mfma_scale_f32_16x16x128_f8f6f4 v[66:69], v[2:9], v[208:215], v[66:69], v194, v169 op_sel_hi:[0,0,0]
	v_mfma_scale_f32_16x16x128_f8f6f4 v[58:61], v[10:17], v[216:223], v[58:61], v194, v169 op_sel_hi:[0,0,0]
	v_mfma_scale_f32_16x16x128_f8f6f4 v[50:53], v[2:9], v[216:223], v[50:53], v194, v169 op_sel_hi:[0,0,0]
	v_mfma_scale_f32_16x16x128_f8f6f4 v[42:45], v[10:17], v[236:243], v[42:45], v194, v169 op_sel_hi:[0,0,0]
	v_mfma_scale_f32_16x16x128_f8f6f4 v[34:37], v[2:9], v[236:243], v[34:37], v194, v169 op_sel_hi:[0,0,0]
	s_setprio 0
	s_barrier
	s_add_u32 s64, s64, 0x100
	s_addc_u32 s65, s65, 0
	s_add_u32 s52, s52, 0x100
	s_addc_u32 s53, s53, 0
	s_cmp_ge_i32 s66, s13
	s_mov_b32 s54, s66
	s_cbranch_scc0 .LBB0_842

.Lpeelph8_0:
	s_add_i32 s75, s62, 2
	s_add_u32 s60, s58, 0x100
	s_addc_u32 s61, s59, 0
	s_add_i32 s76, 0, 0x10000
	s_cmp_eq_u32 s68, s62
	s_cselect_b32 s65, s53, s61
	s_cselect_b32 s64, s52, s60
	s_cselect_b32 s63, s55, s74
	s_cselect_b32 s62, s54, s73
	s_add_i32 s77, 0, 0x14000
	v_add_u32_e32 v2, s76, v200
	v_add_u32_e32 v6, s77, v200
	ds_read_b128 v[26:29], v2
	ds_read_b128 v[30:33], v2 offset:1024
	ds_read_b128 v[18:21], v2 offset:2048
	ds_read_b128 v[22:25], v2 offset:3072
	ds_read_b128 v[10:13], v6
	ds_read_b128 v[14:17], v6 offset:1024
	s_waitcnt lgkmcnt(0)
	ds_read_b128 v[2:5], v6 offset:2048
	ds_read_b128 v[6:9], v6 offset:3072
	v_lshl_add_u64 v[170:171], s[58:59], 0, v[184:185]
	s_add_i32 m0, s15, 0xc000
	ds_read_b128 v[186:189], v204
	ds_read_b128 v[190:193], v204 offset:1024
	ds_read_b128 v[206:209], v204 offset:2048
	ds_read_b128 v[210:213], v204 offset:3072
	ds_read_b128 v[214:217], v204 offset:4096
	ds_read_b128 v[218:221], v204 offset:5120
	ds_read_b128 v[236:239], v204 offset:6144
	ds_read_b128 v[240:243], v204 offset:7168
	global_load_lds_dwordx4 v[170:171], off
	v_lshl_add_u64 v[170:171], s[58:59], 0, v[182:183]
	s_add_i32 m0, s15, 0xe000
	s_nop 0
	global_load_lds_dwordx4 v[170:171], off
	s_waitcnt vmcnt(8) lgkmcnt(0)
	s_barrier
	s_setprio 1
	v_mfma_scale_f32_16x16x128_f8f6f4 v[158:161], v[26:33], v[186:193], 0, v198, v169 op_sel_hi:[0,0,0]
	v_mfma_scale_f32_16x16x128_f8f6f4 v[154:157], v[18:25], v[186:193], 0, v198, v169 op_sel_hi:[0,0,0]
	v_mfma_scale_f32_16x16x128_f8f6f4 v[142:145], v[26:33], v[206:213], 0, v198, v169 op_sel_hi:[0,0,0]
	v_mfma_scale_f32_16x16x128_f8f6f4 v[138:141], v[18:25], v[206:213], 0, v198, v169 op_sel_hi:[0,0,0]
	v_mfma_scale_f32_16x16x128_f8f6f4 v[126:129], v[26:33], v[214:221], 0, v198, v169 op_sel_hi:[0,0,0]
	v_mfma_scale_f32_16x16x128_f8f6f4 v[122:125], v[18:25], v[214:221], 0, v198, v169 op_sel_hi:[0,0,0]
	v_mfma_scale_f32_16x16x128_f8f6f4 v[110:113], v[26:33], v[236:243], 0, v198, v169 op_sel_hi:[0,0,0]
	v_mfma_scale_f32_16x16x128_f8f6f4 v[106:109], v[18:25], v[236:243], 0, v198, v169 op_sel_hi:[0,0,0]
	s_setprio 0
	s_setprio 1
	v_mfma_scale_f32_16x16x128_f8f6f4 v[150:153], v[10:17], v[186:193], 0, v198, v169 op_sel_hi:[0,0,0]
	v_mfma_scale_f32_16x16x128_f8f6f4 v[146:149], v[2:9], v[186:193], 0, v198, v169 op_sel_hi:[0,0,0]
	v_mfma_scale_f32_16x16x128_f8f6f4 v[134:137], v[10:17], v[206:213], 0, v198, v169 op_sel_hi:[0,0,0]
	v_mfma_scale_f32_16x16x128_f8f6f4 v[130:133], v[2:9], v[206:213], 0, v198, v169 op_sel_hi:[0,0,0]
	v_mfma_scale_f32_16x16x128_f8f6f4 v[118:121], v[10:17], v[214:221], 0, v198, v169 op_sel_hi:[0,0,0]
	v_mfma_scale_f32_16x16x128_f8f6f4 v[114:117], v[2:9], v[214:221], 0, v198, v169 op_sel_hi:[0,0,0]
	v_mfma_scale_f32_16x16x128_f8f6f4 v[102:105], v[10:17], v[236:243], 0, v198, v169 op_sel_hi:[0,0,0]
	v_mfma_scale_f32_16x16x128_f8f6f4 v[98:101], v[2:9], v[236:243], 0, v198, v169 op_sel_hi:[0,0,0]
	s_setprio 0
	s_barrier
	s_add_i32 s58, s76, s14
	v_lshl_add_u64 v[186:187], s[62:63], 0, v[166:167]
	s_mov_b32 m0, s58
	ds_read_b128 v[206:209], v204 offset:16384
	ds_read_b128 v[210:213], v204 offset:17408
	ds_read_b128 v[214:217], v204 offset:18432
	ds_read_b128 v[218:221], v204 offset:19456
	ds_read_b128 v[236:239], v204 offset:20480
	ds_read_b128 v[240:243], v204 offset:21504
	ds_read_b128 v[244:247], v204 offset:22528
	ds_read_b128 v[248:251], v204 offset:23552
	global_load_lds_dwordx4 v[186:187], off
	s_add_i32 m0, s58, 0x2000
	s_add_u32 s58, s62, 0x70000
	v_lshl_add_u64 v[188:189], s[62:63], 0, v[162:163]
	s_addc_u32 s59, s63, 0
	s_add_i32 s76, s77, s14
	global_load_lds_dwordx4 v[188:189], off
	v_lshl_add_u64 v[170:171], s[58:59], 0, v[166:167]
	s_mov_b32 m0, s76
	v_lshl_add_u64 v[190:191], s[64:65], 0, v[164:165]
	global_load_lds_dwordx4 v[170:171], off
	v_lshl_add_u64 v[170:171], s[58:59], 0, v[162:163]
	s_add_i32 m0, s76, 0x2000
	v_lshl_add_u64 v[192:193], s[64:65], 0, v[178:179]
	global_load_lds_dwordx4 v[170:171], off
	s_mov_b32 m0, s15
	s_nop 0
	global_load_lds_dwordx4 v[190:191], off
	s_mov_b32 m0, s16
	s_nop 0
	global_load_lds_dwordx4 v[192:193], off
	s_waitcnt vmcnt(8) lgkmcnt(0)
	s_barrier
	s_setprio 1
	v_mfma_scale_f32_16x16x128_f8f6f4 v[94:97], v[26:33], v[206:213], 0, v198, v169 op_sel_hi:[0,0,0]
	v_mfma_scale_f32_16x16x128_f8f6f4 v[90:93], v[18:25], v[206:213], 0, v198, v169 op_sel_hi:[0,0,0]
	v_mfma_scale_f32_16x16x128_f8f6f4 v[78:81], v[26:33], v[214:221], 0, v198, v169 op_sel_hi:[0,0,0]
	v_mfma_scale_f32_16x16x128_f8f6f4 v[74:77], v[18:25], v[214:221], 0, v198, v169 op_sel_hi:[0,0,0]
	v_mfma_scale_f32_16x16x128_f8f6f4 v[62:65], v[26:33], v[236:243], 0, v198, v169 op_sel_hi:[0,0,0]
	v_mfma_scale_f32_16x16x128_f8f6f4 v[58:61], v[18:25], v[236:243], 0, v198, v169 op_sel_hi:[0,0,0]
	v_mfma_scale_f32_16x16x128_f8f6f4 v[46:49], v[26:33], v[244:251], 0, v198, v169 op_sel_hi:[0,0,0]
	v_mfma_scale_f32_16x16x128_f8f6f4 v[42:45], v[18:25], v[244:251], 0, v198, v169 op_sel_hi:[0,0,0]
	s_setprio 0
	s_setprio 1
	v_mfma_scale_f32_16x16x128_f8f6f4 v[86:89], v[10:17], v[206:213], 0, v198, v169 op_sel_hi:[0,0,0]
	v_mfma_scale_f32_16x16x128_f8f6f4 v[82:85], v[2:9], v[206:213], 0, v198, v169 op_sel_hi:[0,0,0]
	v_mfma_scale_f32_16x16x128_f8f6f4 v[70:73], v[10:17], v[214:221], 0, v198, v169 op_sel_hi:[0,0,0]
	v_mfma_scale_f32_16x16x128_f8f6f4 v[66:69], v[2:9], v[214:221], 0, v198, v169 op_sel_hi:[0,0,0]
	v_mfma_scale_f32_16x16x128_f8f6f4 v[54:57], v[10:17], v[236:243], 0, v198, v169 op_sel_hi:[0,0,0]
	v_mfma_scale_f32_16x16x128_f8f6f4 v[50:53], v[2:9], v[236:243], 0, v198, v169 op_sel_hi:[0,0,0]
	v_mfma_scale_f32_16x16x128_f8f6f4 v[38:41], v[10:17], v[244:251], 0, v198, v169 op_sel_hi:[0,0,0]
	v_mfma_scale_f32_16x16x128_f8f6f4 v[34:37], v[2:9], v[244:251], 0, v198, v169 op_sel_hi:[0,0,0]
	s_setprio 0
	s_barrier
	s_add_i32 s76, 0, 0x18000
	s_add_i32 s77, 0, 0x1c000
	v_add_u32_e32 v2, s76, v200
	v_add_u32_e32 v6, s77, v200
	ds_read_b128 v[26:29], v2
	ds_read_b128 v[30:33], v2 offset:1024
	ds_read_b128 v[18:21], v2 offset:2048
	ds_read_b128 v[22:25], v2 offset:3072
	ds_read_b128 v[10:13], v6
	ds_read_b128 v[14:17], v6 offset:1024
	ds_read_b128 v[2:5], v6 offset:2048
	ds_read_b128 v[6:9], v6 offset:3072
	s_add_u32 s58, s64, 0x70000
	s_addc_u32 s59, s65, 0
	s_mov_b32 m0, s20
	v_lshl_add_u64 v[170:171], s[58:59], 0, v[164:165]
	ds_read_b128 v[206:209], v204 offset:32768
	ds_read_b128 v[210:213], v204 offset:33792
	ds_read_b128 v[214:217], v204 offset:34816
	ds_read_b128 v[218:221], v204 offset:35840
	ds_read_b128 v[236:239], v204 offset:36864
	ds_read_b128 v[240:243], v204 offset:37888
	ds_read_b128 v[244:247], v204 offset:38912
	ds_read_b128 v[248:251], v204 offset:39936
	global_load_lds_dwordx4 v[170:171], off
	v_lshl_add_u64 v[170:171], s[58:59], 0, v[178:179]
	s_mov_b32 m0, s21
	s_nop 0
	global_load_lds_dwordx4 v[170:171], off
	s_waitcnt vmcnt(8) lgkmcnt(0)
	s_barrier
	s_setprio 1
	v_mfma_scale_f32_16x16x128_f8f6f4 v[158:161], v[26:33], v[206:213], v[158:161], v198, v169 op_sel_hi:[0,0,0]
	v_mfma_scale_f32_16x16x128_f8f6f4 v[154:157], v[18:25], v[206:213], v[154:157], v198, v169 op_sel_hi:[0,0,0]
	v_mfma_scale_f32_16x16x128_f8f6f4 v[142:145], v[26:33], v[214:221], v[142:145], v198, v169 op_sel_hi:[0,0,0]
	v_mfma_scale_f32_16x16x128_f8f6f4 v[138:141], v[18:25], v[214:221], v[138:141], v198, v169 op_sel_hi:[0,0,0]
	v_mfma_scale_f32_16x16x128_f8f6f4 v[126:129], v[26:33], v[236:243], v[126:129], v198, v169 op_sel_hi:[0,0,0]
	v_mfma_scale_f32_16x16x128_f8f6f4 v[122:125], v[18:25], v[236:243], v[122:125], v198, v169 op_sel_hi:[0,0,0]
	v_mfma_scale_f32_16x16x128_f8f6f4 v[110:113], v[26:33], v[244:251], v[110:113], v198, v169 op_sel_hi:[0,0,0]
	v_mfma_scale_f32_16x16x128_f8f6f4 v[106:109], v[18:25], v[244:251], v[106:109], v198, v169 op_sel_hi:[0,0,0]
	s_setprio 0
	s_setprio 1
	v_mfma_scale_f32_16x16x128_f8f6f4 v[150:153], v[10:17], v[206:213], v[150:153], v198, v169 op_sel_hi:[0,0,0]
	v_mfma_scale_f32_16x16x128_f8f6f4 v[146:149], v[2:9], v[206:213], v[146:149], v198, v169 op_sel_hi:[0,0,0]
	v_mfma_scale_f32_16x16x128_f8f6f4 v[134:137], v[10:17], v[214:221], v[134:137], v198, v169 op_sel_hi:[0,0,0]
	v_mfma_scale_f32_16x16x128_f8f6f4 v[130:133], v[2:9], v[214:221], v[130:133], v198, v169 op_sel_hi:[0,0,0]
	v_mfma_scale_f32_16x16x128_f8f6f4 v[118:121], v[10:17], v[236:243], v[118:121], v198, v169 op_sel_hi:[0,0,0]
	v_mfma_scale_f32_16x16x128_f8f6f4 v[114:117], v[2:9], v[236:243], v[114:117], v198, v169 op_sel_hi:[0,0,0]
	v_mfma_scale_f32_16x16x128_f8f6f4 v[102:105], v[10:17], v[244:251], v[102:105], v198, v169 op_sel_hi:[0,0,0]
	v_mfma_scale_f32_16x16x128_f8f6f4 v[98:101], v[2:9], v[244:251], v[98:101], v198, v169 op_sel_hi:[0,0,0]
	s_setprio 0
	s_barrier
	s_add_i32 s58, s76, s14
	v_lshl_add_u64 v[170:171], v[186:187], 0, s[56:57]
	s_mov_b32 m0, s58
	ds_read_b128 v[206:209], v204 offset:49152
	ds_read_b128 v[210:213], v204 offset:50176
	ds_read_b128 v[214:217], v204 offset:51200
	ds_read_b128 v[218:221], v204 offset:52224
	ds_read_b128 v[236:239], v204 offset:53248
	ds_read_b128 v[240:243], v204 offset:54272
	ds_read_b128 v[244:247], v204 offset:55296
	ds_read_b128 v[248:251], v204 offset:56320
	global_load_lds_dwordx4 v[170:171], off
	s_add_i32 m0, s58, 0x2000
	s_add_u32 s58, s62, 0x70080
	v_lshl_add_u64 v[170:171], v[188:189], 0, s[56:57]
	s_addc_u32 s59, s63, 0
	s_add_i32 s62, s77, s14
	global_load_lds_dwordx4 v[170:171], off
	v_lshl_add_u64 v[170:171], s[58:59], 0, v[166:167]
	s_mov_b32 m0, s62
	s_nop 0
	global_load_lds_dwordx4 v[170:171], off
	v_lshl_add_u64 v[170:171], s[58:59], 0, v[162:163]
	s_add_i32 m0, s62, 0x2000
	s_nop 0
	global_load_lds_dwordx4 v[170:171], off
	v_lshl_add_u64 v[170:171], v[190:191], 0, s[56:57]
	s_mov_b32 m0, s24
	s_nop 0
	global_load_lds_dwordx4 v[170:171], off
	v_lshl_add_u64 v[170:171], v[192:193], 0, s[56:57]
	s_mov_b32 m0, s25
	s_nop 0
	global_load_lds_dwordx4 v[170:171], off
	s_waitcnt vmcnt(8) lgkmcnt(0)
	s_barrier
	s_setprio 1
	v_mfma_scale_f32_16x16x128_f8f6f4 v[94:97], v[26:33], v[206:213], v[94:97], v198, v169 op_sel_hi:[0,0,0]
	v_mfma_scale_f32_16x16x128_f8f6f4 v[90:93], v[18:25], v[206:213], v[90:93], v198, v169 op_sel_hi:[0,0,0]
	v_mfma_scale_f32_16x16x128_f8f6f4 v[78:81], v[26:33], v[214:221], v[78:81], v198, v169 op_sel_hi:[0,0,0]
	v_mfma_scale_f32_16x16x128_f8f6f4 v[74:77], v[18:25], v[214:221], v[74:77], v198, v169 op_sel_hi:[0,0,0]
	v_mfma_scale_f32_16x16x128_f8f6f4 v[62:65], v[26:33], v[236:243], v[62:65], v198, v169 op_sel_hi:[0,0,0]
	v_mfma_scale_f32_16x16x128_f8f6f4 v[58:61], v[18:25], v[236:243], v[58:61], v198, v169 op_sel_hi:[0,0,0]
	v_mfma_scale_f32_16x16x128_f8f6f4 v[46:49], v[26:33], v[244:251], v[46:49], v198, v169 op_sel_hi:[0,0,0]
	v_mfma_scale_f32_16x16x128_f8f6f4 v[42:45], v[18:25], v[244:251], v[42:45], v198, v169 op_sel_hi:[0,0,0]
	s_setprio 0
	s_setprio 1
	v_mfma_scale_f32_16x16x128_f8f6f4 v[86:89], v[10:17], v[206:213], v[86:89], v198, v169 op_sel_hi:[0,0,0]
	v_mfma_scale_f32_16x16x128_f8f6f4 v[82:85], v[2:9], v[206:213], v[82:85], v198, v169 op_sel_hi:[0,0,0]
	v_mfma_scale_f32_16x16x128_f8f6f4 v[70:73], v[10:17], v[214:221], v[70:73], v198, v169 op_sel_hi:[0,0,0]
	v_mfma_scale_f32_16x16x128_f8f6f4 v[66:69], v[2:9], v[214:221], v[66:69], v198, v169 op_sel_hi:[0,0,0]
	v_mfma_scale_f32_16x16x128_f8f6f4 v[54:57], v[10:17], v[236:243], v[54:57], v198, v169 op_sel_hi:[0,0,0]
	v_mfma_scale_f32_16x16x128_f8f6f4 v[50:53], v[2:9], v[236:243], v[50:53], v198, v169 op_sel_hi:[0,0,0]
	v_mfma_scale_f32_16x16x128_f8f6f4 v[38:41], v[10:17], v[244:251], v[38:41], v198, v169 op_sel_hi:[0,0,0]
	v_mfma_scale_f32_16x16x128_f8f6f4 v[34:37], v[2:9], v[244:251], v[34:37], v198, v169 op_sel_hi:[0,0,0]
	s_setprio 0
	s_barrier
	s_add_u32 s73, s73, 0x100
	s_addc_u32 s74, s74, 0
	s_cmp_ge_i32 s75, s1
	s_mov_b64 s[58:59], s[60:61]
	s_mov_b32 s62, s75
	s_cbranch_scc0 .LBB0_924
	s_branch .Lpeelexitph8
.LBB0_924:
	s_add_i32 s75, s62, 2
	s_add_u32 s60, s58, 0x100
	s_addc_u32 s61, s59, 0
	s_add_i32 s76, 0, 0x10000
	s_cmp_eq_u32 s68, s62
	s_cselect_b32 s65, s53, s61
	s_cselect_b32 s64, s52, s60
	s_cselect_b32 s63, s55, s74
	s_cselect_b32 s62, s54, s73
	s_add_i32 s77, 0, 0x14000
	v_add_u32_e32 v2, s76, v200
	v_add_u32_e32 v6, s77, v200
	ds_read_b128 v[26:29], v2
	ds_read_b128 v[30:33], v2 offset:1024
	ds_read_b128 v[18:21], v2 offset:2048
	ds_read_b128 v[22:25], v2 offset:3072
	ds_read_b128 v[10:13], v6
	ds_read_b128 v[14:17], v6 offset:1024
	s_waitcnt lgkmcnt(0)
	ds_read_b128 v[2:5], v6 offset:2048
	ds_read_b128 v[6:9], v6 offset:3072
	v_lshl_add_u64 v[170:171], s[58:59], 0, v[184:185]
	s_add_i32 m0, s15, 0xc000
	ds_read_b128 v[186:189], v204
	ds_read_b128 v[190:193], v204 offset:1024
	ds_read_b128 v[206:209], v204 offset:2048
	ds_read_b128 v[210:213], v204 offset:3072
	ds_read_b128 v[214:217], v204 offset:4096
	ds_read_b128 v[218:221], v204 offset:5120
	ds_read_b128 v[236:239], v204 offset:6144
	ds_read_b128 v[240:243], v204 offset:7168
	global_load_lds_dwordx4 v[170:171], off
	v_lshl_add_u64 v[170:171], s[58:59], 0, v[182:183]
	s_add_i32 m0, s15, 0xe000
	s_nop 0
	global_load_lds_dwordx4 v[170:171], off
	s_waitcnt vmcnt(8) lgkmcnt(0)
	s_barrier
	s_setprio 1
	v_mfma_scale_f32_16x16x128_f8f6f4 v[158:161], v[26:33], v[186:193], v[158:161], v198, v169 op_sel_hi:[0,0,0]
	v_mfma_scale_f32_16x16x128_f8f6f4 v[154:157], v[18:25], v[186:193], v[154:157], v198, v169 op_sel_hi:[0,0,0]
	v_mfma_scale_f32_16x16x128_f8f6f4 v[142:145], v[26:33], v[206:213], v[142:145], v198, v169 op_sel_hi:[0,0,0]
	v_mfma_scale_f32_16x16x128_f8f6f4 v[138:141], v[18:25], v[206:213], v[138:141], v198, v169 op_sel_hi:[0,0,0]
	v_mfma_scale_f32_16x16x128_f8f6f4 v[126:129], v[26:33], v[214:221], v[126:129], v198, v169 op_sel_hi:[0,0,0]
	v_mfma_scale_f32_16x16x128_f8f6f4 v[122:125], v[18:25], v[214:221], v[122:125], v198, v169 op_sel_hi:[0,0,0]
	v_mfma_scale_f32_16x16x128_f8f6f4 v[110:113], v[26:33], v[236:243], v[110:113], v198, v169 op_sel_hi:[0,0,0]
	v_mfma_scale_f32_16x16x128_f8f6f4 v[106:109], v[18:25], v[236:243], v[106:109], v198, v169 op_sel_hi:[0,0,0]
	s_setprio 0
	s_setprio 1
	v_mfma_scale_f32_16x16x128_f8f6f4 v[150:153], v[10:17], v[186:193], v[150:153], v198, v169 op_sel_hi:[0,0,0]
	v_mfma_scale_f32_16x16x128_f8f6f4 v[146:149], v[2:9], v[186:193], v[146:149], v198, v169 op_sel_hi:[0,0,0]
	v_mfma_scale_f32_16x16x128_f8f6f4 v[134:137], v[10:17], v[206:213], v[134:137], v198, v169 op_sel_hi:[0,0,0]
	v_mfma_scale_f32_16x16x128_f8f6f4 v[130:133], v[2:9], v[206:213], v[130:133], v198, v169 op_sel_hi:[0,0,0]
	v_mfma_scale_f32_16x16x128_f8f6f4 v[118:121], v[10:17], v[214:221], v[118:121], v198, v169 op_sel_hi:[0,0,0]
	v_mfma_scale_f32_16x16x128_f8f6f4 v[114:117], v[2:9], v[214:221], v[114:117], v198, v169 op_sel_hi:[0,0,0]
	v_mfma_scale_f32_16x16x128_f8f6f4 v[102:105], v[10:17], v[236:243], v[102:105], v198, v169 op_sel_hi:[0,0,0]
	v_mfma_scale_f32_16x16x128_f8f6f4 v[98:101], v[2:9], v[236:243], v[98:101], v198, v169 op_sel_hi:[0,0,0]
	s_setprio 0
	s_barrier
	s_add_i32 s58, s76, s14
	v_lshl_add_u64 v[186:187], s[62:63], 0, v[166:167]
	s_mov_b32 m0, s58
	ds_read_b128 v[206:209], v204 offset:16384
	ds_read_b128 v[210:213], v204 offset:17408
	ds_read_b128 v[214:217], v204 offset:18432
	ds_read_b128 v[218:221], v204 offset:19456
	ds_read_b128 v[236:239], v204 offset:20480
	ds_read_b128 v[240:243], v204 offset:21504
	ds_read_b128 v[244:247], v204 offset:22528
	ds_read_b128 v[248:251], v204 offset:23552
	global_load_lds_dwordx4 v[186:187], off
	s_add_i32 m0, s58, 0x2000
	s_add_u32 s58, s62, 0x70000
	v_lshl_add_u64 v[188:189], s[62:63], 0, v[162:163]
	s_addc_u32 s59, s63, 0
	s_add_i32 s76, s77, s14
	global_load_lds_dwordx4 v[188:189], off
	v_lshl_add_u64 v[170:171], s[58:59], 0, v[166:167]
	s_mov_b32 m0, s76
	v_lshl_add_u64 v[190:191], s[64:65], 0, v[164:165]
	global_load_lds_dwordx4 v[170:171], off
	v_lshl_add_u64 v[170:171], s[58:59], 0, v[162:163]
	s_add_i32 m0, s76, 0x2000
	v_lshl_add_u64 v[192:193], s[64:65], 0, v[178:179]
	global_load_lds_dwordx4 v[170:171], off
	s_mov_b32 m0, s15
	s_nop 0
	global_load_lds_dwordx4 v[190:191], off
	s_mov_b32 m0, s16
	s_nop 0
	global_load_lds_dwordx4 v[192:193], off
	s_waitcnt vmcnt(8) lgkmcnt(0)
	s_barrier
	s_setprio 1
	v_mfma_scale_f32_16x16x128_f8f6f4 v[94:97], v[26:33], v[206:213], v[94:97], v198, v169 op_sel_hi:[0,0,0]
	v_mfma_scale_f32_16x16x128_f8f6f4 v[90:93], v[18:25], v[206:213], v[90:93], v198, v169 op_sel_hi:[0,0,0]
	v_mfma_scale_f32_16x16x128_f8f6f4 v[78:81], v[26:33], v[214:221], v[78:81], v198, v169 op_sel_hi:[0,0,0]
	v_mfma_scale_f32_16x16x128_f8f6f4 v[74:77], v[18:25], v[214:221], v[74:77], v198, v169 op_sel_hi:[0,0,0]
	v_mfma_scale_f32_16x16x128_f8f6f4 v[62:65], v[26:33], v[236:243], v[62:65], v198, v169 op_sel_hi:[0,0,0]
	v_mfma_scale_f32_16x16x128_f8f6f4 v[58:61], v[18:25], v[236:243], v[58:61], v198, v169 op_sel_hi:[0,0,0]
	v_mfma_scale_f32_16x16x128_f8f6f4 v[46:49], v[26:33], v[244:251], v[46:49], v198, v169 op_sel_hi:[0,0,0]
	v_mfma_scale_f32_16x16x128_f8f6f4 v[42:45], v[18:25], v[244:251], v[42:45], v198, v169 op_sel_hi:[0,0,0]
	s_setprio 0
	s_setprio 1
	v_mfma_scale_f32_16x16x128_f8f6f4 v[86:89], v[10:17], v[206:213], v[86:89], v198, v169 op_sel_hi:[0,0,0]
	v_mfma_scale_f32_16x16x128_f8f6f4 v[82:85], v[2:9], v[206:213], v[82:85], v198, v169 op_sel_hi:[0,0,0]
	v_mfma_scale_f32_16x16x128_f8f6f4 v[70:73], v[10:17], v[214:221], v[70:73], v198, v169 op_sel_hi:[0,0,0]
	v_mfma_scale_f32_16x16x128_f8f6f4 v[66:69], v[2:9], v[214:221], v[66:69], v198, v169 op_sel_hi:[0,0,0]
	v_mfma_scale_f32_16x16x128_f8f6f4 v[54:57], v[10:17], v[236:243], v[54:57], v198, v169 op_sel_hi:[0,0,0]
	v_mfma_scale_f32_16x16x128_f8f6f4 v[50:53], v[2:9], v[236:243], v[50:53], v198, v169 op_sel_hi:[0,0,0]
	v_mfma_scale_f32_16x16x128_f8f6f4 v[38:41], v[10:17], v[244:251], v[38:41], v198, v169 op_sel_hi:[0,0,0]
	v_mfma_scale_f32_16x16x128_f8f6f4 v[34:37], v[2:9], v[244:251], v[34:37], v198, v169 op_sel_hi:[0,0,0]
	s_setprio 0
	s_barrier
	s_add_i32 s76, 0, 0x18000
	s_add_i32 s77, 0, 0x1c000
	v_add_u32_e32 v2, s76, v200
	v_add_u32_e32 v6, s77, v200
	ds_read_b128 v[26:29], v2
	ds_read_b128 v[30:33], v2 offset:1024
	ds_read_b128 v[18:21], v2 offset:2048
	ds_read_b128 v[22:25], v2 offset:3072
	ds_read_b128 v[10:13], v6
	ds_read_b128 v[14:17], v6 offset:1024
	ds_read_b128 v[2:5], v6 offset:2048
	ds_read_b128 v[6:9], v6 offset:3072
	s_add_u32 s58, s64, 0x70000
	s_addc_u32 s59, s65, 0
	s_mov_b32 m0, s20
	v_lshl_add_u64 v[170:171], s[58:59], 0, v[164:165]
	ds_read_b128 v[206:209], v204 offset:32768
	ds_read_b128 v[210:213], v204 offset:33792
	ds_read_b128 v[214:217], v204 offset:34816
	ds_read_b128 v[218:221], v204 offset:35840
	ds_read_b128 v[236:239], v204 offset:36864
	ds_read_b128 v[240:243], v204 offset:37888
	ds_read_b128 v[244:247], v204 offset:38912
	ds_read_b128 v[248:251], v204 offset:39936
	global_load_lds_dwordx4 v[170:171], off
	v_lshl_add_u64 v[170:171], s[58:59], 0, v[178:179]
	s_mov_b32 m0, s21
	s_nop 0
	global_load_lds_dwordx4 v[170:171], off
	s_waitcnt vmcnt(8) lgkmcnt(0)
	s_barrier
	s_setprio 1
	v_mfma_scale_f32_16x16x128_f8f6f4 v[158:161], v[26:33], v[206:213], v[158:161], v198, v169 op_sel_hi:[0,0,0]
	v_mfma_scale_f32_16x16x128_f8f6f4 v[154:157], v[18:25], v[206:213], v[154:157], v198, v169 op_sel_hi:[0,0,0]
	v_mfma_scale_f32_16x16x128_f8f6f4 v[142:145], v[26:33], v[214:221], v[142:145], v198, v169 op_sel_hi:[0,0,0]
	v_mfma_scale_f32_16x16x128_f8f6f4 v[138:141], v[18:25], v[214:221], v[138:141], v198, v169 op_sel_hi:[0,0,0]
	v_mfma_scale_f32_16x16x128_f8f6f4 v[126:129], v[26:33], v[236:243], v[126:129], v198, v169 op_sel_hi:[0,0,0]
	v_mfma_scale_f32_16x16x128_f8f6f4 v[122:125], v[18:25], v[236:243], v[122:125], v198, v169 op_sel_hi:[0,0,0]
	v_mfma_scale_f32_16x16x128_f8f6f4 v[110:113], v[26:33], v[244:251], v[110:113], v198, v169 op_sel_hi:[0,0,0]
	v_mfma_scale_f32_16x16x128_f8f6f4 v[106:109], v[18:25], v[244:251], v[106:109], v198, v169 op_sel_hi:[0,0,0]
	s_setprio 0
	s_setprio 1
	v_mfma_scale_f32_16x16x128_f8f6f4 v[150:153], v[10:17], v[206:213], v[150:153], v198, v169 op_sel_hi:[0,0,0]
	v_mfma_scale_f32_16x16x128_f8f6f4 v[146:149], v[2:9], v[206:213], v[146:149], v198, v169 op_sel_hi:[0,0,0]
	v_mfma_scale_f32_16x16x128_f8f6f4 v[134:137], v[10:17], v[214:221], v[134:137], v198, v169 op_sel_hi:[0,0,0]
	v_mfma_scale_f32_16x16x128_f8f6f4 v[130:133], v[2:9], v[214:221], v[130:133], v198, v169 op_sel_hi:[0,0,0]
	v_mfma_scale_f32_16x16x128_f8f6f4 v[118:121], v[10:17], v[236:243], v[118:121], v198, v169 op_sel_hi:[0,0,0]
	v_mfma_scale_f32_16x16x128_f8f6f4 v[114:117], v[2:9], v[236:243], v[114:117], v198, v169 op_sel_hi:[0,0,0]
	v_mfma_scale_f32_16x16x128_f8f6f4 v[102:105], v[10:17], v[244:251], v[102:105], v198, v169 op_sel_hi:[0,0,0]
	v_mfma_scale_f32_16x16x128_f8f6f4 v[98:101], v[2:9], v[244:251], v[98:101], v198, v169 op_sel_hi:[0,0,0]
	s_setprio 0
	s_barrier
	s_add_i32 s58, s76, s14
	v_lshl_add_u64 v[170:171], v[186:187], 0, s[56:57]
	s_mov_b32 m0, s58
	ds_read_b128 v[206:209], v204 offset:49152
	ds_read_b128 v[210:213], v204 offset:50176
	ds_read_b128 v[214:217], v204 offset:51200
	ds_read_b128 v[218:221], v204 offset:52224
	ds_read_b128 v[236:239], v204 offset:53248
	ds_read_b128 v[240:243], v204 offset:54272
	ds_read_b128 v[244:247], v204 offset:55296
	ds_read_b128 v[248:251], v204 offset:56320
	global_load_lds_dwordx4 v[170:171], off
	s_add_i32 m0, s58, 0x2000
	s_add_u32 s58, s62, 0x70080
	v_lshl_add_u64 v[170:171], v[188:189], 0, s[56:57]
	s_addc_u32 s59, s63, 0
	s_add_i32 s62, s77, s14
	global_load_lds_dwordx4 v[170:171], off
	v_lshl_add_u64 v[170:171], s[58:59], 0, v[166:167]
	s_mov_b32 m0, s62
	s_nop 0
	global_load_lds_dwordx4 v[170:171], off
	v_lshl_add_u64 v[170:171], s[58:59], 0, v[162:163]
	s_add_i32 m0, s62, 0x2000
	s_nop 0
	global_load_lds_dwordx4 v[170:171], off
	v_lshl_add_u64 v[170:171], v[190:191], 0, s[56:57]
	s_mov_b32 m0, s24
	s_nop 0
	global_load_lds_dwordx4 v[170:171], off
	v_lshl_add_u64 v[170:171], v[192:193], 0, s[56:57]
	s_mov_b32 m0, s25
	s_nop 0
	global_load_lds_dwordx4 v[170:171], off
	s_waitcnt vmcnt(8) lgkmcnt(0)
	s_barrier
	s_setprio 1
	v_mfma_scale_f32_16x16x128_f8f6f4 v[94:97], v[26:33], v[206:213], v[94:97], v198, v169 op_sel_hi:[0,0,0]
	v_mfma_scale_f32_16x16x128_f8f6f4 v[90:93], v[18:25], v[206:213], v[90:93], v198, v169 op_sel_hi:[0,0,0]
	v_mfma_scale_f32_16x16x128_f8f6f4 v[78:81], v[26:33], v[214:221], v[78:81], v198, v169 op_sel_hi:[0,0,0]
	v_mfma_scale_f32_16x16x128_f8f6f4 v[74:77], v[18:25], v[214:221], v[74:77], v198, v169 op_sel_hi:[0,0,0]
	v_mfma_scale_f32_16x16x128_f8f6f4 v[62:65], v[26:33], v[236:243], v[62:65], v198, v169 op_sel_hi:[0,0,0]
	v_mfma_scale_f32_16x16x128_f8f6f4 v[58:61], v[18:25], v[236:243], v[58:61], v198, v169 op_sel_hi:[0,0,0]
	v_mfma_scale_f32_16x16x128_f8f6f4 v[46:49], v[26:33], v[244:251], v[46:49], v198, v169 op_sel_hi:[0,0,0]
	v_mfma_scale_f32_16x16x128_f8f6f4 v[42:45], v[18:25], v[244:251], v[42:45], v198, v169 op_sel_hi:[0,0,0]
	s_setprio 0
	s_setprio 1
	v_mfma_scale_f32_16x16x128_f8f6f4 v[86:89], v[10:17], v[206:213], v[86:89], v198, v169 op_sel_hi:[0,0,0]
	v_mfma_scale_f32_16x16x128_f8f6f4 v[82:85], v[2:9], v[206:213], v[82:85], v198, v169 op_sel_hi:[0,0,0]
	v_mfma_scale_f32_16x16x128_f8f6f4 v[70:73], v[10:17], v[214:221], v[70:73], v198, v169 op_sel_hi:[0,0,0]
	v_mfma_scale_f32_16x16x128_f8f6f4 v[66:69], v[2:9], v[214:221], v[66:69], v198, v169 op_sel_hi:[0,0,0]
	v_mfma_scale_f32_16x16x128_f8f6f4 v[54:57], v[10:17], v[236:243], v[54:57], v198, v169 op_sel_hi:[0,0,0]
	v_mfma_scale_f32_16x16x128_f8f6f4 v[50:53], v[2:9], v[236:243], v[50:53], v198, v169 op_sel_hi:[0,0,0]
	v_mfma_scale_f32_16x16x128_f8f6f4 v[38:41], v[10:17], v[244:251], v[38:41], v198, v169 op_sel_hi:[0,0,0]
	v_mfma_scale_f32_16x16x128_f8f6f4 v[34:37], v[2:9], v[244:251], v[34:37], v198, v169 op_sel_hi:[0,0,0]
	s_setprio 0
	s_barrier
	s_add_u32 s73, s73, 0x100
	s_addc_u32 s74, s74, 0
	s_cmp_ge_i32 s75, s1
	s_mov_b64 s[58:59], s[60:61]
	s_mov_b32 s62, s75
	s_cbranch_scc0 .LBB0_924

.Lpeelph9_0:
	s_add_i32 s27, s37, 2
	s_add_u32 s40, s38, 0xfffe0080
	s_addc_u32 s41, s39, -1
	s_add_i32 s65, 0, 0x10000
	s_cmp_eq_u32 s95, s37
	s_cselect_b32 s69, s0, s41
	s_cselect_b32 s68, s1, s40
	s_cselect_b32 s41, s8, s19
	s_cselect_b32 s40, s11, s16
	s_add_i32 s37, 0, 0x14000
	v_add_u32_e32 v2, s65, v221
	v_add_u32_e32 v6, s37, v221
	ds_read_b128 v[26:29], v2
	ds_read_b128 v[30:33], v2 offset:1024
	ds_read_b128 v[18:21], v2 offset:2048
	ds_read_b128 v[22:25], v2 offset:3072
	ds_read_b128 v[10:13], v6
	ds_read_b128 v[14:17], v6 offset:1024
	ds_read_b128 v[2:5], v6 offset:2048
	ds_read_b128 v[6:9], v6 offset:3072
	v_lshl_add_u64 v[170:171], s[38:39], 0, v[192:193]
	s_add_i32 m0, s21, 0xc000
	ds_read_b128 v[194:197], v222
	ds_read_b128 v[198:201], v222 offset:1024
	ds_read_b128 v[202:205], v222 offset:2048
	ds_read_b128 v[206:209], v222 offset:3072
	ds_read_b128 v[210:213], v222 offset:4096
	ds_read_b128 v[214:217], v222 offset:5120
	ds_read_b128 v[236:239], v222 offset:6144
	ds_read_b128 v[240:243], v222 offset:7168
	global_load_lds_dwordx4 v[170:171], off
	v_lshl_add_u64 v[170:171], s[38:39], 0, v[190:191]
	s_add_i32 m0, s21, 0xe000
	s_nop 0
	global_load_lds_dwordx4 v[170:171], off
	s_waitcnt vmcnt(8) lgkmcnt(0)
	s_barrier
	s_setprio 1
	v_mfma_scale_f32_16x16x128_f8f6f4 v[94:97], v[26:33], v[194:201], 0, v183, v169 op_sel_hi:[0,0,0]
	v_mfma_scale_f32_16x16x128_f8f6f4 v[90:93], v[18:25], v[194:201], 0, v183, v169 op_sel_hi:[0,0,0]
	v_mfma_scale_f32_16x16x128_f8f6f4 v[86:89], v[26:33], v[202:209], 0, v183, v169 op_sel_hi:[0,0,0]
	v_mfma_scale_f32_16x16x128_f8f6f4 v[82:85], v[18:25], v[202:209], 0, v183, v169 op_sel_hi:[0,0,0]
	v_mfma_scale_f32_16x16x128_f8f6f4 v[78:81], v[26:33], v[210:217], 0, v183, v169 op_sel_hi:[0,0,0]
	v_mfma_scale_f32_16x16x128_f8f6f4 v[74:77], v[18:25], v[210:217], 0, v183, v169 op_sel_hi:[0,0,0]
	v_mfma_scale_f32_16x16x128_f8f6f4 v[70:73], v[26:33], v[236:243], 0, v183, v169 op_sel_hi:[0,0,0]
	v_mfma_scale_f32_16x16x128_f8f6f4 v[66:69], v[18:25], v[236:243], 0, v183, v169 op_sel_hi:[0,0,0]
	s_setprio 0
	s_setprio 1
	v_mfma_scale_f32_16x16x128_f8f6f4 v[158:161], v[10:17], v[194:201], 0, v183, v169 op_sel_hi:[0,0,0]
	v_mfma_scale_f32_16x16x128_f8f6f4 v[154:157], v[2:9], v[194:201], 0, v183, v169 op_sel_hi:[0,0,0]
	v_mfma_scale_f32_16x16x128_f8f6f4 v[150:153], v[10:17], v[202:209], 0, v183, v169 op_sel_hi:[0,0,0]
	v_mfma_scale_f32_16x16x128_f8f6f4 v[146:149], v[2:9], v[202:209], 0, v183, v169 op_sel_hi:[0,0,0]
	v_mfma_scale_f32_16x16x128_f8f6f4 v[142:145], v[10:17], v[210:217], 0, v183, v169 op_sel_hi:[0,0,0]
	v_mfma_scale_f32_16x16x128_f8f6f4 v[138:141], v[2:9], v[210:217], 0, v183, v169 op_sel_hi:[0,0,0]
	v_mfma_scale_f32_16x16x128_f8f6f4 v[134:137], v[10:17], v[236:243], 0, v183, v169 op_sel_hi:[0,0,0]
	v_mfma_scale_f32_16x16x128_f8f6f4 v[130:133], v[2:9], v[236:243], 0, v183, v169 op_sel_hi:[0,0,0]
	s_setprio 0
	s_barrier
	s_add_i32 s65, s65, s20
	v_lshl_add_u64 v[194:195], s[40:41], 0, v[162:163]
	s_mov_b32 m0, s65
	ds_read_b128 v[202:205], v222 offset:16384
	ds_read_b128 v[206:209], v222 offset:17408
	ds_read_b128 v[210:213], v222 offset:18432
	ds_read_b128 v[214:217], v222 offset:19456
	ds_read_b128 v[236:239], v222 offset:20480
	ds_read_b128 v[240:243], v222 offset:21504
	ds_read_b128 v[244:247], v222 offset:22528
	ds_read_b128 v[248:251], v222 offset:23552
	global_load_lds_dwordx4 v[194:195], off
	s_add_i32 m0, s65, 0x2000
	s_add_u32 s70, s40, 0x20000
	v_lshl_add_u64 v[196:197], s[40:41], 0, v[164:165]
	s_addc_u32 s71, s41, 0
	s_add_i32 s37, s37, s20
	global_load_lds_dwordx4 v[196:197], off
	v_lshl_add_u64 v[170:171], s[70:71], 0, v[162:163]
	s_mov_b32 m0, s37
	v_lshl_add_u64 v[198:199], s[68:69], 0, v[178:179]
	global_load_lds_dwordx4 v[170:171], off
	v_lshl_add_u64 v[170:171], s[70:71], 0, v[164:165]
	s_add_i32 m0, s37, 0x2000
	v_lshl_add_u64 v[200:201], s[68:69], 0, v[180:181]
	global_load_lds_dwordx4 v[170:171], off
	s_mov_b32 m0, s21
	s_nop 0
	global_load_lds_dwordx4 v[198:199], off
	s_mov_b32 m0, s22
	s_nop 0
	global_load_lds_dwordx4 v[200:201], off
	s_waitcnt vmcnt(8) lgkmcnt(0)
	s_barrier
	s_setprio 1
	v_mfma_scale_f32_16x16x128_f8f6f4 v[62:65], v[26:33], v[202:209], 0, v183, v169 op_sel_hi:[0,0,0]
	v_mfma_scale_f32_16x16x128_f8f6f4 v[58:61], v[18:25], v[202:209], 0, v183, v169 op_sel_hi:[0,0,0]
	v_mfma_scale_f32_16x16x128_f8f6f4 v[54:57], v[26:33], v[210:217], 0, v183, v169 op_sel_hi:[0,0,0]
	v_mfma_scale_f32_16x16x128_f8f6f4 v[50:53], v[18:25], v[210:217], 0, v183, v169 op_sel_hi:[0,0,0]
	v_mfma_scale_f32_16x16x128_f8f6f4 v[46:49], v[26:33], v[236:243], 0, v183, v169 op_sel_hi:[0,0,0]
	v_mfma_scale_f32_16x16x128_f8f6f4 v[42:45], v[18:25], v[236:243], 0, v183, v169 op_sel_hi:[0,0,0]
	v_mfma_scale_f32_16x16x128_f8f6f4 v[38:41], v[26:33], v[244:251], 0, v183, v169 op_sel_hi:[0,0,0]
	v_mfma_scale_f32_16x16x128_f8f6f4 v[34:37], v[18:25], v[244:251], 0, v183, v169 op_sel_hi:[0,0,0]
	s_setprio 0
	s_setprio 1
	v_mfma_scale_f32_16x16x128_f8f6f4 v[126:129], v[10:17], v[202:209], 0, v183, v169 op_sel_hi:[0,0,0]
	v_mfma_scale_f32_16x16x128_f8f6f4 v[122:125], v[2:9], v[202:209], 0, v183, v169 op_sel_hi:[0,0,0]
	v_mfma_scale_f32_16x16x128_f8f6f4 v[118:121], v[10:17], v[210:217], 0, v183, v169 op_sel_hi:[0,0,0]
	v_mfma_scale_f32_16x16x128_f8f6f4 v[114:117], v[2:9], v[210:217], 0, v183, v169 op_sel_hi:[0,0,0]
	v_mfma_scale_f32_16x16x128_f8f6f4 v[110:113], v[10:17], v[236:243], 0, v183, v169 op_sel_hi:[0,0,0]
	v_mfma_scale_f32_16x16x128_f8f6f4 v[106:109], v[2:9], v[236:243], 0, v183, v169 op_sel_hi:[0,0,0]
	v_mfma_scale_f32_16x16x128_f8f6f4 v[102:105], v[10:17], v[244:251], 0, v183, v169 op_sel_hi:[0,0,0]
	v_mfma_scale_f32_16x16x128_f8f6f4 v[98:101], v[2:9], v[244:251], 0, v183, v169 op_sel_hi:[0,0,0]
	s_setprio 0
	s_barrier
	s_add_i32 s37, 0, 0x18000
	s_add_i32 s65, 0, 0x1c000
	v_add_u32_e32 v2, s37, v221
	v_add_u32_e32 v6, s65, v221
	ds_read_b128 v[26:29], v2
	ds_read_b128 v[30:33], v2 offset:1024
	ds_read_b128 v[18:21], v2 offset:2048
	ds_read_b128 v[22:25], v2 offset:3072
	ds_read_b128 v[10:13], v6
	ds_read_b128 v[14:17], v6 offset:1024
	ds_read_b128 v[2:5], v6 offset:2048
	ds_read_b128 v[6:9], v6 offset:3072
	s_add_u32 s68, s68, 0x20000
	s_addc_u32 s69, s69, 0
	s_mov_b32 m0, s23
	v_lshl_add_u64 v[170:171], s[68:69], 0, v[178:179]
	ds_read_b128 v[202:205], v222 offset:32768
	ds_read_b128 v[206:209], v222 offset:33792
	ds_read_b128 v[210:213], v222 offset:34816
	ds_read_b128 v[214:217], v222 offset:35840
	ds_read_b128 v[236:239], v222 offset:36864
	ds_read_b128 v[240:243], v222 offset:37888
	ds_read_b128 v[244:247], v222 offset:38912
	ds_read_b128 v[248:251], v222 offset:39936
	global_load_lds_dwordx4 v[170:171], off
	v_lshl_add_u64 v[170:171], s[68:69], 0, v[180:181]
	s_mov_b32 m0, s12
	s_nop 0
	global_load_lds_dwordx4 v[170:171], off
	s_waitcnt vmcnt(8) lgkmcnt(0)
	s_barrier
	s_setprio 1
	v_mfma_scale_f32_16x16x128_f8f6f4 v[94:97], v[26:33], v[202:209], v[94:97], v183, v169 op_sel_hi:[0,0,0]
	v_mfma_scale_f32_16x16x128_f8f6f4 v[90:93], v[18:25], v[202:209], v[90:93], v183, v169 op_sel_hi:[0,0,0]
	v_mfma_scale_f32_16x16x128_f8f6f4 v[86:89], v[26:33], v[210:217], v[86:89], v183, v169 op_sel_hi:[0,0,0]
	v_mfma_scale_f32_16x16x128_f8f6f4 v[82:85], v[18:25], v[210:217], v[82:85], v183, v169 op_sel_hi:[0,0,0]
	v_mfma_scale_f32_16x16x128_f8f6f4 v[78:81], v[26:33], v[236:243], v[78:81], v183, v169 op_sel_hi:[0,0,0]
	v_mfma_scale_f32_16x16x128_f8f6f4 v[74:77], v[18:25], v[236:243], v[74:77], v183, v169 op_sel_hi:[0,0,0]
	v_mfma_scale_f32_16x16x128_f8f6f4 v[70:73], v[26:33], v[244:251], v[70:73], v183, v169 op_sel_hi:[0,0,0]
	v_mfma_scale_f32_16x16x128_f8f6f4 v[66:69], v[18:25], v[244:251], v[66:69], v183, v169 op_sel_hi:[0,0,0]
	s_setprio 0
	s_setprio 1
	v_mfma_scale_f32_16x16x128_f8f6f4 v[158:161], v[10:17], v[202:209], v[158:161], v183, v169 op_sel_hi:[0,0,0]
	v_mfma_scale_f32_16x16x128_f8f6f4 v[154:157], v[2:9], v[202:209], v[154:157], v183, v169 op_sel_hi:[0,0,0]
	v_mfma_scale_f32_16x16x128_f8f6f4 v[150:153], v[10:17], v[210:217], v[150:153], v183, v169 op_sel_hi:[0,0,0]
	v_mfma_scale_f32_16x16x128_f8f6f4 v[146:149], v[2:9], v[210:217], v[146:149], v183, v169 op_sel_hi:[0,0,0]
	v_mfma_scale_f32_16x16x128_f8f6f4 v[142:145], v[10:17], v[236:243], v[142:145], v183, v169 op_sel_hi:[0,0,0]
	v_mfma_scale_f32_16x16x128_f8f6f4 v[138:141], v[2:9], v[236:243], v[138:141], v183, v169 op_sel_hi:[0,0,0]
	v_mfma_scale_f32_16x16x128_f8f6f4 v[134:137], v[10:17], v[244:251], v[134:137], v183, v169 op_sel_hi:[0,0,0]
	v_mfma_scale_f32_16x16x128_f8f6f4 v[130:133], v[2:9], v[244:251], v[130:133], v183, v169 op_sel_hi:[0,0,0]
	s_setprio 0
	s_barrier
	s_add_i32 s37, s37, s20
	v_lshl_add_u64 v[170:171], v[194:195], 0, s[56:57]
	s_mov_b32 m0, s37
	ds_read_b128 v[202:205], v222 offset:49152
	ds_read_b128 v[206:209], v222 offset:50176
	ds_read_b128 v[210:213], v222 offset:51200
	ds_read_b128 v[214:217], v222 offset:52224
	ds_read_b128 v[236:239], v222 offset:53248
	ds_read_b128 v[240:243], v222 offset:54272
	ds_read_b128 v[244:247], v222 offset:55296
	ds_read_b128 v[248:251], v222 offset:56320
	global_load_lds_dwordx4 v[170:171], off
	s_add_i32 m0, s37, 0x2000
	s_add_u32 s40, s40, 0x20080
	v_lshl_add_u64 v[170:171], v[196:197], 0, s[56:57]
	s_addc_u32 s41, s41, 0
	s_add_i32 s37, s65, s20
	global_load_lds_dwordx4 v[170:171], off
	v_lshl_add_u64 v[170:171], s[40:41], 0, v[162:163]
	s_mov_b32 m0, s37
	s_nop 0
	global_load_lds_dwordx4 v[170:171], off
	v_lshl_add_u64 v[170:171], s[40:41], 0, v[164:165]
	s_add_i32 m0, s37, 0x2000
	s_nop 0
	global_load_lds_dwordx4 v[170:171], off
	v_lshl_add_u64 v[170:171], v[198:199], 0, s[56:57]
	s_mov_b32 m0, s92
	s_nop 0
	global_load_lds_dwordx4 v[170:171], off
	v_lshl_add_u64 v[170:171], v[200:201], 0, s[56:57]
	s_mov_b32 m0, s93
	s_nop 0
	global_load_lds_dwordx4 v[170:171], off
	s_waitcnt vmcnt(8) lgkmcnt(0)
	s_barrier
	s_setprio 1
	v_mfma_scale_f32_16x16x128_f8f6f4 v[62:65], v[26:33], v[202:209], v[62:65], v183, v169 op_sel_hi:[0,0,0]
	v_mfma_scale_f32_16x16x128_f8f6f4 v[58:61], v[18:25], v[202:209], v[58:61], v183, v169 op_sel_hi:[0,0,0]
	v_mfma_scale_f32_16x16x128_f8f6f4 v[54:57], v[26:33], v[210:217], v[54:57], v183, v169 op_sel_hi:[0,0,0]
	v_mfma_scale_f32_16x16x128_f8f6f4 v[50:53], v[18:25], v[210:217], v[50:53], v183, v169 op_sel_hi:[0,0,0]
	v_mfma_scale_f32_16x16x128_f8f6f4 v[46:49], v[26:33], v[236:243], v[46:49], v183, v169 op_sel_hi:[0,0,0]
	v_mfma_scale_f32_16x16x128_f8f6f4 v[42:45], v[18:25], v[236:243], v[42:45], v183, v169 op_sel_hi:[0,0,0]
	v_mfma_scale_f32_16x16x128_f8f6f4 v[38:41], v[26:33], v[244:251], v[38:41], v183, v169 op_sel_hi:[0,0,0]
	v_mfma_scale_f32_16x16x128_f8f6f4 v[34:37], v[18:25], v[244:251], v[34:37], v183, v169 op_sel_hi:[0,0,0]
	s_setprio 0
	s_setprio 1
	v_mfma_scale_f32_16x16x128_f8f6f4 v[126:129], v[10:17], v[202:209], v[126:129], v183, v169 op_sel_hi:[0,0,0]
	v_mfma_scale_f32_16x16x128_f8f6f4 v[122:125], v[2:9], v[202:209], v[122:125], v183, v169 op_sel_hi:[0,0,0]
	v_mfma_scale_f32_16x16x128_f8f6f4 v[118:121], v[10:17], v[210:217], v[118:121], v183, v169 op_sel_hi:[0,0,0]
	v_mfma_scale_f32_16x16x128_f8f6f4 v[114:117], v[2:9], v[210:217], v[114:117], v183, v169 op_sel_hi:[0,0,0]
	v_mfma_scale_f32_16x16x128_f8f6f4 v[110:113], v[10:17], v[236:243], v[110:113], v183, v169 op_sel_hi:[0,0,0]
	v_mfma_scale_f32_16x16x128_f8f6f4 v[106:109], v[2:9], v[236:243], v[106:109], v183, v169 op_sel_hi:[0,0,0]
	v_mfma_scale_f32_16x16x128_f8f6f4 v[102:105], v[10:17], v[244:251], v[102:105], v183, v169 op_sel_hi:[0,0,0]
	v_mfma_scale_f32_16x16x128_f8f6f4 v[98:101], v[2:9], v[244:251], v[98:101], v183, v169 op_sel_hi:[0,0,0]
	s_setprio 0
	s_barrier
	s_add_u32 s16, s16, 0x100
	s_addc_u32 s19, s19, 0
	s_add_u32 s38, s38, 0x100
	s_addc_u32 s39, s39, 0
	s_cmp_ge_i32 s27, s74
	s_mov_b32 s37, s27
	s_cbranch_scc0 .LBB0_1016
	s_branch .Lpeelexitph9
.LBB0_1016:
	s_add_i32 s27, s37, 2
	s_add_u32 s40, s38, 0xfffe0080
	s_addc_u32 s41, s39, -1
	s_add_i32 s65, 0, 0x10000
	s_cmp_eq_u32 s95, s37
	s_cselect_b32 s69, s0, s41
	s_cselect_b32 s68, s1, s40
	s_cselect_b32 s41, s8, s19
	s_cselect_b32 s40, s11, s16
	s_add_i32 s37, 0, 0x14000
	v_add_u32_e32 v2, s65, v221
	v_add_u32_e32 v6, s37, v221
	ds_read_b128 v[26:29], v2
	ds_read_b128 v[30:33], v2 offset:1024
	ds_read_b128 v[18:21], v2 offset:2048
	ds_read_b128 v[22:25], v2 offset:3072
	ds_read_b128 v[10:13], v6
	ds_read_b128 v[14:17], v6 offset:1024
	ds_read_b128 v[2:5], v6 offset:2048
	ds_read_b128 v[6:9], v6 offset:3072
	v_lshl_add_u64 v[170:171], s[38:39], 0, v[192:193]
	s_add_i32 m0, s21, 0xc000
	ds_read_b128 v[194:197], v222
	ds_read_b128 v[198:201], v222 offset:1024
	ds_read_b128 v[202:205], v222 offset:2048
	ds_read_b128 v[206:209], v222 offset:3072
	ds_read_b128 v[210:213], v222 offset:4096
	ds_read_b128 v[214:217], v222 offset:5120
	ds_read_b128 v[236:239], v222 offset:6144
	ds_read_b128 v[240:243], v222 offset:7168
	global_load_lds_dwordx4 v[170:171], off
	v_lshl_add_u64 v[170:171], s[38:39], 0, v[190:191]
	s_add_i32 m0, s21, 0xe000
	s_nop 0
	global_load_lds_dwordx4 v[170:171], off
	s_waitcnt vmcnt(8) lgkmcnt(0)
	s_barrier
	s_setprio 1
	v_mfma_scale_f32_16x16x128_f8f6f4 v[94:97], v[26:33], v[194:201], v[94:97], v183, v169 op_sel_hi:[0,0,0]
	v_mfma_scale_f32_16x16x128_f8f6f4 v[90:93], v[18:25], v[194:201], v[90:93], v183, v169 op_sel_hi:[0,0,0]
	v_mfma_scale_f32_16x16x128_f8f6f4 v[86:89], v[26:33], v[202:209], v[86:89], v183, v169 op_sel_hi:[0,0,0]
	v_mfma_scale_f32_16x16x128_f8f6f4 v[82:85], v[18:25], v[202:209], v[82:85], v183, v169 op_sel_hi:[0,0,0]
	v_mfma_scale_f32_16x16x128_f8f6f4 v[78:81], v[26:33], v[210:217], v[78:81], v183, v169 op_sel_hi:[0,0,0]
	v_mfma_scale_f32_16x16x128_f8f6f4 v[74:77], v[18:25], v[210:217], v[74:77], v183, v169 op_sel_hi:[0,0,0]
	v_mfma_scale_f32_16x16x128_f8f6f4 v[70:73], v[26:33], v[236:243], v[70:73], v183, v169 op_sel_hi:[0,0,0]
	v_mfma_scale_f32_16x16x128_f8f6f4 v[66:69], v[18:25], v[236:243], v[66:69], v183, v169 op_sel_hi:[0,0,0]
	s_setprio 0
	s_setprio 1
	v_mfma_scale_f32_16x16x128_f8f6f4 v[158:161], v[10:17], v[194:201], v[158:161], v183, v169 op_sel_hi:[0,0,0]
	v_mfma_scale_f32_16x16x128_f8f6f4 v[154:157], v[2:9], v[194:201], v[154:157], v183, v169 op_sel_hi:[0,0,0]
	v_mfma_scale_f32_16x16x128_f8f6f4 v[150:153], v[10:17], v[202:209], v[150:153], v183, v169 op_sel_hi:[0,0,0]
	v_mfma_scale_f32_16x16x128_f8f6f4 v[146:149], v[2:9], v[202:209], v[146:149], v183, v169 op_sel_hi:[0,0,0]
	v_mfma_scale_f32_16x16x128_f8f6f4 v[142:145], v[10:17], v[210:217], v[142:145], v183, v169 op_sel_hi:[0,0,0]
	v_mfma_scale_f32_16x16x128_f8f6f4 v[138:141], v[2:9], v[210:217], v[138:141], v183, v169 op_sel_hi:[0,0,0]
	v_mfma_scale_f32_16x16x128_f8f6f4 v[134:137], v[10:17], v[236:243], v[134:137], v183, v169 op_sel_hi:[0,0,0]
	v_mfma_scale_f32_16x16x128_f8f6f4 v[130:133], v[2:9], v[236:243], v[130:133], v183, v169 op_sel_hi:[0,0,0]
	s_setprio 0
	s_barrier
	s_add_i32 s65, s65, s20
	v_lshl_add_u64 v[194:195], s[40:41], 0, v[162:163]
	s_mov_b32 m0, s65
	ds_read_b128 v[202:205], v222 offset:16384
	ds_read_b128 v[206:209], v222 offset:17408
	ds_read_b128 v[210:213], v222 offset:18432
	ds_read_b128 v[214:217], v222 offset:19456
	ds_read_b128 v[236:239], v222 offset:20480
	ds_read_b128 v[240:243], v222 offset:21504
	ds_read_b128 v[244:247], v222 offset:22528
	ds_read_b128 v[248:251], v222 offset:23552
	global_load_lds_dwordx4 v[194:195], off
	s_add_i32 m0, s65, 0x2000
	s_add_u32 s70, s40, 0x20000
	v_lshl_add_u64 v[196:197], s[40:41], 0, v[164:165]
	s_addc_u32 s71, s41, 0
	s_add_i32 s37, s37, s20
	global_load_lds_dwordx4 v[196:197], off
	v_lshl_add_u64 v[170:171], s[70:71], 0, v[162:163]
	s_mov_b32 m0, s37
	v_lshl_add_u64 v[198:199], s[68:69], 0, v[178:179]
	global_load_lds_dwordx4 v[170:171], off
	v_lshl_add_u64 v[170:171], s[70:71], 0, v[164:165]
	s_add_i32 m0, s37, 0x2000
	v_lshl_add_u64 v[200:201], s[68:69], 0, v[180:181]
	global_load_lds_dwordx4 v[170:171], off
	s_mov_b32 m0, s21
	s_nop 0
	global_load_lds_dwordx4 v[198:199], off
	s_mov_b32 m0, s22
	s_nop 0
	global_load_lds_dwordx4 v[200:201], off
	s_waitcnt vmcnt(8) lgkmcnt(0)
	s_barrier
	s_setprio 1
	v_mfma_scale_f32_16x16x128_f8f6f4 v[62:65], v[26:33], v[202:209], v[62:65], v183, v169 op_sel_hi:[0,0,0]
	v_mfma_scale_f32_16x16x128_f8f6f4 v[58:61], v[18:25], v[202:209], v[58:61], v183, v169 op_sel_hi:[0,0,0]
	v_mfma_scale_f32_16x16x128_f8f6f4 v[54:57], v[26:33], v[210:217], v[54:57], v183, v169 op_sel_hi:[0,0,0]
	v_mfma_scale_f32_16x16x128_f8f6f4 v[50:53], v[18:25], v[210:217], v[50:53], v183, v169 op_sel_hi:[0,0,0]
	v_mfma_scale_f32_16x16x128_f8f6f4 v[46:49], v[26:33], v[236:243], v[46:49], v183, v169 op_sel_hi:[0,0,0]
	v_mfma_scale_f32_16x16x128_f8f6f4 v[42:45], v[18:25], v[236:243], v[42:45], v183, v169 op_sel_hi:[0,0,0]
	v_mfma_scale_f32_16x16x128_f8f6f4 v[38:41], v[26:33], v[244:251], v[38:41], v183, v169 op_sel_hi:[0,0,0]
	v_mfma_scale_f32_16x16x128_f8f6f4 v[34:37], v[18:25], v[244:251], v[34:37], v183, v169 op_sel_hi:[0,0,0]
	s_setprio 0
	s_setprio 1
	v_mfma_scale_f32_16x16x128_f8f6f4 v[126:129], v[10:17], v[202:209], v[126:129], v183, v169 op_sel_hi:[0,0,0]
	v_mfma_scale_f32_16x16x128_f8f6f4 v[122:125], v[2:9], v[202:209], v[122:125], v183, v169 op_sel_hi:[0,0,0]
	v_mfma_scale_f32_16x16x128_f8f6f4 v[118:121], v[10:17], v[210:217], v[118:121], v183, v169 op_sel_hi:[0,0,0]
	v_mfma_scale_f32_16x16x128_f8f6f4 v[114:117], v[2:9], v[210:217], v[114:117], v183, v169 op_sel_hi:[0,0,0]
	v_mfma_scale_f32_16x16x128_f8f6f4 v[110:113], v[10:17], v[236:243], v[110:113], v183, v169 op_sel_hi:[0,0,0]
	v_mfma_scale_f32_16x16x128_f8f6f4 v[106:109], v[2:9], v[236:243], v[106:109], v183, v169 op_sel_hi:[0,0,0]
	v_mfma_scale_f32_16x16x128_f8f6f4 v[102:105], v[10:17], v[244:251], v[102:105], v183, v169 op_sel_hi:[0,0,0]
	v_mfma_scale_f32_16x16x128_f8f6f4 v[98:101], v[2:9], v[244:251], v[98:101], v183, v169 op_sel_hi:[0,0,0]
	s_setprio 0
	s_barrier
	s_add_i32 s37, 0, 0x18000
	s_add_i32 s65, 0, 0x1c000
	v_add_u32_e32 v2, s37, v221
	v_add_u32_e32 v6, s65, v221
	ds_read_b128 v[26:29], v2
	ds_read_b128 v[30:33], v2 offset:1024
	ds_read_b128 v[18:21], v2 offset:2048
	ds_read_b128 v[22:25], v2 offset:3072
	ds_read_b128 v[10:13], v6
	ds_read_b128 v[14:17], v6 offset:1024
	ds_read_b128 v[2:5], v6 offset:2048
	ds_read_b128 v[6:9], v6 offset:3072
	s_add_u32 s68, s68, 0x20000
	s_addc_u32 s69, s69, 0
	s_mov_b32 m0, s23
	v_lshl_add_u64 v[170:171], s[68:69], 0, v[178:179]
	ds_read_b128 v[202:205], v222 offset:32768
	ds_read_b128 v[206:209], v222 offset:33792
	ds_read_b128 v[210:213], v222 offset:34816
	ds_read_b128 v[214:217], v222 offset:35840
	ds_read_b128 v[236:239], v222 offset:36864
	ds_read_b128 v[240:243], v222 offset:37888
	ds_read_b128 v[244:247], v222 offset:38912
	ds_read_b128 v[248:251], v222 offset:39936
	global_load_lds_dwordx4 v[170:171], off
	v_lshl_add_u64 v[170:171], s[68:69], 0, v[180:181]
	s_mov_b32 m0, s12
	s_nop 0
	global_load_lds_dwordx4 v[170:171], off
	s_waitcnt vmcnt(8) lgkmcnt(0)
	s_barrier
	s_setprio 1
	v_mfma_scale_f32_16x16x128_f8f6f4 v[94:97], v[26:33], v[202:209], v[94:97], v183, v169 op_sel_hi:[0,0,0]
	v_mfma_scale_f32_16x16x128_f8f6f4 v[90:93], v[18:25], v[202:209], v[90:93], v183, v169 op_sel_hi:[0,0,0]
	v_mfma_scale_f32_16x16x128_f8f6f4 v[86:89], v[26:33], v[210:217], v[86:89], v183, v169 op_sel_hi:[0,0,0]
	v_mfma_scale_f32_16x16x128_f8f6f4 v[82:85], v[18:25], v[210:217], v[82:85], v183, v169 op_sel_hi:[0,0,0]
	v_mfma_scale_f32_16x16x128_f8f6f4 v[78:81], v[26:33], v[236:243], v[78:81], v183, v169 op_sel_hi:[0,0,0]
	v_mfma_scale_f32_16x16x128_f8f6f4 v[74:77], v[18:25], v[236:243], v[74:77], v183, v169 op_sel_hi:[0,0,0]
	v_mfma_scale_f32_16x16x128_f8f6f4 v[70:73], v[26:33], v[244:251], v[70:73], v183, v169 op_sel_hi:[0,0,0]
	v_mfma_scale_f32_16x16x128_f8f6f4 v[66:69], v[18:25], v[244:251], v[66:69], v183, v169 op_sel_hi:[0,0,0]
	s_setprio 0
	s_setprio 1
	v_mfma_scale_f32_16x16x128_f8f6f4 v[158:161], v[10:17], v[202:209], v[158:161], v183, v169 op_sel_hi:[0,0,0]
	v_mfma_scale_f32_16x16x128_f8f6f4 v[154:157], v[2:9], v[202:209], v[154:157], v183, v169 op_sel_hi:[0,0,0]
	v_mfma_scale_f32_16x16x128_f8f6f4 v[150:153], v[10:17], v[210:217], v[150:153], v183, v169 op_sel_hi:[0,0,0]
	v_mfma_scale_f32_16x16x128_f8f6f4 v[146:149], v[2:9], v[210:217], v[146:149], v183, v169 op_sel_hi:[0,0,0]
	v_mfma_scale_f32_16x16x128_f8f6f4 v[142:145], v[10:17], v[236:243], v[142:145], v183, v169 op_sel_hi:[0,0,0]
	v_mfma_scale_f32_16x16x128_f8f6f4 v[138:141], v[2:9], v[236:243], v[138:141], v183, v169 op_sel_hi:[0,0,0]
	v_mfma_scale_f32_16x16x128_f8f6f4 v[134:137], v[10:17], v[244:251], v[134:137], v183, v169 op_sel_hi:[0,0,0]
	v_mfma_scale_f32_16x16x128_f8f6f4 v[130:133], v[2:9], v[244:251], v[130:133], v183, v169 op_sel_hi:[0,0,0]
	s_setprio 0
	s_barrier
	s_add_i32 s37, s37, s20
	v_lshl_add_u64 v[170:171], v[194:195], 0, s[56:57]
	s_mov_b32 m0, s37
	ds_read_b128 v[202:205], v222 offset:49152
	ds_read_b128 v[206:209], v222 offset:50176
	ds_read_b128 v[210:213], v222 offset:51200
	ds_read_b128 v[214:217], v222 offset:52224
	ds_read_b128 v[236:239], v222 offset:53248
	ds_read_b128 v[240:243], v222 offset:54272
	ds_read_b128 v[244:247], v222 offset:55296
	ds_read_b128 v[248:251], v222 offset:56320
	global_load_lds_dwordx4 v[170:171], off
	s_add_i32 m0, s37, 0x2000
	s_add_u32 s40, s40, 0x20080
	v_lshl_add_u64 v[170:171], v[196:197], 0, s[56:57]
	s_addc_u32 s41, s41, 0
	s_add_i32 s37, s65, s20
	global_load_lds_dwordx4 v[170:171], off
	v_lshl_add_u64 v[170:171], s[40:41], 0, v[162:163]
	s_mov_b32 m0, s37
	s_nop 0
	global_load_lds_dwordx4 v[170:171], off
	v_lshl_add_u64 v[170:171], s[40:41], 0, v[164:165]
	s_add_i32 m0, s37, 0x2000
	s_nop 0
	global_load_lds_dwordx4 v[170:171], off
	v_lshl_add_u64 v[170:171], v[198:199], 0, s[56:57]
	s_mov_b32 m0, s92
	s_nop 0
	global_load_lds_dwordx4 v[170:171], off
	v_lshl_add_u64 v[170:171], v[200:201], 0, s[56:57]
	s_mov_b32 m0, s93
	s_nop 0
	global_load_lds_dwordx4 v[170:171], off
	s_waitcnt vmcnt(8) lgkmcnt(0)
	s_barrier
	s_setprio 1
	v_mfma_scale_f32_16x16x128_f8f6f4 v[62:65], v[26:33], v[202:209], v[62:65], v183, v169 op_sel_hi:[0,0,0]
	v_mfma_scale_f32_16x16x128_f8f6f4 v[58:61], v[18:25], v[202:209], v[58:61], v183, v169 op_sel_hi:[0,0,0]
	v_mfma_scale_f32_16x16x128_f8f6f4 v[54:57], v[26:33], v[210:217], v[54:57], v183, v169 op_sel_hi:[0,0,0]
	v_mfma_scale_f32_16x16x128_f8f6f4 v[50:53], v[18:25], v[210:217], v[50:53], v183, v169 op_sel_hi:[0,0,0]
	v_mfma_scale_f32_16x16x128_f8f6f4 v[46:49], v[26:33], v[236:243], v[46:49], v183, v169 op_sel_hi:[0,0,0]
	v_mfma_scale_f32_16x16x128_f8f6f4 v[42:45], v[18:25], v[236:243], v[42:45], v183, v169 op_sel_hi:[0,0,0]
	v_mfma_scale_f32_16x16x128_f8f6f4 v[38:41], v[26:33], v[244:251], v[38:41], v183, v169 op_sel_hi:[0,0,0]
	v_mfma_scale_f32_16x16x128_f8f6f4 v[34:37], v[18:25], v[244:251], v[34:37], v183, v169 op_sel_hi:[0,0,0]
	s_setprio 0
	s_setprio 1
	v_mfma_scale_f32_16x16x128_f8f6f4 v[126:129], v[10:17], v[202:209], v[126:129], v183, v169 op_sel_hi:[0,0,0]
	v_mfma_scale_f32_16x16x128_f8f6f4 v[122:125], v[2:9], v[202:209], v[122:125], v183, v169 op_sel_hi:[0,0,0]
	v_mfma_scale_f32_16x16x128_f8f6f4 v[118:121], v[10:17], v[210:217], v[118:121], v183, v169 op_sel_hi:[0,0,0]
	v_mfma_scale_f32_16x16x128_f8f6f4 v[114:117], v[2:9], v[210:217], v[114:117], v183, v169 op_sel_hi:[0,0,0]
	v_mfma_scale_f32_16x16x128_f8f6f4 v[110:113], v[10:17], v[236:243], v[110:113], v183, v169 op_sel_hi:[0,0,0]
	v_mfma_scale_f32_16x16x128_f8f6f4 v[106:109], v[2:9], v[236:243], v[106:109], v183, v169 op_sel_hi:[0,0,0]
	v_mfma_scale_f32_16x16x128_f8f6f4 v[102:105], v[10:17], v[244:251], v[102:105], v183, v169 op_sel_hi:[0,0,0]
	v_mfma_scale_f32_16x16x128_f8f6f4 v[98:101], v[2:9], v[244:251], v[98:101], v183, v169 op_sel_hi:[0,0,0]
	s_setprio 0
	s_barrier
	s_add_u32 s16, s16, 0x100
	s_addc_u32 s19, s19, 0
	s_add_u32 s38, s38, 0x100
	s_addc_u32 s39, s39, 0
	s_cmp_ge_i32 s27, s74
	s_mov_b32 s37, s27
	s_cbranch_scc0 .LBB0_1016

.LBB0_1331:
	v_mfma_f32_32x32x16_bf16 v[50:65], v[138:141], v[98:101], 0
	v_lshl_add_u32 v199, s92, 13, v240
	ds_read_b64_tr_b16 v[162:163], v199 offset:40960
	ds_read_b64_tr_b16 v[164:165], v199 offset:41472
	v_add_f32_e32 v34, v82, v83
	v_add_f32_e32 v35, v84, v85
	v_add_f32_e32 v34, v34, v35
	v_cvt_pk_bf16_f32 v154, v82, v83
	v_cvt_pk_bf16_f32 v155, v84, v85
	ds_read_b64_tr_b16 v[158:159], v199 offset:45056
	ds_read_b64_tr_b16 v[160:161], v199 offset:45568
	v_add_f32_e32 v35, v86, v87
	v_add_f32_e32 v36, v88, v89
	v_add_f32_e32 v35, v35, v36
	v_add_f32_e32 v82, v35, v34
	v_mfma_f32_32x32x16_bf16 v[34:49], v[130:133], v[98:101], 0
	v_cvt_pk_bf16_f32 v156, v86, v87
	v_cvt_pk_bf16_f32 v157, v88, v89
	ds_read_b128 v[170:173], v197 offset:6144
	ds_read_b128 v[174:177], v197 offset:6656
	ds_read_b64_tr_b16 v[150:151], v199 offset:41984
	ds_read_b64_tr_b16 v[152:153], v199 offset:42496
	v_mfma_f32_32x32x16_bf16 v[50:65], v[134:137], v[102:105], v[50:65]
	v_add_f32_e32 v83, v90, v91
	v_add_f32_e32 v84, v92, v93
	v_add_f32_e32 v83, v83, v84
	v_add_f32_e32 v82, v83, v82
	v_cvt_pk_bf16_f32 v142, v90, v91
	v_cvt_pk_bf16_f32 v143, v92, v93
	ds_read_b64_tr_b16 v[146:147], v199 offset:46080
	ds_read_b64_tr_b16 v[148:149], v199 offset:46592
	v_mfma_f32_32x32x16_bf16 v[34:49], v[126:129], v[102:105], v[34:49]
	v_add_f32_e32 v83, v94, v95
	v_add_f32_e32 v84, v96, v97
	v_add_f32_e32 v83, v83, v84
	v_add_f32_e32 v82, v83, v82
	v_cvt_pk_bf16_f32 v144, v94, v95
	v_cvt_pk_bf16_f32 v145, v96, v97
	ds_read_b128 v[248:251], v197 offset:8192
	ds_read_b128 v[232:235], v197 offset:8704
	ds_read_b64_tr_b16 v[90:91], v199 offset:43008
	ds_read_b64_tr_b16 v[92:93], v199 offset:43520
	v_mfma_f32_32x32x16_bf16 v[50:65], v[122:125], v[106:109], v[50:65]
	v_add_f32_e32 v83, v66, v67
	v_add_f32_e32 v84, v68, v69
	v_add_f32_e32 v83, v83, v84
	v_add_f32_e32 v84, v83, v82
	v_cvt_pk_bf16_f32 v82, v66, v67
	v_cvt_pk_bf16_f32 v83, v68, v69
	ds_read_b64_tr_b16 v[86:87], v199 offset:47104
	ds_read_b64_tr_b16 v[88:89], v199 offset:47616
	v_mfma_f32_32x32x16_bf16 v[34:49], v[118:121], v[106:109], v[34:49]
	v_add_f32_e32 v66, v70, v71
	v_add_f32_e32 v67, v72, v73
	v_add_f32_e32 v66, v66, v67
	v_add_f32_e32 v66, v66, v84
	v_cvt_pk_bf16_f32 v84, v70, v71
	v_cvt_pk_bf16_f32 v85, v72, v73
	ds_read_b64_tr_b16 v[70:71], v199 offset:44032
	ds_read_b64_tr_b16 v[72:73], v199 offset:44544
	s_waitcnt lgkmcnt(13)
	v_mfma_f32_32x32x16_bf16 v[50:65], v[170:173], v[110:113], v[50:65]
	v_add_f32_e32 v67, v74, v75
	v_add_f32_e32 v68, v76, v77
	v_add_f32_e32 v67, v67, v68
	v_add_f32_e32 v68, v67, v66
	v_cvt_pk_bf16_f32 v66, v74, v75
	v_cvt_pk_bf16_f32 v67, v76, v77
	ds_read_b64_tr_b16 v[74:75], v199 offset:48128
	ds_read_b64_tr_b16 v[76:77], v199 offset:48640
	s_waitcnt lgkmcnt(14)
	v_mfma_f32_32x32x16_bf16 v[34:49], v[174:177], v[110:113], v[34:49]
	v_add_f32_e32 v69, v78, v79
	v_add_f32_e32 v94, v80, v81
	v_add_f32_e32 v69, v69, v94
	v_add_f32_e32 v94, v69, v68
	v_cvt_pk_bf16_f32 v68, v78, v79
	v_cvt_pk_bf16_f32 v69, v80, v81
	s_waitcnt lgkmcnt(9)
	v_mfma_f32_32x32x16_bf16 v[50:65], v[248:251], v[114:117], v[50:65]
	s_waitcnt lgkmcnt(8)
	v_mfma_f32_32x32x16_bf16 v[34:49], v[232:235], v[114:117], v[34:49]
	s_add_i32 s54, s44, 3
	s_cmp_lt_i32 s54, s71
	s_cselect_b64 s[52:53], -1, 0
	s_cbranch_scc0 .LBB0_1334
	s_ashr_i32 s55, s54, 31
	s_lshl_b64 s[58:59], s[54:55], 17
	s_add_i32 m0, s98, s66
	v_lshl_add_u64 v[78:79], v[212:213], 0, s[58:59]
	global_load_lds_dwordx4 v[78:79], off
	s_and_b64 vcc, exec, s[42:43]
	s_cbranch_vccnz .LBB0_1334
	s_lshl_b64 s[54:55], s[54:55], 11
	s_add_i32 m0, s98, s70
	v_lshl_add_u64 v[78:79], v[214:215], 0, s[54:55]
	global_load_lds_dwordx4 v[78:79], off

.Lpeelph12_0:
	s_add_i32 s66, s54, 2
	s_add_u32 s55, s52, 0xfffc0080
	s_addc_u32 s58, s53, -1
	s_add_i32 s68, 0, 0x10000
	s_cmp_eq_u32 s60, s54
	s_cselect_b32 s59, s41, s58
	s_cselect_b32 s58, s43, s55
	v_add_u32_e32 v144, s68, v147
	s_cselect_b32 s55, s62, s65
	s_cselect_b32 s54, s63, s64
	s_add_i32 s70, 0, 0x14000
	ds_read_b128 v[140:143], v144
	ds_read_b128 v[150:153], v144 offset:1024
	ds_read_b128 v[154:157], v144 offset:2048
	ds_read_b128 v[158:161], v144 offset:3072
	v_add_u32_e32 v144, s70, v147
	ds_read_b128 v[162:165], v144
	ds_read_b128 v[170:173], v144 offset:1024
	ds_read_b128 v[174:177], v144 offset:2048
	ds_read_b128 v[178:181], v144 offset:3072
	v_lshl_add_u64 v[144:145], s[52:53], 0, v[138:139]
	s_add_i32 m0, s16, 0xc000
	ds_read_b128 v[182:185], v149
	ds_read_b128 v[186:189], v149 offset:1024
	ds_read_b128 v[190:193], v149 offset:2048
	ds_read_b128 v[194:197], v149 offset:3072
	ds_read_b128 v[198:201], v149 offset:4096
	ds_read_b128 v[202:205], v149 offset:5120
	ds_read_b128 v[206:209], v149 offset:6144
	ds_read_b128 v[210:213], v149 offset:7168
	global_load_lds_dwordx4 v[144:145], off
	v_lshl_add_u64 v[144:145], s[52:53], 0, v[136:137]
	s_add_i32 m0, s16, 0xe000
	s_nop 0
	global_load_lds_dwordx4 v[144:145], off
	s_waitcnt vmcnt(8) lgkmcnt(0)
	s_barrier
	s_setprio 1
	v_mfma_f32_16x16x32_bf16 v[126:129], v[140:143], v[182:185], 0
	v_mfma_f32_16x16x32_bf16 v[122:125], v[154:157], v[182:185], 0
	v_mfma_f32_16x16x32_bf16 v[110:113], v[140:143], v[190:193], 0
	v_mfma_f32_16x16x32_bf16 v[106:109], v[154:157], v[190:193], 0
	v_mfma_f32_16x16x32_bf16 v[94:97], v[140:143], v[198:201], 0
	v_mfma_f32_16x16x32_bf16 v[90:93], v[154:157], v[198:201], 0
	v_mfma_f32_16x16x32_bf16 v[78:81], v[140:143], v[206:209], 0
	v_mfma_f32_16x16x32_bf16 v[74:77], v[154:157], v[206:209], 0
	v_mfma_f32_16x16x32_bf16 v[126:129], v[150:153], v[186:189], v[126:129]
	v_mfma_f32_16x16x32_bf16 v[122:125], v[158:161], v[186:189], v[122:125]
	v_mfma_f32_16x16x32_bf16 v[110:113], v[150:153], v[194:197], v[110:113]
	v_mfma_f32_16x16x32_bf16 v[106:109], v[158:161], v[194:197], v[106:109]
	v_mfma_f32_16x16x32_bf16 v[94:97], v[150:153], v[202:205], v[94:97]
	v_mfma_f32_16x16x32_bf16 v[90:93], v[158:161], v[202:205], v[90:93]
	v_mfma_f32_16x16x32_bf16 v[78:81], v[150:153], v[210:213], v[78:81]
	v_mfma_f32_16x16x32_bf16 v[74:77], v[158:161], v[210:213], v[74:77]
	s_setprio 0
	s_setprio 1
	v_mfma_f32_16x16x32_bf16 v[118:121], v[162:165], v[182:185], 0
	v_mfma_f32_16x16x32_bf16 v[114:117], v[174:177], v[182:185], 0
	v_mfma_f32_16x16x32_bf16 v[102:105], v[162:165], v[190:193], 0
	v_mfma_f32_16x16x32_bf16 v[98:101], v[174:177], v[190:193], 0
	v_mfma_f32_16x16x32_bf16 v[86:89], v[162:165], v[198:201], 0
	v_mfma_f32_16x16x32_bf16 v[82:85], v[174:177], v[198:201], 0
	v_mfma_f32_16x16x32_bf16 v[70:73], v[162:165], v[206:209], 0
	v_mfma_f32_16x16x32_bf16 v[66:69], v[174:177], v[206:209], 0
	v_mfma_f32_16x16x32_bf16 v[118:121], v[170:173], v[186:189], v[118:121]
	v_mfma_f32_16x16x32_bf16 v[114:117], v[178:181], v[186:189], v[114:117]
	v_mfma_f32_16x16x32_bf16 v[102:105], v[170:173], v[194:197], v[102:105]
	v_mfma_f32_16x16x32_bf16 v[98:101], v[178:181], v[194:197], v[98:101]
	v_mfma_f32_16x16x32_bf16 v[86:89], v[170:173], v[202:205], v[86:89]
	v_mfma_f32_16x16x32_bf16 v[82:85], v[178:181], v[202:205], v[82:85]
	v_mfma_f32_16x16x32_bf16 v[70:73], v[170:173], v[210:213], v[70:73]
	v_mfma_f32_16x16x32_bf16 v[66:69], v[178:181], v[210:213], v[66:69]
	s_setprio 0
	s_barrier
	s_add_i32 s68, s68, s15
	v_lshl_add_u64 v[144:145], s[54:55], 0, v[166:167]
	s_mov_b32 m0, s68
	ds_read_b128 v[182:185], v149 offset:16384
	ds_read_b128 v[186:189], v149 offset:17408
	ds_read_b128 v[190:193], v149 offset:18432
	ds_read_b128 v[194:197], v149 offset:19456
	ds_read_b128 v[198:201], v149 offset:20480
	ds_read_b128 v[202:205], v149 offset:21504
	ds_read_b128 v[206:209], v149 offset:22528
	ds_read_b128 v[210:213], v149 offset:23552
	global_load_lds_dwordx4 v[144:145], off
	s_add_i32 m0, s68, 0x2000
	s_add_u32 s68, s54, 0x40000
	v_lshl_add_u64 v[214:215], s[54:55], 0, v[130:131]
	s_addc_u32 s69, s55, 0
	s_add_i32 s70, s70, s15
	global_load_lds_dwordx4 v[214:215], off
	v_lshl_add_u64 v[216:217], s[68:69], 0, v[166:167]
	s_mov_b32 m0, s70
	v_lshl_add_u64 v[218:219], s[58:59], 0, v[134:135]
	global_load_lds_dwordx4 v[216:217], off
	v_lshl_add_u64 v[216:217], s[68:69], 0, v[130:131]
	s_add_i32 m0, s70, 0x2000
	s_nop 0
	global_load_lds_dwordx4 v[216:217], off
	v_lshl_add_u64 v[216:217], s[58:59], 0, v[132:133]
	s_mov_b32 m0, s16
	s_nop 0
	global_load_lds_dwordx4 v[216:217], off
	s_mov_b32 m0, s20
	s_nop 0
	global_load_lds_dwordx4 v[218:219], off
	s_waitcnt vmcnt(8) lgkmcnt(0)
	s_barrier
	s_setprio 1
	v_mfma_f32_16x16x32_bf16 v[62:65], v[140:143], v[182:185], 0
	v_mfma_f32_16x16x32_bf16 v[58:61], v[154:157], v[182:185], 0
	v_mfma_f32_16x16x32_bf16 v[46:49], v[140:143], v[190:193], 0
	v_mfma_f32_16x16x32_bf16 v[42:45], v[154:157], v[190:193], 0
	v_mfma_f32_16x16x32_bf16 v[30:33], v[140:143], v[198:201], 0
	v_mfma_f32_16x16x32_bf16 v[26:29], v[154:157], v[198:201], 0
	v_mfma_f32_16x16x32_bf16 v[14:17], v[140:143], v[206:209], 0
	v_mfma_f32_16x16x32_bf16 v[10:13], v[154:157], v[206:209], 0
	v_mfma_f32_16x16x32_bf16 v[62:65], v[150:153], v[186:189], v[62:65]
	v_mfma_f32_16x16x32_bf16 v[58:61], v[158:161], v[186:189], v[58:61]
	v_mfma_f32_16x16x32_bf16 v[46:49], v[150:153], v[194:197], v[46:49]
	v_mfma_f32_16x16x32_bf16 v[42:45], v[158:161], v[194:197], v[42:45]
	v_mfma_f32_16x16x32_bf16 v[30:33], v[150:153], v[202:205], v[30:33]
	v_mfma_f32_16x16x32_bf16 v[26:29], v[158:161], v[202:205], v[26:29]
	v_mfma_f32_16x16x32_bf16 v[14:17], v[150:153], v[210:213], v[14:17]
	v_mfma_f32_16x16x32_bf16 v[10:13], v[158:161], v[210:213], v[10:13]
	s_setprio 0
	s_setprio 1
	v_mfma_f32_16x16x32_bf16 v[54:57], v[162:165], v[182:185], 0
	v_mfma_f32_16x16x32_bf16 v[50:53], v[174:177], v[182:185], 0
	v_mfma_f32_16x16x32_bf16 v[38:41], v[162:165], v[190:193], 0
	v_mfma_f32_16x16x32_bf16 v[34:37], v[174:177], v[190:193], 0
	v_mfma_f32_16x16x32_bf16 v[22:25], v[162:165], v[198:201], 0
	v_mfma_f32_16x16x32_bf16 v[18:21], v[174:177], v[198:201], 0
	v_mfma_f32_16x16x32_bf16 v[6:9], v[162:165], v[206:209], 0
	v_mfma_f32_16x16x32_bf16 v[2:5], v[174:177], v[206:209], 0
	v_mfma_f32_16x16x32_bf16 v[54:57], v[170:173], v[186:189], v[54:57]
	v_mfma_f32_16x16x32_bf16 v[50:53], v[178:181], v[186:189], v[50:53]
	v_mfma_f32_16x16x32_bf16 v[38:41], v[170:173], v[194:197], v[38:41]
	v_mfma_f32_16x16x32_bf16 v[34:37], v[178:181], v[194:197], v[34:37]
	v_mfma_f32_16x16x32_bf16 v[22:25], v[170:173], v[202:205], v[22:25]
	v_mfma_f32_16x16x32_bf16 v[18:21], v[178:181], v[202:205], v[18:21]
	v_mfma_f32_16x16x32_bf16 v[6:9], v[170:173], v[210:213], v[6:9]
	v_mfma_f32_16x16x32_bf16 v[2:5], v[178:181], v[210:213], v[2:5]
	s_setprio 0
	s_barrier
	s_add_i32 s68, 0, 0x18000
	s_add_i32 s69, 0, 0x1c000
	v_add_u32_e32 v158, s68, v147
	v_add_u32_e32 v169, s69, v147
	ds_read_b128 v[140:143], v158
	ds_read_b128 v[150:153], v158 offset:1024
	ds_read_b128 v[154:157], v158 offset:2048
	ds_read_b128 v[158:161], v158 offset:3072
	ds_read_b128 v[162:165], v169
	ds_read_b128 v[170:173], v169 offset:1024
	ds_read_b128 v[174:177], v169 offset:2048
	ds_read_b128 v[178:181], v169 offset:3072
	s_add_u32 s58, s58, 0x40000
	s_addc_u32 s59, s59, 0
	s_mov_b32 m0, s21
	v_lshl_add_u64 v[220:221], s[58:59], 0, v[132:133]
	ds_read_b128 v[182:185], v149 offset:32768
	ds_read_b128 v[186:189], v149 offset:33792
	ds_read_b128 v[190:193], v149 offset:34816
	ds_read_b128 v[194:197], v149 offset:35840
	ds_read_b128 v[198:201], v149 offset:36864
	ds_read_b128 v[202:205], v149 offset:37888
	ds_read_b128 v[206:209], v149 offset:38912
	ds_read_b128 v[210:213], v149 offset:39936
	global_load_lds_dwordx4 v[220:221], off
	v_lshl_add_u64 v[220:221], s[58:59], 0, v[134:135]
	s_mov_b32 m0, s22
	s_nop 0
	global_load_lds_dwordx4 v[220:221], off
	s_waitcnt vmcnt(8) lgkmcnt(0)
	s_barrier
	s_setprio 1
	v_mfma_f32_16x16x32_bf16 v[126:129], v[140:143], v[182:185], v[126:129]
	v_mfma_f32_16x16x32_bf16 v[122:125], v[154:157], v[182:185], v[122:125]
	v_mfma_f32_16x16x32_bf16 v[110:113], v[140:143], v[190:193], v[110:113]
	v_mfma_f32_16x16x32_bf16 v[106:109], v[154:157], v[190:193], v[106:109]
	v_mfma_f32_16x16x32_bf16 v[94:97], v[140:143], v[198:201], v[94:97]
	v_mfma_f32_16x16x32_bf16 v[90:93], v[154:157], v[198:201], v[90:93]
	v_mfma_f32_16x16x32_bf16 v[78:81], v[140:143], v[206:209], v[78:81]
	v_mfma_f32_16x16x32_bf16 v[74:77], v[154:157], v[206:209], v[74:77]
	v_mfma_f32_16x16x32_bf16 v[126:129], v[150:153], v[186:189], v[126:129]
	v_mfma_f32_16x16x32_bf16 v[122:125], v[158:161], v[186:189], v[122:125]
	v_mfma_f32_16x16x32_bf16 v[110:113], v[150:153], v[194:197], v[110:113]
	v_mfma_f32_16x16x32_bf16 v[106:109], v[158:161], v[194:197], v[106:109]
	v_mfma_f32_16x16x32_bf16 v[94:97], v[150:153], v[202:205], v[94:97]
	v_mfma_f32_16x16x32_bf16 v[90:93], v[158:161], v[202:205], v[90:93]
	v_mfma_f32_16x16x32_bf16 v[78:81], v[150:153], v[210:213], v[78:81]
	v_mfma_f32_16x16x32_bf16 v[74:77], v[158:161], v[210:213], v[74:77]
	s_setprio 0
	s_setprio 1
	v_mfma_f32_16x16x32_bf16 v[118:121], v[162:165], v[182:185], v[118:121]
	v_mfma_f32_16x16x32_bf16 v[114:117], v[174:177], v[182:185], v[114:117]
	v_mfma_f32_16x16x32_bf16 v[102:105], v[162:165], v[190:193], v[102:105]
	v_mfma_f32_16x16x32_bf16 v[98:101], v[174:177], v[190:193], v[98:101]
	v_mfma_f32_16x16x32_bf16 v[86:89], v[162:165], v[198:201], v[86:89]
	v_mfma_f32_16x16x32_bf16 v[82:85], v[174:177], v[198:201], v[82:85]
	v_mfma_f32_16x16x32_bf16 v[70:73], v[162:165], v[206:209], v[70:73]
	v_mfma_f32_16x16x32_bf16 v[66:69], v[174:177], v[206:209], v[66:69]
	v_mfma_f32_16x16x32_bf16 v[118:121], v[170:173], v[186:189], v[118:121]
	v_mfma_f32_16x16x32_bf16 v[114:117], v[178:181], v[186:189], v[114:117]
	v_mfma_f32_16x16x32_bf16 v[102:105], v[170:173], v[194:197], v[102:105]
	v_mfma_f32_16x16x32_bf16 v[98:101], v[178:181], v[194:197], v[98:101]
	v_mfma_f32_16x16x32_bf16 v[86:89], v[170:173], v[202:205], v[86:89]
	v_mfma_f32_16x16x32_bf16 v[82:85], v[178:181], v[202:205], v[82:85]
	v_mfma_f32_16x16x32_bf16 v[70:73], v[170:173], v[210:213], v[70:73]
	v_mfma_f32_16x16x32_bf16 v[66:69], v[178:181], v[210:213], v[66:69]
	s_setprio 0
	s_barrier
	s_add_i32 s58, s68, s15
	v_lshl_add_u64 v[144:145], v[144:145], 0, s[56:57]
	s_mov_b32 m0, s58
	ds_read_b128 v[182:185], v149 offset:49152
	ds_read_b128 v[186:189], v149 offset:50176
	ds_read_b128 v[190:193], v149 offset:51200
	ds_read_b128 v[194:197], v149 offset:52224
	ds_read_b128 v[198:201], v149 offset:53248
	ds_read_b128 v[202:205], v149 offset:54272
	ds_read_b128 v[206:209], v149 offset:55296
	ds_read_b128 v[210:213], v149 offset:56320
	global_load_lds_dwordx4 v[144:145], off
	s_add_i32 m0, s58, 0x2000
	s_add_u32 s54, s54, 0x40080
	v_lshl_add_u64 v[144:145], v[214:215], 0, s[56:57]
	s_addc_u32 s55, s55, 0
	s_add_i32 s58, s69, s15
	global_load_lds_dwordx4 v[144:145], off
	v_lshl_add_u64 v[144:145], s[54:55], 0, v[166:167]
	s_mov_b32 m0, s58
	s_nop 0
	global_load_lds_dwordx4 v[144:145], off
	v_lshl_add_u64 v[144:145], s[54:55], 0, v[130:131]
	s_add_i32 m0, s58, 0x2000
	s_nop 0
	global_load_lds_dwordx4 v[144:145], off
	v_lshl_add_u64 v[144:145], v[216:217], 0, s[56:57]
	s_mov_b32 m0, s23
	s_nop 0
	global_load_lds_dwordx4 v[144:145], off
	v_lshl_add_u64 v[144:145], v[218:219], 0, s[56:57]
	s_mov_b32 m0, s24
	s_nop 0
	global_load_lds_dwordx4 v[144:145], off
	s_waitcnt vmcnt(8) lgkmcnt(0)
	s_barrier
	s_setprio 1
	v_mfma_f32_16x16x32_bf16 v[62:65], v[140:143], v[182:185], v[62:65]
	v_mfma_f32_16x16x32_bf16 v[58:61], v[154:157], v[182:185], v[58:61]
	v_mfma_f32_16x16x32_bf16 v[46:49], v[140:143], v[190:193], v[46:49]
	v_mfma_f32_16x16x32_bf16 v[42:45], v[154:157], v[190:193], v[42:45]
	v_mfma_f32_16x16x32_bf16 v[30:33], v[140:143], v[198:201], v[30:33]
	v_mfma_f32_16x16x32_bf16 v[26:29], v[154:157], v[198:201], v[26:29]
	v_mfma_f32_16x16x32_bf16 v[14:17], v[140:143], v[206:209], v[14:17]
	v_mfma_f32_16x16x32_bf16 v[10:13], v[154:157], v[206:209], v[10:13]
	v_mfma_f32_16x16x32_bf16 v[62:65], v[150:153], v[186:189], v[62:65]
	v_mfma_f32_16x16x32_bf16 v[58:61], v[158:161], v[186:189], v[58:61]
	v_mfma_f32_16x16x32_bf16 v[46:49], v[150:153], v[194:197], v[46:49]
	v_mfma_f32_16x16x32_bf16 v[42:45], v[158:161], v[194:197], v[42:45]
	v_mfma_f32_16x16x32_bf16 v[30:33], v[150:153], v[202:205], v[30:33]
	v_mfma_f32_16x16x32_bf16 v[26:29], v[158:161], v[202:205], v[26:29]
	v_mfma_f32_16x16x32_bf16 v[14:17], v[150:153], v[210:213], v[14:17]
	v_mfma_f32_16x16x32_bf16 v[10:13], v[158:161], v[210:213], v[10:13]
	s_setprio 0
	s_setprio 1
	v_mfma_f32_16x16x32_bf16 v[54:57], v[162:165], v[182:185], v[54:57]
	v_mfma_f32_16x16x32_bf16 v[50:53], v[174:177], v[182:185], v[50:53]
	v_mfma_f32_16x16x32_bf16 v[38:41], v[162:165], v[190:193], v[38:41]
	v_mfma_f32_16x16x32_bf16 v[34:37], v[174:177], v[190:193], v[34:37]
	v_mfma_f32_16x16x32_bf16 v[22:25], v[162:165], v[198:201], v[22:25]
	v_mfma_f32_16x16x32_bf16 v[18:21], v[174:177], v[198:201], v[18:21]
	v_mfma_f32_16x16x32_bf16 v[6:9], v[162:165], v[206:209], v[6:9]
	v_mfma_f32_16x16x32_bf16 v[2:5], v[174:177], v[206:209], v[2:5]
	v_mfma_f32_16x16x32_bf16 v[54:57], v[170:173], v[186:189], v[54:57]
	v_mfma_f32_16x16x32_bf16 v[50:53], v[178:181], v[186:189], v[50:53]
	v_mfma_f32_16x16x32_bf16 v[38:41], v[170:173], v[194:197], v[38:41]
	v_mfma_f32_16x16x32_bf16 v[34:37], v[178:181], v[194:197], v[34:37]
	v_mfma_f32_16x16x32_bf16 v[22:25], v[170:173], v[202:205], v[22:25]
	v_mfma_f32_16x16x32_bf16 v[18:21], v[178:181], v[202:205], v[18:21]
	v_mfma_f32_16x16x32_bf16 v[6:9], v[170:173], v[210:213], v[6:9]
	v_mfma_f32_16x16x32_bf16 v[2:5], v[178:181], v[210:213], v[2:5]
	s_setprio 0
	s_barrier
	s_add_u32 s64, s64, 0x100
	s_addc_u32 s65, s65, 0
	s_add_u32 s52, s52, 0x100
	s_addc_u32 s53, s53, 0
	s_cmp_ge_i32 s66, s1
	s_mov_b32 s54, s66
	s_cbranch_scc0 .LBB0_1438
	s_branch .Lpeelexitph12
.LBB0_1438:
	s_add_i32 s66, s54, 2
	s_add_u32 s55, s52, 0xfffc0080
	s_addc_u32 s58, s53, -1
	s_add_i32 s68, 0, 0x10000
	s_cmp_eq_u32 s60, s54
	s_cselect_b32 s59, s41, s58
	s_cselect_b32 s58, s43, s55
	v_add_u32_e32 v144, s68, v147
	s_cselect_b32 s55, s62, s65
	s_cselect_b32 s54, s63, s64
	s_add_i32 s70, 0, 0x14000
	ds_read_b128 v[140:143], v144
	ds_read_b128 v[150:153], v144 offset:1024
	ds_read_b128 v[154:157], v144 offset:2048
	ds_read_b128 v[158:161], v144 offset:3072
	v_add_u32_e32 v144, s70, v147
	ds_read_b128 v[162:165], v144
	ds_read_b128 v[170:173], v144 offset:1024
	ds_read_b128 v[174:177], v144 offset:2048
	ds_read_b128 v[178:181], v144 offset:3072
	v_lshl_add_u64 v[144:145], s[52:53], 0, v[138:139]
	s_add_i32 m0, s16, 0xc000
	ds_read_b128 v[182:185], v149
	ds_read_b128 v[186:189], v149 offset:1024
	ds_read_b128 v[190:193], v149 offset:2048
	ds_read_b128 v[194:197], v149 offset:3072
	ds_read_b128 v[198:201], v149 offset:4096
	ds_read_b128 v[202:205], v149 offset:5120
	ds_read_b128 v[206:209], v149 offset:6144
	ds_read_b128 v[210:213], v149 offset:7168
	global_load_lds_dwordx4 v[144:145], off
	v_lshl_add_u64 v[144:145], s[52:53], 0, v[136:137]
	s_add_i32 m0, s16, 0xe000
	s_nop 0
	global_load_lds_dwordx4 v[144:145], off
	s_waitcnt vmcnt(8) lgkmcnt(0)
	s_barrier
	s_setprio 1
	v_mfma_f32_16x16x32_bf16 v[126:129], v[140:143], v[182:185], v[126:129]
	v_mfma_f32_16x16x32_bf16 v[122:125], v[154:157], v[182:185], v[122:125]
	v_mfma_f32_16x16x32_bf16 v[110:113], v[140:143], v[190:193], v[110:113]
	v_mfma_f32_16x16x32_bf16 v[106:109], v[154:157], v[190:193], v[106:109]
	v_mfma_f32_16x16x32_bf16 v[94:97], v[140:143], v[198:201], v[94:97]
	v_mfma_f32_16x16x32_bf16 v[90:93], v[154:157], v[198:201], v[90:93]
	v_mfma_f32_16x16x32_bf16 v[78:81], v[140:143], v[206:209], v[78:81]
	v_mfma_f32_16x16x32_bf16 v[74:77], v[154:157], v[206:209], v[74:77]
	v_mfma_f32_16x16x32_bf16 v[126:129], v[150:153], v[186:189], v[126:129]
	v_mfma_f32_16x16x32_bf16 v[122:125], v[158:161], v[186:189], v[122:125]
	v_mfma_f32_16x16x32_bf16 v[110:113], v[150:153], v[194:197], v[110:113]
	v_mfma_f32_16x16x32_bf16 v[106:109], v[158:161], v[194:197], v[106:109]
	v_mfma_f32_16x16x32_bf16 v[94:97], v[150:153], v[202:205], v[94:97]
	v_mfma_f32_16x16x32_bf16 v[90:93], v[158:161], v[202:205], v[90:93]
	v_mfma_f32_16x16x32_bf16 v[78:81], v[150:153], v[210:213], v[78:81]
	v_mfma_f32_16x16x32_bf16 v[74:77], v[158:161], v[210:213], v[74:77]
	s_setprio 0
	s_setprio 1
	v_mfma_f32_16x16x32_bf16 v[118:121], v[162:165], v[182:185], v[118:121]
	v_mfma_f32_16x16x32_bf16 v[114:117], v[174:177], v[182:185], v[114:117]
	v_mfma_f32_16x16x32_bf16 v[102:105], v[162:165], v[190:193], v[102:105]
	v_mfma_f32_16x16x32_bf16 v[98:101], v[174:177], v[190:193], v[98:101]
	v_mfma_f32_16x16x32_bf16 v[86:89], v[162:165], v[198:201], v[86:89]
	v_mfma_f32_16x16x32_bf16 v[82:85], v[174:177], v[198:201], v[82:85]
	v_mfma_f32_16x16x32_bf16 v[70:73], v[162:165], v[206:209], v[70:73]
	v_mfma_f32_16x16x32_bf16 v[66:69], v[174:177], v[206:209], v[66:69]
	v_mfma_f32_16x16x32_bf16 v[118:121], v[170:173], v[186:189], v[118:121]
	v_mfma_f32_16x16x32_bf16 v[114:117], v[178:181], v[186:189], v[114:117]
	v_mfma_f32_16x16x32_bf16 v[102:105], v[170:173], v[194:197], v[102:105]
	v_mfma_f32_16x16x32_bf16 v[98:101], v[178:181], v[194:197], v[98:101]
	v_mfma_f32_16x16x32_bf16 v[86:89], v[170:173], v[202:205], v[86:89]
	v_mfma_f32_16x16x32_bf16 v[82:85], v[178:181], v[202:205], v[82:85]
	v_mfma_f32_16x16x32_bf16 v[70:73], v[170:173], v[210:213], v[70:73]
	v_mfma_f32_16x16x32_bf16 v[66:69], v[178:181], v[210:213], v[66:69]
	s_setprio 0
	s_barrier
	s_add_i32 s68, s68, s15
	v_lshl_add_u64 v[144:145], s[54:55], 0, v[166:167]
	s_mov_b32 m0, s68
	ds_read_b128 v[182:185], v149 offset:16384
	ds_read_b128 v[186:189], v149 offset:17408
	ds_read_b128 v[190:193], v149 offset:18432
	ds_read_b128 v[194:197], v149 offset:19456
	ds_read_b128 v[198:201], v149 offset:20480
	ds_read_b128 v[202:205], v149 offset:21504
	ds_read_b128 v[206:209], v149 offset:22528
	ds_read_b128 v[210:213], v149 offset:23552
	global_load_lds_dwordx4 v[144:145], off
	s_add_i32 m0, s68, 0x2000
	s_add_u32 s68, s54, 0x40000
	v_lshl_add_u64 v[214:215], s[54:55], 0, v[130:131]
	s_addc_u32 s69, s55, 0
	s_add_i32 s70, s70, s15
	global_load_lds_dwordx4 v[214:215], off
	v_lshl_add_u64 v[216:217], s[68:69], 0, v[166:167]
	s_mov_b32 m0, s70
	v_lshl_add_u64 v[218:219], s[58:59], 0, v[134:135]
	global_load_lds_dwordx4 v[216:217], off
	v_lshl_add_u64 v[216:217], s[68:69], 0, v[130:131]
	s_add_i32 m0, s70, 0x2000
	s_nop 0
	global_load_lds_dwordx4 v[216:217], off
	v_lshl_add_u64 v[216:217], s[58:59], 0, v[132:133]
	s_mov_b32 m0, s16
	s_nop 0
	global_load_lds_dwordx4 v[216:217], off
	s_mov_b32 m0, s20
	s_nop 0
	global_load_lds_dwordx4 v[218:219], off
	s_waitcnt vmcnt(8) lgkmcnt(0)
	s_barrier
	s_setprio 1
	v_mfma_f32_16x16x32_bf16 v[62:65], v[140:143], v[182:185], v[62:65]
	v_mfma_f32_16x16x32_bf16 v[58:61], v[154:157], v[182:185], v[58:61]
	v_mfma_f32_16x16x32_bf16 v[46:49], v[140:143], v[190:193], v[46:49]
	v_mfma_f32_16x16x32_bf16 v[42:45], v[154:157], v[190:193], v[42:45]
	v_mfma_f32_16x16x32_bf16 v[30:33], v[140:143], v[198:201], v[30:33]
	v_mfma_f32_16x16x32_bf16 v[26:29], v[154:157], v[198:201], v[26:29]
	v_mfma_f32_16x16x32_bf16 v[14:17], v[140:143], v[206:209], v[14:17]
	v_mfma_f32_16x16x32_bf16 v[10:13], v[154:157], v[206:209], v[10:13]
	v_mfma_f32_16x16x32_bf16 v[62:65], v[150:153], v[186:189], v[62:65]
	v_mfma_f32_16x16x32_bf16 v[58:61], v[158:161], v[186:189], v[58:61]
	v_mfma_f32_16x16x32_bf16 v[46:49], v[150:153], v[194:197], v[46:49]
	v_mfma_f32_16x16x32_bf16 v[42:45], v[158:161], v[194:197], v[42:45]
	v_mfma_f32_16x16x32_bf16 v[30:33], v[150:153], v[202:205], v[30:33]
	v_mfma_f32_16x16x32_bf16 v[26:29], v[158:161], v[202:205], v[26:29]
	v_mfma_f32_16x16x32_bf16 v[14:17], v[150:153], v[210:213], v[14:17]
	v_mfma_f32_16x16x32_bf16 v[10:13], v[158:161], v[210:213], v[10:13]
	s_setprio 0
	s_setprio 1
	v_mfma_f32_16x16x32_bf16 v[54:57], v[162:165], v[182:185], v[54:57]
	v_mfma_f32_16x16x32_bf16 v[50:53], v[174:177], v[182:185], v[50:53]
	v_mfma_f32_16x16x32_bf16 v[38:41], v[162:165], v[190:193], v[38:41]
	v_mfma_f32_16x16x32_bf16 v[34:37], v[174:177], v[190:193], v[34:37]
	v_mfma_f32_16x16x32_bf16 v[22:25], v[162:165], v[198:201], v[22:25]
	v_mfma_f32_16x16x32_bf16 v[18:21], v[174:177], v[198:201], v[18:21]
	v_mfma_f32_16x16x32_bf16 v[6:9], v[162:165], v[206:209], v[6:9]
	v_mfma_f32_16x16x32_bf16 v[2:5], v[174:177], v[206:209], v[2:5]
	v_mfma_f32_16x16x32_bf16 v[54:57], v[170:173], v[186:189], v[54:57]
	v_mfma_f32_16x16x32_bf16 v[50:53], v[178:181], v[186:189], v[50:53]
	v_mfma_f32_16x16x32_bf16 v[38:41], v[170:173], v[194:197], v[38:41]
	v_mfma_f32_16x16x32_bf16 v[34:37], v[178:181], v[194:197], v[34:37]
	v_mfma_f32_16x16x32_bf16 v[22:25], v[170:173], v[202:205], v[22:25]
	v_mfma_f32_16x16x32_bf16 v[18:21], v[178:181], v[202:205], v[18:21]
	v_mfma_f32_16x16x32_bf16 v[6:9], v[170:173], v[210:213], v[6:9]
	v_mfma_f32_16x16x32_bf16 v[2:5], v[178:181], v[210:213], v[2:5]
	s_setprio 0
	s_barrier
	s_add_i32 s68, 0, 0x18000
	s_add_i32 s69, 0, 0x1c000
	v_add_u32_e32 v158, s68, v147
	v_add_u32_e32 v169, s69, v147
	ds_read_b128 v[140:143], v158
	ds_read_b128 v[150:153], v158 offset:1024
	ds_read_b128 v[154:157], v158 offset:2048
	ds_read_b128 v[158:161], v158 offset:3072
	ds_read_b128 v[162:165], v169
	ds_read_b128 v[170:173], v169 offset:1024
	ds_read_b128 v[174:177], v169 offset:2048
	ds_read_b128 v[178:181], v169 offset:3072
	s_add_u32 s58, s58, 0x40000
	s_addc_u32 s59, s59, 0
	s_mov_b32 m0, s21
	v_lshl_add_u64 v[220:221], s[58:59], 0, v[132:133]
	ds_read_b128 v[182:185], v149 offset:32768
	ds_read_b128 v[186:189], v149 offset:33792
	ds_read_b128 v[190:193], v149 offset:34816
	ds_read_b128 v[194:197], v149 offset:35840
	ds_read_b128 v[198:201], v149 offset:36864
	ds_read_b128 v[202:205], v149 offset:37888
	ds_read_b128 v[206:209], v149 offset:38912
	ds_read_b128 v[210:213], v149 offset:39936
	global_load_lds_dwordx4 v[220:221], off
	v_lshl_add_u64 v[220:221], s[58:59], 0, v[134:135]
	s_mov_b32 m0, s22
	s_nop 0
	global_load_lds_dwordx4 v[220:221], off
	s_waitcnt vmcnt(8) lgkmcnt(0)
	s_barrier
	s_setprio 1
	v_mfma_f32_16x16x32_bf16 v[126:129], v[140:143], v[182:185], v[126:129]
	v_mfma_f32_16x16x32_bf16 v[122:125], v[154:157], v[182:185], v[122:125]
	v_mfma_f32_16x16x32_bf16 v[110:113], v[140:143], v[190:193], v[110:113]
	v_mfma_f32_16x16x32_bf16 v[106:109], v[154:157], v[190:193], v[106:109]
	v_mfma_f32_16x16x32_bf16 v[94:97], v[140:143], v[198:201], v[94:97]
	v_mfma_f32_16x16x32_bf16 v[90:93], v[154:157], v[198:201], v[90:93]
	v_mfma_f32_16x16x32_bf16 v[78:81], v[140:143], v[206:209], v[78:81]
	v_mfma_f32_16x16x32_bf16 v[74:77], v[154:157], v[206:209], v[74:77]
	v_mfma_f32_16x16x32_bf16 v[126:129], v[150:153], v[186:189], v[126:129]
	v_mfma_f32_16x16x32_bf16 v[122:125], v[158:161], v[186:189], v[122:125]
	v_mfma_f32_16x16x32_bf16 v[110:113], v[150:153], v[194:197], v[110:113]
	v_mfma_f32_16x16x32_bf16 v[106:109], v[158:161], v[194:197], v[106:109]
	v_mfma_f32_16x16x32_bf16 v[94:97], v[150:153], v[202:205], v[94:97]
	v_mfma_f32_16x16x32_bf16 v[90:93], v[158:161], v[202:205], v[90:93]
	v_mfma_f32_16x16x32_bf16 v[78:81], v[150:153], v[210:213], v[78:81]
	v_mfma_f32_16x16x32_bf16 v[74:77], v[158:161], v[210:213], v[74:77]
	s_setprio 0
	s_setprio 1
	v_mfma_f32_16x16x32_bf16 v[118:121], v[162:165], v[182:185], v[118:121]
	v_mfma_f32_16x16x32_bf16 v[114:117], v[174:177], v[182:185], v[114:117]
	v_mfma_f32_16x16x32_bf16 v[102:105], v[162:165], v[190:193], v[102:105]
	v_mfma_f32_16x16x32_bf16 v[98:101], v[174:177], v[190:193], v[98:101]
	v_mfma_f32_16x16x32_bf16 v[86:89], v[162:165], v[198:201], v[86:89]
	v_mfma_f32_16x16x32_bf16 v[82:85], v[174:177], v[198:201], v[82:85]
	v_mfma_f32_16x16x32_bf16 v[70:73], v[162:165], v[206:209], v[70:73]
	v_mfma_f32_16x16x32_bf16 v[66:69], v[174:177], v[206:209], v[66:69]
	v_mfma_f32_16x16x32_bf16 v[118:121], v[170:173], v[186:189], v[118:121]
	v_mfma_f32_16x16x32_bf16 v[114:117], v[178:181], v[186:189], v[114:117]
	v_mfma_f32_16x16x32_bf16 v[102:105], v[170:173], v[194:197], v[102:105]
	v_mfma_f32_16x16x32_bf16 v[98:101], v[178:181], v[194:197], v[98:101]
	v_mfma_f32_16x16x32_bf16 v[86:89], v[170:173], v[202:205], v[86:89]
	v_mfma_f32_16x16x32_bf16 v[82:85], v[178:181], v[202:205], v[82:85]
	v_mfma_f32_16x16x32_bf16 v[70:73], v[170:173], v[210:213], v[70:73]
	v_mfma_f32_16x16x32_bf16 v[66:69], v[178:181], v[210:213], v[66:69]
	s_setprio 0
	s_barrier
	s_add_i32 s58, s68, s15
	v_lshl_add_u64 v[144:145], v[144:145], 0, s[56:57]
	s_mov_b32 m0, s58
	ds_read_b128 v[182:185], v149 offset:49152
	ds_read_b128 v[186:189], v149 offset:50176
	ds_read_b128 v[190:193], v149 offset:51200
	ds_read_b128 v[194:197], v149 offset:52224
	ds_read_b128 v[198:201], v149 offset:53248
	ds_read_b128 v[202:205], v149 offset:54272
	ds_read_b128 v[206:209], v149 offset:55296
	ds_read_b128 v[210:213], v149 offset:56320
	global_load_lds_dwordx4 v[144:145], off
	s_add_i32 m0, s58, 0x2000
	s_add_u32 s54, s54, 0x40080
	v_lshl_add_u64 v[144:145], v[214:215], 0, s[56:57]
	s_addc_u32 s55, s55, 0
	s_add_i32 s58, s69, s15
	global_load_lds_dwordx4 v[144:145], off
	v_lshl_add_u64 v[144:145], s[54:55], 0, v[166:167]
	s_mov_b32 m0, s58
	s_nop 0
	global_load_lds_dwordx4 v[144:145], off
	v_lshl_add_u64 v[144:145], s[54:55], 0, v[130:131]
	s_add_i32 m0, s58, 0x2000
	s_nop 0
	global_load_lds_dwordx4 v[144:145], off
	v_lshl_add_u64 v[144:145], v[216:217], 0, s[56:57]
	s_mov_b32 m0, s23
	s_nop 0
	global_load_lds_dwordx4 v[144:145], off
	v_lshl_add_u64 v[144:145], v[218:219], 0, s[56:57]
	s_mov_b32 m0, s24
	s_nop 0
	global_load_lds_dwordx4 v[144:145], off
	s_waitcnt vmcnt(8) lgkmcnt(0)
	s_barrier
	s_setprio 1
	v_mfma_f32_16x16x32_bf16 v[62:65], v[140:143], v[182:185], v[62:65]
	v_mfma_f32_16x16x32_bf16 v[58:61], v[154:157], v[182:185], v[58:61]
	v_mfma_f32_16x16x32_bf16 v[46:49], v[140:143], v[190:193], v[46:49]
	v_mfma_f32_16x16x32_bf16 v[42:45], v[154:157], v[190:193], v[42:45]
	v_mfma_f32_16x16x32_bf16 v[30:33], v[140:143], v[198:201], v[30:33]
	v_mfma_f32_16x16x32_bf16 v[26:29], v[154:157], v[198:201], v[26:29]
	v_mfma_f32_16x16x32_bf16 v[14:17], v[140:143], v[206:209], v[14:17]
	v_mfma_f32_16x16x32_bf16 v[10:13], v[154:157], v[206:209], v[10:13]
	v_mfma_f32_16x16x32_bf16 v[62:65], v[150:153], v[186:189], v[62:65]
	v_mfma_f32_16x16x32_bf16 v[58:61], v[158:161], v[186:189], v[58:61]
	v_mfma_f32_16x16x32_bf16 v[46:49], v[150:153], v[194:197], v[46:49]
	v_mfma_f32_16x16x32_bf16 v[42:45], v[158:161], v[194:197], v[42:45]
	v_mfma_f32_16x16x32_bf16 v[30:33], v[150:153], v[202:205], v[30:33]
	v_mfma_f32_16x16x32_bf16 v[26:29], v[158:161], v[202:205], v[26:29]
	v_mfma_f32_16x16x32_bf16 v[14:17], v[150:153], v[210:213], v[14:17]
	v_mfma_f32_16x16x32_bf16 v[10:13], v[158:161], v[210:213], v[10:13]
	s_setprio 0
	s_setprio 1
	v_mfma_f32_16x16x32_bf16 v[54:57], v[162:165], v[182:185], v[54:57]
	v_mfma_f32_16x16x32_bf16 v[50:53], v[174:177], v[182:185], v[50:53]
	v_mfma_f32_16x16x32_bf16 v[38:41], v[162:165], v[190:193], v[38:41]
	v_mfma_f32_16x16x32_bf16 v[34:37], v[174:177], v[190:193], v[34:37]
	v_mfma_f32_16x16x32_bf16 v[22:25], v[162:165], v[198:201], v[22:25]
	v_mfma_f32_16x16x32_bf16 v[18:21], v[174:177], v[198:201], v[18:21]
	v_mfma_f32_16x16x32_bf16 v[6:9], v[162:165], v[206:209], v[6:9]
	v_mfma_f32_16x16x32_bf16 v[2:5], v[174:177], v[206:209], v[2:5]
	v_mfma_f32_16x16x32_bf16 v[54:57], v[170:173], v[186:189], v[54:57]
	v_mfma_f32_16x16x32_bf16 v[50:53], v[178:181], v[186:189], v[50:53]
	v_mfma_f32_16x16x32_bf16 v[38:41], v[170:173], v[194:197], v[38:41]
	v_mfma_f32_16x16x32_bf16 v[34:37], v[178:181], v[194:197], v[34:37]
	v_mfma_f32_16x16x32_bf16 v[22:25], v[170:173], v[202:205], v[22:25]
	v_mfma_f32_16x16x32_bf16 v[18:21], v[178:181], v[202:205], v[18:21]
	v_mfma_f32_16x16x32_bf16 v[6:9], v[170:173], v[210:213], v[6:9]
	v_mfma_f32_16x16x32_bf16 v[2:5], v[178:181], v[210:213], v[2:5]
	s_setprio 0
	s_barrier
	s_add_u32 s64, s64, 0x100
	s_addc_u32 s65, s65, 0
	s_add_u32 s52, s52, 0x100
	s_addc_u32 s53, s53, 0
	s_cmp_ge_i32 s66, s1
	s_mov_b32 s54, s66
	s_cbranch_scc0 .LBB0_1438

.Lpeelph15_1:
	s_add_i32 s91, s91, 2
	s_add_u32 s64, s70, 0x100
	s_addc_u32 s65, s71, 0
	s_and_b64 s[74:75], s[68:69], exec
	s_cselect_b32 s74, 0, s64
	s_cselect_b32 s75, 0, s65
	s_add_u32 s74, s28, s74
	s_addc_u32 s75, s29, s75
	s_add_u32 s92, s51, s70
	s_addc_u32 s93, s53, s71
	s_and_b64 s[68:69], s[68:69], exec
	s_cselect_b32 s69, s55, s93
	s_cselect_b32 s68, s54, s92
	s_add_i32 s93, 0, 0x10000
	s_add_i32 s92, 0, 0x14000
	v_add_u32_e32 v2, s93, v210
	v_add_u32_e32 v6, s92, v210
	ds_read_b128 v[26:29], v2
	ds_read_b128 v[30:33], v2 offset:1024
	ds_read_b128 v[18:21], v2 offset:2048
	ds_read_b128 v[22:25], v2 offset:3072
	ds_read_b128 v[10:13], v6
	ds_read_b128 v[14:17], v6 offset:1024
	ds_read_b128 v[2:5], v6 offset:2048
	ds_read_b128 v[6:9], v6 offset:3072
	v_lshl_add_u64 v[170:171], v[194:195], 0, s[70:71]
	s_add_i32 m0, s59, 0xc000
	ds_read_b128 v[196:199], v212
	ds_read_b128 v[200:203], v212 offset:1024
	ds_read_b128 v[214:217], v212 offset:2048
	ds_read_b128 v[218:221], v212 offset:3072
	ds_read_b128 v[236:239], v212 offset:4096
	ds_read_b128 v[240:243], v212 offset:5120
	ds_read_b128 v[244:247], v212 offset:6144
	ds_read_b128 v[248:251], v212 offset:7168
	global_load_lds_dwordx4 v[170:171], off
	v_lshl_add_u64 v[170:171], v[192:193], 0, s[70:71]
	s_add_i32 m0, s59, 0xe000
	s_nop 0
	global_load_lds_dwordx4 v[170:171], off
	s_waitcnt vmcnt(8) lgkmcnt(0)
	s_barrier
	s_setprio 1
	v_mfma_scale_f32_16x16x128_f8f6f4 v[154:157], v[26:33], v[196:203], 0, v208, v207 op_sel_hi:[0,0,0]
	v_mfma_scale_f32_16x16x128_f8f6f4 v[150:153], v[18:25], v[196:203], 0, v208, v207 op_sel_hi:[0,0,0]
	v_mfma_scale_f32_16x16x128_f8f6f4 v[142:145], v[26:33], v[214:221], 0, v208, v207 op_sel_hi:[0,0,0]
	v_mfma_scale_f32_16x16x128_f8f6f4 v[134:137], v[18:25], v[214:221], 0, v208, v207 op_sel_hi:[0,0,0]
	v_mfma_scale_f32_16x16x128_f8f6f4 v[126:129], v[26:33], v[236:243], 0, v208, v207 op_sel_hi:[0,0,0]
	v_mfma_scale_f32_16x16x128_f8f6f4 v[118:121], v[18:25], v[236:243], 0, v208, v207 op_sel_hi:[0,0,0]
	v_mfma_scale_f32_16x16x128_f8f6f4 v[110:113], v[26:33], v[244:251], 0, v208, v207 op_sel_hi:[0,0,0]
	v_mfma_scale_f32_16x16x128_f8f6f4 v[102:105], v[18:25], v[244:251], 0, v208, v207 op_sel_hi:[0,0,0]
	s_setprio 0
	s_setprio 1
	v_mfma_scale_f32_16x16x128_f8f6f4 v[158:161], v[10:17], v[196:203], 0, v208, v207 op_sel_hi:[0,0,0]
	v_mfma_scale_f32_16x16x128_f8f6f4 v[146:149], v[2:9], v[196:203], 0, v208, v207 op_sel_hi:[0,0,0]
	v_mfma_scale_f32_16x16x128_f8f6f4 v[138:141], v[10:17], v[214:221], 0, v208, v207 op_sel_hi:[0,0,0]
	v_mfma_scale_f32_16x16x128_f8f6f4 v[130:133], v[2:9], v[214:221], 0, v208, v207 op_sel_hi:[0,0,0]
	v_mfma_scale_f32_16x16x128_f8f6f4 v[122:125], v[10:17], v[236:243], 0, v208, v207 op_sel_hi:[0,0,0]
	v_mfma_scale_f32_16x16x128_f8f6f4 v[114:117], v[2:9], v[236:243], 0, v208, v207 op_sel_hi:[0,0,0]
	v_mfma_scale_f32_16x16x128_f8f6f4 v[106:109], v[10:17], v[244:251], 0, v208, v207 op_sel_hi:[0,0,0]
	v_mfma_scale_f32_16x16x128_f8f6f4 v[98:101], v[2:9], v[244:251], 0, v208, v207 op_sel_hi:[0,0,0]
	s_setprio 0
	s_barrier
	s_add_i32 s70, s93, s72
	v_lshl_add_u64 v[196:197], s[68:69], 0, v[162:163]
	s_mov_b32 m0, s70
	ds_read_b128 v[214:217], v212 offset:16384
	ds_read_b128 v[218:221], v212 offset:17408
	ds_read_b128 v[236:239], v212 offset:18432
	ds_read_b128 v[240:243], v212 offset:19456
	ds_read_b128 v[244:247], v212 offset:20480
	ds_read_b128 v[248:251], v212 offset:21504
	ds_read_b128 v[170:173], v212 offset:22528
	ds_read_b128 v[174:177], v212 offset:23552
	global_load_lds_dwordx4 v[196:197], off
	s_add_i32 m0, s70, 0x2000
	s_add_u32 s70, s68, 0x20000
	v_lshl_add_u64 v[198:199], s[68:69], 0, v[164:165]
	s_addc_u32 s71, s69, 0
	s_add_i32 s92, s92, s72
	global_load_lds_dwordx4 v[198:199], off
	v_lshl_add_u64 v[200:201], s[70:71], 0, v[162:163]
	s_mov_b32 m0, s92
	v_mov_b32_e32 v179, v167
	global_load_lds_dwordx4 v[200:201], off
	v_lshl_add_u64 v[200:201], s[70:71], 0, v[164:165]
	s_add_i32 m0, s92, 0x2000
	v_lshl_add_u64 v[202:203], s[74:75], 0, v[166:167]
	global_load_lds_dwordx4 v[200:201], off
	s_mov_b32 m0, s59
	v_lshl_add_u64 v[200:201], s[74:75], 0, v[178:179]
	global_load_lds_dwordx4 v166, s[74:75]
	s_mov_b32 m0, s61
	s_nop 0
	global_load_lds_dwordx4 v178, s[74:75]
	s_waitcnt vmcnt(8) lgkmcnt(0)
	s_barrier
	s_setprio 1
	v_mfma_scale_f32_16x16x128_f8f6f4 v[94:97], v[26:33], v[214:221], 0, v208, v207 op_sel_hi:[0,0,0]
	v_mfma_scale_f32_16x16x128_f8f6f4 v[86:89], v[18:25], v[214:221], 0, v208, v207 op_sel_hi:[0,0,0]
	v_mfma_scale_f32_16x16x128_f8f6f4 v[78:81], v[26:33], v[236:243], 0, v208, v207 op_sel_hi:[0,0,0]
	v_mfma_scale_f32_16x16x128_f8f6f4 v[70:73], v[18:25], v[236:243], 0, v208, v207 op_sel_hi:[0,0,0]
	v_mfma_scale_f32_16x16x128_f8f6f4 v[62:65], v[26:33], v[244:251], 0, v208, v207 op_sel_hi:[0,0,0]
	v_mfma_scale_f32_16x16x128_f8f6f4 v[54:57], v[18:25], v[244:251], 0, v208, v207 op_sel_hi:[0,0,0]
	v_mfma_scale_f32_16x16x128_f8f6f4 v[46:49], v[26:33], v[170:177], 0, v208, v207 op_sel_hi:[0,0,0]
	v_mfma_scale_f32_16x16x128_f8f6f4 v[38:41], v[18:25], v[170:177], 0, v208, v207 op_sel_hi:[0,0,0]
	s_setprio 0
	s_setprio 1
	v_mfma_scale_f32_16x16x128_f8f6f4 v[90:93], v[10:17], v[214:221], 0, v208, v207 op_sel_hi:[0,0,0]
	v_mfma_scale_f32_16x16x128_f8f6f4 v[82:85], v[2:9], v[214:221], 0, v208, v207 op_sel_hi:[0,0,0]
	v_mfma_scale_f32_16x16x128_f8f6f4 v[74:77], v[10:17], v[236:243], 0, v208, v207 op_sel_hi:[0,0,0]
	v_mfma_scale_f32_16x16x128_f8f6f4 v[66:69], v[2:9], v[236:243], 0, v208, v207 op_sel_hi:[0,0,0]
	v_mfma_scale_f32_16x16x128_f8f6f4 v[58:61], v[10:17], v[244:251], 0, v208, v207 op_sel_hi:[0,0,0]
	v_mfma_scale_f32_16x16x128_f8f6f4 v[50:53], v[2:9], v[244:251], 0, v208, v207 op_sel_hi:[0,0,0]
	v_mfma_scale_f32_16x16x128_f8f6f4 v[42:45], v[10:17], v[170:177], 0, v208, v207 op_sel_hi:[0,0,0]
	v_mfma_scale_f32_16x16x128_f8f6f4 v[34:37], v[2:9], v[170:177], 0, v208, v207 op_sel_hi:[0,0,0]
	s_setprio 0
	s_barrier
	s_add_i32 s70, 0, 0x18000
	s_add_i32 s71, 0, 0x1c000
	v_add_u32_e32 v2, s70, v210
	v_add_u32_e32 v6, s71, v210
	ds_read_b128 v[26:29], v2
	ds_read_b128 v[30:33], v2 offset:1024
	ds_read_b128 v[18:21], v2 offset:2048
	ds_read_b128 v[22:25], v2 offset:3072
	ds_read_b128 v[10:13], v6
	ds_read_b128 v[14:17], v6 offset:1024
	ds_read_b128 v[2:5], v6 offset:2048
	ds_read_b128 v[6:9], v6 offset:3072
	s_mov_b32 m0, s73
	ds_read_b128 v[170:173], v212 offset:32768
	ds_read_b128 v[174:177], v212 offset:33792
	ds_read_b128 v[214:217], v212 offset:34816
	ds_read_b128 v[218:221], v212 offset:35840
	ds_read_b128 v[236:239], v212 offset:36864
	ds_read_b128 v[240:243], v212 offset:37888
	ds_read_b128 v[244:247], v212 offset:38912
	ds_read_b128 v[248:251], v212 offset:39936
	global_load_lds_dwordx4 v180, s[74:75]
	s_mov_b32 m0, s76
	s_nop 0
	global_load_lds_dwordx4 v182, s[74:75]
	s_waitcnt vmcnt(8) lgkmcnt(0)
	s_barrier
	s_setprio 1
	v_mfma_scale_f32_16x16x128_f8f6f4 v[154:157], v[26:33], v[170:177], v[154:157], v208, v207 op_sel_hi:[0,0,0]
	v_mfma_scale_f32_16x16x128_f8f6f4 v[150:153], v[18:25], v[170:177], v[150:153], v208, v207 op_sel_hi:[0,0,0]
	v_mfma_scale_f32_16x16x128_f8f6f4 v[142:145], v[26:33], v[214:221], v[142:145], v208, v207 op_sel_hi:[0,0,0]
	v_mfma_scale_f32_16x16x128_f8f6f4 v[134:137], v[18:25], v[214:221], v[134:137], v208, v207 op_sel_hi:[0,0,0]
	v_mfma_scale_f32_16x16x128_f8f6f4 v[126:129], v[26:33], v[236:243], v[126:129], v208, v207 op_sel_hi:[0,0,0]
	v_mfma_scale_f32_16x16x128_f8f6f4 v[118:121], v[18:25], v[236:243], v[118:121], v208, v207 op_sel_hi:[0,0,0]
	v_mfma_scale_f32_16x16x128_f8f6f4 v[110:113], v[26:33], v[244:251], v[110:113], v208, v207 op_sel_hi:[0,0,0]
	v_mfma_scale_f32_16x16x128_f8f6f4 v[102:105], v[18:25], v[244:251], v[102:105], v208, v207 op_sel_hi:[0,0,0]
	s_setprio 0
	s_setprio 1
	v_mfma_scale_f32_16x16x128_f8f6f4 v[158:161], v[10:17], v[170:177], v[158:161], v208, v207 op_sel_hi:[0,0,0]
	v_mfma_scale_f32_16x16x128_f8f6f4 v[146:149], v[2:9], v[170:177], v[146:149], v208, v207 op_sel_hi:[0,0,0]
	v_mfma_scale_f32_16x16x128_f8f6f4 v[138:141], v[10:17], v[214:221], v[138:141], v208, v207 op_sel_hi:[0,0,0]
	v_mfma_scale_f32_16x16x128_f8f6f4 v[130:133], v[2:9], v[214:221], v[130:133], v208, v207 op_sel_hi:[0,0,0]
	v_mfma_scale_f32_16x16x128_f8f6f4 v[122:125], v[10:17], v[236:243], v[122:125], v208, v207 op_sel_hi:[0,0,0]
	v_mfma_scale_f32_16x16x128_f8f6f4 v[114:117], v[2:9], v[236:243], v[114:117], v208, v207 op_sel_hi:[0,0,0]
	v_mfma_scale_f32_16x16x128_f8f6f4 v[106:109], v[10:17], v[244:251], v[106:109], v208, v207 op_sel_hi:[0,0,0]
	v_mfma_scale_f32_16x16x128_f8f6f4 v[98:101], v[2:9], v[244:251], v[98:101], v208, v207 op_sel_hi:[0,0,0]
	s_setprio 0
	s_barrier
	s_add_i32 s70, s70, s72
	v_lshl_add_u64 v[196:197], v[196:197], 0, s[56:57]
	s_mov_b32 m0, s70
	ds_read_b128 v[170:173], v212 offset:49152
	ds_read_b128 v[174:177], v212 offset:50176
	ds_read_b128 v[214:217], v212 offset:51200
	ds_read_b128 v[218:221], v212 offset:52224
	ds_read_b128 v[236:239], v212 offset:53248
	ds_read_b128 v[240:243], v212 offset:54272
	ds_read_b128 v[244:247], v212 offset:55296
	ds_read_b128 v[248:251], v212 offset:56320
	global_load_lds_dwordx4 v[196:197], off
	s_add_i32 m0, s70, 0x2000
	s_add_u32 s68, s68, 0x20080
	v_lshl_add_u64 v[196:197], v[198:199], 0, s[56:57]
	s_addc_u32 s69, s69, 0
	s_add_i32 s70, s71, s72
	global_load_lds_dwordx4 v[196:197], off
	v_lshl_add_u64 v[196:197], s[68:69], 0, v[162:163]
	s_mov_b32 m0, s70
	s_nop 0
	global_load_lds_dwordx4 v[196:197], off
	v_lshl_add_u64 v[196:197], s[68:69], 0, v[164:165]
	s_add_i32 m0, s70, 0x2000
	s_nop 0
	global_load_lds_dwordx4 v[196:197], off
	v_lshl_add_u64 v[196:197], v[202:203], 0, s[56:57]
	s_mov_b32 m0, s77
	s_nop 0
	global_load_lds_dwordx4 v[196:197], off
	v_lshl_add_u64 v[196:197], v[200:201], 0, s[56:57]
	s_mov_b32 m0, s79
	s_nop 0
	global_load_lds_dwordx4 v[196:197], off
	s_waitcnt vmcnt(8) lgkmcnt(0)
	s_barrier
	s_setprio 1
	v_mfma_scale_f32_16x16x128_f8f6f4 v[94:97], v[26:33], v[170:177], v[94:97], v208, v207 op_sel_hi:[0,0,0]
	v_mfma_scale_f32_16x16x128_f8f6f4 v[86:89], v[18:25], v[170:177], v[86:89], v208, v207 op_sel_hi:[0,0,0]
	v_mfma_scale_f32_16x16x128_f8f6f4 v[78:81], v[26:33], v[214:221], v[78:81], v208, v207 op_sel_hi:[0,0,0]
	v_mfma_scale_f32_16x16x128_f8f6f4 v[70:73], v[18:25], v[214:221], v[70:73], v208, v207 op_sel_hi:[0,0,0]
	v_mfma_scale_f32_16x16x128_f8f6f4 v[62:65], v[26:33], v[236:243], v[62:65], v208, v207 op_sel_hi:[0,0,0]
	v_mfma_scale_f32_16x16x128_f8f6f4 v[54:57], v[18:25], v[236:243], v[54:57], v208, v207 op_sel_hi:[0,0,0]
	v_mfma_scale_f32_16x16x128_f8f6f4 v[46:49], v[26:33], v[244:251], v[46:49], v208, v207 op_sel_hi:[0,0,0]
	v_mfma_scale_f32_16x16x128_f8f6f4 v[38:41], v[18:25], v[244:251], v[38:41], v208, v207 op_sel_hi:[0,0,0]
	s_setprio 0
	s_setprio 1
	v_mfma_scale_f32_16x16x128_f8f6f4 v[90:93], v[10:17], v[170:177], v[90:93], v208, v207 op_sel_hi:[0,0,0]
	v_mfma_scale_f32_16x16x128_f8f6f4 v[82:85], v[2:9], v[170:177], v[82:85], v208, v207 op_sel_hi:[0,0,0]
	v_mfma_scale_f32_16x16x128_f8f6f4 v[74:77], v[10:17], v[214:221], v[74:77], v208, v207 op_sel_hi:[0,0,0]
	v_mfma_scale_f32_16x16x128_f8f6f4 v[66:69], v[2:9], v[214:221], v[66:69], v208, v207 op_sel_hi:[0,0,0]
	v_mfma_scale_f32_16x16x128_f8f6f4 v[58:61], v[10:17], v[236:243], v[58:61], v208, v207 op_sel_hi:[0,0,0]
	v_mfma_scale_f32_16x16x128_f8f6f4 v[50:53], v[2:9], v[236:243], v[50:53], v208, v207 op_sel_hi:[0,0,0]
	v_mfma_scale_f32_16x16x128_f8f6f4 v[42:45], v[10:17], v[244:251], v[42:45], v208, v207 op_sel_hi:[0,0,0]
	v_mfma_scale_f32_16x16x128_f8f6f4 v[34:37], v[2:9], v[244:251], v[34:37], v208, v207 op_sel_hi:[0,0,0]
	s_setprio 0
	s_barrier
	s_cmp_ge_i32 s91, s11
	s_cbranch_scc1 .LBB0_1695
	s_mov_b64 s[70:71], s[64:65]
	s_branch .LBB0_1691

.LBB0_1693:
	s_add_i32 s91, s91, 2
	s_add_u32 s64, s70, 0x100
	s_addc_u32 s65, s71, 0
	s_and_b64 s[74:75], s[68:69], exec
	s_cselect_b32 s74, 0, s64
	s_cselect_b32 s75, 0, s65
	s_add_u32 s74, s28, s74
	s_addc_u32 s75, s29, s75
	s_add_u32 s92, s51, s70
	s_addc_u32 s93, s53, s71
	s_and_b64 s[68:69], s[68:69], exec
	s_cselect_b32 s69, s55, s93
	s_cselect_b32 s68, s54, s92
	s_add_i32 s93, 0, 0x10000
	s_add_i32 s92, 0, 0x14000
	v_add_u32_e32 v2, s93, v210
	v_add_u32_e32 v6, s92, v210
	ds_read_b128 v[26:29], v2
	ds_read_b128 v[30:33], v2 offset:1024
	ds_read_b128 v[18:21], v2 offset:2048
	ds_read_b128 v[22:25], v2 offset:3072
	ds_read_b128 v[10:13], v6
	ds_read_b128 v[14:17], v6 offset:1024
	ds_read_b128 v[2:5], v6 offset:2048
	ds_read_b128 v[6:9], v6 offset:3072
	v_lshl_add_u64 v[170:171], v[194:195], 0, s[70:71]
	s_add_i32 m0, s59, 0xc000
	ds_read_b128 v[196:199], v212
	ds_read_b128 v[200:203], v212 offset:1024
	ds_read_b128 v[214:217], v212 offset:2048
	ds_read_b128 v[218:221], v212 offset:3072
	ds_read_b128 v[236:239], v212 offset:4096
	ds_read_b128 v[240:243], v212 offset:5120
	ds_read_b128 v[244:247], v212 offset:6144
	ds_read_b128 v[248:251], v212 offset:7168
	global_load_lds_dwordx4 v[170:171], off
	v_lshl_add_u64 v[170:171], v[192:193], 0, s[70:71]
	s_add_i32 m0, s59, 0xe000
	s_nop 0
	global_load_lds_dwordx4 v[170:171], off
	s_waitcnt vmcnt(8) lgkmcnt(0)
	s_barrier
	s_setprio 1
	v_mfma_scale_f32_16x16x128_f8f6f4 v[154:157], v[26:33], v[196:203], v[154:157], v208, v207 op_sel_hi:[0,0,0]
	v_mfma_scale_f32_16x16x128_f8f6f4 v[150:153], v[18:25], v[196:203], v[150:153], v208, v207 op_sel_hi:[0,0,0]
	v_mfma_scale_f32_16x16x128_f8f6f4 v[142:145], v[26:33], v[214:221], v[142:145], v208, v207 op_sel_hi:[0,0,0]
	v_mfma_scale_f32_16x16x128_f8f6f4 v[134:137], v[18:25], v[214:221], v[134:137], v208, v207 op_sel_hi:[0,0,0]
	v_mfma_scale_f32_16x16x128_f8f6f4 v[126:129], v[26:33], v[236:243], v[126:129], v208, v207 op_sel_hi:[0,0,0]
	v_mfma_scale_f32_16x16x128_f8f6f4 v[118:121], v[18:25], v[236:243], v[118:121], v208, v207 op_sel_hi:[0,0,0]
	v_mfma_scale_f32_16x16x128_f8f6f4 v[110:113], v[26:33], v[244:251], v[110:113], v208, v207 op_sel_hi:[0,0,0]
	v_mfma_scale_f32_16x16x128_f8f6f4 v[102:105], v[18:25], v[244:251], v[102:105], v208, v207 op_sel_hi:[0,0,0]
	s_setprio 0
	s_setprio 1
	v_mfma_scale_f32_16x16x128_f8f6f4 v[158:161], v[10:17], v[196:203], v[158:161], v208, v207 op_sel_hi:[0,0,0]
	v_mfma_scale_f32_16x16x128_f8f6f4 v[146:149], v[2:9], v[196:203], v[146:149], v208, v207 op_sel_hi:[0,0,0]
	v_mfma_scale_f32_16x16x128_f8f6f4 v[138:141], v[10:17], v[214:221], v[138:141], v208, v207 op_sel_hi:[0,0,0]
	v_mfma_scale_f32_16x16x128_f8f6f4 v[130:133], v[2:9], v[214:221], v[130:133], v208, v207 op_sel_hi:[0,0,0]
	v_mfma_scale_f32_16x16x128_f8f6f4 v[122:125], v[10:17], v[236:243], v[122:125], v208, v207 op_sel_hi:[0,0,0]
	v_mfma_scale_f32_16x16x128_f8f6f4 v[114:117], v[2:9], v[236:243], v[114:117], v208, v207 op_sel_hi:[0,0,0]
	v_mfma_scale_f32_16x16x128_f8f6f4 v[106:109], v[10:17], v[244:251], v[106:109], v208, v207 op_sel_hi:[0,0,0]
	v_mfma_scale_f32_16x16x128_f8f6f4 v[98:101], v[2:9], v[244:251], v[98:101], v208, v207 op_sel_hi:[0,0,0]
	s_setprio 0
	s_barrier
	s_add_i32 s70, s93, s72
	v_lshl_add_u64 v[196:197], s[68:69], 0, v[162:163]
	s_mov_b32 m0, s70
	ds_read_b128 v[214:217], v212 offset:16384
	ds_read_b128 v[218:221], v212 offset:17408
	ds_read_b128 v[236:239], v212 offset:18432
	ds_read_b128 v[240:243], v212 offset:19456
	ds_read_b128 v[244:247], v212 offset:20480
	ds_read_b128 v[248:251], v212 offset:21504
	ds_read_b128 v[170:173], v212 offset:22528
	ds_read_b128 v[174:177], v212 offset:23552
	global_load_lds_dwordx4 v[196:197], off
	s_add_i32 m0, s70, 0x2000
	s_add_u32 s70, s68, 0x20000
	v_lshl_add_u64 v[198:199], s[68:69], 0, v[164:165]
	s_addc_u32 s71, s69, 0
	s_add_i32 s92, s92, s72
	global_load_lds_dwordx4 v[198:199], off
	v_lshl_add_u64 v[200:201], s[70:71], 0, v[162:163]
	s_mov_b32 m0, s92
	v_mov_b32_e32 v179, v167
	global_load_lds_dwordx4 v[200:201], off
	v_lshl_add_u64 v[200:201], s[70:71], 0, v[164:165]
	s_add_i32 m0, s92, 0x2000
	v_lshl_add_u64 v[202:203], s[74:75], 0, v[166:167]
	global_load_lds_dwordx4 v[200:201], off
	s_mov_b32 m0, s59
	v_lshl_add_u64 v[200:201], s[74:75], 0, v[178:179]
	global_load_lds_dwordx4 v166, s[74:75]
	s_mov_b32 m0, s61
	s_nop 0
	global_load_lds_dwordx4 v178, s[74:75]
	s_waitcnt vmcnt(8) lgkmcnt(0)
	s_barrier
	s_setprio 1
	v_mfma_scale_f32_16x16x128_f8f6f4 v[94:97], v[26:33], v[214:221], v[94:97], v208, v207 op_sel_hi:[0,0,0]
	v_mfma_scale_f32_16x16x128_f8f6f4 v[86:89], v[18:25], v[214:221], v[86:89], v208, v207 op_sel_hi:[0,0,0]
	v_mfma_scale_f32_16x16x128_f8f6f4 v[78:81], v[26:33], v[236:243], v[78:81], v208, v207 op_sel_hi:[0,0,0]
	v_mfma_scale_f32_16x16x128_f8f6f4 v[70:73], v[18:25], v[236:243], v[70:73], v208, v207 op_sel_hi:[0,0,0]
	v_mfma_scale_f32_16x16x128_f8f6f4 v[62:65], v[26:33], v[244:251], v[62:65], v208, v207 op_sel_hi:[0,0,0]
	v_mfma_scale_f32_16x16x128_f8f6f4 v[54:57], v[18:25], v[244:251], v[54:57], v208, v207 op_sel_hi:[0,0,0]
	v_mfma_scale_f32_16x16x128_f8f6f4 v[46:49], v[26:33], v[170:177], v[46:49], v208, v207 op_sel_hi:[0,0,0]
	v_mfma_scale_f32_16x16x128_f8f6f4 v[38:41], v[18:25], v[170:177], v[38:41], v208, v207 op_sel_hi:[0,0,0]
	s_setprio 0
	s_setprio 1
	v_mfma_scale_f32_16x16x128_f8f6f4 v[90:93], v[10:17], v[214:221], v[90:93], v208, v207 op_sel_hi:[0,0,0]
	v_mfma_scale_f32_16x16x128_f8f6f4 v[82:85], v[2:9], v[214:221], v[82:85], v208, v207 op_sel_hi:[0,0,0]
	v_mfma_scale_f32_16x16x128_f8f6f4 v[74:77], v[10:17], v[236:243], v[74:77], v208, v207 op_sel_hi:[0,0,0]
	v_mfma_scale_f32_16x16x128_f8f6f4 v[66:69], v[2:9], v[236:243], v[66:69], v208, v207 op_sel_hi:[0,0,0]
	v_mfma_scale_f32_16x16x128_f8f6f4 v[58:61], v[10:17], v[244:251], v[58:61], v208, v207 op_sel_hi:[0,0,0]
	v_mfma_scale_f32_16x16x128_f8f6f4 v[50:53], v[2:9], v[244:251], v[50:53], v208, v207 op_sel_hi:[0,0,0]
	v_mfma_scale_f32_16x16x128_f8f6f4 v[42:45], v[10:17], v[170:177], v[42:45], v208, v207 op_sel_hi:[0,0,0]
	v_mfma_scale_f32_16x16x128_f8f6f4 v[34:37], v[2:9], v[170:177], v[34:37], v208, v207 op_sel_hi:[0,0,0]
	s_setprio 0
	s_barrier
	s_add_i32 s70, 0, 0x18000
	s_add_i32 s71, 0, 0x1c000
	v_add_u32_e32 v2, s70, v210
	v_add_u32_e32 v6, s71, v210
	ds_read_b128 v[26:29], v2
	ds_read_b128 v[30:33], v2 offset:1024
	ds_read_b128 v[18:21], v2 offset:2048
	ds_read_b128 v[22:25], v2 offset:3072
	ds_read_b128 v[10:13], v6
	ds_read_b128 v[14:17], v6 offset:1024
	ds_read_b128 v[2:5], v6 offset:2048
	ds_read_b128 v[6:9], v6 offset:3072
	s_mov_b32 m0, s73
	ds_read_b128 v[170:173], v212 offset:32768
	ds_read_b128 v[174:177], v212 offset:33792
	ds_read_b128 v[214:217], v212 offset:34816
	ds_read_b128 v[218:221], v212 offset:35840
	ds_read_b128 v[236:239], v212 offset:36864
	ds_read_b128 v[240:243], v212 offset:37888
	ds_read_b128 v[244:247], v212 offset:38912
	ds_read_b128 v[248:251], v212 offset:39936
	global_load_lds_dwordx4 v180, s[74:75]
	s_mov_b32 m0, s76
	s_nop 0
	global_load_lds_dwordx4 v182, s[74:75]
	s_waitcnt vmcnt(8) lgkmcnt(0)
	s_barrier
	s_setprio 1
	v_mfma_scale_f32_16x16x128_f8f6f4 v[154:157], v[26:33], v[170:177], v[154:157], v208, v207 op_sel_hi:[0,0,0]
	v_mfma_scale_f32_16x16x128_f8f6f4 v[150:153], v[18:25], v[170:177], v[150:153], v208, v207 op_sel_hi:[0,0,0]
	v_mfma_scale_f32_16x16x128_f8f6f4 v[142:145], v[26:33], v[214:221], v[142:145], v208, v207 op_sel_hi:[0,0,0]
	v_mfma_scale_f32_16x16x128_f8f6f4 v[134:137], v[18:25], v[214:221], v[134:137], v208, v207 op_sel_hi:[0,0,0]
	v_mfma_scale_f32_16x16x128_f8f6f4 v[126:129], v[26:33], v[236:243], v[126:129], v208, v207 op_sel_hi:[0,0,0]
	v_mfma_scale_f32_16x16x128_f8f6f4 v[118:121], v[18:25], v[236:243], v[118:121], v208, v207 op_sel_hi:[0,0,0]
	v_mfma_scale_f32_16x16x128_f8f6f4 v[110:113], v[26:33], v[244:251], v[110:113], v208, v207 op_sel_hi:[0,0,0]
	v_mfma_scale_f32_16x16x128_f8f6f4 v[102:105], v[18:25], v[244:251], v[102:105], v208, v207 op_sel_hi:[0,0,0]
	s_setprio 0
	s_setprio 1
	v_mfma_scale_f32_16x16x128_f8f6f4 v[158:161], v[10:17], v[170:177], v[158:161], v208, v207 op_sel_hi:[0,0,0]
	v_mfma_scale_f32_16x16x128_f8f6f4 v[146:149], v[2:9], v[170:177], v[146:149], v208, v207 op_sel_hi:[0,0,0]
	v_mfma_scale_f32_16x16x128_f8f6f4 v[138:141], v[10:17], v[214:221], v[138:141], v208, v207 op_sel_hi:[0,0,0]
	v_mfma_scale_f32_16x16x128_f8f6f4 v[130:133], v[2:9], v[214:221], v[130:133], v208, v207 op_sel_hi:[0,0,0]
	v_mfma_scale_f32_16x16x128_f8f6f4 v[122:125], v[10:17], v[236:243], v[122:125], v208, v207 op_sel_hi:[0,0,0]
	v_mfma_scale_f32_16x16x128_f8f6f4 v[114:117], v[2:9], v[236:243], v[114:117], v208, v207 op_sel_hi:[0,0,0]
	v_mfma_scale_f32_16x16x128_f8f6f4 v[106:109], v[10:17], v[244:251], v[106:109], v208, v207 op_sel_hi:[0,0,0]
	v_mfma_scale_f32_16x16x128_f8f6f4 v[98:101], v[2:9], v[244:251], v[98:101], v208, v207 op_sel_hi:[0,0,0]
	s_setprio 0
	s_barrier
	s_add_i32 s70, s70, s72
	v_lshl_add_u64 v[196:197], v[196:197], 0, s[56:57]
	s_mov_b32 m0, s70
	ds_read_b128 v[170:173], v212 offset:49152
	ds_read_b128 v[174:177], v212 offset:50176
	ds_read_b128 v[214:217], v212 offset:51200
	ds_read_b128 v[218:221], v212 offset:52224
	ds_read_b128 v[236:239], v212 offset:53248
	ds_read_b128 v[240:243], v212 offset:54272
	ds_read_b128 v[244:247], v212 offset:55296
	ds_read_b128 v[248:251], v212 offset:56320
	global_load_lds_dwordx4 v[196:197], off
	s_add_i32 m0, s70, 0x2000
	s_add_u32 s68, s68, 0x20080
	v_lshl_add_u64 v[196:197], v[198:199], 0, s[56:57]
	s_addc_u32 s69, s69, 0
	s_add_i32 s70, s71, s72
	global_load_lds_dwordx4 v[196:197], off
	v_lshl_add_u64 v[196:197], s[68:69], 0, v[162:163]
	s_mov_b32 m0, s70
	s_nop 0
	global_load_lds_dwordx4 v[196:197], off
	v_lshl_add_u64 v[196:197], s[68:69], 0, v[164:165]
	s_add_i32 m0, s70, 0x2000
	s_nop 0
	global_load_lds_dwordx4 v[196:197], off
	v_lshl_add_u64 v[196:197], v[202:203], 0, s[56:57]
	s_mov_b32 m0, s77
	s_nop 0
	global_load_lds_dwordx4 v[196:197], off
	v_lshl_add_u64 v[196:197], v[200:201], 0, s[56:57]
	s_mov_b32 m0, s79
	s_nop 0
	global_load_lds_dwordx4 v[196:197], off
	s_waitcnt vmcnt(8) lgkmcnt(0)
	s_barrier
	s_setprio 1
	v_mfma_scale_f32_16x16x128_f8f6f4 v[94:97], v[26:33], v[170:177], v[94:97], v208, v207 op_sel_hi:[0,0,0]
	v_mfma_scale_f32_16x16x128_f8f6f4 v[86:89], v[18:25], v[170:177], v[86:89], v208, v207 op_sel_hi:[0,0,0]
	v_mfma_scale_f32_16x16x128_f8f6f4 v[78:81], v[26:33], v[214:221], v[78:81], v208, v207 op_sel_hi:[0,0,0]
	v_mfma_scale_f32_16x16x128_f8f6f4 v[70:73], v[18:25], v[214:221], v[70:73], v208, v207 op_sel_hi:[0,0,0]
	v_mfma_scale_f32_16x16x128_f8f6f4 v[62:65], v[26:33], v[236:243], v[62:65], v208, v207 op_sel_hi:[0,0,0]
	v_mfma_scale_f32_16x16x128_f8f6f4 v[54:57], v[18:25], v[236:243], v[54:57], v208, v207 op_sel_hi:[0,0,0]
	v_mfma_scale_f32_16x16x128_f8f6f4 v[46:49], v[26:33], v[244:251], v[46:49], v208, v207 op_sel_hi:[0,0,0]
	v_mfma_scale_f32_16x16x128_f8f6f4 v[38:41], v[18:25], v[244:251], v[38:41], v208, v207 op_sel_hi:[0,0,0]
	s_setprio 0
	s_setprio 1
	v_mfma_scale_f32_16x16x128_f8f6f4 v[90:93], v[10:17], v[170:177], v[90:93], v208, v207 op_sel_hi:[0,0,0]
	v_mfma_scale_f32_16x16x128_f8f6f4 v[82:85], v[2:9], v[170:177], v[82:85], v208, v207 op_sel_hi:[0,0,0]
	v_mfma_scale_f32_16x16x128_f8f6f4 v[74:77], v[10:17], v[214:221], v[74:77], v208, v207 op_sel_hi:[0,0,0]
	v_mfma_scale_f32_16x16x128_f8f6f4 v[66:69], v[2:9], v[214:221], v[66:69], v208, v207 op_sel_hi:[0,0,0]
	v_mfma_scale_f32_16x16x128_f8f6f4 v[58:61], v[10:17], v[236:243], v[58:61], v208, v207 op_sel_hi:[0,0,0]
	v_mfma_scale_f32_16x16x128_f8f6f4 v[50:53], v[2:9], v[236:243], v[50:53], v208, v207 op_sel_hi:[0,0,0]
	v_mfma_scale_f32_16x16x128_f8f6f4 v[42:45], v[10:17], v[244:251], v[42:45], v208, v207 op_sel_hi:[0,0,0]
	v_mfma_scale_f32_16x16x128_f8f6f4 v[34:37], v[2:9], v[244:251], v[34:37], v208, v207 op_sel_hi:[0,0,0]
	s_setprio 0
	s_barrier
	s_cmp_ge_i32 s91, s11
	s_cbranch_scc1 .LBB0_1695
	s_mov_b64 s[70:71], s[64:65]
	s_branch .LBB0_1691

.Lpeelph16_0:
	s_add_i32 s91, s64, 2
	s_add_u32 s62, s60, 0x100
	s_addc_u32 s63, s61, 0
	s_add_i32 s92, 0, 0x10000
	s_cmp_eq_u32 s74, s64
	s_cselect_b32 s69, s53, s63
	s_cselect_b32 s68, s52, s62
	s_cselect_b32 s65, s55, s59
	s_cselect_b32 s64, s54, s51
	s_add_i32 s93, 0, 0x14000
	v_add_u32_e32 v2, s92, v196
	v_add_u32_e32 v6, s93, v196
	ds_read_b128 v[26:29], v2
	ds_read_b128 v[30:33], v2 offset:1024
	ds_read_b128 v[18:21], v2 offset:2048
	ds_read_b128 v[22:25], v2 offset:3072
	ds_read_b128 v[10:13], v6
	ds_read_b128 v[14:17], v6 offset:1024
	ds_read_b128 v[2:5], v6 offset:2048
	ds_read_b128 v[6:9], v6 offset:3072
	v_lshl_add_u64 v[216:217], s[60:61], 0, v[184:185]
	s_add_i32 m0, s21, 0xc000
	ds_read_b128 v[170:173], v198
	ds_read_b128 v[174:177], v198 offset:1024
	ds_read_b128 v[186:189], v198 offset:2048
	ds_read_b128 v[190:193], v198 offset:3072
	ds_read_b128 v[200:203], v198 offset:4096
	ds_read_b128 v[204:207], v198 offset:5120
	ds_read_b128 v[208:211], v198 offset:6144
	ds_read_b128 v[212:215], v198 offset:7168
	global_load_lds_dwordx4 v[216:217], off
	v_lshl_add_u64 v[216:217], s[60:61], 0, v[182:183]
	s_add_i32 m0, s21, 0xe000
	s_nop 0
	global_load_lds_dwordx4 v[216:217], off
	s_waitcnt vmcnt(8) lgkmcnt(0)
	s_barrier
	s_setprio 1
	v_mfma_scale_f32_16x16x128_f8f6f4 v[154:157], v[26:33], v[170:177], 0, v194, v169 op_sel_hi:[0,0,0]
	v_mfma_scale_f32_16x16x128_f8f6f4 v[158:161], v[18:25], v[170:177], 0, v194, v169 op_sel_hi:[0,0,0]
	v_mfma_scale_f32_16x16x128_f8f6f4 v[138:141], v[26:33], v[186:193], 0, v194, v169 op_sel_hi:[0,0,0]
	v_mfma_scale_f32_16x16x128_f8f6f4 v[142:145], v[18:25], v[186:193], 0, v194, v169 op_sel_hi:[0,0,0]
	v_mfma_scale_f32_16x16x128_f8f6f4 v[122:125], v[26:33], v[200:207], 0, v194, v169 op_sel_hi:[0,0,0]
	v_mfma_scale_f32_16x16x128_f8f6f4 v[126:129], v[18:25], v[200:207], 0, v194, v169 op_sel_hi:[0,0,0]
	v_mfma_scale_f32_16x16x128_f8f6f4 v[106:109], v[26:33], v[208:215], 0, v194, v169 op_sel_hi:[0,0,0]
	v_mfma_scale_f32_16x16x128_f8f6f4 v[110:113], v[18:25], v[208:215], 0, v194, v169 op_sel_hi:[0,0,0]
	s_setprio 0
	s_setprio 1
	v_mfma_scale_f32_16x16x128_f8f6f4 v[146:149], v[10:17], v[170:177], 0, v194, v169 op_sel_hi:[0,0,0]
	v_mfma_scale_f32_16x16x128_f8f6f4 v[150:153], v[2:9], v[170:177], 0, v194, v169 op_sel_hi:[0,0,0]
	v_mfma_scale_f32_16x16x128_f8f6f4 v[130:133], v[10:17], v[186:193], 0, v194, v169 op_sel_hi:[0,0,0]
	v_mfma_scale_f32_16x16x128_f8f6f4 v[134:137], v[2:9], v[186:193], 0, v194, v169 op_sel_hi:[0,0,0]
	v_mfma_scale_f32_16x16x128_f8f6f4 v[114:117], v[10:17], v[200:207], 0, v194, v169 op_sel_hi:[0,0,0]
	v_mfma_scale_f32_16x16x128_f8f6f4 v[118:121], v[2:9], v[200:207], 0, v194, v169 op_sel_hi:[0,0,0]
	v_mfma_scale_f32_16x16x128_f8f6f4 v[98:101], v[10:17], v[208:215], 0, v194, v169 op_sel_hi:[0,0,0]
	v_mfma_scale_f32_16x16x128_f8f6f4 v[102:105], v[2:9], v[208:215], 0, v194, v169 op_sel_hi:[0,0,0]
	s_setprio 0
	s_barrier
	s_add_i32 s60, s92, s20
	v_lshl_add_u64 v[186:187], s[64:65], 0, v[164:165]
	s_mov_b32 m0, s60
	ds_read_b128 v[170:173], v198 offset:16384
	ds_read_b128 v[174:177], v198 offset:17408
	ds_read_b128 v[200:203], v198 offset:18432
	ds_read_b128 v[204:207], v198 offset:19456
	ds_read_b128 v[208:211], v198 offset:20480
	ds_read_b128 v[212:215], v198 offset:21504
	ds_read_b128 v[216:219], v198 offset:22528
	ds_read_b128 v[220:223], v198 offset:23552
	global_load_lds_dwordx4 v[186:187], off
	s_add_i32 m0, s60, 0x2000
	s_add_u32 s60, s64, 0x70000
	v_lshl_add_u64 v[188:189], s[64:65], 0, v[180:181]
	s_addc_u32 s61, s65, 0
	s_add_i32 s92, s93, s20
	global_load_lds_dwordx4 v[188:189], off
	v_lshl_add_u64 v[190:191], s[60:61], 0, v[164:165]
	s_mov_b32 m0, s92
	v_lshl_add_u64 v[192:193], s[68:69], 0, v[178:179]
	global_load_lds_dwordx4 v[190:191], off
	v_lshl_add_u64 v[190:191], s[60:61], 0, v[180:181]
	s_add_i32 m0, s92, 0x2000
	s_nop 0
	global_load_lds_dwordx4 v[190:191], off
	v_lshl_add_u64 v[190:191], s[68:69], 0, v[162:163]
	s_mov_b32 m0, s21
	s_nop 0
	global_load_lds_dwordx4 v[190:191], off
	s_mov_b32 m0, s22
	s_nop 0
	global_load_lds_dwordx4 v[192:193], off
	s_waitcnt vmcnt(8) lgkmcnt(0)
	s_barrier
	s_setprio 1
	v_mfma_scale_f32_16x16x128_f8f6f4 v[90:93], v[26:33], v[170:177], 0, v194, v169 op_sel_hi:[0,0,0]
	v_mfma_scale_f32_16x16x128_f8f6f4 v[94:97], v[18:25], v[170:177], 0, v194, v169 op_sel_hi:[0,0,0]
	v_mfma_scale_f32_16x16x128_f8f6f4 v[74:77], v[26:33], v[200:207], 0, v194, v169 op_sel_hi:[0,0,0]
	v_mfma_scale_f32_16x16x128_f8f6f4 v[78:81], v[18:25], v[200:207], 0, v194, v169 op_sel_hi:[0,0,0]
	v_mfma_scale_f32_16x16x128_f8f6f4 v[58:61], v[26:33], v[208:215], 0, v194, v169 op_sel_hi:[0,0,0]
	v_mfma_scale_f32_16x16x128_f8f6f4 v[62:65], v[18:25], v[208:215], 0, v194, v169 op_sel_hi:[0,0,0]
	v_mfma_scale_f32_16x16x128_f8f6f4 v[42:45], v[26:33], v[216:223], 0, v194, v169 op_sel_hi:[0,0,0]
	v_mfma_scale_f32_16x16x128_f8f6f4 v[46:49], v[18:25], v[216:223], 0, v194, v169 op_sel_hi:[0,0,0]
	s_setprio 0
	s_setprio 1
	v_mfma_scale_f32_16x16x128_f8f6f4 v[82:85], v[10:17], v[170:177], 0, v194, v169 op_sel_hi:[0,0,0]
	v_mfma_scale_f32_16x16x128_f8f6f4 v[86:89], v[2:9], v[170:177], 0, v194, v169 op_sel_hi:[0,0,0]
	v_mfma_scale_f32_16x16x128_f8f6f4 v[66:69], v[10:17], v[200:207], 0, v194, v169 op_sel_hi:[0,0,0]
	v_mfma_scale_f32_16x16x128_f8f6f4 v[70:73], v[2:9], v[200:207], 0, v194, v169 op_sel_hi:[0,0,0]
	v_mfma_scale_f32_16x16x128_f8f6f4 v[50:53], v[10:17], v[208:215], 0, v194, v169 op_sel_hi:[0,0,0]
	v_mfma_scale_f32_16x16x128_f8f6f4 v[54:57], v[2:9], v[208:215], 0, v194, v169 op_sel_hi:[0,0,0]
	v_mfma_scale_f32_16x16x128_f8f6f4 v[34:37], v[10:17], v[216:223], 0, v194, v169 op_sel_hi:[0,0,0]
	v_mfma_scale_f32_16x16x128_f8f6f4 v[38:41], v[2:9], v[216:223], 0, v194, v169 op_sel_hi:[0,0,0]
	s_setprio 0
	s_barrier
	s_add_i32 s92, 0, 0x18000
	s_add_i32 s93, 0, 0x1c000
	v_add_u32_e32 v2, s92, v196
	v_add_u32_e32 v6, s93, v196
	ds_read_b128 v[26:29], v2
	ds_read_b128 v[30:33], v2 offset:1024
	ds_read_b128 v[18:21], v2 offset:2048
	ds_read_b128 v[22:25], v2 offset:3072
	ds_read_b128 v[10:13], v6
	ds_read_b128 v[14:17], v6 offset:1024
	ds_read_b128 v[2:5], v6 offset:2048
	ds_read_b128 v[6:9], v6 offset:3072
	s_add_u32 s60, s68, 0x70000
	s_addc_u32 s61, s69, 0
	s_mov_b32 m0, s23
	v_lshl_add_u64 v[232:233], s[60:61], 0, v[162:163]
	ds_read_b128 v[170:173], v198 offset:32768
	ds_read_b128 v[174:177], v198 offset:33792
	ds_read_b128 v[200:203], v198 offset:34816
	ds_read_b128 v[204:207], v198 offset:35840
	ds_read_b128 v[208:211], v198 offset:36864
	ds_read_b128 v[212:215], v198 offset:37888
	ds_read_b128 v[216:219], v198 offset:38912
	ds_read_b128 v[220:223], v198 offset:39936
	global_load_lds_dwordx4 v[232:233], off
	v_lshl_add_u64 v[232:233], s[60:61], 0, v[178:179]
	s_mov_b32 m0, s70
	s_nop 0
	global_load_lds_dwordx4 v[232:233], off
	s_waitcnt vmcnt(8) lgkmcnt(0)
	s_barrier
	s_setprio 1
	v_mfma_scale_f32_16x16x128_f8f6f4 v[154:157], v[26:33], v[170:177], v[154:157], v194, v169 op_sel_hi:[0,0,0]
	v_mfma_scale_f32_16x16x128_f8f6f4 v[158:161], v[18:25], v[170:177], v[158:161], v194, v169 op_sel_hi:[0,0,0]
	v_mfma_scale_f32_16x16x128_f8f6f4 v[138:141], v[26:33], v[200:207], v[138:141], v194, v169 op_sel_hi:[0,0,0]
	v_mfma_scale_f32_16x16x128_f8f6f4 v[142:145], v[18:25], v[200:207], v[142:145], v194, v169 op_sel_hi:[0,0,0]
	v_mfma_scale_f32_16x16x128_f8f6f4 v[122:125], v[26:33], v[208:215], v[122:125], v194, v169 op_sel_hi:[0,0,0]
	v_mfma_scale_f32_16x16x128_f8f6f4 v[126:129], v[18:25], v[208:215], v[126:129], v194, v169 op_sel_hi:[0,0,0]
	v_mfma_scale_f32_16x16x128_f8f6f4 v[106:109], v[26:33], v[216:223], v[106:109], v194, v169 op_sel_hi:[0,0,0]
	v_mfma_scale_f32_16x16x128_f8f6f4 v[110:113], v[18:25], v[216:223], v[110:113], v194, v169 op_sel_hi:[0,0,0]
	s_setprio 0
	s_setprio 1
	v_mfma_scale_f32_16x16x128_f8f6f4 v[146:149], v[10:17], v[170:177], v[146:149], v194, v169 op_sel_hi:[0,0,0]
	v_mfma_scale_f32_16x16x128_f8f6f4 v[150:153], v[2:9], v[170:177], v[150:153], v194, v169 op_sel_hi:[0,0,0]
	v_mfma_scale_f32_16x16x128_f8f6f4 v[130:133], v[10:17], v[200:207], v[130:133], v194, v169 op_sel_hi:[0,0,0]
	v_mfma_scale_f32_16x16x128_f8f6f4 v[134:137], v[2:9], v[200:207], v[134:137], v194, v169 op_sel_hi:[0,0,0]
	v_mfma_scale_f32_16x16x128_f8f6f4 v[114:117], v[10:17], v[208:215], v[114:117], v194, v169 op_sel_hi:[0,0,0]
	v_mfma_scale_f32_16x16x128_f8f6f4 v[118:121], v[2:9], v[208:215], v[118:121], v194, v169 op_sel_hi:[0,0,0]
	v_mfma_scale_f32_16x16x128_f8f6f4 v[98:101], v[10:17], v[216:223], v[98:101], v194, v169 op_sel_hi:[0,0,0]
	v_mfma_scale_f32_16x16x128_f8f6f4 v[102:105], v[2:9], v[216:223], v[102:105], v194, v169 op_sel_hi:[0,0,0]
	s_setprio 0
	s_barrier
	s_add_i32 s60, s92, s20
	v_lshl_add_u64 v[186:187], v[186:187], 0, s[56:57]
	s_mov_b32 m0, s60
	ds_read_b128 v[170:173], v198 offset:49152
	ds_read_b128 v[174:177], v198 offset:50176
	ds_read_b128 v[200:203], v198 offset:51200
	ds_read_b128 v[204:207], v198 offset:52224
	ds_read_b128 v[208:211], v198 offset:53248
	ds_read_b128 v[212:215], v198 offset:54272
	ds_read_b128 v[216:219], v198 offset:55296
	ds_read_b128 v[220:223], v198 offset:56320
	global_load_lds_dwordx4 v[186:187], off
	s_add_i32 m0, s60, 0x2000
	s_add_u32 s60, s64, 0x70080
	v_lshl_add_u64 v[186:187], v[188:189], 0, s[56:57]
	s_addc_u32 s61, s65, 0
	s_add_i32 s64, s93, s20
	global_load_lds_dwordx4 v[186:187], off
	v_lshl_add_u64 v[186:187], s[60:61], 0, v[164:165]
	s_mov_b32 m0, s64
	s_nop 0
	global_load_lds_dwordx4 v[186:187], off
	v_lshl_add_u64 v[186:187], s[60:61], 0, v[180:181]
	s_add_i32 m0, s64, 0x2000
	s_nop 0
	global_load_lds_dwordx4 v[186:187], off
	v_lshl_add_u64 v[186:187], v[190:191], 0, s[56:57]
	s_mov_b32 m0, s71
	s_nop 0
	global_load_lds_dwordx4 v[186:187], off
	v_lshl_add_u64 v[186:187], v[192:193], 0, s[56:57]
	s_mov_b32 m0, s72
	s_nop 0
	global_load_lds_dwordx4 v[186:187], off
	s_waitcnt vmcnt(8) lgkmcnt(0)
	s_barrier
	s_setprio 1
	v_mfma_scale_f32_16x16x128_f8f6f4 v[90:93], v[26:33], v[170:177], v[90:93], v194, v169 op_sel_hi:[0,0,0]
	v_mfma_scale_f32_16x16x128_f8f6f4 v[94:97], v[18:25], v[170:177], v[94:97], v194, v169 op_sel_hi:[0,0,0]
	v_mfma_scale_f32_16x16x128_f8f6f4 v[74:77], v[26:33], v[200:207], v[74:77], v194, v169 op_sel_hi:[0,0,0]
	v_mfma_scale_f32_16x16x128_f8f6f4 v[78:81], v[18:25], v[200:207], v[78:81], v194, v169 op_sel_hi:[0,0,0]
	v_mfma_scale_f32_16x16x128_f8f6f4 v[58:61], v[26:33], v[208:215], v[58:61], v194, v169 op_sel_hi:[0,0,0]
	v_mfma_scale_f32_16x16x128_f8f6f4 v[62:65], v[18:25], v[208:215], v[62:65], v194, v169 op_sel_hi:[0,0,0]
	v_mfma_scale_f32_16x16x128_f8f6f4 v[42:45], v[26:33], v[216:223], v[42:45], v194, v169 op_sel_hi:[0,0,0]
	v_mfma_scale_f32_16x16x128_f8f6f4 v[46:49], v[18:25], v[216:223], v[46:49], v194, v169 op_sel_hi:[0,0,0]
	s_setprio 0
	s_setprio 1
	v_mfma_scale_f32_16x16x128_f8f6f4 v[82:85], v[10:17], v[170:177], v[82:85], v194, v169 op_sel_hi:[0,0,0]
	v_mfma_scale_f32_16x16x128_f8f6f4 v[86:89], v[2:9], v[170:177], v[86:89], v194, v169 op_sel_hi:[0,0,0]
	v_mfma_scale_f32_16x16x128_f8f6f4 v[66:69], v[10:17], v[200:207], v[66:69], v194, v169 op_sel_hi:[0,0,0]
	v_mfma_scale_f32_16x16x128_f8f6f4 v[70:73], v[2:9], v[200:207], v[70:73], v194, v169 op_sel_hi:[0,0,0]
	v_mfma_scale_f32_16x16x128_f8f6f4 v[50:53], v[10:17], v[208:215], v[50:53], v194, v169 op_sel_hi:[0,0,0]
	v_mfma_scale_f32_16x16x128_f8f6f4 v[54:57], v[2:9], v[208:215], v[54:57], v194, v169 op_sel_hi:[0,0,0]
	v_mfma_scale_f32_16x16x128_f8f6f4 v[34:37], v[10:17], v[216:223], v[34:37], v194, v169 op_sel_hi:[0,0,0]
	v_mfma_scale_f32_16x16x128_f8f6f4 v[38:41], v[2:9], v[216:223], v[38:41], v194, v169 op_sel_hi:[0,0,0]
	s_setprio 0
	s_barrier
	s_add_u32 s51, s51, 0x100
	s_addc_u32 s59, s59, 0
	s_cmp_ge_i32 s91, s8
	s_mov_b64 s[60:61], s[62:63]
	s_mov_b32 s64, s91
	s_cbranch_scc0 .LBB0_1777
	s_branch .Lpeelexitph16
.LBB0_1777:
	s_add_i32 s91, s64, 2
	s_add_u32 s62, s60, 0x100
	s_addc_u32 s63, s61, 0
	s_add_i32 s92, 0, 0x10000
	s_cmp_eq_u32 s74, s64
	s_cselect_b32 s69, s53, s63
	s_cselect_b32 s68, s52, s62
	s_cselect_b32 s65, s55, s59
	s_cselect_b32 s64, s54, s51
	s_add_i32 s93, 0, 0x14000
	v_add_u32_e32 v2, s92, v196
	v_add_u32_e32 v6, s93, v196
	ds_read_b128 v[26:29], v2
	ds_read_b128 v[30:33], v2 offset:1024
	ds_read_b128 v[18:21], v2 offset:2048
	ds_read_b128 v[22:25], v2 offset:3072
	ds_read_b128 v[10:13], v6
	ds_read_b128 v[14:17], v6 offset:1024
	ds_read_b128 v[2:5], v6 offset:2048
	ds_read_b128 v[6:9], v6 offset:3072
	v_lshl_add_u64 v[216:217], s[60:61], 0, v[184:185]
	s_add_i32 m0, s21, 0xc000
	ds_read_b128 v[170:173], v198
	ds_read_b128 v[174:177], v198 offset:1024
	ds_read_b128 v[186:189], v198 offset:2048
	ds_read_b128 v[190:193], v198 offset:3072
	ds_read_b128 v[200:203], v198 offset:4096
	ds_read_b128 v[204:207], v198 offset:5120
	ds_read_b128 v[208:211], v198 offset:6144
	ds_read_b128 v[212:215], v198 offset:7168
	global_load_lds_dwordx4 v[216:217], off
	v_lshl_add_u64 v[216:217], s[60:61], 0, v[182:183]
	s_add_i32 m0, s21, 0xe000
	s_nop 0
	global_load_lds_dwordx4 v[216:217], off
	s_waitcnt vmcnt(8) lgkmcnt(0)
	s_barrier
	s_setprio 1
	v_mfma_scale_f32_16x16x128_f8f6f4 v[154:157], v[26:33], v[170:177], v[154:157], v194, v169 op_sel_hi:[0,0,0]
	v_mfma_scale_f32_16x16x128_f8f6f4 v[158:161], v[18:25], v[170:177], v[158:161], v194, v169 op_sel_hi:[0,0,0]
	v_mfma_scale_f32_16x16x128_f8f6f4 v[138:141], v[26:33], v[186:193], v[138:141], v194, v169 op_sel_hi:[0,0,0]
	v_mfma_scale_f32_16x16x128_f8f6f4 v[142:145], v[18:25], v[186:193], v[142:145], v194, v169 op_sel_hi:[0,0,0]
	v_mfma_scale_f32_16x16x128_f8f6f4 v[122:125], v[26:33], v[200:207], v[122:125], v194, v169 op_sel_hi:[0,0,0]
	v_mfma_scale_f32_16x16x128_f8f6f4 v[126:129], v[18:25], v[200:207], v[126:129], v194, v169 op_sel_hi:[0,0,0]
	v_mfma_scale_f32_16x16x128_f8f6f4 v[106:109], v[26:33], v[208:215], v[106:109], v194, v169 op_sel_hi:[0,0,0]
	v_mfma_scale_f32_16x16x128_f8f6f4 v[110:113], v[18:25], v[208:215], v[110:113], v194, v169 op_sel_hi:[0,0,0]
	s_setprio 0
	s_setprio 1
	v_mfma_scale_f32_16x16x128_f8f6f4 v[146:149], v[10:17], v[170:177], v[146:149], v194, v169 op_sel_hi:[0,0,0]
	v_mfma_scale_f32_16x16x128_f8f6f4 v[150:153], v[2:9], v[170:177], v[150:153], v194, v169 op_sel_hi:[0,0,0]
	v_mfma_scale_f32_16x16x128_f8f6f4 v[130:133], v[10:17], v[186:193], v[130:133], v194, v169 op_sel_hi:[0,0,0]
	v_mfma_scale_f32_16x16x128_f8f6f4 v[134:137], v[2:9], v[186:193], v[134:137], v194, v169 op_sel_hi:[0,0,0]
	v_mfma_scale_f32_16x16x128_f8f6f4 v[114:117], v[10:17], v[200:207], v[114:117], v194, v169 op_sel_hi:[0,0,0]
	v_mfma_scale_f32_16x16x128_f8f6f4 v[118:121], v[2:9], v[200:207], v[118:121], v194, v169 op_sel_hi:[0,0,0]
	v_mfma_scale_f32_16x16x128_f8f6f4 v[98:101], v[10:17], v[208:215], v[98:101], v194, v169 op_sel_hi:[0,0,0]
	v_mfma_scale_f32_16x16x128_f8f6f4 v[102:105], v[2:9], v[208:215], v[102:105], v194, v169 op_sel_hi:[0,0,0]
	s_setprio 0
	s_barrier
	s_add_i32 s60, s92, s20
	v_lshl_add_u64 v[186:187], s[64:65], 0, v[164:165]
	s_mov_b32 m0, s60
	ds_read_b128 v[170:173], v198 offset:16384
	ds_read_b128 v[174:177], v198 offset:17408
	ds_read_b128 v[200:203], v198 offset:18432
	ds_read_b128 v[204:207], v198 offset:19456
	ds_read_b128 v[208:211], v198 offset:20480
	ds_read_b128 v[212:215], v198 offset:21504
	ds_read_b128 v[216:219], v198 offset:22528
	ds_read_b128 v[220:223], v198 offset:23552
	global_load_lds_dwordx4 v[186:187], off
	s_add_i32 m0, s60, 0x2000
	s_add_u32 s60, s64, 0x70000
	v_lshl_add_u64 v[188:189], s[64:65], 0, v[180:181]
	s_addc_u32 s61, s65, 0
	s_add_i32 s92, s93, s20
	global_load_lds_dwordx4 v[188:189], off
	v_lshl_add_u64 v[190:191], s[60:61], 0, v[164:165]
	s_mov_b32 m0, s92
	v_lshl_add_u64 v[192:193], s[68:69], 0, v[178:179]
	global_load_lds_dwordx4 v[190:191], off
	v_lshl_add_u64 v[190:191], s[60:61], 0, v[180:181]
	s_add_i32 m0, s92, 0x2000
	s_nop 0
	global_load_lds_dwordx4 v[190:191], off
	v_lshl_add_u64 v[190:191], s[68:69], 0, v[162:163]
	s_mov_b32 m0, s21
	s_nop 0
	global_load_lds_dwordx4 v[190:191], off
	s_mov_b32 m0, s22
	s_nop 0
	global_load_lds_dwordx4 v[192:193], off
	s_waitcnt vmcnt(8) lgkmcnt(0)
	s_barrier
	s_setprio 1
	v_mfma_scale_f32_16x16x128_f8f6f4 v[90:93], v[26:33], v[170:177], v[90:93], v194, v169 op_sel_hi:[0,0,0]
	v_mfma_scale_f32_16x16x128_f8f6f4 v[94:97], v[18:25], v[170:177], v[94:97], v194, v169 op_sel_hi:[0,0,0]
	v_mfma_scale_f32_16x16x128_f8f6f4 v[74:77], v[26:33], v[200:207], v[74:77], v194, v169 op_sel_hi:[0,0,0]
	v_mfma_scale_f32_16x16x128_f8f6f4 v[78:81], v[18:25], v[200:207], v[78:81], v194, v169 op_sel_hi:[0,0,0]
	v_mfma_scale_f32_16x16x128_f8f6f4 v[58:61], v[26:33], v[208:215], v[58:61], v194, v169 op_sel_hi:[0,0,0]
	v_mfma_scale_f32_16x16x128_f8f6f4 v[62:65], v[18:25], v[208:215], v[62:65], v194, v169 op_sel_hi:[0,0,0]
	v_mfma_scale_f32_16x16x128_f8f6f4 v[42:45], v[26:33], v[216:223], v[42:45], v194, v169 op_sel_hi:[0,0,0]
	v_mfma_scale_f32_16x16x128_f8f6f4 v[46:49], v[18:25], v[216:223], v[46:49], v194, v169 op_sel_hi:[0,0,0]
	s_setprio 0
	s_setprio 1
	v_mfma_scale_f32_16x16x128_f8f6f4 v[82:85], v[10:17], v[170:177], v[82:85], v194, v169 op_sel_hi:[0,0,0]
	v_mfma_scale_f32_16x16x128_f8f6f4 v[86:89], v[2:9], v[170:177], v[86:89], v194, v169 op_sel_hi:[0,0,0]
	v_mfma_scale_f32_16x16x128_f8f6f4 v[66:69], v[10:17], v[200:207], v[66:69], v194, v169 op_sel_hi:[0,0,0]
	v_mfma_scale_f32_16x16x128_f8f6f4 v[70:73], v[2:9], v[200:207], v[70:73], v194, v169 op_sel_hi:[0,0,0]
	v_mfma_scale_f32_16x16x128_f8f6f4 v[50:53], v[10:17], v[208:215], v[50:53], v194, v169 op_sel_hi:[0,0,0]
	v_mfma_scale_f32_16x16x128_f8f6f4 v[54:57], v[2:9], v[208:215], v[54:57], v194, v169 op_sel_hi:[0,0,0]
	v_mfma_scale_f32_16x16x128_f8f6f4 v[34:37], v[10:17], v[216:223], v[34:37], v194, v169 op_sel_hi:[0,0,0]
	v_mfma_scale_f32_16x16x128_f8f6f4 v[38:41], v[2:9], v[216:223], v[38:41], v194, v169 op_sel_hi:[0,0,0]
	s_setprio 0
	s_barrier
	s_add_i32 s92, 0, 0x18000
	s_add_i32 s93, 0, 0x1c000
	v_add_u32_e32 v2, s92, v196
	v_add_u32_e32 v6, s93, v196
	ds_read_b128 v[26:29], v2
	ds_read_b128 v[30:33], v2 offset:1024
	ds_read_b128 v[18:21], v2 offset:2048
	ds_read_b128 v[22:25], v2 offset:3072
	ds_read_b128 v[10:13], v6
	ds_read_b128 v[14:17], v6 offset:1024
	ds_read_b128 v[2:5], v6 offset:2048
	ds_read_b128 v[6:9], v6 offset:3072
	s_add_u32 s60, s68, 0x70000
	s_addc_u32 s61, s69, 0
	s_mov_b32 m0, s23
	v_lshl_add_u64 v[232:233], s[60:61], 0, v[162:163]
	ds_read_b128 v[170:173], v198 offset:32768
	ds_read_b128 v[174:177], v198 offset:33792
	ds_read_b128 v[200:203], v198 offset:34816
	ds_read_b128 v[204:207], v198 offset:35840
	ds_read_b128 v[208:211], v198 offset:36864
	ds_read_b128 v[212:215], v198 offset:37888
	ds_read_b128 v[216:219], v198 offset:38912
	ds_read_b128 v[220:223], v198 offset:39936
	global_load_lds_dwordx4 v[232:233], off
	v_lshl_add_u64 v[232:233], s[60:61], 0, v[178:179]
	s_mov_b32 m0, s70
	s_nop 0
	global_load_lds_dwordx4 v[232:233], off
	s_waitcnt vmcnt(8) lgkmcnt(0)
	s_barrier
	s_setprio 1
	v_mfma_scale_f32_16x16x128_f8f6f4 v[154:157], v[26:33], v[170:177], v[154:157], v194, v169 op_sel_hi:[0,0,0]
	v_mfma_scale_f32_16x16x128_f8f6f4 v[158:161], v[18:25], v[170:177], v[158:161], v194, v169 op_sel_hi:[0,0,0]
	v_mfma_scale_f32_16x16x128_f8f6f4 v[138:141], v[26:33], v[200:207], v[138:141], v194, v169 op_sel_hi:[0,0,0]
	v_mfma_scale_f32_16x16x128_f8f6f4 v[142:145], v[18:25], v[200:207], v[142:145], v194, v169 op_sel_hi:[0,0,0]
	v_mfma_scale_f32_16x16x128_f8f6f4 v[122:125], v[26:33], v[208:215], v[122:125], v194, v169 op_sel_hi:[0,0,0]
	v_mfma_scale_f32_16x16x128_f8f6f4 v[126:129], v[18:25], v[208:215], v[126:129], v194, v169 op_sel_hi:[0,0,0]
	v_mfma_scale_f32_16x16x128_f8f6f4 v[106:109], v[26:33], v[216:223], v[106:109], v194, v169 op_sel_hi:[0,0,0]
	v_mfma_scale_f32_16x16x128_f8f6f4 v[110:113], v[18:25], v[216:223], v[110:113], v194, v169 op_sel_hi:[0,0,0]
	s_setprio 0
	s_setprio 1
	v_mfma_scale_f32_16x16x128_f8f6f4 v[146:149], v[10:17], v[170:177], v[146:149], v194, v169 op_sel_hi:[0,0,0]
	v_mfma_scale_f32_16x16x128_f8f6f4 v[150:153], v[2:9], v[170:177], v[150:153], v194, v169 op_sel_hi:[0,0,0]
	v_mfma_scale_f32_16x16x128_f8f6f4 v[130:133], v[10:17], v[200:207], v[130:133], v194, v169 op_sel_hi:[0,0,0]
	v_mfma_scale_f32_16x16x128_f8f6f4 v[134:137], v[2:9], v[200:207], v[134:137], v194, v169 op_sel_hi:[0,0,0]
	v_mfma_scale_f32_16x16x128_f8f6f4 v[114:117], v[10:17], v[208:215], v[114:117], v194, v169 op_sel_hi:[0,0,0]
	v_mfma_scale_f32_16x16x128_f8f6f4 v[118:121], v[2:9], v[208:215], v[118:121], v194, v169 op_sel_hi:[0,0,0]
	v_mfma_scale_f32_16x16x128_f8f6f4 v[98:101], v[10:17], v[216:223], v[98:101], v194, v169 op_sel_hi:[0,0,0]
	v_mfma_scale_f32_16x16x128_f8f6f4 v[102:105], v[2:9], v[216:223], v[102:105], v194, v169 op_sel_hi:[0,0,0]
	s_setprio 0
	s_barrier
	s_add_i32 s60, s92, s20
	v_lshl_add_u64 v[186:187], v[186:187], 0, s[56:57]
	s_mov_b32 m0, s60
	ds_read_b128 v[170:173], v198 offset:49152
	ds_read_b128 v[174:177], v198 offset:50176
	ds_read_b128 v[200:203], v198 offset:51200
	ds_read_b128 v[204:207], v198 offset:52224
	ds_read_b128 v[208:211], v198 offset:53248
	ds_read_b128 v[212:215], v198 offset:54272
	ds_read_b128 v[216:219], v198 offset:55296
	ds_read_b128 v[220:223], v198 offset:56320
	global_load_lds_dwordx4 v[186:187], off
	s_add_i32 m0, s60, 0x2000
	s_add_u32 s60, s64, 0x70080
	v_lshl_add_u64 v[186:187], v[188:189], 0, s[56:57]
	s_addc_u32 s61, s65, 0
	s_add_i32 s64, s93, s20
	global_load_lds_dwordx4 v[186:187], off
	v_lshl_add_u64 v[186:187], s[60:61], 0, v[164:165]
	s_mov_b32 m0, s64
	s_nop 0
	global_load_lds_dwordx4 v[186:187], off
	v_lshl_add_u64 v[186:187], s[60:61], 0, v[180:181]
	s_add_i32 m0, s64, 0x2000
	s_nop 0
	global_load_lds_dwordx4 v[186:187], off
	v_lshl_add_u64 v[186:187], v[190:191], 0, s[56:57]
	s_mov_b32 m0, s71
	s_nop 0
	global_load_lds_dwordx4 v[186:187], off
	v_lshl_add_u64 v[186:187], v[192:193], 0, s[56:57]
	s_mov_b32 m0, s72
	s_nop 0
	global_load_lds_dwordx4 v[186:187], off
	s_waitcnt vmcnt(8) lgkmcnt(0)
	s_barrier
	s_setprio 1
	v_mfma_scale_f32_16x16x128_f8f6f4 v[90:93], v[26:33], v[170:177], v[90:93], v194, v169 op_sel_hi:[0,0,0]
	v_mfma_scale_f32_16x16x128_f8f6f4 v[94:97], v[18:25], v[170:177], v[94:97], v194, v169 op_sel_hi:[0,0,0]
	v_mfma_scale_f32_16x16x128_f8f6f4 v[74:77], v[26:33], v[200:207], v[74:77], v194, v169 op_sel_hi:[0,0,0]
	v_mfma_scale_f32_16x16x128_f8f6f4 v[78:81], v[18:25], v[200:207], v[78:81], v194, v169 op_sel_hi:[0,0,0]
	v_mfma_scale_f32_16x16x128_f8f6f4 v[58:61], v[26:33], v[208:215], v[58:61], v194, v169 op_sel_hi:[0,0,0]
	v_mfma_scale_f32_16x16x128_f8f6f4 v[62:65], v[18:25], v[208:215], v[62:65], v194, v169 op_sel_hi:[0,0,0]
	v_mfma_scale_f32_16x16x128_f8f6f4 v[42:45], v[26:33], v[216:223], v[42:45], v194, v169 op_sel_hi:[0,0,0]
	v_mfma_scale_f32_16x16x128_f8f6f4 v[46:49], v[18:25], v[216:223], v[46:49], v194, v169 op_sel_hi:[0,0,0]
	s_setprio 0
	s_setprio 1
	v_mfma_scale_f32_16x16x128_f8f6f4 v[82:85], v[10:17], v[170:177], v[82:85], v194, v169 op_sel_hi:[0,0,0]
	v_mfma_scale_f32_16x16x128_f8f6f4 v[86:89], v[2:9], v[170:177], v[86:89], v194, v169 op_sel_hi:[0,0,0]
	v_mfma_scale_f32_16x16x128_f8f6f4 v[66:69], v[10:17], v[200:207], v[66:69], v194, v169 op_sel_hi:[0,0,0]
	v_mfma_scale_f32_16x16x128_f8f6f4 v[70:73], v[2:9], v[200:207], v[70:73], v194, v169 op_sel_hi:[0,0,0]
	v_mfma_scale_f32_16x16x128_f8f6f4 v[50:53], v[10:17], v[208:215], v[50:53], v194, v169 op_sel_hi:[0,0,0]
	v_mfma_scale_f32_16x16x128_f8f6f4 v[54:57], v[2:9], v[208:215], v[54:57], v194, v169 op_sel_hi:[0,0,0]
	v_mfma_scale_f32_16x16x128_f8f6f4 v[34:37], v[10:17], v[216:223], v[34:37], v194, v169 op_sel_hi:[0,0,0]
	v_mfma_scale_f32_16x16x128_f8f6f4 v[38:41], v[2:9], v[216:223], v[38:41], v194, v169 op_sel_hi:[0,0,0]
	s_setprio 0
	s_barrier
	s_add_u32 s51, s51, 0x100
	s_addc_u32 s59, s59, 0
	s_cmp_ge_i32 s91, s8
	s_mov_b64 s[60:61], s[62:63]
	s_mov_b32 s64, s91
	s_cbranch_scc0 .LBB0_1777

.Lpeelph17_1:
	s_add_i32 s55, s55, 2
	s_add_u32 s60, s64, 0x100
	s_addc_u32 s61, s65, 0
	s_and_b64 s[68:69], s[62:63], exec
	s_cselect_b32 s68, 0, s60
	s_cselect_b32 s69, 0, s61
	s_add_u32 s68, s30, s68
	s_addc_u32 s69, s31, s69
	s_add_u32 s91, s47, s64
	s_addc_u32 s92, s49, s65
	s_and_b64 s[62:63], s[62:63], exec
	s_cselect_b32 s63, s53, s92
	s_cselect_b32 s62, s52, s91
	s_add_i32 s92, 0, 0x10000
	s_add_i32 s91, 0, 0x14000
	v_add_u32_e32 v2, s92, v210
	v_add_u32_e32 v6, s91, v210
	ds_read_b128 v[26:29], v2
	ds_read_b128 v[30:33], v2 offset:1024
	ds_read_b128 v[18:21], v2 offset:2048
	ds_read_b128 v[22:25], v2 offset:3072
	ds_read_b128 v[10:13], v6
	ds_read_b128 v[14:17], v6 offset:1024
	ds_read_b128 v[2:5], v6 offset:2048
	ds_read_b128 v[6:9], v6 offset:3072
	v_lshl_add_u64 v[222:223], v[194:195], 0, s[64:65]
	s_add_i32 m0, s59, 0xc000
	ds_read_b128 v[170:173], v212
	ds_read_b128 v[174:177], v212 offset:1024
	ds_read_b128 v[196:199], v212 offset:2048
	ds_read_b128 v[200:203], v212 offset:3072
	ds_read_b128 v[214:217], v212 offset:4096
	ds_read_b128 v[218:221], v212 offset:5120
	ds_read_b128 v[236:239], v212 offset:6144
	ds_read_b128 v[240:243], v212 offset:7168
	global_load_lds_dwordx4 v[222:223], off
	v_lshl_add_u64 v[222:223], v[192:193], 0, s[64:65]
	s_add_i32 m0, s59, 0xe000
	s_nop 0
	global_load_lds_dwordx4 v[222:223], off
	s_waitcnt vmcnt(8) lgkmcnt(0)
	s_barrier
	s_setprio 1
	v_mfma_scale_f32_16x16x128_f8f6f4 v[154:157], v[26:33], v[170:177], 0, v208, v207 op_sel_hi:[0,0,0]
	v_mfma_scale_f32_16x16x128_f8f6f4 v[150:153], v[18:25], v[170:177], 0, v208, v207 op_sel_hi:[0,0,0]
	v_mfma_scale_f32_16x16x128_f8f6f4 v[142:145], v[26:33], v[196:203], 0, v208, v207 op_sel_hi:[0,0,0]
	v_mfma_scale_f32_16x16x128_f8f6f4 v[134:137], v[18:25], v[196:203], 0, v208, v207 op_sel_hi:[0,0,0]
	v_mfma_scale_f32_16x16x128_f8f6f4 v[126:129], v[26:33], v[214:221], 0, v208, v207 op_sel_hi:[0,0,0]
	v_mfma_scale_f32_16x16x128_f8f6f4 v[118:121], v[18:25], v[214:221], 0, v208, v207 op_sel_hi:[0,0,0]
	v_mfma_scale_f32_16x16x128_f8f6f4 v[110:113], v[26:33], v[236:243], 0, v208, v207 op_sel_hi:[0,0,0]
	v_mfma_scale_f32_16x16x128_f8f6f4 v[102:105], v[18:25], v[236:243], 0, v208, v207 op_sel_hi:[0,0,0]
	s_setprio 0
	s_setprio 1
	v_mfma_scale_f32_16x16x128_f8f6f4 v[158:161], v[10:17], v[170:177], 0, v208, v207 op_sel_hi:[0,0,0]
	v_mfma_scale_f32_16x16x128_f8f6f4 v[146:149], v[2:9], v[170:177], 0, v208, v207 op_sel_hi:[0,0,0]
	v_mfma_scale_f32_16x16x128_f8f6f4 v[138:141], v[10:17], v[196:203], 0, v208, v207 op_sel_hi:[0,0,0]
	v_mfma_scale_f32_16x16x128_f8f6f4 v[130:133], v[2:9], v[196:203], 0, v208, v207 op_sel_hi:[0,0,0]
	v_mfma_scale_f32_16x16x128_f8f6f4 v[122:125], v[10:17], v[214:221], 0, v208, v207 op_sel_hi:[0,0,0]
	v_mfma_scale_f32_16x16x128_f8f6f4 v[114:117], v[2:9], v[214:221], 0, v208, v207 op_sel_hi:[0,0,0]
	v_mfma_scale_f32_16x16x128_f8f6f4 v[106:109], v[10:17], v[236:243], 0, v208, v207 op_sel_hi:[0,0,0]
	v_mfma_scale_f32_16x16x128_f8f6f4 v[98:101], v[2:9], v[236:243], 0, v208, v207 op_sel_hi:[0,0,0]
	s_setprio 0
	s_barrier
	s_add_i32 s64, s92, s22
	v_lshl_add_u64 v[196:197], s[62:63], 0, v[162:163]
	s_mov_b32 m0, s64
	ds_read_b128 v[170:173], v212 offset:16384
	ds_read_b128 v[174:177], v212 offset:17408
	ds_read_b128 v[214:217], v212 offset:18432
	ds_read_b128 v[218:221], v212 offset:19456
	ds_read_b128 v[236:239], v212 offset:20480
	ds_read_b128 v[240:243], v212 offset:21504
	ds_read_b128 v[244:247], v212 offset:22528
	ds_read_b128 v[248:251], v212 offset:23552
	global_load_lds_dwordx4 v[196:197], off
	s_add_i32 m0, s64, 0x2000
	s_add_u32 s64, s62, 0x20000
	v_lshl_add_u64 v[198:199], s[62:63], 0, v[164:165]
	s_addc_u32 s65, s63, 0
	s_add_i32 s91, s91, s22
	global_load_lds_dwordx4 v[198:199], off
	v_lshl_add_u64 v[200:201], s[64:65], 0, v[162:163]
	s_mov_b32 m0, s91
	v_mov_b32_e32 v179, v167
	global_load_lds_dwordx4 v[200:201], off
	v_lshl_add_u64 v[200:201], s[64:65], 0, v[164:165]
	s_add_i32 m0, s91, 0x2000
	v_lshl_add_u64 v[202:203], s[68:69], 0, v[166:167]
	global_load_lds_dwordx4 v[200:201], off
	s_mov_b32 m0, s59
	v_lshl_add_u64 v[200:201], s[68:69], 0, v[178:179]
	global_load_lds_dwordx4 v166, s[68:69]
	s_mov_b32 m0, s71
	s_nop 0
	global_load_lds_dwordx4 v178, s[68:69]
	s_waitcnt vmcnt(8) lgkmcnt(0)
	s_barrier
	s_setprio 1
	v_mfma_scale_f32_16x16x128_f8f6f4 v[94:97], v[26:33], v[170:177], 0, v208, v207 op_sel_hi:[0,0,0]
	v_mfma_scale_f32_16x16x128_f8f6f4 v[86:89], v[18:25], v[170:177], 0, v208, v207 op_sel_hi:[0,0,0]
	v_mfma_scale_f32_16x16x128_f8f6f4 v[78:81], v[26:33], v[214:221], 0, v208, v207 op_sel_hi:[0,0,0]
	v_mfma_scale_f32_16x16x128_f8f6f4 v[70:73], v[18:25], v[214:221], 0, v208, v207 op_sel_hi:[0,0,0]
	v_mfma_scale_f32_16x16x128_f8f6f4 v[62:65], v[26:33], v[236:243], 0, v208, v207 op_sel_hi:[0,0,0]
	v_mfma_scale_f32_16x16x128_f8f6f4 v[54:57], v[18:25], v[236:243], 0, v208, v207 op_sel_hi:[0,0,0]
	v_mfma_scale_f32_16x16x128_f8f6f4 v[46:49], v[26:33], v[244:251], 0, v208, v207 op_sel_hi:[0,0,0]
	v_mfma_scale_f32_16x16x128_f8f6f4 v[38:41], v[18:25], v[244:251], 0, v208, v207 op_sel_hi:[0,0,0]
	s_setprio 0
	s_setprio 1
	v_mfma_scale_f32_16x16x128_f8f6f4 v[90:93], v[10:17], v[170:177], 0, v208, v207 op_sel_hi:[0,0,0]
	v_mfma_scale_f32_16x16x128_f8f6f4 v[82:85], v[2:9], v[170:177], 0, v208, v207 op_sel_hi:[0,0,0]
	v_mfma_scale_f32_16x16x128_f8f6f4 v[74:77], v[10:17], v[214:221], 0, v208, v207 op_sel_hi:[0,0,0]
	v_mfma_scale_f32_16x16x128_f8f6f4 v[66:69], v[2:9], v[214:221], 0, v208, v207 op_sel_hi:[0,0,0]
	v_mfma_scale_f32_16x16x128_f8f6f4 v[58:61], v[10:17], v[236:243], 0, v208, v207 op_sel_hi:[0,0,0]
	v_mfma_scale_f32_16x16x128_f8f6f4 v[50:53], v[2:9], v[236:243], 0, v208, v207 op_sel_hi:[0,0,0]
	v_mfma_scale_f32_16x16x128_f8f6f4 v[42:45], v[10:17], v[244:251], 0, v208, v207 op_sel_hi:[0,0,0]
	v_mfma_scale_f32_16x16x128_f8f6f4 v[34:37], v[2:9], v[244:251], 0, v208, v207 op_sel_hi:[0,0,0]
	s_setprio 0
	s_barrier
	s_add_i32 s64, 0, 0x18000
	s_add_i32 s65, 0, 0x1c000
	v_add_u32_e32 v2, s64, v210
	v_add_u32_e32 v6, s65, v210
	ds_read_b128 v[26:29], v2
	ds_read_b128 v[30:33], v2 offset:1024
	ds_read_b128 v[18:21], v2 offset:2048
	ds_read_b128 v[22:25], v2 offset:3072
	ds_read_b128 v[10:13], v6
	ds_read_b128 v[14:17], v6 offset:1024
	ds_read_b128 v[2:5], v6 offset:2048
	ds_read_b128 v[6:9], v6 offset:3072
	s_mov_b32 m0, s72
	ds_read_b128 v[170:173], v212 offset:32768
	ds_read_b128 v[174:177], v212 offset:33792
	ds_read_b128 v[214:217], v212 offset:34816
	ds_read_b128 v[218:221], v212 offset:35840
	ds_read_b128 v[236:239], v212 offset:36864
	ds_read_b128 v[240:243], v212 offset:37888
	ds_read_b128 v[244:247], v212 offset:38912
	ds_read_b128 v[248:251], v212 offset:39936
	global_load_lds_dwordx4 v180, s[68:69]
	s_mov_b32 m0, s73
	s_nop 0
	global_load_lds_dwordx4 v182, s[68:69]
	s_waitcnt vmcnt(8) lgkmcnt(0)
	s_barrier
	s_setprio 1
	v_mfma_scale_f32_16x16x128_f8f6f4 v[154:157], v[26:33], v[170:177], v[154:157], v208, v207 op_sel_hi:[0,0,0]
	v_mfma_scale_f32_16x16x128_f8f6f4 v[150:153], v[18:25], v[170:177], v[150:153], v208, v207 op_sel_hi:[0,0,0]
	v_mfma_scale_f32_16x16x128_f8f6f4 v[142:145], v[26:33], v[214:221], v[142:145], v208, v207 op_sel_hi:[0,0,0]
	v_mfma_scale_f32_16x16x128_f8f6f4 v[134:137], v[18:25], v[214:221], v[134:137], v208, v207 op_sel_hi:[0,0,0]
	v_mfma_scale_f32_16x16x128_f8f6f4 v[126:129], v[26:33], v[236:243], v[126:129], v208, v207 op_sel_hi:[0,0,0]
	v_mfma_scale_f32_16x16x128_f8f6f4 v[118:121], v[18:25], v[236:243], v[118:121], v208, v207 op_sel_hi:[0,0,0]
	v_mfma_scale_f32_16x16x128_f8f6f4 v[110:113], v[26:33], v[244:251], v[110:113], v208, v207 op_sel_hi:[0,0,0]
	v_mfma_scale_f32_16x16x128_f8f6f4 v[102:105], v[18:25], v[244:251], v[102:105], v208, v207 op_sel_hi:[0,0,0]
	s_setprio 0
	s_setprio 1
	v_mfma_scale_f32_16x16x128_f8f6f4 v[158:161], v[10:17], v[170:177], v[158:161], v208, v207 op_sel_hi:[0,0,0]
	v_mfma_scale_f32_16x16x128_f8f6f4 v[146:149], v[2:9], v[170:177], v[146:149], v208, v207 op_sel_hi:[0,0,0]
	v_mfma_scale_f32_16x16x128_f8f6f4 v[138:141], v[10:17], v[214:221], v[138:141], v208, v207 op_sel_hi:[0,0,0]
	v_mfma_scale_f32_16x16x128_f8f6f4 v[130:133], v[2:9], v[214:221], v[130:133], v208, v207 op_sel_hi:[0,0,0]
	v_mfma_scale_f32_16x16x128_f8f6f4 v[122:125], v[10:17], v[236:243], v[122:125], v208, v207 op_sel_hi:[0,0,0]
	v_mfma_scale_f32_16x16x128_f8f6f4 v[114:117], v[2:9], v[236:243], v[114:117], v208, v207 op_sel_hi:[0,0,0]
	v_mfma_scale_f32_16x16x128_f8f6f4 v[106:109], v[10:17], v[244:251], v[106:109], v208, v207 op_sel_hi:[0,0,0]
	v_mfma_scale_f32_16x16x128_f8f6f4 v[98:101], v[2:9], v[244:251], v[98:101], v208, v207 op_sel_hi:[0,0,0]
	s_setprio 0
	s_barrier
	s_add_i32 s64, s64, s22
	v_lshl_add_u64 v[196:197], v[196:197], 0, s[56:57]
	s_mov_b32 m0, s64
	ds_read_b128 v[170:173], v212 offset:49152
	ds_read_b128 v[174:177], v212 offset:50176
	ds_read_b128 v[214:217], v212 offset:51200
	ds_read_b128 v[218:221], v212 offset:52224
	ds_read_b128 v[236:239], v212 offset:53248
	ds_read_b128 v[240:243], v212 offset:54272
	ds_read_b128 v[244:247], v212 offset:55296
	ds_read_b128 v[248:251], v212 offset:56320
	global_load_lds_dwordx4 v[196:197], off
	s_add_i32 m0, s64, 0x2000
	s_add_u32 s62, s62, 0x20080
	v_lshl_add_u64 v[196:197], v[198:199], 0, s[56:57]
	s_addc_u32 s63, s63, 0
	s_add_i32 s64, s65, s22
	global_load_lds_dwordx4 v[196:197], off
	v_lshl_add_u64 v[196:197], s[62:63], 0, v[162:163]
	s_mov_b32 m0, s64
	s_nop 0
	global_load_lds_dwordx4 v[196:197], off
	v_lshl_add_u64 v[196:197], s[62:63], 0, v[164:165]
	s_add_i32 m0, s64, 0x2000
	s_nop 0
	global_load_lds_dwordx4 v[196:197], off
	v_lshl_add_u64 v[196:197], v[202:203], 0, s[56:57]
	s_mov_b32 m0, s74
	s_nop 0
	global_load_lds_dwordx4 v[196:197], off
	v_lshl_add_u64 v[196:197], v[200:201], 0, s[56:57]
	s_mov_b32 m0, s75
	s_nop 0
	global_load_lds_dwordx4 v[196:197], off
	s_waitcnt vmcnt(8) lgkmcnt(0)
	s_barrier
	s_setprio 1
	v_mfma_scale_f32_16x16x128_f8f6f4 v[94:97], v[26:33], v[170:177], v[94:97], v208, v207 op_sel_hi:[0,0,0]
	v_mfma_scale_f32_16x16x128_f8f6f4 v[86:89], v[18:25], v[170:177], v[86:89], v208, v207 op_sel_hi:[0,0,0]
	v_mfma_scale_f32_16x16x128_f8f6f4 v[78:81], v[26:33], v[214:221], v[78:81], v208, v207 op_sel_hi:[0,0,0]
	v_mfma_scale_f32_16x16x128_f8f6f4 v[70:73], v[18:25], v[214:221], v[70:73], v208, v207 op_sel_hi:[0,0,0]
	v_mfma_scale_f32_16x16x128_f8f6f4 v[62:65], v[26:33], v[236:243], v[62:65], v208, v207 op_sel_hi:[0,0,0]
	v_mfma_scale_f32_16x16x128_f8f6f4 v[54:57], v[18:25], v[236:243], v[54:57], v208, v207 op_sel_hi:[0,0,0]
	v_mfma_scale_f32_16x16x128_f8f6f4 v[46:49], v[26:33], v[244:251], v[46:49], v208, v207 op_sel_hi:[0,0,0]
	v_mfma_scale_f32_16x16x128_f8f6f4 v[38:41], v[18:25], v[244:251], v[38:41], v208, v207 op_sel_hi:[0,0,0]
	s_setprio 0
	s_setprio 1
	v_mfma_scale_f32_16x16x128_f8f6f4 v[90:93], v[10:17], v[170:177], v[90:93], v208, v207 op_sel_hi:[0,0,0]
	v_mfma_scale_f32_16x16x128_f8f6f4 v[82:85], v[2:9], v[170:177], v[82:85], v208, v207 op_sel_hi:[0,0,0]
	v_mfma_scale_f32_16x16x128_f8f6f4 v[74:77], v[10:17], v[214:221], v[74:77], v208, v207 op_sel_hi:[0,0,0]
	v_mfma_scale_f32_16x16x128_f8f6f4 v[66:69], v[2:9], v[214:221], v[66:69], v208, v207 op_sel_hi:[0,0,0]
	v_mfma_scale_f32_16x16x128_f8f6f4 v[58:61], v[10:17], v[236:243], v[58:61], v208, v207 op_sel_hi:[0,0,0]
	v_mfma_scale_f32_16x16x128_f8f6f4 v[50:53], v[2:9], v[236:243], v[50:53], v208, v207 op_sel_hi:[0,0,0]
	v_mfma_scale_f32_16x16x128_f8f6f4 v[42:45], v[10:17], v[244:251], v[42:45], v208, v207 op_sel_hi:[0,0,0]
	v_mfma_scale_f32_16x16x128_f8f6f4 v[34:37], v[2:9], v[244:251], v[34:37], v208, v207 op_sel_hi:[0,0,0]
	s_setprio 0
	s_barrier
	s_cmp_lt_i32 s55, s11
	s_cbranch_scc0 .LBB0_1841
	s_mov_b64 s[64:65], s[60:61]
	s_branch .LBB0_1836

.LBB0_1838:
	s_add_i32 s55, s55, 2
	s_add_u32 s60, s64, 0x100
	s_addc_u32 s61, s65, 0
	s_and_b64 s[68:69], s[62:63], exec
	s_cselect_b32 s68, 0, s60
	s_cselect_b32 s69, 0, s61
	s_add_u32 s68, s30, s68
	s_addc_u32 s69, s31, s69
	s_add_u32 s91, s47, s64
	s_addc_u32 s92, s49, s65
	s_and_b64 s[62:63], s[62:63], exec
	s_cselect_b32 s63, s53, s92
	s_cselect_b32 s62, s52, s91
	s_add_i32 s92, 0, 0x10000
	s_add_i32 s91, 0, 0x14000
	v_add_u32_e32 v2, s92, v210
	v_add_u32_e32 v6, s91, v210
	ds_read_b128 v[26:29], v2
	ds_read_b128 v[30:33], v2 offset:1024
	ds_read_b128 v[18:21], v2 offset:2048
	ds_read_b128 v[22:25], v2 offset:3072
	ds_read_b128 v[10:13], v6
	ds_read_b128 v[14:17], v6 offset:1024
	ds_read_b128 v[2:5], v6 offset:2048
	ds_read_b128 v[6:9], v6 offset:3072
	v_lshl_add_u64 v[222:223], v[194:195], 0, s[64:65]
	s_add_i32 m0, s59, 0xc000
	ds_read_b128 v[170:173], v212
	ds_read_b128 v[174:177], v212 offset:1024
	ds_read_b128 v[196:199], v212 offset:2048
	ds_read_b128 v[200:203], v212 offset:3072
	ds_read_b128 v[214:217], v212 offset:4096
	ds_read_b128 v[218:221], v212 offset:5120
	ds_read_b128 v[236:239], v212 offset:6144
	ds_read_b128 v[240:243], v212 offset:7168
	global_load_lds_dwordx4 v[222:223], off
	v_lshl_add_u64 v[222:223], v[192:193], 0, s[64:65]
	s_add_i32 m0, s59, 0xe000
	s_nop 0
	global_load_lds_dwordx4 v[222:223], off
	s_waitcnt vmcnt(8) lgkmcnt(0)
	s_barrier
	s_setprio 1
	v_mfma_scale_f32_16x16x128_f8f6f4 v[154:157], v[26:33], v[170:177], v[154:157], v208, v207 op_sel_hi:[0,0,0]
	v_mfma_scale_f32_16x16x128_f8f6f4 v[150:153], v[18:25], v[170:177], v[150:153], v208, v207 op_sel_hi:[0,0,0]
	v_mfma_scale_f32_16x16x128_f8f6f4 v[142:145], v[26:33], v[196:203], v[142:145], v208, v207 op_sel_hi:[0,0,0]
	v_mfma_scale_f32_16x16x128_f8f6f4 v[134:137], v[18:25], v[196:203], v[134:137], v208, v207 op_sel_hi:[0,0,0]
	v_mfma_scale_f32_16x16x128_f8f6f4 v[126:129], v[26:33], v[214:221], v[126:129], v208, v207 op_sel_hi:[0,0,0]
	v_mfma_scale_f32_16x16x128_f8f6f4 v[118:121], v[18:25], v[214:221], v[118:121], v208, v207 op_sel_hi:[0,0,0]
	v_mfma_scale_f32_16x16x128_f8f6f4 v[110:113], v[26:33], v[236:243], v[110:113], v208, v207 op_sel_hi:[0,0,0]
	v_mfma_scale_f32_16x16x128_f8f6f4 v[102:105], v[18:25], v[236:243], v[102:105], v208, v207 op_sel_hi:[0,0,0]
	s_setprio 0
	s_setprio 1
	v_mfma_scale_f32_16x16x128_f8f6f4 v[158:161], v[10:17], v[170:177], v[158:161], v208, v207 op_sel_hi:[0,0,0]
	v_mfma_scale_f32_16x16x128_f8f6f4 v[146:149], v[2:9], v[170:177], v[146:149], v208, v207 op_sel_hi:[0,0,0]
	v_mfma_scale_f32_16x16x128_f8f6f4 v[138:141], v[10:17], v[196:203], v[138:141], v208, v207 op_sel_hi:[0,0,0]
	v_mfma_scale_f32_16x16x128_f8f6f4 v[130:133], v[2:9], v[196:203], v[130:133], v208, v207 op_sel_hi:[0,0,0]
	v_mfma_scale_f32_16x16x128_f8f6f4 v[122:125], v[10:17], v[214:221], v[122:125], v208, v207 op_sel_hi:[0,0,0]
	v_mfma_scale_f32_16x16x128_f8f6f4 v[114:117], v[2:9], v[214:221], v[114:117], v208, v207 op_sel_hi:[0,0,0]
	v_mfma_scale_f32_16x16x128_f8f6f4 v[106:109], v[10:17], v[236:243], v[106:109], v208, v207 op_sel_hi:[0,0,0]
	v_mfma_scale_f32_16x16x128_f8f6f4 v[98:101], v[2:9], v[236:243], v[98:101], v208, v207 op_sel_hi:[0,0,0]
	s_setprio 0
	s_barrier
	s_add_i32 s64, s92, s22
	v_lshl_add_u64 v[196:197], s[62:63], 0, v[162:163]
	s_mov_b32 m0, s64
	ds_read_b128 v[170:173], v212 offset:16384
	ds_read_b128 v[174:177], v212 offset:17408
	ds_read_b128 v[214:217], v212 offset:18432
	ds_read_b128 v[218:221], v212 offset:19456
	ds_read_b128 v[236:239], v212 offset:20480
	ds_read_b128 v[240:243], v212 offset:21504
	ds_read_b128 v[244:247], v212 offset:22528
	ds_read_b128 v[248:251], v212 offset:23552
	global_load_lds_dwordx4 v[196:197], off
	s_add_i32 m0, s64, 0x2000
	s_add_u32 s64, s62, 0x20000
	v_lshl_add_u64 v[198:199], s[62:63], 0, v[164:165]
	s_addc_u32 s65, s63, 0
	s_add_i32 s91, s91, s22
	global_load_lds_dwordx4 v[198:199], off
	v_lshl_add_u64 v[200:201], s[64:65], 0, v[162:163]
	s_mov_b32 m0, s91
	v_mov_b32_e32 v179, v167
	global_load_lds_dwordx4 v[200:201], off
	v_lshl_add_u64 v[200:201], s[64:65], 0, v[164:165]
	s_add_i32 m0, s91, 0x2000
	v_lshl_add_u64 v[202:203], s[68:69], 0, v[166:167]
	global_load_lds_dwordx4 v[200:201], off
	s_mov_b32 m0, s59
	v_lshl_add_u64 v[200:201], s[68:69], 0, v[178:179]
	global_load_lds_dwordx4 v166, s[68:69]
	s_mov_b32 m0, s71
	s_nop 0
	global_load_lds_dwordx4 v178, s[68:69]
	s_waitcnt vmcnt(8) lgkmcnt(0)
	s_barrier
	s_setprio 1
	v_mfma_scale_f32_16x16x128_f8f6f4 v[94:97], v[26:33], v[170:177], v[94:97], v208, v207 op_sel_hi:[0,0,0]
	v_mfma_scale_f32_16x16x128_f8f6f4 v[86:89], v[18:25], v[170:177], v[86:89], v208, v207 op_sel_hi:[0,0,0]
	v_mfma_scale_f32_16x16x128_f8f6f4 v[78:81], v[26:33], v[214:221], v[78:81], v208, v207 op_sel_hi:[0,0,0]
	v_mfma_scale_f32_16x16x128_f8f6f4 v[70:73], v[18:25], v[214:221], v[70:73], v208, v207 op_sel_hi:[0,0,0]
	v_mfma_scale_f32_16x16x128_f8f6f4 v[62:65], v[26:33], v[236:243], v[62:65], v208, v207 op_sel_hi:[0,0,0]
	v_mfma_scale_f32_16x16x128_f8f6f4 v[54:57], v[18:25], v[236:243], v[54:57], v208, v207 op_sel_hi:[0,0,0]
	v_mfma_scale_f32_16x16x128_f8f6f4 v[46:49], v[26:33], v[244:251], v[46:49], v208, v207 op_sel_hi:[0,0,0]
	v_mfma_scale_f32_16x16x128_f8f6f4 v[38:41], v[18:25], v[244:251], v[38:41], v208, v207 op_sel_hi:[0,0,0]
	s_setprio 0
	s_setprio 1
	v_mfma_scale_f32_16x16x128_f8f6f4 v[90:93], v[10:17], v[170:177], v[90:93], v208, v207 op_sel_hi:[0,0,0]
	v_mfma_scale_f32_16x16x128_f8f6f4 v[82:85], v[2:9], v[170:177], v[82:85], v208, v207 op_sel_hi:[0,0,0]
	v_mfma_scale_f32_16x16x128_f8f6f4 v[74:77], v[10:17], v[214:221], v[74:77], v208, v207 op_sel_hi:[0,0,0]
	v_mfma_scale_f32_16x16x128_f8f6f4 v[66:69], v[2:9], v[214:221], v[66:69], v208, v207 op_sel_hi:[0,0,0]
	v_mfma_scale_f32_16x16x128_f8f6f4 v[58:61], v[10:17], v[236:243], v[58:61], v208, v207 op_sel_hi:[0,0,0]
	v_mfma_scale_f32_16x16x128_f8f6f4 v[50:53], v[2:9], v[236:243], v[50:53], v208, v207 op_sel_hi:[0,0,0]
	v_mfma_scale_f32_16x16x128_f8f6f4 v[42:45], v[10:17], v[244:251], v[42:45], v208, v207 op_sel_hi:[0,0,0]
	v_mfma_scale_f32_16x16x128_f8f6f4 v[34:37], v[2:9], v[244:251], v[34:37], v208, v207 op_sel_hi:[0,0,0]
	s_setprio 0
	s_barrier
	s_add_i32 s64, 0, 0x18000
	s_add_i32 s65, 0, 0x1c000
	v_add_u32_e32 v2, s64, v210
	v_add_u32_e32 v6, s65, v210
	ds_read_b128 v[26:29], v2
	ds_read_b128 v[30:33], v2 offset:1024
	ds_read_b128 v[18:21], v2 offset:2048
	ds_read_b128 v[22:25], v2 offset:3072
	ds_read_b128 v[10:13], v6
	ds_read_b128 v[14:17], v6 offset:1024
	ds_read_b128 v[2:5], v6 offset:2048
	ds_read_b128 v[6:9], v6 offset:3072
	s_mov_b32 m0, s72
	ds_read_b128 v[170:173], v212 offset:32768
	ds_read_b128 v[174:177], v212 offset:33792
	ds_read_b128 v[214:217], v212 offset:34816
	ds_read_b128 v[218:221], v212 offset:35840
	ds_read_b128 v[236:239], v212 offset:36864
	ds_read_b128 v[240:243], v212 offset:37888
	ds_read_b128 v[244:247], v212 offset:38912
	ds_read_b128 v[248:251], v212 offset:39936
	global_load_lds_dwordx4 v180, s[68:69]
	s_mov_b32 m0, s73
	s_nop 0
	global_load_lds_dwordx4 v182, s[68:69]
	s_waitcnt vmcnt(8) lgkmcnt(0)
	s_barrier
	s_setprio 1
	v_mfma_scale_f32_16x16x128_f8f6f4 v[154:157], v[26:33], v[170:177], v[154:157], v208, v207 op_sel_hi:[0,0,0]
	v_mfma_scale_f32_16x16x128_f8f6f4 v[150:153], v[18:25], v[170:177], v[150:153], v208, v207 op_sel_hi:[0,0,0]
	v_mfma_scale_f32_16x16x128_f8f6f4 v[142:145], v[26:33], v[214:221], v[142:145], v208, v207 op_sel_hi:[0,0,0]
	v_mfma_scale_f32_16x16x128_f8f6f4 v[134:137], v[18:25], v[214:221], v[134:137], v208, v207 op_sel_hi:[0,0,0]
	v_mfma_scale_f32_16x16x128_f8f6f4 v[126:129], v[26:33], v[236:243], v[126:129], v208, v207 op_sel_hi:[0,0,0]
	v_mfma_scale_f32_16x16x128_f8f6f4 v[118:121], v[18:25], v[236:243], v[118:121], v208, v207 op_sel_hi:[0,0,0]
	v_mfma_scale_f32_16x16x128_f8f6f4 v[110:113], v[26:33], v[244:251], v[110:113], v208, v207 op_sel_hi:[0,0,0]
	v_mfma_scale_f32_16x16x128_f8f6f4 v[102:105], v[18:25], v[244:251], v[102:105], v208, v207 op_sel_hi:[0,0,0]
	s_setprio 0
	s_setprio 1
	v_mfma_scale_f32_16x16x128_f8f6f4 v[158:161], v[10:17], v[170:177], v[158:161], v208, v207 op_sel_hi:[0,0,0]
	v_mfma_scale_f32_16x16x128_f8f6f4 v[146:149], v[2:9], v[170:177], v[146:149], v208, v207 op_sel_hi:[0,0,0]
	v_mfma_scale_f32_16x16x128_f8f6f4 v[138:141], v[10:17], v[214:221], v[138:141], v208, v207 op_sel_hi:[0,0,0]
	v_mfma_scale_f32_16x16x128_f8f6f4 v[130:133], v[2:9], v[214:221], v[130:133], v208, v207 op_sel_hi:[0,0,0]
	v_mfma_scale_f32_16x16x128_f8f6f4 v[122:125], v[10:17], v[236:243], v[122:125], v208, v207 op_sel_hi:[0,0,0]
	v_mfma_scale_f32_16x16x128_f8f6f4 v[114:117], v[2:9], v[236:243], v[114:117], v208, v207 op_sel_hi:[0,0,0]
	v_mfma_scale_f32_16x16x128_f8f6f4 v[106:109], v[10:17], v[244:251], v[106:109], v208, v207 op_sel_hi:[0,0,0]
	v_mfma_scale_f32_16x16x128_f8f6f4 v[98:101], v[2:9], v[244:251], v[98:101], v208, v207 op_sel_hi:[0,0,0]
	s_setprio 0
	s_barrier
	s_add_i32 s64, s64, s22
	v_lshl_add_u64 v[196:197], v[196:197], 0, s[56:57]
	s_mov_b32 m0, s64
	ds_read_b128 v[170:173], v212 offset:49152
	ds_read_b128 v[174:177], v212 offset:50176
	ds_read_b128 v[214:217], v212 offset:51200
	ds_read_b128 v[218:221], v212 offset:52224
	ds_read_b128 v[236:239], v212 offset:53248
	ds_read_b128 v[240:243], v212 offset:54272
	ds_read_b128 v[244:247], v212 offset:55296
	ds_read_b128 v[248:251], v212 offset:56320
	global_load_lds_dwordx4 v[196:197], off
	s_add_i32 m0, s64, 0x2000
	s_add_u32 s62, s62, 0x20080
	v_lshl_add_u64 v[196:197], v[198:199], 0, s[56:57]
	s_addc_u32 s63, s63, 0
	s_add_i32 s64, s65, s22
	global_load_lds_dwordx4 v[196:197], off
	v_lshl_add_u64 v[196:197], s[62:63], 0, v[162:163]
	s_mov_b32 m0, s64
	s_nop 0
	global_load_lds_dwordx4 v[196:197], off
	v_lshl_add_u64 v[196:197], s[62:63], 0, v[164:165]
	s_add_i32 m0, s64, 0x2000
	s_nop 0
	global_load_lds_dwordx4 v[196:197], off
	v_lshl_add_u64 v[196:197], v[202:203], 0, s[56:57]
	s_mov_b32 m0, s74
	s_nop 0
	global_load_lds_dwordx4 v[196:197], off
	v_lshl_add_u64 v[196:197], v[200:201], 0, s[56:57]
	s_mov_b32 m0, s75
	s_nop 0
	global_load_lds_dwordx4 v[196:197], off
	s_waitcnt vmcnt(8) lgkmcnt(0)
	s_barrier
	s_setprio 1
	v_mfma_scale_f32_16x16x128_f8f6f4 v[94:97], v[26:33], v[170:177], v[94:97], v208, v207 op_sel_hi:[0,0,0]
	v_mfma_scale_f32_16x16x128_f8f6f4 v[86:89], v[18:25], v[170:177], v[86:89], v208, v207 op_sel_hi:[0,0,0]
	v_mfma_scale_f32_16x16x128_f8f6f4 v[78:81], v[26:33], v[214:221], v[78:81], v208, v207 op_sel_hi:[0,0,0]
	v_mfma_scale_f32_16x16x128_f8f6f4 v[70:73], v[18:25], v[214:221], v[70:73], v208, v207 op_sel_hi:[0,0,0]
	v_mfma_scale_f32_16x16x128_f8f6f4 v[62:65], v[26:33], v[236:243], v[62:65], v208, v207 op_sel_hi:[0,0,0]
	v_mfma_scale_f32_16x16x128_f8f6f4 v[54:57], v[18:25], v[236:243], v[54:57], v208, v207 op_sel_hi:[0,0,0]
	v_mfma_scale_f32_16x16x128_f8f6f4 v[46:49], v[26:33], v[244:251], v[46:49], v208, v207 op_sel_hi:[0,0,0]
	v_mfma_scale_f32_16x16x128_f8f6f4 v[38:41], v[18:25], v[244:251], v[38:41], v208, v207 op_sel_hi:[0,0,0]
	s_setprio 0
	s_setprio 1
	v_mfma_scale_f32_16x16x128_f8f6f4 v[90:93], v[10:17], v[170:177], v[90:93], v208, v207 op_sel_hi:[0,0,0]
	v_mfma_scale_f32_16x16x128_f8f6f4 v[82:85], v[2:9], v[170:177], v[82:85], v208, v207 op_sel_hi:[0,0,0]
	v_mfma_scale_f32_16x16x128_f8f6f4 v[74:77], v[10:17], v[214:221], v[74:77], v208, v207 op_sel_hi:[0,0,0]
	v_mfma_scale_f32_16x16x128_f8f6f4 v[66:69], v[2:9], v[214:221], v[66:69], v208, v207 op_sel_hi:[0,0,0]
	v_mfma_scale_f32_16x16x128_f8f6f4 v[58:61], v[10:17], v[236:243], v[58:61], v208, v207 op_sel_hi:[0,0,0]
	v_mfma_scale_f32_16x16x128_f8f6f4 v[50:53], v[2:9], v[236:243], v[50:53], v208, v207 op_sel_hi:[0,0,0]
	v_mfma_scale_f32_16x16x128_f8f6f4 v[42:45], v[10:17], v[244:251], v[42:45], v208, v207 op_sel_hi:[0,0,0]
	v_mfma_scale_f32_16x16x128_f8f6f4 v[34:37], v[2:9], v[244:251], v[34:37], v208, v207 op_sel_hi:[0,0,0]
	s_setprio 0
	s_barrier
	s_cmp_lt_i32 s55, s11
	s_cbranch_scc0 .LBB0_1841
	s_mov_b64 s[64:65], s[60:61]
	s_branch .LBB0_1836

.Lpeelph18_0:
	s_add_i32 s75, s70, 2
	s_add_u32 s42, s18, 0x100
	s_addc_u32 s43, s19, 0
	s_add_i32 s46, 0, 0x10000
	s_cmp_eq_u32 s14, s70
	s_cselect_b32 vcc_hi, s69, s43
	s_cselect_b32 vcc_lo, s68, s42
	s_cselect_b32 s71, s37, s45
	s_cselect_b32 s70, s36, s35
	s_add_i32 s47, 0, 0x14000
	v_add_u32_e32 v2, s46, v196
	v_add_u32_e32 v6, s47, v196
	ds_read_b128 v[26:29], v2
	ds_read_b128 v[30:33], v2 offset:1024
	ds_read_b128 v[18:21], v2 offset:2048
	ds_read_b128 v[22:25], v2 offset:3072
	ds_read_b128 v[10:13], v6
	ds_read_b128 v[14:17], v6 offset:1024
	ds_read_b128 v[2:5], v6 offset:2048
	ds_read_b128 v[6:9], v6 offset:3072
	v_lshl_add_u64 v[218:219], s[18:19], 0, v[184:185]
	s_add_i32 m0, s73, 0xc000
	ds_read_b128 v[170:173], v201
	ds_read_b128 v[174:177], v201 offset:1024
	ds_read_b128 v[186:189], v201 offset:2048
	ds_read_b128 v[190:193], v201 offset:3072
	ds_read_b128 v[202:205], v201 offset:4096
	ds_read_b128 v[206:209], v201 offset:5120
	ds_read_b128 v[210:213], v201 offset:6144
	ds_read_b128 v[214:217], v201 offset:7168
	global_load_lds_dwordx4 v[218:219], off
	v_lshl_add_u64 v[218:219], s[18:19], 0, v[182:183]
	s_add_i32 m0, s73, 0xe000
	s_nop 0
	global_load_lds_dwordx4 v[218:219], off
	s_waitcnt vmcnt(8) lgkmcnt(0)
	s_barrier
	s_setprio 1
	v_mfma_scale_f32_16x16x128_f8f6f4 v[158:161], v[26:33], v[170:177], 0, v194, v169 op_sel_hi:[0,0,0]
	v_mfma_scale_f32_16x16x128_f8f6f4 v[154:157], v[18:25], v[170:177], 0, v194, v169 op_sel_hi:[0,0,0]
	v_mfma_scale_f32_16x16x128_f8f6f4 v[142:145], v[26:33], v[186:193], 0, v194, v169 op_sel_hi:[0,0,0]
	v_mfma_scale_f32_16x16x128_f8f6f4 v[138:141], v[18:25], v[186:193], 0, v194, v169 op_sel_hi:[0,0,0]
	v_mfma_scale_f32_16x16x128_f8f6f4 v[126:129], v[26:33], v[202:209], 0, v194, v169 op_sel_hi:[0,0,0]
	v_mfma_scale_f32_16x16x128_f8f6f4 v[122:125], v[18:25], v[202:209], 0, v194, v169 op_sel_hi:[0,0,0]
	v_mfma_scale_f32_16x16x128_f8f6f4 v[110:113], v[26:33], v[210:217], 0, v194, v169 op_sel_hi:[0,0,0]
	v_mfma_scale_f32_16x16x128_f8f6f4 v[106:109], v[18:25], v[210:217], 0, v194, v169 op_sel_hi:[0,0,0]
	s_setprio 0
	s_setprio 1
	v_mfma_scale_f32_16x16x128_f8f6f4 v[150:153], v[10:17], v[170:177], 0, v194, v169 op_sel_hi:[0,0,0]
	v_mfma_scale_f32_16x16x128_f8f6f4 v[146:149], v[2:9], v[170:177], 0, v194, v169 op_sel_hi:[0,0,0]
	v_mfma_scale_f32_16x16x128_f8f6f4 v[134:137], v[10:17], v[186:193], 0, v194, v169 op_sel_hi:[0,0,0]
	v_mfma_scale_f32_16x16x128_f8f6f4 v[130:133], v[2:9], v[186:193], 0, v194, v169 op_sel_hi:[0,0,0]
	v_mfma_scale_f32_16x16x128_f8f6f4 v[118:121], v[10:17], v[202:209], 0, v194, v169 op_sel_hi:[0,0,0]
	v_mfma_scale_f32_16x16x128_f8f6f4 v[114:117], v[2:9], v[202:209], 0, v194, v169 op_sel_hi:[0,0,0]
	v_mfma_scale_f32_16x16x128_f8f6f4 v[102:105], v[10:17], v[210:217], 0, v194, v169 op_sel_hi:[0,0,0]
	v_mfma_scale_f32_16x16x128_f8f6f4 v[98:101], v[2:9], v[210:217], 0, v194, v169 op_sel_hi:[0,0,0]
	s_setprio 0
	s_barrier
	s_add_i32 s18, s46, s95
	v_lshl_add_u64 v[186:187], s[70:71], 0, v[164:165]
	s_mov_b32 m0, s18
	ds_read_b128 v[170:173], v201 offset:16384
	ds_read_b128 v[174:177], v201 offset:17408
	ds_read_b128 v[202:205], v201 offset:18432
	ds_read_b128 v[206:209], v201 offset:19456
	ds_read_b128 v[210:213], v201 offset:20480
	ds_read_b128 v[214:217], v201 offset:21504
	ds_read_b128 v[236:239], v201 offset:22528
	ds_read_b128 v[240:243], v201 offset:23552
	global_load_lds_dwordx4 v[186:187], off
	s_add_i32 m0, s18, 0x2000
	s_add_u32 s18, s70, 0x70000
	v_lshl_add_u64 v[188:189], s[70:71], 0, v[180:181]
	s_addc_u32 s19, s71, 0
	s_add_i32 s46, s47, s95
	global_load_lds_dwordx4 v[188:189], off
	v_lshl_add_u64 v[190:191], s[18:19], 0, v[164:165]
	s_mov_b32 m0, s46
	v_lshl_add_u64 v[192:193], vcc, 0, v[178:179]
	global_load_lds_dwordx4 v[190:191], off
	v_lshl_add_u64 v[190:191], s[18:19], 0, v[180:181]
	s_add_i32 m0, s46, 0x2000
	s_nop 0
	global_load_lds_dwordx4 v[190:191], off
	v_lshl_add_u64 v[190:191], vcc, 0, v[162:163]
	s_mov_b32 m0, s73
	s_nop 0
	global_load_lds_dwordx4 v[190:191], off
	s_mov_b32 m0, s8
	s_nop 0
	global_load_lds_dwordx4 v[192:193], off
	s_waitcnt vmcnt(8) lgkmcnt(0)
	s_barrier
	s_setprio 1
	v_mfma_scale_f32_16x16x128_f8f6f4 v[94:97], v[26:33], v[170:177], 0, v194, v169 op_sel_hi:[0,0,0]
	v_mfma_scale_f32_16x16x128_f8f6f4 v[90:93], v[18:25], v[170:177], 0, v194, v169 op_sel_hi:[0,0,0]
	v_mfma_scale_f32_16x16x128_f8f6f4 v[78:81], v[26:33], v[202:209], 0, v194, v169 op_sel_hi:[0,0,0]
	v_mfma_scale_f32_16x16x128_f8f6f4 v[74:77], v[18:25], v[202:209], 0, v194, v169 op_sel_hi:[0,0,0]
	v_mfma_scale_f32_16x16x128_f8f6f4 v[62:65], v[26:33], v[210:217], 0, v194, v169 op_sel_hi:[0,0,0]
	v_mfma_scale_f32_16x16x128_f8f6f4 v[58:61], v[18:25], v[210:217], 0, v194, v169 op_sel_hi:[0,0,0]
	v_mfma_scale_f32_16x16x128_f8f6f4 v[46:49], v[26:33], v[236:243], 0, v194, v169 op_sel_hi:[0,0,0]
	v_mfma_scale_f32_16x16x128_f8f6f4 v[42:45], v[18:25], v[236:243], 0, v194, v169 op_sel_hi:[0,0,0]
	s_setprio 0
	s_setprio 1
	v_mfma_scale_f32_16x16x128_f8f6f4 v[86:89], v[10:17], v[170:177], 0, v194, v169 op_sel_hi:[0,0,0]
	v_mfma_scale_f32_16x16x128_f8f6f4 v[82:85], v[2:9], v[170:177], 0, v194, v169 op_sel_hi:[0,0,0]
	v_mfma_scale_f32_16x16x128_f8f6f4 v[70:73], v[10:17], v[202:209], 0, v194, v169 op_sel_hi:[0,0,0]
	v_mfma_scale_f32_16x16x128_f8f6f4 v[66:69], v[2:9], v[202:209], 0, v194, v169 op_sel_hi:[0,0,0]
	v_mfma_scale_f32_16x16x128_f8f6f4 v[54:57], v[10:17], v[210:217], 0, v194, v169 op_sel_hi:[0,0,0]
	v_mfma_scale_f32_16x16x128_f8f6f4 v[50:53], v[2:9], v[210:217], 0, v194, v169 op_sel_hi:[0,0,0]
	v_mfma_scale_f32_16x16x128_f8f6f4 v[38:41], v[10:17], v[236:243], 0, v194, v169 op_sel_hi:[0,0,0]
	v_mfma_scale_f32_16x16x128_f8f6f4 v[34:37], v[2:9], v[236:243], 0, v194, v169 op_sel_hi:[0,0,0]
	s_setprio 0
	s_barrier
	s_add_i32 s46, 0, 0x18000
	s_add_i32 s47, 0, 0x1c000
	v_add_u32_e32 v2, s46, v196
	v_add_u32_e32 v6, s47, v196
	ds_read_b128 v[26:29], v2
	ds_read_b128 v[30:33], v2 offset:1024
	ds_read_b128 v[18:21], v2 offset:2048
	ds_read_b128 v[22:25], v2 offset:3072
	ds_read_b128 v[10:13], v6
	ds_read_b128 v[14:17], v6 offset:1024
	ds_read_b128 v[2:5], v6 offset:2048
	ds_read_b128 v[6:9], v6 offset:3072
	s_add_u32 s18, vcc_lo, 0x70000
	s_addc_u32 s19, vcc_hi, 0
	s_mov_b32 m0, s11
	v_lshl_add_u64 v[218:219], s[18:19], 0, v[162:163]
	ds_read_b128 v[170:173], v201 offset:32768
	ds_read_b128 v[174:177], v201 offset:33792
	ds_read_b128 v[202:205], v201 offset:34816
	ds_read_b128 v[206:209], v201 offset:35840
	ds_read_b128 v[210:213], v201 offset:36864
	ds_read_b128 v[214:217], v201 offset:37888
	ds_read_b128 v[236:239], v201 offset:38912
	ds_read_b128 v[240:243], v201 offset:39936
	global_load_lds_dwordx4 v[218:219], off
	v_lshl_add_u64 v[218:219], s[18:19], 0, v[178:179]
	s_mov_b32 m0, s84
	s_nop 0
	global_load_lds_dwordx4 v[218:219], off
	s_waitcnt vmcnt(8) lgkmcnt(0)
	s_barrier
	s_setprio 1
	v_mfma_scale_f32_16x16x128_f8f6f4 v[158:161], v[26:33], v[170:177], v[158:161], v194, v169 op_sel_hi:[0,0,0]
	v_mfma_scale_f32_16x16x128_f8f6f4 v[154:157], v[18:25], v[170:177], v[154:157], v194, v169 op_sel_hi:[0,0,0]
	v_mfma_scale_f32_16x16x128_f8f6f4 v[142:145], v[26:33], v[202:209], v[142:145], v194, v169 op_sel_hi:[0,0,0]
	v_mfma_scale_f32_16x16x128_f8f6f4 v[138:141], v[18:25], v[202:209], v[138:141], v194, v169 op_sel_hi:[0,0,0]
	v_mfma_scale_f32_16x16x128_f8f6f4 v[126:129], v[26:33], v[210:217], v[126:129], v194, v169 op_sel_hi:[0,0,0]
	v_mfma_scale_f32_16x16x128_f8f6f4 v[122:125], v[18:25], v[210:217], v[122:125], v194, v169 op_sel_hi:[0,0,0]
	v_mfma_scale_f32_16x16x128_f8f6f4 v[110:113], v[26:33], v[236:243], v[110:113], v194, v169 op_sel_hi:[0,0,0]
	v_mfma_scale_f32_16x16x128_f8f6f4 v[106:109], v[18:25], v[236:243], v[106:109], v194, v169 op_sel_hi:[0,0,0]
	s_setprio 0
	s_setprio 1
	v_mfma_scale_f32_16x16x128_f8f6f4 v[150:153], v[10:17], v[170:177], v[150:153], v194, v169 op_sel_hi:[0,0,0]
	v_mfma_scale_f32_16x16x128_f8f6f4 v[146:149], v[2:9], v[170:177], v[146:149], v194, v169 op_sel_hi:[0,0,0]
	v_mfma_scale_f32_16x16x128_f8f6f4 v[134:137], v[10:17], v[202:209], v[134:137], v194, v169 op_sel_hi:[0,0,0]
	v_mfma_scale_f32_16x16x128_f8f6f4 v[130:133], v[2:9], v[202:209], v[130:133], v194, v169 op_sel_hi:[0,0,0]
	v_mfma_scale_f32_16x16x128_f8f6f4 v[118:121], v[10:17], v[210:217], v[118:121], v194, v169 op_sel_hi:[0,0,0]
	v_mfma_scale_f32_16x16x128_f8f6f4 v[114:117], v[2:9], v[210:217], v[114:117], v194, v169 op_sel_hi:[0,0,0]
	v_mfma_scale_f32_16x16x128_f8f6f4 v[102:105], v[10:17], v[236:243], v[102:105], v194, v169 op_sel_hi:[0,0,0]
	v_mfma_scale_f32_16x16x128_f8f6f4 v[98:101], v[2:9], v[236:243], v[98:101], v194, v169 op_sel_hi:[0,0,0]
	s_setprio 0
	s_barrier
	s_add_i32 s18, s46, s95
	v_lshl_add_u64 v[186:187], v[186:187], 0, s[56:57]
	s_mov_b32 m0, s18
	ds_read_b128 v[170:173], v201 offset:49152
	ds_read_b128 v[174:177], v201 offset:50176
	ds_read_b128 v[202:205], v201 offset:51200
	ds_read_b128 v[206:209], v201 offset:52224
	ds_read_b128 v[210:213], v201 offset:53248
	ds_read_b128 v[214:217], v201 offset:54272
	ds_read_b128 v[236:239], v201 offset:55296
	ds_read_b128 v[240:243], v201 offset:56320
	global_load_lds_dwordx4 v[186:187], off
	s_add_i32 m0, s18, 0x2000
	s_add_u32 s18, s70, 0x70080
	v_lshl_add_u64 v[186:187], v[188:189], 0, s[56:57]
	s_addc_u32 s19, s71, 0
	s_add_i32 s46, s47, s95
	global_load_lds_dwordx4 v[186:187], off
	v_lshl_add_u64 v[186:187], s[18:19], 0, v[164:165]
	s_mov_b32 m0, s46
	s_nop 0
	global_load_lds_dwordx4 v[186:187], off
	v_lshl_add_u64 v[186:187], s[18:19], 0, v[180:181]
	s_add_i32 m0, s46, 0x2000
	s_nop 0
	global_load_lds_dwordx4 v[186:187], off
	v_lshl_add_u64 v[186:187], v[190:191], 0, s[56:57]
	s_mov_b32 m0, s0
	s_nop 0
	global_load_lds_dwordx4 v[186:187], off
	v_lshl_add_u64 v[186:187], v[192:193], 0, s[56:57]
	s_mov_b32 m0, s88
	s_nop 0
	global_load_lds_dwordx4 v[186:187], off
	s_waitcnt vmcnt(8) lgkmcnt(0)
	s_barrier
	s_setprio 1
	v_mfma_scale_f32_16x16x128_f8f6f4 v[94:97], v[26:33], v[170:177], v[94:97], v194, v169 op_sel_hi:[0,0,0]
	v_mfma_scale_f32_16x16x128_f8f6f4 v[90:93], v[18:25], v[170:177], v[90:93], v194, v169 op_sel_hi:[0,0,0]
	v_mfma_scale_f32_16x16x128_f8f6f4 v[78:81], v[26:33], v[202:209], v[78:81], v194, v169 op_sel_hi:[0,0,0]
	v_mfma_scale_f32_16x16x128_f8f6f4 v[74:77], v[18:25], v[202:209], v[74:77], v194, v169 op_sel_hi:[0,0,0]
	v_mfma_scale_f32_16x16x128_f8f6f4 v[62:65], v[26:33], v[210:217], v[62:65], v194, v169 op_sel_hi:[0,0,0]
	v_mfma_scale_f32_16x16x128_f8f6f4 v[58:61], v[18:25], v[210:217], v[58:61], v194, v169 op_sel_hi:[0,0,0]
	v_mfma_scale_f32_16x16x128_f8f6f4 v[46:49], v[26:33], v[236:243], v[46:49], v194, v169 op_sel_hi:[0,0,0]
	v_mfma_scale_f32_16x16x128_f8f6f4 v[42:45], v[18:25], v[236:243], v[42:45], v194, v169 op_sel_hi:[0,0,0]
	s_setprio 0
	s_setprio 1
	v_mfma_scale_f32_16x16x128_f8f6f4 v[86:89], v[10:17], v[170:177], v[86:89], v194, v169 op_sel_hi:[0,0,0]
	v_mfma_scale_f32_16x16x128_f8f6f4 v[82:85], v[2:9], v[170:177], v[82:85], v194, v169 op_sel_hi:[0,0,0]
	v_mfma_scale_f32_16x16x128_f8f6f4 v[70:73], v[10:17], v[202:209], v[70:73], v194, v169 op_sel_hi:[0,0,0]
	v_mfma_scale_f32_16x16x128_f8f6f4 v[66:69], v[2:9], v[202:209], v[66:69], v194, v169 op_sel_hi:[0,0,0]
	v_mfma_scale_f32_16x16x128_f8f6f4 v[54:57], v[10:17], v[210:217], v[54:57], v194, v169 op_sel_hi:[0,0,0]
	v_mfma_scale_f32_16x16x128_f8f6f4 v[50:53], v[2:9], v[210:217], v[50:53], v194, v169 op_sel_hi:[0,0,0]
	v_mfma_scale_f32_16x16x128_f8f6f4 v[38:41], v[10:17], v[236:243], v[38:41], v194, v169 op_sel_hi:[0,0,0]
	v_mfma_scale_f32_16x16x128_f8f6f4 v[34:37], v[2:9], v[236:243], v[34:37], v194, v169 op_sel_hi:[0,0,0]
	s_setprio 0
	s_barrier
	s_add_u32 s35, s35, 0x100
	s_addc_u32 s45, s45, 0
	s_cmp_lt_i32 s75, s16
	s_mov_b64 s[18:19], s[42:43]
	s_mov_b32 s70, s75
	s_cbranch_scc1 .LBB0_1923
	s_branch .Lpeelexitph18
.LBB0_1923:
	s_add_i32 s75, s70, 2
	s_add_u32 s42, s18, 0x100
	s_addc_u32 s43, s19, 0
	s_add_i32 s46, 0, 0x10000
	s_cmp_eq_u32 s14, s70
	s_cselect_b32 vcc_hi, s69, s43
	s_cselect_b32 vcc_lo, s68, s42
	s_cselect_b32 s71, s37, s45
	s_cselect_b32 s70, s36, s35
	s_add_i32 s47, 0, 0x14000
	v_add_u32_e32 v2, s46, v196
	v_add_u32_e32 v6, s47, v196
	ds_read_b128 v[26:29], v2
	ds_read_b128 v[30:33], v2 offset:1024
	ds_read_b128 v[18:21], v2 offset:2048
	ds_read_b128 v[22:25], v2 offset:3072
	ds_read_b128 v[10:13], v6
	ds_read_b128 v[14:17], v6 offset:1024
	ds_read_b128 v[2:5], v6 offset:2048
	ds_read_b128 v[6:9], v6 offset:3072
	v_lshl_add_u64 v[218:219], s[18:19], 0, v[184:185]
	s_add_i32 m0, s73, 0xc000
	ds_read_b128 v[170:173], v201
	ds_read_b128 v[174:177], v201 offset:1024
	ds_read_b128 v[186:189], v201 offset:2048
	ds_read_b128 v[190:193], v201 offset:3072
	ds_read_b128 v[202:205], v201 offset:4096
	ds_read_b128 v[206:209], v201 offset:5120
	ds_read_b128 v[210:213], v201 offset:6144
	ds_read_b128 v[214:217], v201 offset:7168
	global_load_lds_dwordx4 v[218:219], off
	v_lshl_add_u64 v[218:219], s[18:19], 0, v[182:183]
	s_add_i32 m0, s73, 0xe000
	s_nop 0
	global_load_lds_dwordx4 v[218:219], off
	s_waitcnt vmcnt(8) lgkmcnt(0)
	s_barrier
	s_setprio 1
	v_mfma_scale_f32_16x16x128_f8f6f4 v[158:161], v[26:33], v[170:177], v[158:161], v194, v169 op_sel_hi:[0,0,0]
	v_mfma_scale_f32_16x16x128_f8f6f4 v[154:157], v[18:25], v[170:177], v[154:157], v194, v169 op_sel_hi:[0,0,0]
	v_mfma_scale_f32_16x16x128_f8f6f4 v[142:145], v[26:33], v[186:193], v[142:145], v194, v169 op_sel_hi:[0,0,0]
	v_mfma_scale_f32_16x16x128_f8f6f4 v[138:141], v[18:25], v[186:193], v[138:141], v194, v169 op_sel_hi:[0,0,0]
	v_mfma_scale_f32_16x16x128_f8f6f4 v[126:129], v[26:33], v[202:209], v[126:129], v194, v169 op_sel_hi:[0,0,0]
	v_mfma_scale_f32_16x16x128_f8f6f4 v[122:125], v[18:25], v[202:209], v[122:125], v194, v169 op_sel_hi:[0,0,0]
	v_mfma_scale_f32_16x16x128_f8f6f4 v[110:113], v[26:33], v[210:217], v[110:113], v194, v169 op_sel_hi:[0,0,0]
	v_mfma_scale_f32_16x16x128_f8f6f4 v[106:109], v[18:25], v[210:217], v[106:109], v194, v169 op_sel_hi:[0,0,0]
	s_setprio 0
	s_setprio 1
	v_mfma_scale_f32_16x16x128_f8f6f4 v[150:153], v[10:17], v[170:177], v[150:153], v194, v169 op_sel_hi:[0,0,0]
	v_mfma_scale_f32_16x16x128_f8f6f4 v[146:149], v[2:9], v[170:177], v[146:149], v194, v169 op_sel_hi:[0,0,0]
	v_mfma_scale_f32_16x16x128_f8f6f4 v[134:137], v[10:17], v[186:193], v[134:137], v194, v169 op_sel_hi:[0,0,0]
	v_mfma_scale_f32_16x16x128_f8f6f4 v[130:133], v[2:9], v[186:193], v[130:133], v194, v169 op_sel_hi:[0,0,0]
	v_mfma_scale_f32_16x16x128_f8f6f4 v[118:121], v[10:17], v[202:209], v[118:121], v194, v169 op_sel_hi:[0,0,0]
	v_mfma_scale_f32_16x16x128_f8f6f4 v[114:117], v[2:9], v[202:209], v[114:117], v194, v169 op_sel_hi:[0,0,0]
	v_mfma_scale_f32_16x16x128_f8f6f4 v[102:105], v[10:17], v[210:217], v[102:105], v194, v169 op_sel_hi:[0,0,0]
	v_mfma_scale_f32_16x16x128_f8f6f4 v[98:101], v[2:9], v[210:217], v[98:101], v194, v169 op_sel_hi:[0,0,0]
	s_setprio 0
	s_barrier
	s_add_i32 s18, s46, s95
	v_lshl_add_u64 v[186:187], s[70:71], 0, v[164:165]
	s_mov_b32 m0, s18
	ds_read_b128 v[170:173], v201 offset:16384
	ds_read_b128 v[174:177], v201 offset:17408
	ds_read_b128 v[202:205], v201 offset:18432
	ds_read_b128 v[206:209], v201 offset:19456
	ds_read_b128 v[210:213], v201 offset:20480
	ds_read_b128 v[214:217], v201 offset:21504
	ds_read_b128 v[236:239], v201 offset:22528
	ds_read_b128 v[240:243], v201 offset:23552
	global_load_lds_dwordx4 v[186:187], off
	s_add_i32 m0, s18, 0x2000
	s_add_u32 s18, s70, 0x70000
	v_lshl_add_u64 v[188:189], s[70:71], 0, v[180:181]
	s_addc_u32 s19, s71, 0
	s_add_i32 s46, s47, s95
	global_load_lds_dwordx4 v[188:189], off
	v_lshl_add_u64 v[190:191], s[18:19], 0, v[164:165]
	s_mov_b32 m0, s46
	v_lshl_add_u64 v[192:193], vcc, 0, v[178:179]
	global_load_lds_dwordx4 v[190:191], off
	v_lshl_add_u64 v[190:191], s[18:19], 0, v[180:181]
	s_add_i32 m0, s46, 0x2000
	s_nop 0
	global_load_lds_dwordx4 v[190:191], off
	v_lshl_add_u64 v[190:191], vcc, 0, v[162:163]
	s_mov_b32 m0, s73
	s_nop 0
	global_load_lds_dwordx4 v[190:191], off
	s_mov_b32 m0, s8
	s_nop 0
	global_load_lds_dwordx4 v[192:193], off
	s_waitcnt vmcnt(8) lgkmcnt(0)
	s_barrier
	s_setprio 1
	v_mfma_scale_f32_16x16x128_f8f6f4 v[94:97], v[26:33], v[170:177], v[94:97], v194, v169 op_sel_hi:[0,0,0]
	v_mfma_scale_f32_16x16x128_f8f6f4 v[90:93], v[18:25], v[170:177], v[90:93], v194, v169 op_sel_hi:[0,0,0]
	v_mfma_scale_f32_16x16x128_f8f6f4 v[78:81], v[26:33], v[202:209], v[78:81], v194, v169 op_sel_hi:[0,0,0]
	v_mfma_scale_f32_16x16x128_f8f6f4 v[74:77], v[18:25], v[202:209], v[74:77], v194, v169 op_sel_hi:[0,0,0]
	v_mfma_scale_f32_16x16x128_f8f6f4 v[62:65], v[26:33], v[210:217], v[62:65], v194, v169 op_sel_hi:[0,0,0]
	v_mfma_scale_f32_16x16x128_f8f6f4 v[58:61], v[18:25], v[210:217], v[58:61], v194, v169 op_sel_hi:[0,0,0]
	v_mfma_scale_f32_16x16x128_f8f6f4 v[46:49], v[26:33], v[236:243], v[46:49], v194, v169 op_sel_hi:[0,0,0]
	v_mfma_scale_f32_16x16x128_f8f6f4 v[42:45], v[18:25], v[236:243], v[42:45], v194, v169 op_sel_hi:[0,0,0]
	s_setprio 0
	s_setprio 1
	v_mfma_scale_f32_16x16x128_f8f6f4 v[86:89], v[10:17], v[170:177], v[86:89], v194, v169 op_sel_hi:[0,0,0]
	v_mfma_scale_f32_16x16x128_f8f6f4 v[82:85], v[2:9], v[170:177], v[82:85], v194, v169 op_sel_hi:[0,0,0]
	v_mfma_scale_f32_16x16x128_f8f6f4 v[70:73], v[10:17], v[202:209], v[70:73], v194, v169 op_sel_hi:[0,0,0]
	v_mfma_scale_f32_16x16x128_f8f6f4 v[66:69], v[2:9], v[202:209], v[66:69], v194, v169 op_sel_hi:[0,0,0]
	v_mfma_scale_f32_16x16x128_f8f6f4 v[54:57], v[10:17], v[210:217], v[54:57], v194, v169 op_sel_hi:[0,0,0]
	v_mfma_scale_f32_16x16x128_f8f6f4 v[50:53], v[2:9], v[210:217], v[50:53], v194, v169 op_sel_hi:[0,0,0]
	v_mfma_scale_f32_16x16x128_f8f6f4 v[38:41], v[10:17], v[236:243], v[38:41], v194, v169 op_sel_hi:[0,0,0]
	v_mfma_scale_f32_16x16x128_f8f6f4 v[34:37], v[2:9], v[236:243], v[34:37], v194, v169 op_sel_hi:[0,0,0]
	s_setprio 0
	s_barrier
	s_add_i32 s46, 0, 0x18000
	s_add_i32 s47, 0, 0x1c000
	v_add_u32_e32 v2, s46, v196
	v_add_u32_e32 v6, s47, v196
	ds_read_b128 v[26:29], v2
	ds_read_b128 v[30:33], v2 offset:1024
	ds_read_b128 v[18:21], v2 offset:2048
	ds_read_b128 v[22:25], v2 offset:3072
	ds_read_b128 v[10:13], v6
	ds_read_b128 v[14:17], v6 offset:1024
	ds_read_b128 v[2:5], v6 offset:2048
	ds_read_b128 v[6:9], v6 offset:3072
	s_add_u32 s18, vcc_lo, 0x70000
	s_addc_u32 s19, vcc_hi, 0
	s_mov_b32 m0, s11
	v_lshl_add_u64 v[218:219], s[18:19], 0, v[162:163]
	ds_read_b128 v[170:173], v201 offset:32768
	ds_read_b128 v[174:177], v201 offset:33792
	ds_read_b128 v[202:205], v201 offset:34816
	ds_read_b128 v[206:209], v201 offset:35840
	ds_read_b128 v[210:213], v201 offset:36864
	ds_read_b128 v[214:217], v201 offset:37888
	ds_read_b128 v[236:239], v201 offset:38912
	ds_read_b128 v[240:243], v201 offset:39936
	global_load_lds_dwordx4 v[218:219], off
	v_lshl_add_u64 v[218:219], s[18:19], 0, v[178:179]
	s_mov_b32 m0, s84
	s_nop 0
	global_load_lds_dwordx4 v[218:219], off
	s_waitcnt vmcnt(8) lgkmcnt(0)
	s_barrier
	s_setprio 1
	v_mfma_scale_f32_16x16x128_f8f6f4 v[158:161], v[26:33], v[170:177], v[158:161], v194, v169 op_sel_hi:[0,0,0]
	v_mfma_scale_f32_16x16x128_f8f6f4 v[154:157], v[18:25], v[170:177], v[154:157], v194, v169 op_sel_hi:[0,0,0]
	v_mfma_scale_f32_16x16x128_f8f6f4 v[142:145], v[26:33], v[202:209], v[142:145], v194, v169 op_sel_hi:[0,0,0]
	v_mfma_scale_f32_16x16x128_f8f6f4 v[138:141], v[18:25], v[202:209], v[138:141], v194, v169 op_sel_hi:[0,0,0]
	v_mfma_scale_f32_16x16x128_f8f6f4 v[126:129], v[26:33], v[210:217], v[126:129], v194, v169 op_sel_hi:[0,0,0]
	v_mfma_scale_f32_16x16x128_f8f6f4 v[122:125], v[18:25], v[210:217], v[122:125], v194, v169 op_sel_hi:[0,0,0]
	v_mfma_scale_f32_16x16x128_f8f6f4 v[110:113], v[26:33], v[236:243], v[110:113], v194, v169 op_sel_hi:[0,0,0]
	v_mfma_scale_f32_16x16x128_f8f6f4 v[106:109], v[18:25], v[236:243], v[106:109], v194, v169 op_sel_hi:[0,0,0]
	s_setprio 0
	s_setprio 1
	v_mfma_scale_f32_16x16x128_f8f6f4 v[150:153], v[10:17], v[170:177], v[150:153], v194, v169 op_sel_hi:[0,0,0]
	v_mfma_scale_f32_16x16x128_f8f6f4 v[146:149], v[2:9], v[170:177], v[146:149], v194, v169 op_sel_hi:[0,0,0]
	v_mfma_scale_f32_16x16x128_f8f6f4 v[134:137], v[10:17], v[202:209], v[134:137], v194, v169 op_sel_hi:[0,0,0]
	v_mfma_scale_f32_16x16x128_f8f6f4 v[130:133], v[2:9], v[202:209], v[130:133], v194, v169 op_sel_hi:[0,0,0]
	v_mfma_scale_f32_16x16x128_f8f6f4 v[118:121], v[10:17], v[210:217], v[118:121], v194, v169 op_sel_hi:[0,0,0]
	v_mfma_scale_f32_16x16x128_f8f6f4 v[114:117], v[2:9], v[210:217], v[114:117], v194, v169 op_sel_hi:[0,0,0]
	v_mfma_scale_f32_16x16x128_f8f6f4 v[102:105], v[10:17], v[236:243], v[102:105], v194, v169 op_sel_hi:[0,0,0]
	v_mfma_scale_f32_16x16x128_f8f6f4 v[98:101], v[2:9], v[236:243], v[98:101], v194, v169 op_sel_hi:[0,0,0]
	s_setprio 0
	s_barrier
	s_add_i32 s18, s46, s95
	v_lshl_add_u64 v[186:187], v[186:187], 0, s[56:57]
	s_mov_b32 m0, s18
	ds_read_b128 v[170:173], v201 offset:49152
	ds_read_b128 v[174:177], v201 offset:50176
	ds_read_b128 v[202:205], v201 offset:51200
	ds_read_b128 v[206:209], v201 offset:52224
	ds_read_b128 v[210:213], v201 offset:53248
	ds_read_b128 v[214:217], v201 offset:54272
	ds_read_b128 v[236:239], v201 offset:55296
	ds_read_b128 v[240:243], v201 offset:56320
	global_load_lds_dwordx4 v[186:187], off
	s_add_i32 m0, s18, 0x2000
	s_add_u32 s18, s70, 0x70080
	v_lshl_add_u64 v[186:187], v[188:189], 0, s[56:57]
	s_addc_u32 s19, s71, 0
	s_add_i32 s46, s47, s95
	global_load_lds_dwordx4 v[186:187], off
	v_lshl_add_u64 v[186:187], s[18:19], 0, v[164:165]
	s_mov_b32 m0, s46
	s_nop 0
	global_load_lds_dwordx4 v[186:187], off
	v_lshl_add_u64 v[186:187], s[18:19], 0, v[180:181]
	s_add_i32 m0, s46, 0x2000
	s_nop 0
	global_load_lds_dwordx4 v[186:187], off
	v_lshl_add_u64 v[186:187], v[190:191], 0, s[56:57]
	s_mov_b32 m0, s0
	s_nop 0
	global_load_lds_dwordx4 v[186:187], off
	v_lshl_add_u64 v[186:187], v[192:193], 0, s[56:57]
	s_mov_b32 m0, s88
	s_nop 0
	global_load_lds_dwordx4 v[186:187], off
	s_waitcnt vmcnt(8) lgkmcnt(0)
	s_barrier
	s_setprio 1
	v_mfma_scale_f32_16x16x128_f8f6f4 v[94:97], v[26:33], v[170:177], v[94:97], v194, v169 op_sel_hi:[0,0,0]
	v_mfma_scale_f32_16x16x128_f8f6f4 v[90:93], v[18:25], v[170:177], v[90:93], v194, v169 op_sel_hi:[0,0,0]
	v_mfma_scale_f32_16x16x128_f8f6f4 v[78:81], v[26:33], v[202:209], v[78:81], v194, v169 op_sel_hi:[0,0,0]
	v_mfma_scale_f32_16x16x128_f8f6f4 v[74:77], v[18:25], v[202:209], v[74:77], v194, v169 op_sel_hi:[0,0,0]
	v_mfma_scale_f32_16x16x128_f8f6f4 v[62:65], v[26:33], v[210:217], v[62:65], v194, v169 op_sel_hi:[0,0,0]
	v_mfma_scale_f32_16x16x128_f8f6f4 v[58:61], v[18:25], v[210:217], v[58:61], v194, v169 op_sel_hi:[0,0,0]
	v_mfma_scale_f32_16x16x128_f8f6f4 v[46:49], v[26:33], v[236:243], v[46:49], v194, v169 op_sel_hi:[0,0,0]
	v_mfma_scale_f32_16x16x128_f8f6f4 v[42:45], v[18:25], v[236:243], v[42:45], v194, v169 op_sel_hi:[0,0,0]
	s_setprio 0
	s_setprio 1
	v_mfma_scale_f32_16x16x128_f8f6f4 v[86:89], v[10:17], v[170:177], v[86:89], v194, v169 op_sel_hi:[0,0,0]
	v_mfma_scale_f32_16x16x128_f8f6f4 v[82:85], v[2:9], v[170:177], v[82:85], v194, v169 op_sel_hi:[0,0,0]
	v_mfma_scale_f32_16x16x128_f8f6f4 v[70:73], v[10:17], v[202:209], v[70:73], v194, v169 op_sel_hi:[0,0,0]
	v_mfma_scale_f32_16x16x128_f8f6f4 v[66:69], v[2:9], v[202:209], v[66:69], v194, v169 op_sel_hi:[0,0,0]
	v_mfma_scale_f32_16x16x128_f8f6f4 v[54:57], v[10:17], v[210:217], v[54:57], v194, v169 op_sel_hi:[0,0,0]
	v_mfma_scale_f32_16x16x128_f8f6f4 v[50:53], v[2:9], v[210:217], v[50:53], v194, v169 op_sel_hi:[0,0,0]
	v_mfma_scale_f32_16x16x128_f8f6f4 v[38:41], v[10:17], v[236:243], v[38:41], v194, v169 op_sel_hi:[0,0,0]
	v_mfma_scale_f32_16x16x128_f8f6f4 v[34:37], v[2:9], v[236:243], v[34:37], v194, v169 op_sel_hi:[0,0,0]
	s_setprio 0
	s_barrier
	s_add_u32 s35, s35, 0x100
	s_addc_u32 s45, s45, 0
	s_cmp_lt_i32 s75, s16
	s_mov_b64 s[18:19], s[42:43]
	s_mov_b32 s70, s75
	s_cbranch_scc1 .LBB0_1923
